# speedup vs baseline: 1.0220x; 1.0220x over previous
.Lpf_vQ:
	s_lshl_b32 s25, s25, 6
	s_add_u32 s29, s10, s25
	s_lshr_b32 s29, s29, 4
	v_add_u32_e32 v5, s25, v3
	v_lshlrev_b32_e32 v5, 7, v5
	v_add_u32_e32 v15, v5, v6
	v_add_u32_e32 v16, v5, v7
	v_add_u32_e32 v5, 0x8000, v9
	v_add_u32_e32 v17, v5, v6
	v_add_u32_e32 v18, v5, v7
	v_add_u32_e32 v19, 0x18000, v15
	v_add_u32_e32 v20, 0x18000, v16
	v_add_u32_e32 v21, 0x18000, v17
	v_add_u32_e32 v22, 0x18000, v18
	v_lshlrev_b32_e32 v5, 4, v4
	global_load_dwordx4 v[24:27], v5, s[14:15] offset:0
	global_load_dwordx4 v[28:31], v5, s[14:15] offset:64
	global_load_dwordx4 v[32:35], v5, s[14:15] offset:128
	global_load_dwordx4 v[36:39], v5, s[14:15] offset:192
	global_load_dwordx4 v[40:43], v5, s[16:17] offset:0
	global_load_dwordx4 v[44:47], v5, s[16:17] offset:64
	global_load_dwordx4 v[48:51], v5, s[16:17] offset:128
	global_load_dwordx4 v[52:55], v5, s[16:17] offset:192
	s_add_u32 m0, s28, 0x0
	s_nop 0
	global_load_lds_dwordx4 v10, s[4:5]
	s_add_u32 m0, s28, 0x2000
	s_nop 0
	global_load_lds_dwordx4 v11, s[4:5]
	s_add_u32 m0, s28, 0x4000
	s_nop 0
	global_load_lds_dwordx4 v12, s[4:5]
	s_add_u32 m0, s28, 0x6000
	s_nop 0
	global_load_lds_dwordx4 v13, s[4:5]
	s_add_u32 s4, s4, s20
	s_addc_u32 s5, s5, 0
	s_add_u32 m0, s28, 0x8000
	s_nop 0
	global_load_lds_dwordx4 v10, s[6:7]
	s_add_u32 m0, s28, 0xa000
	s_nop 0
	global_load_lds_dwordx4 v11, s[6:7]
	s_add_u32 s6, s6, s20
	s_addc_u32 s7, s7, 0
	s_add_u32 m0, s28, 0xc000
	s_nop 0
	global_load_lds_dwordx4 v10, s[4:5]
	s_add_u32 m0, s28, 0xe000
	s_nop 0
	global_load_lds_dwordx4 v11, s[4:5]
	s_add_u32 m0, s28, 0x10000
	s_nop 0
	global_load_lds_dwordx4 v12, s[4:5]
	s_add_u32 m0, s28, 0x12000
	s_nop 0
	global_load_lds_dwordx4 v13, s[4:5]
	s_add_u32 s4, s4, s20
	s_addc_u32 s5, s5, 0
	s_add_u32 m0, s28, 0x14000
	s_nop 0
	global_load_lds_dwordx4 v10, s[6:7]
	s_add_u32 m0, s28, 0x16000
	s_nop 0
	global_load_lds_dwordx4 v11, s[6:7]
	s_add_u32 s6, s6, s20
	s_addc_u32 s7, s7, 0
	s_add_u32 m0, s28, 0x18000
	s_nop 0
	global_load_lds_dwordx4 v10, s[4:5]
	s_add_u32 m0, s28, 0x1a000
	s_nop 0
	global_load_lds_dwordx4 v11, s[4:5]
	s_add_u32 m0, s28, 0x1c000
	s_nop 0
	global_load_lds_dwordx4 v12, s[4:5]
	s_add_u32 m0, s28, 0x1e000
	s_nop 0
	global_load_lds_dwordx4 v13, s[4:5]
	s_add_u32 s4, s4, s20
	s_addc_u32 s5, s5, 0
	s_add_u32 m0, s28, 0x20000
	s_nop 0
	global_load_lds_dwordx4 v10, s[6:7]
	s_add_u32 m0, s28, 0x22000
	s_nop 0
	global_load_lds_dwordx4 v11, s[6:7]
	s_add_u32 s6, s6, s20
	s_addc_u32 s7, s7, 0
	s_waitcnt vmcnt(12) lgkmcnt(0)
	s_barrier
	s_waitcnt lgkmcnt(7)
	ds_read_b128 v[136:139], v15
	ds_read_b128 v[156:159], v17
	ds_read_b128 v[160:163], v17 offset:2048
	ds_read_b128 v[164:167], v17 offset:4096
	ds_read_b128 v[168:171], v17 offset:6144
	ds_read_b128 v[140:143], v15 offset:2048
	ds_read_b128 v[144:147], v15 offset:4096
	ds_read_b128 v[148:151], v15 offset:6144
	s_waitcnt lgkmcnt(7)
	ds_read_b128 v[172:175], v16
	ds_read_b128 v[192:195], v18
	ds_read_b128 v[196:199], v18 offset:2048
	ds_read_b128 v[200:203], v18 offset:4096
	ds_read_b128 v[204:207], v18 offset:6144
	ds_read_b128 v[176:179], v16 offset:2048
	ds_read_b128 v[180:183], v16 offset:4096
	ds_read_b128 v[184:187], v16 offset:6144
	s_waitcnt lgkmcnt(14)
	v_mfma_f32_16x16x32_f16 v[56:59], v[156:159], v[136:139], 0
	s_waitcnt lgkmcnt(13)
	v_mfma_f32_16x16x32_f16 v[60:63], v[160:163], v[136:139], 0
	s_waitcnt lgkmcnt(12)
	v_mfma_f32_16x16x32_f16 v[64:67], v[164:167], v[136:139], 0
	s_waitcnt lgkmcnt(11)
	v_mfma_f32_16x16x32_f16 v[68:71], v[168:171], v[136:139], 0
	s_waitcnt lgkmcnt(10)
	v_mfma_f32_16x16x32_f16 v[72:75], v[156:159], v[140:143], 0
	v_mfma_f32_16x16x32_f16 v[76:79], v[160:163], v[140:143], 0
	v_mfma_f32_16x16x32_f16 v[80:83], v[164:167], v[140:143], 0
	v_mfma_f32_16x16x32_f16 v[84:87], v[168:171], v[140:143], 0
	s_waitcnt lgkmcnt(9)
	v_mfma_f32_16x16x32_f16 v[88:91], v[156:159], v[144:147], 0
	v_mfma_f32_16x16x32_f16 v[92:95], v[160:163], v[144:147], 0
	v_mfma_f32_16x16x32_f16 v[96:99], v[164:167], v[144:147], 0
	v_mfma_f32_16x16x32_f16 v[100:103], v[168:171], v[144:147], 0
	s_waitcnt lgkmcnt(8)
	v_mfma_f32_16x16x32_f16 v[104:107], v[156:159], v[148:151], 0
	v_mfma_f32_16x16x32_f16 v[108:111], v[160:163], v[148:151], 0
	v_mfma_f32_16x16x32_f16 v[112:115], v[164:167], v[148:151], 0
	v_mfma_f32_16x16x32_f16 v[116:119], v[168:171], v[148:151], 0
	s_waitcnt vmcnt(6) lgkmcnt(0)
	s_barrier
	s_waitcnt lgkmcnt(7)
	ds_read_b128 v[136:139], v15 offset:49152
	ds_read_b128 v[156:159], v17 offset:49152
	ds_read_b128 v[160:163], v17 offset:51200
	ds_read_b128 v[164:167], v17 offset:53248
	ds_read_b128 v[168:171], v17 offset:55296
	ds_read_b128 v[140:143], v15 offset:51200
	ds_read_b128 v[144:147], v15 offset:53248
	ds_read_b128 v[148:151], v15 offset:55296
	s_waitcnt lgkmcnt(14)
	v_mfma_f32_16x16x32_f16 v[56:59], v[192:195], v[172:175], v[56:59]
	s_add_u32 m0, s28, 0x0
	s_nop 0
	global_load_lds_dwordx4 v10, s[4:5]
	s_waitcnt lgkmcnt(13)
	v_mfma_f32_16x16x32_f16 v[60:63], v[196:199], v[172:175], v[60:63]
	s_waitcnt lgkmcnt(12)
	v_mfma_f32_16x16x32_f16 v[64:67], v[200:203], v[172:175], v[64:67]
	s_waitcnt lgkmcnt(11)
	v_mfma_f32_16x16x32_f16 v[68:71], v[204:207], v[172:175], v[68:71]
	s_waitcnt lgkmcnt(10)
	v_mfma_f32_16x16x32_f16 v[72:75], v[192:195], v[176:179], v[72:75]
	v_mfma_f32_16x16x32_f16 v[76:79], v[196:199], v[176:179], v[76:79]
	s_add_u32 m0, s28, 0x2000
	s_nop 0
	global_load_lds_dwordx4 v11, s[4:5]
	v_mfma_f32_16x16x32_f16 v[80:83], v[200:203], v[176:179], v[80:83]
	v_mfma_f32_16x16x32_f16 v[84:87], v[204:207], v[176:179], v[84:87]
	s_waitcnt lgkmcnt(9)
	v_mfma_f32_16x16x32_f16 v[88:91], v[192:195], v[180:183], v[88:91]
	v_mfma_f32_16x16x32_f16 v[92:95], v[196:199], v[180:183], v[92:95]
	v_mfma_f32_16x16x32_f16 v[96:99], v[200:203], v[180:183], v[96:99]
	s_add_u32 m0, s28, 0x4000
	s_nop 0
	global_load_lds_dwordx4 v12, s[4:5]
	v_mfma_f32_16x16x32_f16 v[100:103], v[204:207], v[180:183], v[100:103]
	s_waitcnt lgkmcnt(8)
	v_mfma_f32_16x16x32_f16 v[104:107], v[192:195], v[184:187], v[104:107]
	v_mfma_f32_16x16x32_f16 v[108:111], v[196:199], v[184:187], v[108:111]
	v_mfma_f32_16x16x32_f16 v[112:115], v[200:203], v[184:187], v[112:115]
	v_mfma_f32_16x16x32_f16 v[116:119], v[204:207], v[184:187], v[116:119]
	s_waitcnt lgkmcnt(7)
	ds_read_b128 v[172:175], v16 offset:49152
	ds_read_b128 v[192:195], v18 offset:49152
	ds_read_b128 v[196:199], v18 offset:51200
	ds_read_b128 v[200:203], v18 offset:53248
	ds_read_b128 v[204:207], v18 offset:55296
	ds_read_b128 v[176:179], v16 offset:51200
	ds_read_b128 v[180:183], v16 offset:53248
	ds_read_b128 v[184:187], v16 offset:55296
	s_waitcnt lgkmcnt(14)
	v_mfma_f32_16x16x32_f16 v[56:59], v[156:159], v[136:139], v[56:59]
	s_add_u32 m0, s28, 0x6000
	s_nop 0
	global_load_lds_dwordx4 v13, s[4:5]
	s_add_u32 s4, s4, s20
	s_addc_u32 s5, s5, 0
	s_waitcnt lgkmcnt(13)
	v_mfma_f32_16x16x32_f16 v[60:63], v[160:163], v[136:139], v[60:63]
	s_waitcnt lgkmcnt(12)
	v_mfma_f32_16x16x32_f16 v[64:67], v[164:167], v[136:139], v[64:67]
	s_waitcnt lgkmcnt(11)
	v_mfma_f32_16x16x32_f16 v[68:71], v[168:171], v[136:139], v[68:71]
	s_waitcnt lgkmcnt(10)
	v_mfma_f32_16x16x32_f16 v[72:75], v[156:159], v[140:143], v[72:75]
	v_mfma_f32_16x16x32_f16 v[76:79], v[160:163], v[140:143], v[76:79]
	s_add_u32 m0, s28, 0x8000
	s_nop 0
	global_load_lds_dwordx4 v10, s[6:7]
	v_mfma_f32_16x16x32_f16 v[80:83], v[164:167], v[140:143], v[80:83]
	v_mfma_f32_16x16x32_f16 v[84:87], v[168:171], v[140:143], v[84:87]
	s_waitcnt lgkmcnt(9)
	v_mfma_f32_16x16x32_f16 v[88:91], v[156:159], v[144:147], v[88:91]
	v_mfma_f32_16x16x32_f16 v[92:95], v[160:163], v[144:147], v[92:95]
	v_mfma_f32_16x16x32_f16 v[96:99], v[164:167], v[144:147], v[96:99]
	s_add_u32 m0, s28, 0xa000
	s_nop 0
	global_load_lds_dwordx4 v11, s[6:7]
	s_add_u32 s6, s6, s20
	s_addc_u32 s7, s7, 0
	v_mfma_f32_16x16x32_f16 v[100:103], v[168:171], v[144:147], v[100:103]
	s_waitcnt lgkmcnt(8)
	v_mfma_f32_16x16x32_f16 v[104:107], v[156:159], v[148:151], v[104:107]
	v_mfma_f32_16x16x32_f16 v[108:111], v[160:163], v[148:151], v[108:111]
	v_mfma_f32_16x16x32_f16 v[112:115], v[164:167], v[148:151], v[112:115]
	v_mfma_f32_16x16x32_f16 v[116:119], v[168:171], v[148:151], v[116:119]
	s_waitcnt vmcnt(6) lgkmcnt(0)
	s_barrier
	s_waitcnt lgkmcnt(7)
	ds_read_b128 v[136:139], v19
	ds_read_b128 v[156:159], v21
	ds_read_b128 v[160:163], v21 offset:2048
	ds_read_b128 v[164:167], v21 offset:4096
	ds_read_b128 v[168:171], v21 offset:6144
	ds_read_b128 v[140:143], v19 offset:2048
	ds_read_b128 v[144:147], v19 offset:4096
	ds_read_b128 v[148:151], v19 offset:6144
	s_waitcnt lgkmcnt(14)
	v_mfma_f32_16x16x32_f16 v[56:59], v[192:195], v[172:175], v[56:59]
	s_add_u32 m0, s28, 0xc000
	s_nop 0
	global_load_lds_dwordx4 v10, s[4:5]
	s_waitcnt lgkmcnt(13)
	v_mfma_f32_16x16x32_f16 v[60:63], v[196:199], v[172:175], v[60:63]
	s_waitcnt lgkmcnt(12)
	v_mfma_f32_16x16x32_f16 v[64:67], v[200:203], v[172:175], v[64:67]
	s_waitcnt lgkmcnt(11)
	v_mfma_f32_16x16x32_f16 v[68:71], v[204:207], v[172:175], v[68:71]
	s_waitcnt lgkmcnt(10)
	v_mfma_f32_16x16x32_f16 v[72:75], v[192:195], v[176:179], v[72:75]
	v_mfma_f32_16x16x32_f16 v[76:79], v[196:199], v[176:179], v[76:79]
	s_add_u32 m0, s28, 0xe000
	s_nop 0
	global_load_lds_dwordx4 v11, s[4:5]
	v_mfma_f32_16x16x32_f16 v[80:83], v[200:203], v[176:179], v[80:83]
	v_mfma_f32_16x16x32_f16 v[84:87], v[204:207], v[176:179], v[84:87]
	s_waitcnt lgkmcnt(9)
	v_mfma_f32_16x16x32_f16 v[88:91], v[192:195], v[180:183], v[88:91]
	v_mfma_f32_16x16x32_f16 v[92:95], v[196:199], v[180:183], v[92:95]
	v_mfma_f32_16x16x32_f16 v[96:99], v[200:203], v[180:183], v[96:99]
	s_add_u32 m0, s28, 0x10000
	s_nop 0
	global_load_lds_dwordx4 v12, s[4:5]
	v_mfma_f32_16x16x32_f16 v[100:103], v[204:207], v[180:183], v[100:103]
	s_waitcnt lgkmcnt(8)
	v_mfma_f32_16x16x32_f16 v[104:107], v[192:195], v[184:187], v[104:107]
	v_mfma_f32_16x16x32_f16 v[108:111], v[196:199], v[184:187], v[108:111]
	v_mfma_f32_16x16x32_f16 v[112:115], v[200:203], v[184:187], v[112:115]
	v_mfma_f32_16x16x32_f16 v[116:119], v[204:207], v[184:187], v[116:119]
	s_waitcnt lgkmcnt(7)
	ds_read_b128 v[172:175], v20
	ds_read_b128 v[192:195], v22
	ds_read_b128 v[196:199], v22 offset:2048
	ds_read_b128 v[200:203], v22 offset:4096
	ds_read_b128 v[204:207], v22 offset:6144
	ds_read_b128 v[176:179], v20 offset:2048
	ds_read_b128 v[180:183], v20 offset:4096
	ds_read_b128 v[184:187], v20 offset:6144
	s_waitcnt lgkmcnt(14)
	v_mfma_f32_16x16x32_f16 v[56:59], v[156:159], v[136:139], v[56:59]
	s_add_u32 m0, s28, 0x12000
	s_nop 0
	global_load_lds_dwordx4 v13, s[4:5]
	s_add_u32 s4, s4, s20
	s_addc_u32 s5, s5, 0
	s_waitcnt lgkmcnt(13)
	v_mfma_f32_16x16x32_f16 v[60:63], v[160:163], v[136:139], v[60:63]
	s_waitcnt lgkmcnt(12)
	v_mfma_f32_16x16x32_f16 v[64:67], v[164:167], v[136:139], v[64:67]
	s_waitcnt lgkmcnt(11)
	v_mfma_f32_16x16x32_f16 v[68:71], v[168:171], v[136:139], v[68:71]
	s_waitcnt lgkmcnt(10)
	v_mfma_f32_16x16x32_f16 v[72:75], v[156:159], v[140:143], v[72:75]
	v_mfma_f32_16x16x32_f16 v[76:79], v[160:163], v[140:143], v[76:79]
	s_add_u32 m0, s28, 0x14000
	s_nop 0
	global_load_lds_dwordx4 v10, s[6:7]
	v_mfma_f32_16x16x32_f16 v[80:83], v[164:167], v[140:143], v[80:83]
	v_mfma_f32_16x16x32_f16 v[84:87], v[168:171], v[140:143], v[84:87]
	s_waitcnt lgkmcnt(9)
	v_mfma_f32_16x16x32_f16 v[88:91], v[156:159], v[144:147], v[88:91]
	v_mfma_f32_16x16x32_f16 v[92:95], v[160:163], v[144:147], v[92:95]
	v_mfma_f32_16x16x32_f16 v[96:99], v[164:167], v[144:147], v[96:99]
	s_add_u32 m0, s28, 0x16000
	s_nop 0
	global_load_lds_dwordx4 v11, s[6:7]
	s_add_u32 s6, s6, s20
	s_addc_u32 s7, s7, 0
	v_mfma_f32_16x16x32_f16 v[100:103], v[168:171], v[144:147], v[100:103]
	s_waitcnt lgkmcnt(8)
	v_mfma_f32_16x16x32_f16 v[104:107], v[156:159], v[148:151], v[104:107]
	v_mfma_f32_16x16x32_f16 v[108:111], v[160:163], v[148:151], v[108:111]
	v_mfma_f32_16x16x32_f16 v[112:115], v[164:167], v[148:151], v[112:115]
	v_mfma_f32_16x16x32_f16 v[116:119], v[168:171], v[148:151], v[116:119]
	s_waitcnt vmcnt(6) lgkmcnt(0)
	s_barrier
	s_waitcnt lgkmcnt(7)
	ds_read_b128 v[136:139], v15
	ds_read_b128 v[156:159], v17
	ds_read_b128 v[160:163], v17 offset:2048
	ds_read_b128 v[164:167], v17 offset:4096
	ds_read_b128 v[168:171], v17 offset:6144
	ds_read_b128 v[140:143], v15 offset:2048
	ds_read_b128 v[144:147], v15 offset:4096
	ds_read_b128 v[148:151], v15 offset:6144
	s_waitcnt lgkmcnt(14)
	v_mfma_f32_16x16x32_f16 v[56:59], v[192:195], v[172:175], v[56:59]
	s_add_u32 m0, s28, 0x18000
	s_nop 0
	global_load_lds_dwordx4 v10, s[4:5]
	s_waitcnt lgkmcnt(13)
	v_mfma_f32_16x16x32_f16 v[60:63], v[196:199], v[172:175], v[60:63]
	s_waitcnt lgkmcnt(12)
	v_mfma_f32_16x16x32_f16 v[64:67], v[200:203], v[172:175], v[64:67]
	s_waitcnt lgkmcnt(11)
	v_mfma_f32_16x16x32_f16 v[68:71], v[204:207], v[172:175], v[68:71]
	s_waitcnt lgkmcnt(10)
	v_mfma_f32_16x16x32_f16 v[72:75], v[192:195], v[176:179], v[72:75]
	v_mfma_f32_16x16x32_f16 v[76:79], v[196:199], v[176:179], v[76:79]
	s_add_u32 m0, s28, 0x1a000
	s_nop 0
	global_load_lds_dwordx4 v11, s[4:5]
	v_mfma_f32_16x16x32_f16 v[80:83], v[200:203], v[176:179], v[80:83]
	v_mfma_f32_16x16x32_f16 v[84:87], v[204:207], v[176:179], v[84:87]
	s_waitcnt lgkmcnt(9)
	v_mfma_f32_16x16x32_f16 v[88:91], v[192:195], v[180:183], v[88:91]
	v_mfma_f32_16x16x32_f16 v[92:95], v[196:199], v[180:183], v[92:95]
	v_mfma_f32_16x16x32_f16 v[96:99], v[200:203], v[180:183], v[96:99]
	s_add_u32 m0, s28, 0x1c000
	s_nop 0
	global_load_lds_dwordx4 v12, s[4:5]
	v_mfma_f32_16x16x32_f16 v[100:103], v[204:207], v[180:183], v[100:103]
	s_waitcnt lgkmcnt(8)
	v_mfma_f32_16x16x32_f16 v[104:107], v[192:195], v[184:187], v[104:107]
	v_mfma_f32_16x16x32_f16 v[108:111], v[196:199], v[184:187], v[108:111]
	v_mfma_f32_16x16x32_f16 v[112:115], v[200:203], v[184:187], v[112:115]
	v_mfma_f32_16x16x32_f16 v[116:119], v[204:207], v[184:187], v[116:119]
	s_waitcnt lgkmcnt(7)
	ds_read_b128 v[172:175], v16
	ds_read_b128 v[192:195], v18
	ds_read_b128 v[196:199], v18 offset:2048
	ds_read_b128 v[200:203], v18 offset:4096
	ds_read_b128 v[204:207], v18 offset:6144
	ds_read_b128 v[176:179], v16 offset:2048
	ds_read_b128 v[180:183], v16 offset:4096
	ds_read_b128 v[184:187], v16 offset:6144
	s_waitcnt lgkmcnt(14)
	v_mfma_f32_16x16x32_f16 v[56:59], v[156:159], v[136:139], v[56:59]
	s_add_u32 m0, s28, 0x1e000
	s_nop 0
	global_load_lds_dwordx4 v13, s[4:5]
	s_add_u32 s4, s4, s20
	s_addc_u32 s5, s5, 0
	s_waitcnt lgkmcnt(13)
	v_mfma_f32_16x16x32_f16 v[60:63], v[160:163], v[136:139], v[60:63]
	s_waitcnt lgkmcnt(12)
	v_mfma_f32_16x16x32_f16 v[64:67], v[164:167], v[136:139], v[64:67]
	s_waitcnt lgkmcnt(11)
	v_mfma_f32_16x16x32_f16 v[68:71], v[168:171], v[136:139], v[68:71]
	s_waitcnt lgkmcnt(10)
	v_mfma_f32_16x16x32_f16 v[72:75], v[156:159], v[140:143], v[72:75]
	v_mfma_f32_16x16x32_f16 v[76:79], v[160:163], v[140:143], v[76:79]
	s_add_u32 m0, s28, 0x20000
	s_nop 0
	global_load_lds_dwordx4 v10, s[6:7]
	v_mfma_f32_16x16x32_f16 v[80:83], v[164:167], v[140:143], v[80:83]
	v_mfma_f32_16x16x32_f16 v[84:87], v[168:171], v[140:143], v[84:87]
	s_waitcnt lgkmcnt(9)
	v_mfma_f32_16x16x32_f16 v[88:91], v[156:159], v[144:147], v[88:91]
	v_mfma_f32_16x16x32_f16 v[92:95], v[160:163], v[144:147], v[92:95]
	v_mfma_f32_16x16x32_f16 v[96:99], v[164:167], v[144:147], v[96:99]
	s_add_u32 m0, s28, 0x22000
	s_nop 0
	global_load_lds_dwordx4 v11, s[6:7]
	s_add_u32 s6, s6, s20
	s_addc_u32 s7, s7, 0
	v_mfma_f32_16x16x32_f16 v[100:103], v[168:171], v[144:147], v[100:103]
	s_waitcnt lgkmcnt(8)
	v_mfma_f32_16x16x32_f16 v[104:107], v[156:159], v[148:151], v[104:107]
	v_mfma_f32_16x16x32_f16 v[108:111], v[160:163], v[148:151], v[108:111]
	v_mfma_f32_16x16x32_f16 v[112:115], v[164:167], v[148:151], v[112:115]
	v_mfma_f32_16x16x32_f16 v[116:119], v[168:171], v[148:151], v[116:119]
	s_waitcnt vmcnt(6) lgkmcnt(0)
	s_barrier
	s_waitcnt lgkmcnt(7)
	ds_read_b128 v[136:139], v15 offset:49152
	ds_read_b128 v[156:159], v17 offset:49152
	ds_read_b128 v[160:163], v17 offset:51200
	ds_read_b128 v[164:167], v17 offset:53248
	ds_read_b128 v[168:171], v17 offset:55296
	ds_read_b128 v[140:143], v15 offset:51200
	ds_read_b128 v[144:147], v15 offset:53248
	ds_read_b128 v[148:151], v15 offset:55296
	s_waitcnt lgkmcnt(14)
	v_mfma_f32_16x16x32_f16 v[56:59], v[192:195], v[172:175], v[56:59]
	s_add_u32 m0, s28, 0x0
	s_nop 0
	global_load_lds_dwordx4 v10, s[4:5]
	s_waitcnt lgkmcnt(13)
	v_mfma_f32_16x16x32_f16 v[60:63], v[196:199], v[172:175], v[60:63]
	s_waitcnt lgkmcnt(12)
	v_mfma_f32_16x16x32_f16 v[64:67], v[200:203], v[172:175], v[64:67]
	s_waitcnt lgkmcnt(11)
	v_mfma_f32_16x16x32_f16 v[68:71], v[204:207], v[172:175], v[68:71]
	s_waitcnt lgkmcnt(10)
	v_mfma_f32_16x16x32_f16 v[72:75], v[192:195], v[176:179], v[72:75]
	v_mfma_f32_16x16x32_f16 v[76:79], v[196:199], v[176:179], v[76:79]
	s_add_u32 m0, s28, 0x2000
	s_nop 0
	global_load_lds_dwordx4 v11, s[4:5]
	v_mfma_f32_16x16x32_f16 v[80:83], v[200:203], v[176:179], v[80:83]
	v_mfma_f32_16x16x32_f16 v[84:87], v[204:207], v[176:179], v[84:87]
	s_waitcnt lgkmcnt(9)
	v_mfma_f32_16x16x32_f16 v[88:91], v[192:195], v[180:183], v[88:91]
	v_mfma_f32_16x16x32_f16 v[92:95], v[196:199], v[180:183], v[92:95]
	v_mfma_f32_16x16x32_f16 v[96:99], v[200:203], v[180:183], v[96:99]
	s_add_u32 m0, s28, 0x4000
	s_nop 0
	global_load_lds_dwordx4 v12, s[4:5]
	v_mfma_f32_16x16x32_f16 v[100:103], v[204:207], v[180:183], v[100:103]
	s_waitcnt lgkmcnt(8)
	v_mfma_f32_16x16x32_f16 v[104:107], v[192:195], v[184:187], v[104:107]
	v_mfma_f32_16x16x32_f16 v[108:111], v[196:199], v[184:187], v[108:111]
	v_mfma_f32_16x16x32_f16 v[112:115], v[200:203], v[184:187], v[112:115]
	v_mfma_f32_16x16x32_f16 v[116:119], v[204:207], v[184:187], v[116:119]
	s_waitcnt lgkmcnt(7)
	ds_read_b128 v[172:175], v16 offset:49152
	ds_read_b128 v[192:195], v18 offset:49152
	ds_read_b128 v[196:199], v18 offset:51200
	ds_read_b128 v[200:203], v18 offset:53248
	ds_read_b128 v[204:207], v18 offset:55296
	ds_read_b128 v[176:179], v16 offset:51200
	ds_read_b128 v[180:183], v16 offset:53248
	ds_read_b128 v[184:187], v16 offset:55296
	s_waitcnt lgkmcnt(14)
	v_mfma_f32_16x16x32_f16 v[56:59], v[156:159], v[136:139], v[56:59]
	s_add_u32 m0, s28, 0x6000
	s_nop 0
	global_load_lds_dwordx4 v13, s[4:5]
	s_add_u32 s4, s4, s20
	s_addc_u32 s5, s5, 0
	s_waitcnt lgkmcnt(13)
	v_mfma_f32_16x16x32_f16 v[60:63], v[160:163], v[136:139], v[60:63]
	s_waitcnt lgkmcnt(12)
	v_mfma_f32_16x16x32_f16 v[64:67], v[164:167], v[136:139], v[64:67]
	s_waitcnt lgkmcnt(11)
	v_mfma_f32_16x16x32_f16 v[68:71], v[168:171], v[136:139], v[68:71]
	s_waitcnt lgkmcnt(10)
	v_mfma_f32_16x16x32_f16 v[72:75], v[156:159], v[140:143], v[72:75]
	v_mfma_f32_16x16x32_f16 v[76:79], v[160:163], v[140:143], v[76:79]
	s_add_u32 m0, s28, 0x8000
	s_nop 0
	global_load_lds_dwordx4 v10, s[6:7]
	v_mfma_f32_16x16x32_f16 v[80:83], v[164:167], v[140:143], v[80:83]
	v_mfma_f32_16x16x32_f16 v[84:87], v[168:171], v[140:143], v[84:87]
	s_waitcnt lgkmcnt(9)
	v_mfma_f32_16x16x32_f16 v[88:91], v[156:159], v[144:147], v[88:91]
	v_mfma_f32_16x16x32_f16 v[92:95], v[160:163], v[144:147], v[92:95]
	v_mfma_f32_16x16x32_f16 v[96:99], v[164:167], v[144:147], v[96:99]
	s_add_u32 m0, s28, 0xa000
	s_nop 0
	global_load_lds_dwordx4 v11, s[6:7]
	s_add_u32 s6, s6, s20
	s_addc_u32 s7, s7, 0
	v_mfma_f32_16x16x32_f16 v[100:103], v[168:171], v[144:147], v[100:103]
	s_waitcnt lgkmcnt(8)
	v_mfma_f32_16x16x32_f16 v[104:107], v[156:159], v[148:151], v[104:107]
	v_mfma_f32_16x16x32_f16 v[108:111], v[160:163], v[148:151], v[108:111]
	v_mfma_f32_16x16x32_f16 v[112:115], v[164:167], v[148:151], v[112:115]
	v_mfma_f32_16x16x32_f16 v[116:119], v[168:171], v[148:151], v[116:119]
	s_waitcnt vmcnt(6) lgkmcnt(0)
	s_barrier
	s_waitcnt lgkmcnt(7)
	ds_read_b128 v[136:139], v19
	ds_read_b128 v[156:159], v21
	ds_read_b128 v[160:163], v21 offset:2048
	ds_read_b128 v[164:167], v21 offset:4096
	ds_read_b128 v[168:171], v21 offset:6144
	ds_read_b128 v[140:143], v19 offset:2048
	ds_read_b128 v[144:147], v19 offset:4096
	ds_read_b128 v[148:151], v19 offset:6144
	s_waitcnt lgkmcnt(14)
	v_mfma_f32_16x16x32_f16 v[56:59], v[192:195], v[172:175], v[56:59]
	s_add_u32 m0, s28, 0xc000
	s_nop 0
	global_load_lds_dwordx4 v10, s[4:5]
	s_waitcnt lgkmcnt(13)
	v_mfma_f32_16x16x32_f16 v[60:63], v[196:199], v[172:175], v[60:63]
	s_waitcnt lgkmcnt(12)
	v_mfma_f32_16x16x32_f16 v[64:67], v[200:203], v[172:175], v[64:67]
	s_waitcnt lgkmcnt(11)
	v_mfma_f32_16x16x32_f16 v[68:71], v[204:207], v[172:175], v[68:71]
	s_waitcnt lgkmcnt(10)
	v_mfma_f32_16x16x32_f16 v[72:75], v[192:195], v[176:179], v[72:75]
	v_mfma_f32_16x16x32_f16 v[76:79], v[196:199], v[176:179], v[76:79]
	s_add_u32 m0, s28, 0xe000
	s_nop 0
	global_load_lds_dwordx4 v11, s[4:5]
	v_mfma_f32_16x16x32_f16 v[80:83], v[200:203], v[176:179], v[80:83]
	v_mfma_f32_16x16x32_f16 v[84:87], v[204:207], v[176:179], v[84:87]
	s_waitcnt lgkmcnt(9)
	v_mfma_f32_16x16x32_f16 v[88:91], v[192:195], v[180:183], v[88:91]
	v_mfma_f32_16x16x32_f16 v[92:95], v[196:199], v[180:183], v[92:95]
	v_mfma_f32_16x16x32_f16 v[96:99], v[200:203], v[180:183], v[96:99]
	s_add_u32 m0, s28, 0x10000
	s_nop 0
	global_load_lds_dwordx4 v12, s[4:5]
	v_mfma_f32_16x16x32_f16 v[100:103], v[204:207], v[180:183], v[100:103]
	s_waitcnt lgkmcnt(8)
	v_mfma_f32_16x16x32_f16 v[104:107], v[192:195], v[184:187], v[104:107]
	v_mfma_f32_16x16x32_f16 v[108:111], v[196:199], v[184:187], v[108:111]
	v_mfma_f32_16x16x32_f16 v[112:115], v[200:203], v[184:187], v[112:115]
	v_mfma_f32_16x16x32_f16 v[116:119], v[204:207], v[184:187], v[116:119]
	s_waitcnt lgkmcnt(7)
	ds_read_b128 v[172:175], v20
	ds_read_b128 v[192:195], v22
	ds_read_b128 v[196:199], v22 offset:2048
	ds_read_b128 v[200:203], v22 offset:4096
	ds_read_b128 v[204:207], v22 offset:6144
	ds_read_b128 v[176:179], v20 offset:2048
	ds_read_b128 v[180:183], v20 offset:4096
	ds_read_b128 v[184:187], v20 offset:6144
	s_waitcnt lgkmcnt(14)
	v_mfma_f32_16x16x32_f16 v[56:59], v[156:159], v[136:139], v[56:59]
	s_add_u32 m0, s28, 0x12000
	s_nop 0
	global_load_lds_dwordx4 v13, s[4:5]
	s_add_u32 s4, s4, s20
	s_addc_u32 s5, s5, 0
	s_waitcnt lgkmcnt(13)
	v_mfma_f32_16x16x32_f16 v[60:63], v[160:163], v[136:139], v[60:63]
	s_waitcnt lgkmcnt(12)
	v_mfma_f32_16x16x32_f16 v[64:67], v[164:167], v[136:139], v[64:67]
	s_waitcnt lgkmcnt(11)
	v_mfma_f32_16x16x32_f16 v[68:71], v[168:171], v[136:139], v[68:71]
	s_waitcnt lgkmcnt(10)
	v_mfma_f32_16x16x32_f16 v[72:75], v[156:159], v[140:143], v[72:75]
	v_mfma_f32_16x16x32_f16 v[76:79], v[160:163], v[140:143], v[76:79]
	s_add_u32 m0, s28, 0x14000
	s_nop 0
	global_load_lds_dwordx4 v10, s[6:7]
	v_mfma_f32_16x16x32_f16 v[80:83], v[164:167], v[140:143], v[80:83]
	v_mfma_f32_16x16x32_f16 v[84:87], v[168:171], v[140:143], v[84:87]
	s_waitcnt lgkmcnt(9)
	v_mfma_f32_16x16x32_f16 v[88:91], v[156:159], v[144:147], v[88:91]
	v_mfma_f32_16x16x32_f16 v[92:95], v[160:163], v[144:147], v[92:95]
	v_mfma_f32_16x16x32_f16 v[96:99], v[164:167], v[144:147], v[96:99]
	s_add_u32 m0, s28, 0x16000
	s_nop 0
	global_load_lds_dwordx4 v11, s[6:7]
	s_add_u32 s6, s6, s20
	s_addc_u32 s7, s7, 0
	v_mfma_f32_16x16x32_f16 v[100:103], v[168:171], v[144:147], v[100:103]
	s_waitcnt lgkmcnt(8)
	v_mfma_f32_16x16x32_f16 v[104:107], v[156:159], v[148:151], v[104:107]
	v_mfma_f32_16x16x32_f16 v[108:111], v[160:163], v[148:151], v[108:111]
	v_mfma_f32_16x16x32_f16 v[112:115], v[164:167], v[148:151], v[112:115]
	v_mfma_f32_16x16x32_f16 v[116:119], v[168:171], v[148:151], v[116:119]
	s_waitcnt vmcnt(6) lgkmcnt(0)
	s_barrier
	s_waitcnt lgkmcnt(7)
	ds_read_b128 v[136:139], v15
	ds_read_b128 v[156:159], v17
	ds_read_b128 v[160:163], v17 offset:2048
	ds_read_b128 v[164:167], v17 offset:4096
	ds_read_b128 v[168:171], v17 offset:6144
	ds_read_b128 v[140:143], v15 offset:2048
	ds_read_b128 v[144:147], v15 offset:4096
	ds_read_b128 v[148:151], v15 offset:6144
	s_waitcnt lgkmcnt(14)
	v_mfma_f32_16x16x32_f16 v[56:59], v[192:195], v[172:175], v[56:59]
	s_add_u32 m0, s28, 0x18000
	s_nop 0
	global_load_lds_dwordx4 v10, s[4:5]
	s_waitcnt lgkmcnt(13)
	v_mfma_f32_16x16x32_f16 v[60:63], v[196:199], v[172:175], v[60:63]
	s_waitcnt lgkmcnt(12)
	v_mfma_f32_16x16x32_f16 v[64:67], v[200:203], v[172:175], v[64:67]
	s_waitcnt lgkmcnt(11)
	v_mfma_f32_16x16x32_f16 v[68:71], v[204:207], v[172:175], v[68:71]
	s_waitcnt lgkmcnt(10)
	v_mfma_f32_16x16x32_f16 v[72:75], v[192:195], v[176:179], v[72:75]
	v_mfma_f32_16x16x32_f16 v[76:79], v[196:199], v[176:179], v[76:79]
	s_add_u32 m0, s28, 0x1a000
	s_nop 0
	global_load_lds_dwordx4 v11, s[4:5]
	v_mfma_f32_16x16x32_f16 v[80:83], v[200:203], v[176:179], v[80:83]
	v_mfma_f32_16x16x32_f16 v[84:87], v[204:207], v[176:179], v[84:87]
	s_waitcnt lgkmcnt(9)
	v_mfma_f32_16x16x32_f16 v[88:91], v[192:195], v[180:183], v[88:91]
	v_mfma_f32_16x16x32_f16 v[92:95], v[196:199], v[180:183], v[92:95]
	v_mfma_f32_16x16x32_f16 v[96:99], v[200:203], v[180:183], v[96:99]
	s_add_u32 m0, s28, 0x1c000
	s_nop 0
	global_load_lds_dwordx4 v12, s[4:5]
	v_mfma_f32_16x16x32_f16 v[100:103], v[204:207], v[180:183], v[100:103]
	s_waitcnt lgkmcnt(8)
	v_mfma_f32_16x16x32_f16 v[104:107], v[192:195], v[184:187], v[104:107]
	v_mfma_f32_16x16x32_f16 v[108:111], v[196:199], v[184:187], v[108:111]
	v_mfma_f32_16x16x32_f16 v[112:115], v[200:203], v[184:187], v[112:115]
	v_mfma_f32_16x16x32_f16 v[116:119], v[204:207], v[184:187], v[116:119]
	s_waitcnt lgkmcnt(7)
	ds_read_b128 v[172:175], v16
	ds_read_b128 v[192:195], v18
	ds_read_b128 v[196:199], v18 offset:2048
	ds_read_b128 v[200:203], v18 offset:4096
	ds_read_b128 v[204:207], v18 offset:6144
	ds_read_b128 v[176:179], v16 offset:2048
	ds_read_b128 v[180:183], v16 offset:4096
	ds_read_b128 v[184:187], v16 offset:6144
	s_waitcnt lgkmcnt(14)
	v_mfma_f32_16x16x32_f16 v[56:59], v[156:159], v[136:139], v[56:59]
	s_add_u32 m0, s28, 0x1e000
	s_nop 0
	global_load_lds_dwordx4 v13, s[4:5]
	s_add_u32 s4, s4, s20
	s_addc_u32 s5, s5, 0
	s_waitcnt lgkmcnt(13)
	v_mfma_f32_16x16x32_f16 v[60:63], v[160:163], v[136:139], v[60:63]
	s_waitcnt lgkmcnt(12)
	v_mfma_f32_16x16x32_f16 v[64:67], v[164:167], v[136:139], v[64:67]
	s_waitcnt lgkmcnt(11)
	v_mfma_f32_16x16x32_f16 v[68:71], v[168:171], v[136:139], v[68:71]
	s_waitcnt lgkmcnt(10)
	v_mfma_f32_16x16x32_f16 v[72:75], v[156:159], v[140:143], v[72:75]
	v_mfma_f32_16x16x32_f16 v[76:79], v[160:163], v[140:143], v[76:79]
	s_add_u32 m0, s28, 0x20000
	s_nop 0
	global_load_lds_dwordx4 v10, s[6:7]
	v_mfma_f32_16x16x32_f16 v[80:83], v[164:167], v[140:143], v[80:83]
	v_mfma_f32_16x16x32_f16 v[84:87], v[168:171], v[140:143], v[84:87]
	s_waitcnt lgkmcnt(9)
	v_mfma_f32_16x16x32_f16 v[88:91], v[156:159], v[144:147], v[88:91]
	v_mfma_f32_16x16x32_f16 v[92:95], v[160:163], v[144:147], v[92:95]
	v_mfma_f32_16x16x32_f16 v[96:99], v[164:167], v[144:147], v[96:99]
	s_add_u32 m0, s28, 0x22000
	s_nop 0
	global_load_lds_dwordx4 v11, s[6:7]
	s_add_u32 s6, s6, s20
	s_addc_u32 s7, s7, 0
	v_mfma_f32_16x16x32_f16 v[100:103], v[168:171], v[144:147], v[100:103]
	s_waitcnt lgkmcnt(8)
	v_mfma_f32_16x16x32_f16 v[104:107], v[156:159], v[148:151], v[104:107]
	v_mfma_f32_16x16x32_f16 v[108:111], v[160:163], v[148:151], v[108:111]
	v_mfma_f32_16x16x32_f16 v[112:115], v[164:167], v[148:151], v[112:115]
	v_mfma_f32_16x16x32_f16 v[116:119], v[168:171], v[148:151], v[116:119]
	s_waitcnt vmcnt(6) lgkmcnt(0)
	s_barrier
	s_waitcnt lgkmcnt(7)
	ds_read_b128 v[136:139], v15 offset:49152
	ds_read_b128 v[156:159], v17 offset:49152
	ds_read_b128 v[160:163], v17 offset:51200
	ds_read_b128 v[164:167], v17 offset:53248
	ds_read_b128 v[168:171], v17 offset:55296
	ds_read_b128 v[140:143], v15 offset:51200
	ds_read_b128 v[144:147], v15 offset:53248
	ds_read_b128 v[148:151], v15 offset:55296
	s_waitcnt lgkmcnt(14)
	v_mfma_f32_16x16x32_f16 v[56:59], v[192:195], v[172:175], v[56:59]
	s_add_u32 m0, s28, 0x0
	s_nop 0
	global_load_lds_dwordx4 v10, s[4:5]
	s_waitcnt lgkmcnt(13)
	v_mfma_f32_16x16x32_f16 v[60:63], v[196:199], v[172:175], v[60:63]
	s_waitcnt lgkmcnt(12)
	v_mfma_f32_16x16x32_f16 v[64:67], v[200:203], v[172:175], v[64:67]
	s_waitcnt lgkmcnt(11)
	v_mfma_f32_16x16x32_f16 v[68:71], v[204:207], v[172:175], v[68:71]
	s_waitcnt lgkmcnt(10)
	v_mfma_f32_16x16x32_f16 v[72:75], v[192:195], v[176:179], v[72:75]
	v_mfma_f32_16x16x32_f16 v[76:79], v[196:199], v[176:179], v[76:79]
	s_add_u32 m0, s28, 0x2000
	s_nop 0
	global_load_lds_dwordx4 v11, s[4:5]
	v_mfma_f32_16x16x32_f16 v[80:83], v[200:203], v[176:179], v[80:83]
	v_mfma_f32_16x16x32_f16 v[84:87], v[204:207], v[176:179], v[84:87]
	s_waitcnt lgkmcnt(9)
	v_mfma_f32_16x16x32_f16 v[88:91], v[192:195], v[180:183], v[88:91]
	v_mfma_f32_16x16x32_f16 v[92:95], v[196:199], v[180:183], v[92:95]
	v_mfma_f32_16x16x32_f16 v[96:99], v[200:203], v[180:183], v[96:99]
	s_add_u32 m0, s28, 0x4000
	s_nop 0
	global_load_lds_dwordx4 v12, s[4:5]
	v_mfma_f32_16x16x32_f16 v[100:103], v[204:207], v[180:183], v[100:103]
	s_waitcnt lgkmcnt(8)
	v_mfma_f32_16x16x32_f16 v[104:107], v[192:195], v[184:187], v[104:107]
	v_mfma_f32_16x16x32_f16 v[108:111], v[196:199], v[184:187], v[108:111]
	v_mfma_f32_16x16x32_f16 v[112:115], v[200:203], v[184:187], v[112:115]
	v_mfma_f32_16x16x32_f16 v[116:119], v[204:207], v[184:187], v[116:119]
	s_waitcnt lgkmcnt(7)
	ds_read_b128 v[172:175], v16 offset:49152
	ds_read_b128 v[192:195], v18 offset:49152
	ds_read_b128 v[196:199], v18 offset:51200
	ds_read_b128 v[200:203], v18 offset:53248
	ds_read_b128 v[204:207], v18 offset:55296
	ds_read_b128 v[176:179], v16 offset:51200
	ds_read_b128 v[180:183], v16 offset:53248
	ds_read_b128 v[184:187], v16 offset:55296
	s_waitcnt lgkmcnt(14)
	v_mfma_f32_16x16x32_f16 v[56:59], v[156:159], v[136:139], v[56:59]
	s_add_u32 m0, s28, 0x6000
	s_nop 0
	global_load_lds_dwordx4 v13, s[4:5]
	s_add_u32 s4, s4, s20
	s_addc_u32 s5, s5, 0
	s_waitcnt lgkmcnt(13)
	v_mfma_f32_16x16x32_f16 v[60:63], v[160:163], v[136:139], v[60:63]
	s_waitcnt lgkmcnt(12)
	v_mfma_f32_16x16x32_f16 v[64:67], v[164:167], v[136:139], v[64:67]
	s_waitcnt lgkmcnt(11)
	v_mfma_f32_16x16x32_f16 v[68:71], v[168:171], v[136:139], v[68:71]
	s_waitcnt lgkmcnt(10)
	v_mfma_f32_16x16x32_f16 v[72:75], v[156:159], v[140:143], v[72:75]
	v_mfma_f32_16x16x32_f16 v[76:79], v[160:163], v[140:143], v[76:79]
	s_add_u32 m0, s28, 0x8000
	s_nop 0
	global_load_lds_dwordx4 v10, s[6:7]
	v_mfma_f32_16x16x32_f16 v[80:83], v[164:167], v[140:143], v[80:83]
	v_mfma_f32_16x16x32_f16 v[84:87], v[168:171], v[140:143], v[84:87]
	s_waitcnt lgkmcnt(9)
	v_mfma_f32_16x16x32_f16 v[88:91], v[156:159], v[144:147], v[88:91]
	v_mfma_f32_16x16x32_f16 v[92:95], v[160:163], v[144:147], v[92:95]
	v_mfma_f32_16x16x32_f16 v[96:99], v[164:167], v[144:147], v[96:99]
	s_add_u32 m0, s28, 0xa000
	s_nop 0
	global_load_lds_dwordx4 v11, s[6:7]
	s_add_u32 s6, s6, s20
	s_addc_u32 s7, s7, 0
	v_mfma_f32_16x16x32_f16 v[100:103], v[168:171], v[144:147], v[100:103]
	s_waitcnt lgkmcnt(8)
	v_mfma_f32_16x16x32_f16 v[104:107], v[156:159], v[148:151], v[104:107]
	v_mfma_f32_16x16x32_f16 v[108:111], v[160:163], v[148:151], v[108:111]
	v_mfma_f32_16x16x32_f16 v[112:115], v[164:167], v[148:151], v[112:115]
	v_mfma_f32_16x16x32_f16 v[116:119], v[168:171], v[148:151], v[116:119]
	s_waitcnt vmcnt(6) lgkmcnt(0)
	s_barrier
	s_waitcnt lgkmcnt(7)
	ds_read_b128 v[136:139], v19
	ds_read_b128 v[156:159], v21
	ds_read_b128 v[160:163], v21 offset:2048
	ds_read_b128 v[164:167], v21 offset:4096
	ds_read_b128 v[168:171], v21 offset:6144
	ds_read_b128 v[140:143], v19 offset:2048
	ds_read_b128 v[144:147], v19 offset:4096
	ds_read_b128 v[148:151], v19 offset:6144
	s_waitcnt lgkmcnt(14)
	v_mfma_f32_16x16x32_f16 v[56:59], v[192:195], v[172:175], v[56:59]
	s_add_u32 m0, s28, 0xc000
	s_nop 0
	global_load_lds_dwordx4 v10, s[4:5]
	s_waitcnt lgkmcnt(13)
	v_mfma_f32_16x16x32_f16 v[60:63], v[196:199], v[172:175], v[60:63]
	s_waitcnt lgkmcnt(12)
	v_mfma_f32_16x16x32_f16 v[64:67], v[200:203], v[172:175], v[64:67]
	s_waitcnt lgkmcnt(11)
	v_mfma_f32_16x16x32_f16 v[68:71], v[204:207], v[172:175], v[68:71]
	s_waitcnt lgkmcnt(10)
	v_mfma_f32_16x16x32_f16 v[72:75], v[192:195], v[176:179], v[72:75]
	v_mfma_f32_16x16x32_f16 v[76:79], v[196:199], v[176:179], v[76:79]
	s_add_u32 m0, s28, 0xe000
	s_nop 0
	global_load_lds_dwordx4 v11, s[4:5]
	v_mfma_f32_16x16x32_f16 v[80:83], v[200:203], v[176:179], v[80:83]
	v_mfma_f32_16x16x32_f16 v[84:87], v[204:207], v[176:179], v[84:87]
	s_waitcnt lgkmcnt(9)
	v_mfma_f32_16x16x32_f16 v[88:91], v[192:195], v[180:183], v[88:91]
	v_mfma_f32_16x16x32_f16 v[92:95], v[196:199], v[180:183], v[92:95]
	v_mfma_f32_16x16x32_f16 v[96:99], v[200:203], v[180:183], v[96:99]
	s_add_u32 m0, s28, 0x10000
	s_nop 0
	global_load_lds_dwordx4 v12, s[4:5]
	v_mfma_f32_16x16x32_f16 v[100:103], v[204:207], v[180:183], v[100:103]
	s_waitcnt lgkmcnt(8)
	v_mfma_f32_16x16x32_f16 v[104:107], v[192:195], v[184:187], v[104:107]
	v_mfma_f32_16x16x32_f16 v[108:111], v[196:199], v[184:187], v[108:111]
	v_mfma_f32_16x16x32_f16 v[112:115], v[200:203], v[184:187], v[112:115]
	v_mfma_f32_16x16x32_f16 v[116:119], v[204:207], v[184:187], v[116:119]
	s_waitcnt lgkmcnt(7)
	ds_read_b128 v[172:175], v20
	ds_read_b128 v[192:195], v22
	ds_read_b128 v[196:199], v22 offset:2048
	ds_read_b128 v[200:203], v22 offset:4096
	ds_read_b128 v[204:207], v22 offset:6144
	ds_read_b128 v[176:179], v20 offset:2048
	ds_read_b128 v[180:183], v20 offset:4096
	ds_read_b128 v[184:187], v20 offset:6144
	s_waitcnt lgkmcnt(14)
	v_mfma_f32_16x16x32_f16 v[56:59], v[156:159], v[136:139], v[56:59]
	s_add_u32 m0, s28, 0x12000
	s_nop 0
	global_load_lds_dwordx4 v13, s[4:5]
	s_add_u32 s4, s4, s20
	s_addc_u32 s5, s5, 0
	s_waitcnt lgkmcnt(13)
	v_mfma_f32_16x16x32_f16 v[60:63], v[160:163], v[136:139], v[60:63]
	s_waitcnt lgkmcnt(12)
	v_mfma_f32_16x16x32_f16 v[64:67], v[164:167], v[136:139], v[64:67]
	s_waitcnt lgkmcnt(11)
	v_mfma_f32_16x16x32_f16 v[68:71], v[168:171], v[136:139], v[68:71]
	s_waitcnt lgkmcnt(10)
	v_mfma_f32_16x16x32_f16 v[72:75], v[156:159], v[140:143], v[72:75]
	v_mfma_f32_16x16x32_f16 v[76:79], v[160:163], v[140:143], v[76:79]
	s_add_u32 m0, s28, 0x14000
	s_nop 0
	global_load_lds_dwordx4 v10, s[6:7]
	v_mfma_f32_16x16x32_f16 v[80:83], v[164:167], v[140:143], v[80:83]
	v_mfma_f32_16x16x32_f16 v[84:87], v[168:171], v[140:143], v[84:87]
	s_waitcnt lgkmcnt(9)
	v_mfma_f32_16x16x32_f16 v[88:91], v[156:159], v[144:147], v[88:91]
	v_mfma_f32_16x16x32_f16 v[92:95], v[160:163], v[144:147], v[92:95]
	v_mfma_f32_16x16x32_f16 v[96:99], v[164:167], v[144:147], v[96:99]
	s_add_u32 m0, s28, 0x16000
	s_nop 0
	global_load_lds_dwordx4 v11, s[6:7]
	s_add_u32 s6, s6, s20
	s_addc_u32 s7, s7, 0
	v_mfma_f32_16x16x32_f16 v[100:103], v[168:171], v[144:147], v[100:103]
	s_waitcnt lgkmcnt(8)
	v_mfma_f32_16x16x32_f16 v[104:107], v[156:159], v[148:151], v[104:107]
	v_mfma_f32_16x16x32_f16 v[108:111], v[160:163], v[148:151], v[108:111]
	v_mfma_f32_16x16x32_f16 v[112:115], v[164:167], v[148:151], v[112:115]
	v_mfma_f32_16x16x32_f16 v[116:119], v[168:171], v[148:151], v[116:119]
	s_waitcnt vmcnt(6) lgkmcnt(0)
	s_barrier
	s_waitcnt lgkmcnt(7)
	ds_read_b128 v[136:139], v15
	ds_read_b128 v[156:159], v17
	ds_read_b128 v[160:163], v17 offset:2048
	ds_read_b128 v[164:167], v17 offset:4096
	ds_read_b128 v[168:171], v17 offset:6144
	ds_read_b128 v[140:143], v15 offset:2048
	ds_read_b128 v[144:147], v15 offset:4096
	ds_read_b128 v[148:151], v15 offset:6144
	s_waitcnt lgkmcnt(14)
	v_mfma_f32_16x16x32_f16 v[56:59], v[192:195], v[172:175], v[56:59]
	s_add_u32 m0, s28, 0x18000
	s_nop 0
	global_load_lds_dwordx4 v10, s[4:5]
	s_waitcnt lgkmcnt(13)
	v_mfma_f32_16x16x32_f16 v[60:63], v[196:199], v[172:175], v[60:63]
	s_waitcnt lgkmcnt(12)
	v_mfma_f32_16x16x32_f16 v[64:67], v[200:203], v[172:175], v[64:67]
	s_waitcnt lgkmcnt(11)
	v_mfma_f32_16x16x32_f16 v[68:71], v[204:207], v[172:175], v[68:71]
	s_waitcnt lgkmcnt(10)
	v_mfma_f32_16x16x32_f16 v[72:75], v[192:195], v[176:179], v[72:75]
	v_mfma_f32_16x16x32_f16 v[76:79], v[196:199], v[176:179], v[76:79]
	s_add_u32 m0, s28, 0x1a000
	s_nop 0
	global_load_lds_dwordx4 v11, s[4:5]
	v_mfma_f32_16x16x32_f16 v[80:83], v[200:203], v[176:179], v[80:83]
	v_mfma_f32_16x16x32_f16 v[84:87], v[204:207], v[176:179], v[84:87]
	s_waitcnt lgkmcnt(9)
	v_mfma_f32_16x16x32_f16 v[88:91], v[192:195], v[180:183], v[88:91]
	v_mfma_f32_16x16x32_f16 v[92:95], v[196:199], v[180:183], v[92:95]
	v_mfma_f32_16x16x32_f16 v[96:99], v[200:203], v[180:183], v[96:99]
	s_add_u32 m0, s28, 0x1c000
	s_nop 0
	global_load_lds_dwordx4 v12, s[4:5]
	v_mfma_f32_16x16x32_f16 v[100:103], v[204:207], v[180:183], v[100:103]
	s_waitcnt lgkmcnt(8)
	v_mfma_f32_16x16x32_f16 v[104:107], v[192:195], v[184:187], v[104:107]
	v_mfma_f32_16x16x32_f16 v[108:111], v[196:199], v[184:187], v[108:111]
	v_mfma_f32_16x16x32_f16 v[112:115], v[200:203], v[184:187], v[112:115]
	v_mfma_f32_16x16x32_f16 v[116:119], v[204:207], v[184:187], v[116:119]
	s_waitcnt lgkmcnt(7)
	ds_read_b128 v[172:175], v16
	ds_read_b128 v[192:195], v18
	ds_read_b128 v[196:199], v18 offset:2048
	ds_read_b128 v[200:203], v18 offset:4096
	ds_read_b128 v[204:207], v18 offset:6144
	ds_read_b128 v[176:179], v16 offset:2048
	ds_read_b128 v[180:183], v16 offset:4096
	ds_read_b128 v[184:187], v16 offset:6144
	s_waitcnt lgkmcnt(14)
	v_mfma_f32_16x16x32_f16 v[56:59], v[156:159], v[136:139], v[56:59]
	s_add_u32 m0, s28, 0x1e000
	s_nop 0
	global_load_lds_dwordx4 v13, s[4:5]
	s_add_u32 s4, s4, s20
	s_addc_u32 s5, s5, 0
	s_waitcnt lgkmcnt(13)
	v_mfma_f32_16x16x32_f16 v[60:63], v[160:163], v[136:139], v[60:63]
	s_waitcnt lgkmcnt(12)
	v_mfma_f32_16x16x32_f16 v[64:67], v[164:167], v[136:139], v[64:67]
	s_waitcnt lgkmcnt(11)
	v_mfma_f32_16x16x32_f16 v[68:71], v[168:171], v[136:139], v[68:71]
	s_waitcnt lgkmcnt(10)
	v_mfma_f32_16x16x32_f16 v[72:75], v[156:159], v[140:143], v[72:75]
	v_mfma_f32_16x16x32_f16 v[76:79], v[160:163], v[140:143], v[76:79]
	s_add_u32 m0, s28, 0x20000
	s_nop 0
	global_load_lds_dwordx4 v10, s[6:7]
	v_mfma_f32_16x16x32_f16 v[80:83], v[164:167], v[140:143], v[80:83]
	v_mfma_f32_16x16x32_f16 v[84:87], v[168:171], v[140:143], v[84:87]
	s_waitcnt lgkmcnt(9)
	v_mfma_f32_16x16x32_f16 v[88:91], v[156:159], v[144:147], v[88:91]
	v_mfma_f32_16x16x32_f16 v[92:95], v[160:163], v[144:147], v[92:95]
	v_mfma_f32_16x16x32_f16 v[96:99], v[164:167], v[144:147], v[96:99]
	s_add_u32 m0, s28, 0x22000
	s_nop 0
	global_load_lds_dwordx4 v11, s[6:7]
	s_add_u32 s6, s6, s20
	s_addc_u32 s7, s7, 0
	v_mfma_f32_16x16x32_f16 v[100:103], v[168:171], v[144:147], v[100:103]
	s_waitcnt lgkmcnt(8)
	v_mfma_f32_16x16x32_f16 v[104:107], v[156:159], v[148:151], v[104:107]
	v_mfma_f32_16x16x32_f16 v[108:111], v[160:163], v[148:151], v[108:111]
	v_mfma_f32_16x16x32_f16 v[112:115], v[164:167], v[148:151], v[112:115]
	v_mfma_f32_16x16x32_f16 v[116:119], v[168:171], v[148:151], v[116:119]
	s_waitcnt vmcnt(6) lgkmcnt(0)
	s_barrier
	s_waitcnt lgkmcnt(7)
	ds_read_b128 v[136:139], v15 offset:49152
	ds_read_b128 v[156:159], v17 offset:49152
	ds_read_b128 v[160:163], v17 offset:51200
	ds_read_b128 v[164:167], v17 offset:53248
	ds_read_b128 v[168:171], v17 offset:55296
	ds_read_b128 v[140:143], v15 offset:51200
	ds_read_b128 v[144:147], v15 offset:53248
	ds_read_b128 v[148:151], v15 offset:55296
	s_waitcnt lgkmcnt(14)
	v_mfma_f32_16x16x32_f16 v[56:59], v[192:195], v[172:175], v[56:59]
	s_add_u32 m0, s28, 0x0
	s_nop 0
	global_load_lds_dwordx4 v10, s[4:5]
	s_waitcnt lgkmcnt(13)
	v_mfma_f32_16x16x32_f16 v[60:63], v[196:199], v[172:175], v[60:63]
	s_waitcnt lgkmcnt(12)
	v_mfma_f32_16x16x32_f16 v[64:67], v[200:203], v[172:175], v[64:67]
	s_waitcnt lgkmcnt(11)
	v_mfma_f32_16x16x32_f16 v[68:71], v[204:207], v[172:175], v[68:71]
	s_waitcnt lgkmcnt(10)
	v_mfma_f32_16x16x32_f16 v[72:75], v[192:195], v[176:179], v[72:75]
	v_mfma_f32_16x16x32_f16 v[76:79], v[196:199], v[176:179], v[76:79]
	s_add_u32 m0, s28, 0x2000
	s_nop 0
	global_load_lds_dwordx4 v11, s[4:5]
	v_mfma_f32_16x16x32_f16 v[80:83], v[200:203], v[176:179], v[80:83]
	v_mfma_f32_16x16x32_f16 v[84:87], v[204:207], v[176:179], v[84:87]
	s_waitcnt lgkmcnt(9)
	v_mfma_f32_16x16x32_f16 v[88:91], v[192:195], v[180:183], v[88:91]
	v_mfma_f32_16x16x32_f16 v[92:95], v[196:199], v[180:183], v[92:95]
	v_mfma_f32_16x16x32_f16 v[96:99], v[200:203], v[180:183], v[96:99]
	s_add_u32 m0, s28, 0x4000
	s_nop 0
	global_load_lds_dwordx4 v12, s[4:5]
	v_mfma_f32_16x16x32_f16 v[100:103], v[204:207], v[180:183], v[100:103]
	s_waitcnt lgkmcnt(8)
	v_mfma_f32_16x16x32_f16 v[104:107], v[192:195], v[184:187], v[104:107]
	v_mfma_f32_16x16x32_f16 v[108:111], v[196:199], v[184:187], v[108:111]
	v_mfma_f32_16x16x32_f16 v[112:115], v[200:203], v[184:187], v[112:115]
	v_mfma_f32_16x16x32_f16 v[116:119], v[204:207], v[184:187], v[116:119]
	s_waitcnt lgkmcnt(7)
	ds_read_b128 v[172:175], v16 offset:49152
	ds_read_b128 v[192:195], v18 offset:49152
	ds_read_b128 v[196:199], v18 offset:51200
	ds_read_b128 v[200:203], v18 offset:53248
	ds_read_b128 v[204:207], v18 offset:55296
	ds_read_b128 v[176:179], v16 offset:51200
	ds_read_b128 v[180:183], v16 offset:53248
	ds_read_b128 v[184:187], v16 offset:55296
	s_waitcnt lgkmcnt(14)
	v_mfma_f32_16x16x32_f16 v[56:59], v[156:159], v[136:139], v[56:59]
	s_add_u32 m0, s28, 0x6000
	s_nop 0
	global_load_lds_dwordx4 v13, s[4:5]
	s_add_u32 s4, s4, s20
	s_addc_u32 s5, s5, 0
	s_waitcnt lgkmcnt(13)
	v_mfma_f32_16x16x32_f16 v[60:63], v[160:163], v[136:139], v[60:63]
	s_waitcnt lgkmcnt(12)
	v_mfma_f32_16x16x32_f16 v[64:67], v[164:167], v[136:139], v[64:67]
	s_waitcnt lgkmcnt(11)
	v_mfma_f32_16x16x32_f16 v[68:71], v[168:171], v[136:139], v[68:71]
	s_waitcnt lgkmcnt(10)
	v_mfma_f32_16x16x32_f16 v[72:75], v[156:159], v[140:143], v[72:75]
	v_mfma_f32_16x16x32_f16 v[76:79], v[160:163], v[140:143], v[76:79]
	s_add_u32 m0, s28, 0x8000
	s_nop 0
	global_load_lds_dwordx4 v10, s[6:7]
	v_mfma_f32_16x16x32_f16 v[80:83], v[164:167], v[140:143], v[80:83]
	v_mfma_f32_16x16x32_f16 v[84:87], v[168:171], v[140:143], v[84:87]
	s_waitcnt lgkmcnt(9)
	v_mfma_f32_16x16x32_f16 v[88:91], v[156:159], v[144:147], v[88:91]
	v_mfma_f32_16x16x32_f16 v[92:95], v[160:163], v[144:147], v[92:95]
	v_mfma_f32_16x16x32_f16 v[96:99], v[164:167], v[144:147], v[96:99]
	s_add_u32 m0, s28, 0xa000
	s_nop 0
	global_load_lds_dwordx4 v11, s[6:7]
	s_add_u32 s6, s6, s20
	s_addc_u32 s7, s7, 0
	v_mfma_f32_16x16x32_f16 v[100:103], v[168:171], v[144:147], v[100:103]
	s_waitcnt lgkmcnt(8)
	v_mfma_f32_16x16x32_f16 v[104:107], v[156:159], v[148:151], v[104:107]
	v_mfma_f32_16x16x32_f16 v[108:111], v[160:163], v[148:151], v[108:111]
	v_mfma_f32_16x16x32_f16 v[112:115], v[164:167], v[148:151], v[112:115]
	v_mfma_f32_16x16x32_f16 v[116:119], v[168:171], v[148:151], v[116:119]
	s_waitcnt vmcnt(6) lgkmcnt(0)
	s_barrier
	s_waitcnt lgkmcnt(7)
	ds_read_b128 v[136:139], v19
	ds_read_b128 v[156:159], v21
	ds_read_b128 v[160:163], v21 offset:2048
	ds_read_b128 v[164:167], v21 offset:4096
	ds_read_b128 v[168:171], v21 offset:6144
	ds_read_b128 v[140:143], v19 offset:2048
	ds_read_b128 v[144:147], v19 offset:4096
	ds_read_b128 v[148:151], v19 offset:6144
	s_waitcnt lgkmcnt(14)
	v_mfma_f32_16x16x32_f16 v[56:59], v[192:195], v[172:175], v[56:59]
	s_add_u32 m0, s28, 0xc000
	s_nop 0
	global_load_lds_dwordx4 v10, s[4:5]
	s_waitcnt lgkmcnt(13)
	v_mfma_f32_16x16x32_f16 v[60:63], v[196:199], v[172:175], v[60:63]
	s_waitcnt lgkmcnt(12)
	v_mfma_f32_16x16x32_f16 v[64:67], v[200:203], v[172:175], v[64:67]
	s_waitcnt lgkmcnt(11)
	v_mfma_f32_16x16x32_f16 v[68:71], v[204:207], v[172:175], v[68:71]
	s_waitcnt lgkmcnt(10)
	v_mfma_f32_16x16x32_f16 v[72:75], v[192:195], v[176:179], v[72:75]
	v_mfma_f32_16x16x32_f16 v[76:79], v[196:199], v[176:179], v[76:79]
	s_add_u32 m0, s28, 0xe000
	s_nop 0
	global_load_lds_dwordx4 v11, s[4:5]
	v_mfma_f32_16x16x32_f16 v[80:83], v[200:203], v[176:179], v[80:83]
	v_mfma_f32_16x16x32_f16 v[84:87], v[204:207], v[176:179], v[84:87]
	s_waitcnt lgkmcnt(9)
	v_mfma_f32_16x16x32_f16 v[88:91], v[192:195], v[180:183], v[88:91]
	v_mfma_f32_16x16x32_f16 v[92:95], v[196:199], v[180:183], v[92:95]
	v_mfma_f32_16x16x32_f16 v[96:99], v[200:203], v[180:183], v[96:99]
	s_add_u32 m0, s28, 0x10000
	s_nop 0
	global_load_lds_dwordx4 v12, s[4:5]
	v_mfma_f32_16x16x32_f16 v[100:103], v[204:207], v[180:183], v[100:103]
	s_waitcnt lgkmcnt(8)
	v_mfma_f32_16x16x32_f16 v[104:107], v[192:195], v[184:187], v[104:107]
	v_mfma_f32_16x16x32_f16 v[108:111], v[196:199], v[184:187], v[108:111]
	v_mfma_f32_16x16x32_f16 v[112:115], v[200:203], v[184:187], v[112:115]
	v_mfma_f32_16x16x32_f16 v[116:119], v[204:207], v[184:187], v[116:119]
	s_waitcnt lgkmcnt(7)
	ds_read_b128 v[172:175], v20
	ds_read_b128 v[192:195], v22
	ds_read_b128 v[196:199], v22 offset:2048
	ds_read_b128 v[200:203], v22 offset:4096
	ds_read_b128 v[204:207], v22 offset:6144
	ds_read_b128 v[176:179], v20 offset:2048
	ds_read_b128 v[180:183], v20 offset:4096
	ds_read_b128 v[184:187], v20 offset:6144
	s_waitcnt lgkmcnt(14)
	v_mfma_f32_16x16x32_f16 v[56:59], v[156:159], v[136:139], v[56:59]
	s_add_u32 m0, s28, 0x12000
	s_nop 0
	global_load_lds_dwordx4 v13, s[4:5]
	s_add_u32 s4, s4, s20
	s_addc_u32 s5, s5, 0
	s_waitcnt lgkmcnt(13)
	v_mfma_f32_16x16x32_f16 v[60:63], v[160:163], v[136:139], v[60:63]
	s_waitcnt lgkmcnt(12)
	v_mfma_f32_16x16x32_f16 v[64:67], v[164:167], v[136:139], v[64:67]
	s_waitcnt lgkmcnt(11)
	v_mfma_f32_16x16x32_f16 v[68:71], v[168:171], v[136:139], v[68:71]
	s_waitcnt lgkmcnt(10)
	v_mfma_f32_16x16x32_f16 v[72:75], v[156:159], v[140:143], v[72:75]
	v_mfma_f32_16x16x32_f16 v[76:79], v[160:163], v[140:143], v[76:79]
	s_add_u32 m0, s28, 0x14000
	s_nop 0
	global_load_lds_dwordx4 v10, s[6:7]
	v_mfma_f32_16x16x32_f16 v[80:83], v[164:167], v[140:143], v[80:83]
	v_mfma_f32_16x16x32_f16 v[84:87], v[168:171], v[140:143], v[84:87]
	s_waitcnt lgkmcnt(9)
	v_mfma_f32_16x16x32_f16 v[88:91], v[156:159], v[144:147], v[88:91]
	v_mfma_f32_16x16x32_f16 v[92:95], v[160:163], v[144:147], v[92:95]
	v_mfma_f32_16x16x32_f16 v[96:99], v[164:167], v[144:147], v[96:99]
	s_add_u32 m0, s28, 0x16000
	s_nop 0
	global_load_lds_dwordx4 v11, s[6:7]
	s_add_u32 s6, s6, s20
	s_addc_u32 s7, s7, 0
	v_mfma_f32_16x16x32_f16 v[100:103], v[168:171], v[144:147], v[100:103]
	s_waitcnt lgkmcnt(8)
	v_mfma_f32_16x16x32_f16 v[104:107], v[156:159], v[148:151], v[104:107]
	v_mfma_f32_16x16x32_f16 v[108:111], v[160:163], v[148:151], v[108:111]
	v_mfma_f32_16x16x32_f16 v[112:115], v[164:167], v[148:151], v[112:115]
	v_mfma_f32_16x16x32_f16 v[116:119], v[168:171], v[148:151], v[116:119]
	s_waitcnt vmcnt(6) lgkmcnt(0)
	s_barrier
	s_waitcnt lgkmcnt(7)
	ds_read_b128 v[136:139], v15
	ds_read_b128 v[156:159], v17
	ds_read_b128 v[160:163], v17 offset:2048
	ds_read_b128 v[164:167], v17 offset:4096
	ds_read_b128 v[168:171], v17 offset:6144
	ds_read_b128 v[140:143], v15 offset:2048
	ds_read_b128 v[144:147], v15 offset:4096
	ds_read_b128 v[148:151], v15 offset:6144
	s_waitcnt lgkmcnt(14)
	v_mfma_f32_16x16x32_f16 v[56:59], v[192:195], v[172:175], v[56:59]
	s_add_u32 m0, s28, 0x18000
	s_nop 0
	global_load_lds_dwordx4 v10, s[4:5]
	s_waitcnt lgkmcnt(13)
	v_mfma_f32_16x16x32_f16 v[60:63], v[196:199], v[172:175], v[60:63]
	s_waitcnt lgkmcnt(12)
	v_mfma_f32_16x16x32_f16 v[64:67], v[200:203], v[172:175], v[64:67]
	s_waitcnt lgkmcnt(11)
	v_mfma_f32_16x16x32_f16 v[68:71], v[204:207], v[172:175], v[68:71]
	s_waitcnt lgkmcnt(10)
	v_mfma_f32_16x16x32_f16 v[72:75], v[192:195], v[176:179], v[72:75]
	v_mfma_f32_16x16x32_f16 v[76:79], v[196:199], v[176:179], v[76:79]
	s_add_u32 m0, s28, 0x1a000
	s_nop 0
	global_load_lds_dwordx4 v11, s[4:5]
	v_mfma_f32_16x16x32_f16 v[80:83], v[200:203], v[176:179], v[80:83]
	v_mfma_f32_16x16x32_f16 v[84:87], v[204:207], v[176:179], v[84:87]
	s_waitcnt lgkmcnt(9)
	v_mfma_f32_16x16x32_f16 v[88:91], v[192:195], v[180:183], v[88:91]
	v_mfma_f32_16x16x32_f16 v[92:95], v[196:199], v[180:183], v[92:95]
	v_mfma_f32_16x16x32_f16 v[96:99], v[200:203], v[180:183], v[96:99]
	s_add_u32 m0, s28, 0x1c000
	s_nop 0
	global_load_lds_dwordx4 v12, s[4:5]
	v_mfma_f32_16x16x32_f16 v[100:103], v[204:207], v[180:183], v[100:103]
	s_waitcnt lgkmcnt(8)
	v_mfma_f32_16x16x32_f16 v[104:107], v[192:195], v[184:187], v[104:107]
	v_mfma_f32_16x16x32_f16 v[108:111], v[196:199], v[184:187], v[108:111]
	v_mfma_f32_16x16x32_f16 v[112:115], v[200:203], v[184:187], v[112:115]
	v_mfma_f32_16x16x32_f16 v[116:119], v[204:207], v[184:187], v[116:119]
	s_waitcnt lgkmcnt(7)
	ds_read_b128 v[172:175], v16
	ds_read_b128 v[192:195], v18
	ds_read_b128 v[196:199], v18 offset:2048
	ds_read_b128 v[200:203], v18 offset:4096
	ds_read_b128 v[204:207], v18 offset:6144
	ds_read_b128 v[176:179], v16 offset:2048
	ds_read_b128 v[180:183], v16 offset:4096
	ds_read_b128 v[184:187], v16 offset:6144
	s_waitcnt lgkmcnt(14)
	v_mfma_f32_16x16x32_f16 v[56:59], v[156:159], v[136:139], v[56:59]
	s_add_u32 m0, s28, 0x1e000
	s_nop 0
	global_load_lds_dwordx4 v13, s[4:5]
	s_add_u32 s4, s4, s20
	s_addc_u32 s5, s5, 0
	s_waitcnt lgkmcnt(13)
	v_mfma_f32_16x16x32_f16 v[60:63], v[160:163], v[136:139], v[60:63]
	s_waitcnt lgkmcnt(12)
	v_mfma_f32_16x16x32_f16 v[64:67], v[164:167], v[136:139], v[64:67]
	s_waitcnt lgkmcnt(11)
	v_mfma_f32_16x16x32_f16 v[68:71], v[168:171], v[136:139], v[68:71]
	s_waitcnt lgkmcnt(10)
	v_mfma_f32_16x16x32_f16 v[72:75], v[156:159], v[140:143], v[72:75]
	v_mfma_f32_16x16x32_f16 v[76:79], v[160:163], v[140:143], v[76:79]
	s_add_u32 m0, s28, 0x20000
	s_nop 0
	global_load_lds_dwordx4 v10, s[6:7]
	v_mfma_f32_16x16x32_f16 v[80:83], v[164:167], v[140:143], v[80:83]
	v_mfma_f32_16x16x32_f16 v[84:87], v[168:171], v[140:143], v[84:87]
	s_waitcnt lgkmcnt(9)
	v_mfma_f32_16x16x32_f16 v[88:91], v[156:159], v[144:147], v[88:91]
	v_mfma_f32_16x16x32_f16 v[92:95], v[160:163], v[144:147], v[92:95]
	v_mfma_f32_16x16x32_f16 v[96:99], v[164:167], v[144:147], v[96:99]
	s_add_u32 m0, s28, 0x22000
	s_nop 0
	global_load_lds_dwordx4 v11, s[6:7]
	s_add_u32 s6, s6, s20
	s_addc_u32 s7, s7, 0
	v_mfma_f32_16x16x32_f16 v[100:103], v[168:171], v[144:147], v[100:103]
	s_waitcnt lgkmcnt(8)
	v_mfma_f32_16x16x32_f16 v[104:107], v[156:159], v[148:151], v[104:107]
	v_mfma_f32_16x16x32_f16 v[108:111], v[160:163], v[148:151], v[108:111]
	v_mfma_f32_16x16x32_f16 v[112:115], v[164:167], v[148:151], v[112:115]
	v_mfma_f32_16x16x32_f16 v[116:119], v[168:171], v[148:151], v[116:119]
	s_waitcnt vmcnt(6) lgkmcnt(0)
	s_barrier
	s_waitcnt lgkmcnt(7)
	ds_read_b128 v[136:139], v15 offset:49152
	ds_read_b128 v[156:159], v17 offset:49152
	ds_read_b128 v[160:163], v17 offset:51200
	ds_read_b128 v[164:167], v17 offset:53248
	ds_read_b128 v[168:171], v17 offset:55296
	ds_read_b128 v[140:143], v15 offset:51200
	ds_read_b128 v[144:147], v15 offset:53248
	ds_read_b128 v[148:151], v15 offset:55296
	s_waitcnt lgkmcnt(14)
	v_mfma_f32_16x16x32_f16 v[56:59], v[192:195], v[172:175], v[56:59]
	s_add_u32 m0, s28, 0x0
	s_nop 0
	global_load_lds_dwordx4 v10, s[4:5]
	s_waitcnt lgkmcnt(13)
	v_mfma_f32_16x16x32_f16 v[60:63], v[196:199], v[172:175], v[60:63]
	s_waitcnt lgkmcnt(12)
	v_mfma_f32_16x16x32_f16 v[64:67], v[200:203], v[172:175], v[64:67]
	s_waitcnt lgkmcnt(11)
	v_mfma_f32_16x16x32_f16 v[68:71], v[204:207], v[172:175], v[68:71]
	s_waitcnt lgkmcnt(10)
	v_mfma_f32_16x16x32_f16 v[72:75], v[192:195], v[176:179], v[72:75]
	v_mfma_f32_16x16x32_f16 v[76:79], v[196:199], v[176:179], v[76:79]
	s_add_u32 m0, s28, 0x2000
	s_nop 0
	global_load_lds_dwordx4 v11, s[4:5]
	v_mfma_f32_16x16x32_f16 v[80:83], v[200:203], v[176:179], v[80:83]
	v_mfma_f32_16x16x32_f16 v[84:87], v[204:207], v[176:179], v[84:87]
	s_waitcnt lgkmcnt(9)
	v_mfma_f32_16x16x32_f16 v[88:91], v[192:195], v[180:183], v[88:91]
	v_mfma_f32_16x16x32_f16 v[92:95], v[196:199], v[180:183], v[92:95]
	v_mfma_f32_16x16x32_f16 v[96:99], v[200:203], v[180:183], v[96:99]
	s_add_u32 m0, s28, 0x4000
	s_nop 0
	global_load_lds_dwordx4 v12, s[4:5]
	v_mfma_f32_16x16x32_f16 v[100:103], v[204:207], v[180:183], v[100:103]
	s_waitcnt lgkmcnt(8)
	v_mfma_f32_16x16x32_f16 v[104:107], v[192:195], v[184:187], v[104:107]
	v_mfma_f32_16x16x32_f16 v[108:111], v[196:199], v[184:187], v[108:111]
	v_mfma_f32_16x16x32_f16 v[112:115], v[200:203], v[184:187], v[112:115]
	v_mfma_f32_16x16x32_f16 v[116:119], v[204:207], v[184:187], v[116:119]
	s_waitcnt lgkmcnt(7)
	ds_read_b128 v[172:175], v16 offset:49152
	ds_read_b128 v[192:195], v18 offset:49152
	ds_read_b128 v[196:199], v18 offset:51200
	ds_read_b128 v[200:203], v18 offset:53248
	ds_read_b128 v[204:207], v18 offset:55296
	ds_read_b128 v[176:179], v16 offset:51200
	ds_read_b128 v[180:183], v16 offset:53248
	ds_read_b128 v[184:187], v16 offset:55296
	s_waitcnt lgkmcnt(14)
	v_mfma_f32_16x16x32_f16 v[56:59], v[156:159], v[136:139], v[56:59]
	s_add_u32 m0, s28, 0x6000
	s_nop 0
	global_load_lds_dwordx4 v13, s[4:5]
	s_add_u32 s4, s4, s20
	s_addc_u32 s5, s5, 0
	s_waitcnt lgkmcnt(13)
	v_mfma_f32_16x16x32_f16 v[60:63], v[160:163], v[136:139], v[60:63]
	s_waitcnt lgkmcnt(12)
	v_mfma_f32_16x16x32_f16 v[64:67], v[164:167], v[136:139], v[64:67]
	s_waitcnt lgkmcnt(11)
	v_mfma_f32_16x16x32_f16 v[68:71], v[168:171], v[136:139], v[68:71]
	s_waitcnt lgkmcnt(10)
	v_mfma_f32_16x16x32_f16 v[72:75], v[156:159], v[140:143], v[72:75]
	v_mfma_f32_16x16x32_f16 v[76:79], v[160:163], v[140:143], v[76:79]
	s_add_u32 m0, s28, 0x8000
	s_nop 0
	global_load_lds_dwordx4 v10, s[6:7]
	v_mfma_f32_16x16x32_f16 v[80:83], v[164:167], v[140:143], v[80:83]
	v_mfma_f32_16x16x32_f16 v[84:87], v[168:171], v[140:143], v[84:87]
	s_waitcnt lgkmcnt(9)
	v_mfma_f32_16x16x32_f16 v[88:91], v[156:159], v[144:147], v[88:91]
	v_mfma_f32_16x16x32_f16 v[92:95], v[160:163], v[144:147], v[92:95]
	v_mfma_f32_16x16x32_f16 v[96:99], v[164:167], v[144:147], v[96:99]
	s_add_u32 m0, s28, 0xa000
	s_nop 0
	global_load_lds_dwordx4 v11, s[6:7]
	s_add_u32 s6, s6, s20
	s_addc_u32 s7, s7, 0
	v_mfma_f32_16x16x32_f16 v[100:103], v[168:171], v[144:147], v[100:103]
	s_waitcnt lgkmcnt(8)
	v_mfma_f32_16x16x32_f16 v[104:107], v[156:159], v[148:151], v[104:107]
	v_mfma_f32_16x16x32_f16 v[108:111], v[160:163], v[148:151], v[108:111]
	v_mfma_f32_16x16x32_f16 v[112:115], v[164:167], v[148:151], v[112:115]
	v_mfma_f32_16x16x32_f16 v[116:119], v[168:171], v[148:151], v[116:119]
	s_waitcnt vmcnt(6) lgkmcnt(0)
	s_barrier
	s_waitcnt lgkmcnt(7)
	ds_read_b128 v[136:139], v19
	ds_read_b128 v[156:159], v21
	ds_read_b128 v[160:163], v21 offset:2048
	ds_read_b128 v[164:167], v21 offset:4096
	ds_read_b128 v[168:171], v21 offset:6144
	ds_read_b128 v[140:143], v19 offset:2048
	ds_read_b128 v[144:147], v19 offset:4096
	ds_read_b128 v[148:151], v19 offset:6144
	s_waitcnt lgkmcnt(14)
	v_mfma_f32_16x16x32_f16 v[56:59], v[192:195], v[172:175], v[56:59]
	s_waitcnt lgkmcnt(13)
	v_mfma_f32_16x16x32_f16 v[60:63], v[196:199], v[172:175], v[60:63]
	s_waitcnt lgkmcnt(12)
	v_mfma_f32_16x16x32_f16 v[64:67], v[200:203], v[172:175], v[64:67]
	s_waitcnt lgkmcnt(11)
	v_mfma_f32_16x16x32_f16 v[68:71], v[204:207], v[172:175], v[68:71]
	s_waitcnt lgkmcnt(10)
	v_mfma_f32_16x16x32_f16 v[72:75], v[192:195], v[176:179], v[72:75]
	v_mfma_f32_16x16x32_f16 v[76:79], v[196:199], v[176:179], v[76:79]
	v_mfma_f32_16x16x32_f16 v[80:83], v[200:203], v[176:179], v[80:83]
	v_mfma_f32_16x16x32_f16 v[84:87], v[204:207], v[176:179], v[84:87]
	s_waitcnt lgkmcnt(9)
	v_mfma_f32_16x16x32_f16 v[88:91], v[192:195], v[180:183], v[88:91]
	v_mfma_f32_16x16x32_f16 v[92:95], v[196:199], v[180:183], v[92:95]
	v_mfma_f32_16x16x32_f16 v[96:99], v[200:203], v[180:183], v[96:99]
	v_mfma_f32_16x16x32_f16 v[100:103], v[204:207], v[180:183], v[100:103]
	s_waitcnt lgkmcnt(8)
	v_mfma_f32_16x16x32_f16 v[104:107], v[192:195], v[184:187], v[104:107]
	v_mfma_f32_16x16x32_f16 v[108:111], v[196:199], v[184:187], v[108:111]
	v_mfma_f32_16x16x32_f16 v[112:115], v[200:203], v[184:187], v[112:115]
	v_mfma_f32_16x16x32_f16 v[116:119], v[204:207], v[184:187], v[116:119]
	s_waitcnt lgkmcnt(7)
	ds_read_b128 v[172:175], v20
	ds_read_b128 v[192:195], v22
	ds_read_b128 v[196:199], v22 offset:2048
	ds_read_b128 v[200:203], v22 offset:4096
	ds_read_b128 v[204:207], v22 offset:6144
	ds_read_b128 v[176:179], v20 offset:2048
	ds_read_b128 v[180:183], v20 offset:4096
	ds_read_b128 v[184:187], v20 offset:6144
	s_waitcnt lgkmcnt(14)
	v_mfma_f32_16x16x32_f16 v[56:59], v[156:159], v[136:139], v[56:59]
	s_waitcnt lgkmcnt(13)
	v_mfma_f32_16x16x32_f16 v[60:63], v[160:163], v[136:139], v[60:63]
	s_waitcnt lgkmcnt(12)
	v_mfma_f32_16x16x32_f16 v[64:67], v[164:167], v[136:139], v[64:67]
	s_waitcnt lgkmcnt(11)
	v_mfma_f32_16x16x32_f16 v[68:71], v[168:171], v[136:139], v[68:71]
	s_waitcnt lgkmcnt(10)
	v_mfma_f32_16x16x32_f16 v[72:75], v[156:159], v[140:143], v[72:75]
	v_mfma_f32_16x16x32_f16 v[76:79], v[160:163], v[140:143], v[76:79]
	v_mfma_f32_16x16x32_f16 v[80:83], v[164:167], v[140:143], v[80:83]
	v_mfma_f32_16x16x32_f16 v[84:87], v[168:171], v[140:143], v[84:87]
	s_waitcnt lgkmcnt(9)
	v_mfma_f32_16x16x32_f16 v[88:91], v[156:159], v[144:147], v[88:91]
	v_mfma_f32_16x16x32_f16 v[92:95], v[160:163], v[144:147], v[92:95]
	v_mfma_f32_16x16x32_f16 v[96:99], v[164:167], v[144:147], v[96:99]
	v_mfma_f32_16x16x32_f16 v[100:103], v[168:171], v[144:147], v[100:103]
	s_waitcnt lgkmcnt(8)
	v_mfma_f32_16x16x32_f16 v[104:107], v[156:159], v[148:151], v[104:107]
	v_mfma_f32_16x16x32_f16 v[108:111], v[160:163], v[148:151], v[108:111]
	v_mfma_f32_16x16x32_f16 v[112:115], v[164:167], v[148:151], v[112:115]
	v_mfma_f32_16x16x32_f16 v[116:119], v[168:171], v[148:151], v[116:119]
	s_waitcnt vmcnt(0) lgkmcnt(0)
	s_barrier
	s_waitcnt lgkmcnt(7)
	ds_read_b128 v[136:139], v15
	ds_read_b128 v[156:159], v17
	ds_read_b128 v[160:163], v17 offset:2048
	ds_read_b128 v[164:167], v17 offset:4096
	ds_read_b128 v[168:171], v17 offset:6144
	ds_read_b128 v[140:143], v15 offset:2048
	ds_read_b128 v[144:147], v15 offset:4096
	ds_read_b128 v[148:151], v15 offset:6144
	s_waitcnt lgkmcnt(14)
	v_mfma_f32_16x16x32_f16 v[56:59], v[192:195], v[172:175], v[56:59]
	s_waitcnt lgkmcnt(13)
	v_mfma_f32_16x16x32_f16 v[60:63], v[196:199], v[172:175], v[60:63]
	s_waitcnt lgkmcnt(12)
	v_mfma_f32_16x16x32_f16 v[64:67], v[200:203], v[172:175], v[64:67]
	s_waitcnt lgkmcnt(11)
	v_mfma_f32_16x16x32_f16 v[68:71], v[204:207], v[172:175], v[68:71]
	s_waitcnt lgkmcnt(10)
	v_mfma_f32_16x16x32_f16 v[72:75], v[192:195], v[176:179], v[72:75]
	v_mfma_f32_16x16x32_f16 v[76:79], v[196:199], v[176:179], v[76:79]
	v_mfma_f32_16x16x32_f16 v[80:83], v[200:203], v[176:179], v[80:83]
	v_mfma_f32_16x16x32_f16 v[84:87], v[204:207], v[176:179], v[84:87]
	s_waitcnt lgkmcnt(9)
	v_mfma_f32_16x16x32_f16 v[88:91], v[192:195], v[180:183], v[88:91]
	v_mfma_f32_16x16x32_f16 v[92:95], v[196:199], v[180:183], v[92:95]
	v_mfma_f32_16x16x32_f16 v[96:99], v[200:203], v[180:183], v[96:99]
	v_mfma_f32_16x16x32_f16 v[100:103], v[204:207], v[180:183], v[100:103]
	s_waitcnt lgkmcnt(8)
	v_mfma_f32_16x16x32_f16 v[104:107], v[192:195], v[184:187], v[104:107]
	v_mfma_f32_16x16x32_f16 v[108:111], v[196:199], v[184:187], v[108:111]
	v_mfma_f32_16x16x32_f16 v[112:115], v[200:203], v[184:187], v[112:115]
	v_mfma_f32_16x16x32_f16 v[116:119], v[204:207], v[184:187], v[116:119]
	s_waitcnt lgkmcnt(7)
	ds_read_b128 v[172:175], v16
	ds_read_b128 v[192:195], v18
	ds_read_b128 v[196:199], v18 offset:2048
	ds_read_b128 v[200:203], v18 offset:4096
	ds_read_b128 v[204:207], v18 offset:6144
	ds_read_b128 v[176:179], v16 offset:2048
	ds_read_b128 v[180:183], v16 offset:4096
	ds_read_b128 v[184:187], v16 offset:6144
	s_waitcnt lgkmcnt(14)
	v_mfma_f32_16x16x32_f16 v[56:59], v[156:159], v[136:139], v[56:59]
	s_waitcnt lgkmcnt(13)
	v_mfma_f32_16x16x32_f16 v[60:63], v[160:163], v[136:139], v[60:63]
	s_waitcnt lgkmcnt(12)
	v_mfma_f32_16x16x32_f16 v[64:67], v[164:167], v[136:139], v[64:67]
	s_waitcnt lgkmcnt(11)
	v_mfma_f32_16x16x32_f16 v[68:71], v[168:171], v[136:139], v[68:71]
	s_waitcnt lgkmcnt(10)
	v_mfma_f32_16x16x32_f16 v[72:75], v[156:159], v[140:143], v[72:75]
	v_mfma_f32_16x16x32_f16 v[76:79], v[160:163], v[140:143], v[76:79]
	v_mfma_f32_16x16x32_f16 v[80:83], v[164:167], v[140:143], v[80:83]
	v_mfma_f32_16x16x32_f16 v[84:87], v[168:171], v[140:143], v[84:87]
	s_waitcnt lgkmcnt(9)
	v_mfma_f32_16x16x32_f16 v[88:91], v[156:159], v[144:147], v[88:91]
	v_mfma_f32_16x16x32_f16 v[92:95], v[160:163], v[144:147], v[92:95]
	v_mfma_f32_16x16x32_f16 v[96:99], v[164:167], v[144:147], v[96:99]
	v_mfma_f32_16x16x32_f16 v[100:103], v[168:171], v[144:147], v[100:103]
	s_waitcnt lgkmcnt(8)
	v_mfma_f32_16x16x32_f16 v[104:107], v[156:159], v[148:151], v[104:107]
	v_mfma_f32_16x16x32_f16 v[108:111], v[160:163], v[148:151], v[108:111]
	v_mfma_f32_16x16x32_f16 v[112:115], v[164:167], v[148:151], v[112:115]
	v_mfma_f32_16x16x32_f16 v[116:119], v[168:171], v[148:151], v[116:119]
	s_waitcnt lgkmcnt(6)
	v_mfma_f32_16x16x32_f16 v[56:59], v[192:195], v[172:175], v[56:59]
	s_waitcnt lgkmcnt(5)
	v_mfma_f32_16x16x32_f16 v[60:63], v[196:199], v[172:175], v[60:63]
	s_waitcnt lgkmcnt(4)
	v_mfma_f32_16x16x32_f16 v[64:67], v[200:203], v[172:175], v[64:67]
	s_waitcnt lgkmcnt(3)
	v_mfma_f32_16x16x32_f16 v[68:71], v[204:207], v[172:175], v[68:71]
	s_waitcnt lgkmcnt(2)
	v_mfma_f32_16x16x32_f16 v[72:75], v[192:195], v[176:179], v[72:75]
	v_mfma_f32_16x16x32_f16 v[76:79], v[196:199], v[176:179], v[76:79]
	v_mfma_f32_16x16x32_f16 v[80:83], v[200:203], v[176:179], v[80:83]
	v_mfma_f32_16x16x32_f16 v[84:87], v[204:207], v[176:179], v[84:87]
	s_waitcnt lgkmcnt(1)
	v_mfma_f32_16x16x32_f16 v[88:91], v[192:195], v[180:183], v[88:91]
	v_mfma_f32_16x16x32_f16 v[92:95], v[196:199], v[180:183], v[92:95]
	v_mfma_f32_16x16x32_f16 v[96:99], v[200:203], v[180:183], v[96:99]
	v_mfma_f32_16x16x32_f16 v[100:103], v[204:207], v[180:183], v[100:103]
	s_waitcnt lgkmcnt(0)
	v_mfma_f32_16x16x32_f16 v[104:107], v[192:195], v[184:187], v[104:107]
	v_mfma_f32_16x16x32_f16 v[108:111], v[196:199], v[184:187], v[108:111]
	v_mfma_f32_16x16x32_f16 v[112:115], v[200:203], v[184:187], v[112:115]
	v_mfma_f32_16x16x32_f16 v[116:119], v[204:207], v[184:187], v[116:119]
	s_nop 7
	s_nop 1
	v_mov_b32_e32 v213, s19
	v_pk_add_f32 v[56:57], v[56:57], v[24:25]
	v_pk_add_f32 v[58:59], v[58:59], v[26:27]
	v_pk_add_f32 v[60:61], v[60:61], v[28:29]
	v_pk_add_f32 v[62:63], v[62:63], v[30:31]
	v_pk_add_f32 v[64:65], v[64:65], v[32:33]
	v_pk_add_f32 v[66:67], v[66:67], v[34:35]
	v_pk_add_f32 v[68:69], v[68:69], v[36:37]
	v_pk_add_f32 v[70:71], v[70:71], v[38:39]
	v_pk_mul_f32 v[208:209], v[56:57], v[56:57]
	v_pk_fma_f32 v[208:209], v[58:59], v[58:59], v[208:209]
	v_pk_fma_f32 v[208:209], v[60:61], v[60:61], v[208:209]
	v_pk_fma_f32 v[208:209], v[62:63], v[62:63], v[208:209]
	v_pk_fma_f32 v[208:209], v[64:65], v[64:65], v[208:209]
	v_pk_fma_f32 v[208:209], v[66:67], v[66:67], v[208:209]
	v_pk_fma_f32 v[208:209], v[68:69], v[68:69], v[208:209]
	v_pk_fma_f32 v[208:209], v[70:71], v[70:71], v[208:209]
	v_add_f32_e32 v208, v208, v209
	v_mov_b32_e32 v209, v208
	s_nop 1
	v_permlane16_swap_b32_e32 v208, v209
	v_add_f32_e32 v208, v208, v209
	v_mov_b32_e32 v209, v208
	s_nop 1
	v_permlane32_swap_b32_e32 v208, v209
	v_add_f32_e32 v208, v208, v209
	v_mov_b32_e32 v210, 0x358637bd
	v_fmac_f32_e32 v210, 0x3c800000, v208
	v_rsq_f32_e32 v210, v210
	s_add_u32 s24, s29, 0
	s_lshr_b32 s8, s24, 1
	s_lshl_b32 s8, s8, 12
	s_and_b32 s24, s24, 1
	s_lshl_b32 s24, s24, 8
	s_add_u32 s8, s8, s24
	v_mul_f32_e32 v210, v213, v210
	v_add_u32_e32 v212, s8, v23
	v_pk_mul_f32 v[56:57], v[56:57], v[210:211] op_sel_hi:[1,0]
	v_pk_mul_f32 v[58:59], v[58:59], v[210:211] op_sel_hi:[1,0]
	v_pk_mul_f32 v[56:57], v[56:57], v[40:41]
	v_pk_mul_f32 v[58:59], v[58:59], v[42:43]
	v_cvt_pk_f16_f32 v56, v56, v57
	v_cvt_pk_f16_f32 v57, v58, v59
	global_store_dwordx2 v212, v[56:57], s[22:23] offset:0 sc0 sc1
	v_pk_mul_f32 v[60:61], v[60:61], v[210:211] op_sel_hi:[1,0]
	v_pk_mul_f32 v[62:63], v[62:63], v[210:211] op_sel_hi:[1,0]
	v_pk_mul_f32 v[60:61], v[60:61], v[44:45]
	v_pk_mul_f32 v[62:63], v[62:63], v[46:47]
	v_cvt_pk_f16_f32 v60, v60, v61
	v_cvt_pk_f16_f32 v61, v62, v63
	global_store_dwordx2 v212, v[60:61], s[22:23] offset:1024 sc0 sc1
	v_pk_mul_f32 v[64:65], v[64:65], v[210:211] op_sel_hi:[1,0]
	v_pk_mul_f32 v[66:67], v[66:67], v[210:211] op_sel_hi:[1,0]
	v_pk_mul_f32 v[64:65], v[64:65], v[48:49]
	v_pk_mul_f32 v[66:67], v[66:67], v[50:51]
	v_cvt_pk_f16_f32 v64, v64, v65
	v_cvt_pk_f16_f32 v65, v66, v67
	global_store_dwordx2 v212, v[64:65], s[22:23] offset:2048 sc0 sc1
	v_pk_mul_f32 v[68:69], v[68:69], v[210:211] op_sel_hi:[1,0]
	v_pk_mul_f32 v[70:71], v[70:71], v[210:211] op_sel_hi:[1,0]
	v_pk_mul_f32 v[68:69], v[68:69], v[52:53]
	v_pk_mul_f32 v[70:71], v[70:71], v[54:55]
	v_cvt_pk_f16_f32 v68, v68, v69
	v_cvt_pk_f16_f32 v69, v70, v71
	global_store_dwordx2 v212, v[68:69], s[22:23] offset:3072 sc0 sc1
	v_pk_add_f32 v[72:73], v[72:73], v[24:25]
	v_pk_add_f32 v[74:75], v[74:75], v[26:27]
	v_pk_add_f32 v[76:77], v[76:77], v[28:29]
	v_pk_add_f32 v[78:79], v[78:79], v[30:31]
	v_pk_add_f32 v[80:81], v[80:81], v[32:33]
	v_pk_add_f32 v[82:83], v[82:83], v[34:35]
	v_pk_add_f32 v[84:85], v[84:85], v[36:37]
	v_pk_add_f32 v[86:87], v[86:87], v[38:39]
	v_pk_mul_f32 v[208:209], v[72:73], v[72:73]
	v_pk_fma_f32 v[208:209], v[74:75], v[74:75], v[208:209]
	v_pk_fma_f32 v[208:209], v[76:77], v[76:77], v[208:209]
	v_pk_fma_f32 v[208:209], v[78:79], v[78:79], v[208:209]
	v_pk_fma_f32 v[208:209], v[80:81], v[80:81], v[208:209]
	v_pk_fma_f32 v[208:209], v[82:83], v[82:83], v[208:209]
	v_pk_fma_f32 v[208:209], v[84:85], v[84:85], v[208:209]
	v_pk_fma_f32 v[208:209], v[86:87], v[86:87], v[208:209]
	v_add_f32_e32 v208, v208, v209
	v_mov_b32_e32 v209, v208
	s_nop 1
	v_permlane16_swap_b32_e32 v208, v209
	v_add_f32_e32 v208, v208, v209
	v_mov_b32_e32 v209, v208
	s_nop 1
	v_permlane32_swap_b32_e32 v208, v209
	v_add_f32_e32 v208, v208, v209
	v_mov_b32_e32 v210, 0x358637bd
	v_fmac_f32_e32 v210, 0x3c800000, v208
	v_rsq_f32_e32 v210, v210
	s_add_u32 s24, s29, 1
	s_lshr_b32 s8, s24, 1
	s_lshl_b32 s8, s8, 12
	s_and_b32 s24, s24, 1
	s_lshl_b32 s24, s24, 8
	s_add_u32 s8, s8, s24
	v_mul_f32_e32 v210, v213, v210
	v_add_u32_e32 v212, s8, v23
	v_pk_mul_f32 v[72:73], v[72:73], v[210:211] op_sel_hi:[1,0]
	v_pk_mul_f32 v[74:75], v[74:75], v[210:211] op_sel_hi:[1,0]
	v_pk_mul_f32 v[72:73], v[72:73], v[40:41]
	v_pk_mul_f32 v[74:75], v[74:75], v[42:43]
	v_cvt_pk_f16_f32 v72, v72, v73
	v_cvt_pk_f16_f32 v73, v74, v75
	global_store_dwordx2 v212, v[72:73], s[22:23] offset:0 sc0 sc1
	v_pk_mul_f32 v[76:77], v[76:77], v[210:211] op_sel_hi:[1,0]
	v_pk_mul_f32 v[78:79], v[78:79], v[210:211] op_sel_hi:[1,0]
	v_pk_mul_f32 v[76:77], v[76:77], v[44:45]
	v_pk_mul_f32 v[78:79], v[78:79], v[46:47]
	v_cvt_pk_f16_f32 v76, v76, v77
	v_cvt_pk_f16_f32 v77, v78, v79
	global_store_dwordx2 v212, v[76:77], s[22:23] offset:1024 sc0 sc1
	v_pk_mul_f32 v[80:81], v[80:81], v[210:211] op_sel_hi:[1,0]
	v_pk_mul_f32 v[82:83], v[82:83], v[210:211] op_sel_hi:[1,0]
	v_pk_mul_f32 v[80:81], v[80:81], v[48:49]
	v_pk_mul_f32 v[82:83], v[82:83], v[50:51]
	v_cvt_pk_f16_f32 v80, v80, v81
	v_cvt_pk_f16_f32 v81, v82, v83
	global_store_dwordx2 v212, v[80:81], s[22:23] offset:2048 sc0 sc1
	v_pk_mul_f32 v[84:85], v[84:85], v[210:211] op_sel_hi:[1,0]
	v_pk_mul_f32 v[86:87], v[86:87], v[210:211] op_sel_hi:[1,0]
	v_pk_mul_f32 v[84:85], v[84:85], v[52:53]
	v_pk_mul_f32 v[86:87], v[86:87], v[54:55]
	v_cvt_pk_f16_f32 v84, v84, v85
	v_cvt_pk_f16_f32 v85, v86, v87
	global_store_dwordx2 v212, v[84:85], s[22:23] offset:3072 sc0 sc1
	v_pk_add_f32 v[88:89], v[88:89], v[24:25]
	v_pk_add_f32 v[90:91], v[90:91], v[26:27]
	v_pk_add_f32 v[92:93], v[92:93], v[28:29]
	v_pk_add_f32 v[94:95], v[94:95], v[30:31]
	v_pk_add_f32 v[96:97], v[96:97], v[32:33]
	v_pk_add_f32 v[98:99], v[98:99], v[34:35]
	v_pk_add_f32 v[100:101], v[100:101], v[36:37]
	v_pk_add_f32 v[102:103], v[102:103], v[38:39]
	v_pk_mul_f32 v[208:209], v[88:89], v[88:89]
	v_pk_fma_f32 v[208:209], v[90:91], v[90:91], v[208:209]
	v_pk_fma_f32 v[208:209], v[92:93], v[92:93], v[208:209]
	v_pk_fma_f32 v[208:209], v[94:95], v[94:95], v[208:209]
	v_pk_fma_f32 v[208:209], v[96:97], v[96:97], v[208:209]
	v_pk_fma_f32 v[208:209], v[98:99], v[98:99], v[208:209]
	v_pk_fma_f32 v[208:209], v[100:101], v[100:101], v[208:209]
	v_pk_fma_f32 v[208:209], v[102:103], v[102:103], v[208:209]
	v_add_f32_e32 v208, v208, v209
	v_mov_b32_e32 v209, v208
	s_nop 1
	v_permlane16_swap_b32_e32 v208, v209
	v_add_f32_e32 v208, v208, v209
	v_mov_b32_e32 v209, v208
	s_nop 1
	v_permlane32_swap_b32_e32 v208, v209
	v_add_f32_e32 v208, v208, v209
	v_mov_b32_e32 v210, 0x358637bd
	v_fmac_f32_e32 v210, 0x3c800000, v208
	v_rsq_f32_e32 v210, v210
	s_add_u32 s24, s29, 2
	s_lshr_b32 s8, s24, 1
	s_lshl_b32 s8, s8, 12
	s_and_b32 s24, s24, 1
	s_lshl_b32 s24, s24, 8
	s_add_u32 s8, s8, s24
	v_mul_f32_e32 v210, v213, v210
	v_add_u32_e32 v212, s8, v23
	v_pk_mul_f32 v[88:89], v[88:89], v[210:211] op_sel_hi:[1,0]
	v_pk_mul_f32 v[90:91], v[90:91], v[210:211] op_sel_hi:[1,0]
	v_pk_mul_f32 v[88:89], v[88:89], v[40:41]
	v_pk_mul_f32 v[90:91], v[90:91], v[42:43]
	v_cvt_pk_f16_f32 v88, v88, v89
	v_cvt_pk_f16_f32 v89, v90, v91
	global_store_dwordx2 v212, v[88:89], s[22:23] offset:0 sc0 sc1
	v_pk_mul_f32 v[92:93], v[92:93], v[210:211] op_sel_hi:[1,0]
	v_pk_mul_f32 v[94:95], v[94:95], v[210:211] op_sel_hi:[1,0]
	v_pk_mul_f32 v[92:93], v[92:93], v[44:45]
	v_pk_mul_f32 v[94:95], v[94:95], v[46:47]
	v_cvt_pk_f16_f32 v92, v92, v93
	v_cvt_pk_f16_f32 v93, v94, v95
	global_store_dwordx2 v212, v[92:93], s[22:23] offset:1024 sc0 sc1
	v_pk_mul_f32 v[96:97], v[96:97], v[210:211] op_sel_hi:[1,0]
	v_pk_mul_f32 v[98:99], v[98:99], v[210:211] op_sel_hi:[1,0]
	v_pk_mul_f32 v[96:97], v[96:97], v[48:49]
	v_pk_mul_f32 v[98:99], v[98:99], v[50:51]
	v_cvt_pk_f16_f32 v96, v96, v97
	v_cvt_pk_f16_f32 v97, v98, v99
	global_store_dwordx2 v212, v[96:97], s[22:23] offset:2048 sc0 sc1
	v_pk_mul_f32 v[100:101], v[100:101], v[210:211] op_sel_hi:[1,0]
	v_pk_mul_f32 v[102:103], v[102:103], v[210:211] op_sel_hi:[1,0]
	v_pk_mul_f32 v[100:101], v[100:101], v[52:53]
	v_pk_mul_f32 v[102:103], v[102:103], v[54:55]
	v_cvt_pk_f16_f32 v100, v100, v101
	v_cvt_pk_f16_f32 v101, v102, v103
	global_store_dwordx2 v212, v[100:101], s[22:23] offset:3072 sc0 sc1
	v_pk_add_f32 v[104:105], v[104:105], v[24:25]
	v_pk_add_f32 v[106:107], v[106:107], v[26:27]
	v_pk_add_f32 v[108:109], v[108:109], v[28:29]
	v_pk_add_f32 v[110:111], v[110:111], v[30:31]
	v_pk_add_f32 v[112:113], v[112:113], v[32:33]
	v_pk_add_f32 v[114:115], v[114:115], v[34:35]
	v_pk_add_f32 v[116:117], v[116:117], v[36:37]
	v_pk_add_f32 v[118:119], v[118:119], v[38:39]
	v_pk_mul_f32 v[208:209], v[104:105], v[104:105]
	v_pk_fma_f32 v[208:209], v[106:107], v[106:107], v[208:209]
	v_pk_fma_f32 v[208:209], v[108:109], v[108:109], v[208:209]
	v_pk_fma_f32 v[208:209], v[110:111], v[110:111], v[208:209]
	v_pk_fma_f32 v[208:209], v[112:113], v[112:113], v[208:209]
	v_pk_fma_f32 v[208:209], v[114:115], v[114:115], v[208:209]
	v_pk_fma_f32 v[208:209], v[116:117], v[116:117], v[208:209]
	v_pk_fma_f32 v[208:209], v[118:119], v[118:119], v[208:209]
	v_add_f32_e32 v208, v208, v209
	v_mov_b32_e32 v209, v208
	s_nop 1
	v_permlane16_swap_b32_e32 v208, v209
	v_add_f32_e32 v208, v208, v209
	v_mov_b32_e32 v209, v208
	s_nop 1
	v_permlane32_swap_b32_e32 v208, v209
	v_add_f32_e32 v208, v208, v209
	v_mov_b32_e32 v210, 0x358637bd
	v_fmac_f32_e32 v210, 0x3c800000, v208
	v_rsq_f32_e32 v210, v210
	s_add_u32 s24, s29, 3
	s_lshr_b32 s8, s24, 1
	s_lshl_b32 s8, s8, 12
	s_and_b32 s24, s24, 1
	s_lshl_b32 s24, s24, 8
	s_add_u32 s8, s8, s24
	v_mul_f32_e32 v210, v213, v210
	v_add_u32_e32 v212, s8, v23
	v_pk_mul_f32 v[104:105], v[104:105], v[210:211] op_sel_hi:[1,0]
	v_pk_mul_f32 v[106:107], v[106:107], v[210:211] op_sel_hi:[1,0]
	v_pk_mul_f32 v[104:105], v[104:105], v[40:41]
	v_pk_mul_f32 v[106:107], v[106:107], v[42:43]
	v_cvt_pk_f16_f32 v104, v104, v105
	v_cvt_pk_f16_f32 v105, v106, v107
	global_store_dwordx2 v212, v[104:105], s[22:23] offset:0 sc0 sc1
	v_pk_mul_f32 v[108:109], v[108:109], v[210:211] op_sel_hi:[1,0]
	v_pk_mul_f32 v[110:111], v[110:111], v[210:211] op_sel_hi:[1,0]
	v_pk_mul_f32 v[108:109], v[108:109], v[44:45]
	v_pk_mul_f32 v[110:111], v[110:111], v[46:47]
	v_cvt_pk_f16_f32 v108, v108, v109
	v_cvt_pk_f16_f32 v109, v110, v111
	global_store_dwordx2 v212, v[108:109], s[22:23] offset:1024 sc0 sc1
	v_pk_mul_f32 v[112:113], v[112:113], v[210:211] op_sel_hi:[1,0]
	v_pk_mul_f32 v[114:115], v[114:115], v[210:211] op_sel_hi:[1,0]
	v_pk_mul_f32 v[112:113], v[112:113], v[48:49]
	v_pk_mul_f32 v[114:115], v[114:115], v[50:51]
	v_cvt_pk_f16_f32 v112, v112, v113
	v_cvt_pk_f16_f32 v113, v114, v115
	global_store_dwordx2 v212, v[112:113], s[22:23] offset:2048 sc0 sc1
	v_pk_mul_f32 v[116:117], v[116:117], v[210:211] op_sel_hi:[1,0]
	v_pk_mul_f32 v[118:119], v[118:119], v[210:211] op_sel_hi:[1,0]
	v_pk_mul_f32 v[116:117], v[116:117], v[52:53]
	v_pk_mul_f32 v[118:119], v[118:119], v[54:55]
	v_cvt_pk_f16_f32 v116, v116, v117
	v_cvt_pk_f16_f32 v117, v118, v119
	global_store_dwordx2 v212, v[116:117], s[22:23] offset:3072 sc0 sc1
	s_branch .Lpf_done
.Lpf_vKA:
	s_mul_i32 s25, s25, 0x50
	s_add_u32 s29, s10, s25
	s_lshr_b32 s29, s29, 4
	v_add_u32_e32 v5, s25, v3
	v_lshlrev_b32_e32 v5, 7, v5
	v_add_u32_e32 v15, v5, v6
	v_add_u32_e32 v16, v5, v7
	v_add_u32_e32 v5, 0x9000, v9
	v_add_u32_e32 v17, v5, v6
	v_add_u32_e32 v18, v5, v7
	v_add_u32_e32 v19, 0x1a000, v15
	v_add_u32_e32 v20, 0x1a000, v16
	v_add_u32_e32 v21, 0x1a000, v17
	v_add_u32_e32 v22, 0x1a000, v18
	v_lshlrev_b32_e32 v5, 4, v4
	global_load_dwordx4 v[24:27], v5, s[14:15] offset:0
	global_load_dwordx4 v[28:31], v5, s[14:15] offset:64
	global_load_dwordx4 v[32:35], v5, s[14:15] offset:128
	global_load_dwordx4 v[36:39], v5, s[14:15] offset:192
	global_load_dwordx4 v[40:43], v5, s[16:17] offset:0
	global_load_dwordx4 v[44:47], v5, s[16:17] offset:64
	global_load_dwordx4 v[48:51], v5, s[16:17] offset:128
	global_load_dwordx4 v[52:55], v5, s[16:17] offset:192
	s_add_u32 m0, s28, 0x0
	s_nop 0
	global_load_lds_dwordx4 v10, s[4:5]
	s_add_u32 m0, s28, 0x2000
	s_nop 0
	global_load_lds_dwordx4 v11, s[4:5]
	s_add_u32 m0, s28, 0x4000
	s_nop 0
	global_load_lds_dwordx4 v12, s[4:5]
	s_add_u32 m0, s28, 0x6000
	s_nop 0
	global_load_lds_dwordx4 v13, s[4:5]
	s_add_u32 m0, s28, 0x8000
	s_nop 0
	global_load_lds_dwordx4 v14, s[4:5]
	s_add_u32 s4, s4, s20
	s_addc_u32 s5, s5, 0
	s_add_u32 m0, s28, 0x9000
	s_nop 0
	global_load_lds_dwordx4 v10, s[6:7]
	s_add_u32 m0, s28, 0xb000
	s_nop 0
	global_load_lds_dwordx4 v11, s[6:7]
	s_add_u32 s6, s6, s20
	s_addc_u32 s7, s7, 0
	s_add_u32 m0, s28, 0xd000
	s_nop 0
	global_load_lds_dwordx4 v10, s[4:5]
	s_add_u32 m0, s28, 0xf000
	s_nop 0
	global_load_lds_dwordx4 v11, s[4:5]
	s_add_u32 m0, s28, 0x11000
	s_nop 0
	global_load_lds_dwordx4 v12, s[4:5]
	s_add_u32 m0, s28, 0x13000
	s_nop 0
	global_load_lds_dwordx4 v13, s[4:5]
	s_add_u32 m0, s28, 0x15000
	s_nop 0
	global_load_lds_dwordx4 v14, s[4:5]
	s_add_u32 s4, s4, s20
	s_addc_u32 s5, s5, 0
	s_add_u32 m0, s28, 0x16000
	s_nop 0
	global_load_lds_dwordx4 v10, s[6:7]
	s_add_u32 m0, s28, 0x18000
	s_nop 0
	global_load_lds_dwordx4 v11, s[6:7]
	s_add_u32 s6, s6, s20
	s_addc_u32 s7, s7, 0
	s_add_u32 m0, s28, 0x1a000
	s_nop 0
	global_load_lds_dwordx4 v10, s[4:5]
	s_add_u32 m0, s28, 0x1c000
	s_nop 0
	global_load_lds_dwordx4 v11, s[4:5]
	s_add_u32 m0, s28, 0x1e000
	s_nop 0
	global_load_lds_dwordx4 v12, s[4:5]
	s_add_u32 m0, s28, 0x20000
	s_nop 0
	global_load_lds_dwordx4 v13, s[4:5]
	s_add_u32 m0, s28, 0x22000
	s_nop 0
	global_load_lds_dwordx4 v14, s[4:5]
	s_add_u32 s4, s4, s20
	s_addc_u32 s5, s5, 0
	s_add_u32 m0, s28, 0x23000
	s_nop 0
	global_load_lds_dwordx4 v10, s[6:7]
	s_add_u32 m0, s28, 0x25000
	s_nop 0
	global_load_lds_dwordx4 v11, s[6:7]
	s_add_u32 s6, s6, s20
	s_addc_u32 s7, s7, 0
	s_waitcnt vmcnt(14) lgkmcnt(0)
	s_barrier
	s_waitcnt lgkmcnt(6)
	ds_read_b128 v[136:139], v15
	ds_read_b128 v[156:159], v17
	ds_read_b128 v[160:163], v17 offset:2048
	ds_read_b128 v[164:167], v17 offset:4096
	ds_read_b128 v[168:171], v17 offset:6144
	ds_read_b128 v[140:143], v15 offset:2048
	ds_read_b128 v[144:147], v15 offset:4096
	ds_read_b128 v[148:151], v15 offset:6144
	ds_read_b128 v[152:155], v15 offset:8192
	s_waitcnt lgkmcnt(6)
	ds_read_b128 v[172:175], v16
	ds_read_b128 v[192:195], v18
	ds_read_b128 v[196:199], v18 offset:2048
	ds_read_b128 v[200:203], v18 offset:4096
	ds_read_b128 v[204:207], v18 offset:6144
	ds_read_b128 v[176:179], v16 offset:2048
	ds_read_b128 v[180:183], v16 offset:4096
	ds_read_b128 v[184:187], v16 offset:6144
	ds_read_b128 v[188:191], v16 offset:8192
	v_mfma_f32_16x16x32_f16 v[56:59], v[156:159], v[136:139], 0
	s_waitcnt lgkmcnt(15)
	v_mfma_f32_16x16x32_f16 v[60:63], v[160:163], v[136:139], 0
	s_waitcnt lgkmcnt(14)
	v_mfma_f32_16x16x32_f16 v[64:67], v[164:167], v[136:139], 0
	s_waitcnt lgkmcnt(13)
	v_mfma_f32_16x16x32_f16 v[68:71], v[168:171], v[136:139], 0
	s_waitcnt lgkmcnt(12)
	v_mfma_f32_16x16x32_f16 v[72:75], v[156:159], v[140:143], 0
	v_mfma_f32_16x16x32_f16 v[76:79], v[160:163], v[140:143], 0
	v_mfma_f32_16x16x32_f16 v[80:83], v[164:167], v[140:143], 0
	v_mfma_f32_16x16x32_f16 v[84:87], v[168:171], v[140:143], 0
	s_waitcnt lgkmcnt(11)
	v_mfma_f32_16x16x32_f16 v[88:91], v[156:159], v[144:147], 0
	v_mfma_f32_16x16x32_f16 v[92:95], v[160:163], v[144:147], 0
	v_mfma_f32_16x16x32_f16 v[96:99], v[164:167], v[144:147], 0
	v_mfma_f32_16x16x32_f16 v[100:103], v[168:171], v[144:147], 0
	s_waitcnt lgkmcnt(10)
	v_mfma_f32_16x16x32_f16 v[104:107], v[156:159], v[148:151], 0
	v_mfma_f32_16x16x32_f16 v[108:111], v[160:163], v[148:151], 0
	v_mfma_f32_16x16x32_f16 v[112:115], v[164:167], v[148:151], 0
	v_mfma_f32_16x16x32_f16 v[116:119], v[168:171], v[148:151], 0
	s_waitcnt lgkmcnt(9)
	v_mfma_f32_16x16x32_f16 v[120:123], v[156:159], v[152:155], 0
	v_mfma_f32_16x16x32_f16 v[124:127], v[160:163], v[152:155], 0
	v_mfma_f32_16x16x32_f16 v[128:131], v[164:167], v[152:155], 0
	v_mfma_f32_16x16x32_f16 v[132:135], v[168:171], v[152:155], 0
	s_waitcnt vmcnt(7) lgkmcnt(0)
	s_barrier
	s_waitcnt lgkmcnt(6)
	ds_read_b128 v[136:139], v15 offset:53248
	ds_read_b128 v[156:159], v17 offset:53248
	ds_read_b128 v[160:163], v17 offset:55296
	ds_read_b128 v[164:167], v17 offset:57344
	ds_read_b128 v[168:171], v17 offset:59392
	ds_read_b128 v[140:143], v15 offset:55296
	ds_read_b128 v[144:147], v15 offset:57344
	ds_read_b128 v[148:151], v15 offset:59392
	ds_read_b128 v[152:155], v15 offset:61440
	v_mfma_f32_16x16x32_f16 v[56:59], v[192:195], v[172:175], v[56:59]
	s_add_u32 m0, s28, 0x0
	s_nop 0
	global_load_lds_dwordx4 v10, s[4:5]
	s_waitcnt lgkmcnt(15)
	v_mfma_f32_16x16x32_f16 v[60:63], v[196:199], v[172:175], v[60:63]
	s_waitcnt lgkmcnt(14)
	v_mfma_f32_16x16x32_f16 v[64:67], v[200:203], v[172:175], v[64:67]
	s_waitcnt lgkmcnt(13)
	v_mfma_f32_16x16x32_f16 v[68:71], v[204:207], v[172:175], v[68:71]
	s_waitcnt lgkmcnt(12)
	v_mfma_f32_16x16x32_f16 v[72:75], v[192:195], v[176:179], v[72:75]
	v_mfma_f32_16x16x32_f16 v[76:79], v[196:199], v[176:179], v[76:79]
	s_add_u32 m0, s28, 0x2000
	s_nop 0
	global_load_lds_dwordx4 v11, s[4:5]
	v_mfma_f32_16x16x32_f16 v[80:83], v[200:203], v[176:179], v[80:83]
	v_mfma_f32_16x16x32_f16 v[84:87], v[204:207], v[176:179], v[84:87]
	s_waitcnt lgkmcnt(11)
	v_mfma_f32_16x16x32_f16 v[88:91], v[192:195], v[180:183], v[88:91]
	v_mfma_f32_16x16x32_f16 v[92:95], v[196:199], v[180:183], v[92:95]
	v_mfma_f32_16x16x32_f16 v[96:99], v[200:203], v[180:183], v[96:99]
	s_add_u32 m0, s28, 0x4000
	s_nop 0
	global_load_lds_dwordx4 v12, s[4:5]
	v_mfma_f32_16x16x32_f16 v[100:103], v[204:207], v[180:183], v[100:103]
	s_waitcnt lgkmcnt(10)
	v_mfma_f32_16x16x32_f16 v[104:107], v[192:195], v[184:187], v[104:107]
	v_mfma_f32_16x16x32_f16 v[108:111], v[196:199], v[184:187], v[108:111]
	v_mfma_f32_16x16x32_f16 v[112:115], v[200:203], v[184:187], v[112:115]
	v_mfma_f32_16x16x32_f16 v[116:119], v[204:207], v[184:187], v[116:119]
	s_add_u32 m0, s28, 0x6000
	s_nop 0
	global_load_lds_dwordx4 v13, s[4:5]
	s_waitcnt lgkmcnt(9)
	v_mfma_f32_16x16x32_f16 v[120:123], v[192:195], v[188:191], v[120:123]
	v_mfma_f32_16x16x32_f16 v[124:127], v[196:199], v[188:191], v[124:127]
	v_mfma_f32_16x16x32_f16 v[128:131], v[200:203], v[188:191], v[128:131]
	v_mfma_f32_16x16x32_f16 v[132:135], v[204:207], v[188:191], v[132:135]
	s_waitcnt lgkmcnt(6)
	ds_read_b128 v[172:175], v16 offset:53248
	ds_read_b128 v[192:195], v18 offset:53248
	ds_read_b128 v[196:199], v18 offset:55296
	ds_read_b128 v[200:203], v18 offset:57344
	ds_read_b128 v[204:207], v18 offset:59392
	ds_read_b128 v[176:179], v16 offset:55296
	ds_read_b128 v[180:183], v16 offset:57344
	ds_read_b128 v[184:187], v16 offset:59392
	ds_read_b128 v[188:191], v16 offset:61440
	v_mfma_f32_16x16x32_f16 v[56:59], v[156:159], v[136:139], v[56:59]
	s_add_u32 m0, s28, 0x8000
	s_nop 0
	global_load_lds_dwordx4 v14, s[4:5]
	s_add_u32 s4, s4, s20
	s_addc_u32 s5, s5, 0
	s_waitcnt lgkmcnt(15)
	v_mfma_f32_16x16x32_f16 v[60:63], v[160:163], v[136:139], v[60:63]
	s_waitcnt lgkmcnt(14)
	v_mfma_f32_16x16x32_f16 v[64:67], v[164:167], v[136:139], v[64:67]
	s_waitcnt lgkmcnt(13)
	v_mfma_f32_16x16x32_f16 v[68:71], v[168:171], v[136:139], v[68:71]
	s_waitcnt lgkmcnt(12)
	v_mfma_f32_16x16x32_f16 v[72:75], v[156:159], v[140:143], v[72:75]
	v_mfma_f32_16x16x32_f16 v[76:79], v[160:163], v[140:143], v[76:79]
	v_mfma_f32_16x16x32_f16 v[80:83], v[164:167], v[140:143], v[80:83]
	s_add_u32 m0, s28, 0x9000
	s_nop 0
	global_load_lds_dwordx4 v10, s[6:7]
	v_mfma_f32_16x16x32_f16 v[84:87], v[168:171], v[140:143], v[84:87]
	s_waitcnt lgkmcnt(11)
	v_mfma_f32_16x16x32_f16 v[88:91], v[156:159], v[144:147], v[88:91]
	v_mfma_f32_16x16x32_f16 v[92:95], v[160:163], v[144:147], v[92:95]
	v_mfma_f32_16x16x32_f16 v[96:99], v[164:167], v[144:147], v[96:99]
	v_mfma_f32_16x16x32_f16 v[100:103], v[168:171], v[144:147], v[100:103]
	s_waitcnt lgkmcnt(10)
	v_mfma_f32_16x16x32_f16 v[104:107], v[156:159], v[148:151], v[104:107]
	v_mfma_f32_16x16x32_f16 v[108:111], v[160:163], v[148:151], v[108:111]
	s_add_u32 m0, s28, 0xb000
	s_nop 0
	global_load_lds_dwordx4 v11, s[6:7]
	s_add_u32 s6, s6, s20
	s_addc_u32 s7, s7, 0
	v_mfma_f32_16x16x32_f16 v[112:115], v[164:167], v[148:151], v[112:115]
	v_mfma_f32_16x16x32_f16 v[116:119], v[168:171], v[148:151], v[116:119]
	s_waitcnt lgkmcnt(9)
	v_mfma_f32_16x16x32_f16 v[120:123], v[156:159], v[152:155], v[120:123]
	v_mfma_f32_16x16x32_f16 v[124:127], v[160:163], v[152:155], v[124:127]
	v_mfma_f32_16x16x32_f16 v[128:131], v[164:167], v[152:155], v[128:131]
	v_mfma_f32_16x16x32_f16 v[132:135], v[168:171], v[152:155], v[132:135]
	s_waitcnt vmcnt(7) lgkmcnt(0)
	s_barrier
	s_waitcnt lgkmcnt(6)
	ds_read_b128 v[136:139], v19
	ds_read_b128 v[156:159], v21
	ds_read_b128 v[160:163], v21 offset:2048
	ds_read_b128 v[164:167], v21 offset:4096
	ds_read_b128 v[168:171], v21 offset:6144
	ds_read_b128 v[140:143], v19 offset:2048
	ds_read_b128 v[144:147], v19 offset:4096
	ds_read_b128 v[148:151], v19 offset:6144
	ds_read_b128 v[152:155], v19 offset:8192
	v_mfma_f32_16x16x32_f16 v[56:59], v[192:195], v[172:175], v[56:59]
	s_add_u32 m0, s28, 0xd000
	s_nop 0
	global_load_lds_dwordx4 v10, s[4:5]
	s_waitcnt lgkmcnt(15)
	v_mfma_f32_16x16x32_f16 v[60:63], v[196:199], v[172:175], v[60:63]
	s_waitcnt lgkmcnt(14)
	v_mfma_f32_16x16x32_f16 v[64:67], v[200:203], v[172:175], v[64:67]
	s_waitcnt lgkmcnt(13)
	v_mfma_f32_16x16x32_f16 v[68:71], v[204:207], v[172:175], v[68:71]
	s_waitcnt lgkmcnt(12)
	v_mfma_f32_16x16x32_f16 v[72:75], v[192:195], v[176:179], v[72:75]
	v_mfma_f32_16x16x32_f16 v[76:79], v[196:199], v[176:179], v[76:79]
	s_add_u32 m0, s28, 0xf000
	s_nop 0
	global_load_lds_dwordx4 v11, s[4:5]
	v_mfma_f32_16x16x32_f16 v[80:83], v[200:203], v[176:179], v[80:83]
	v_mfma_f32_16x16x32_f16 v[84:87], v[204:207], v[176:179], v[84:87]
	s_waitcnt lgkmcnt(11)
	v_mfma_f32_16x16x32_f16 v[88:91], v[192:195], v[180:183], v[88:91]
	v_mfma_f32_16x16x32_f16 v[92:95], v[196:199], v[180:183], v[92:95]
	v_mfma_f32_16x16x32_f16 v[96:99], v[200:203], v[180:183], v[96:99]
	s_add_u32 m0, s28, 0x11000
	s_nop 0
	global_load_lds_dwordx4 v12, s[4:5]
	v_mfma_f32_16x16x32_f16 v[100:103], v[204:207], v[180:183], v[100:103]
	s_waitcnt lgkmcnt(10)
	v_mfma_f32_16x16x32_f16 v[104:107], v[192:195], v[184:187], v[104:107]
	v_mfma_f32_16x16x32_f16 v[108:111], v[196:199], v[184:187], v[108:111]
	v_mfma_f32_16x16x32_f16 v[112:115], v[200:203], v[184:187], v[112:115]
	v_mfma_f32_16x16x32_f16 v[116:119], v[204:207], v[184:187], v[116:119]
	s_add_u32 m0, s28, 0x13000
	s_nop 0
	global_load_lds_dwordx4 v13, s[4:5]
	s_waitcnt lgkmcnt(9)
	v_mfma_f32_16x16x32_f16 v[120:123], v[192:195], v[188:191], v[120:123]
	v_mfma_f32_16x16x32_f16 v[124:127], v[196:199], v[188:191], v[124:127]
	v_mfma_f32_16x16x32_f16 v[128:131], v[200:203], v[188:191], v[128:131]
	v_mfma_f32_16x16x32_f16 v[132:135], v[204:207], v[188:191], v[132:135]
	s_waitcnt lgkmcnt(6)
	ds_read_b128 v[172:175], v20
	ds_read_b128 v[192:195], v22
	ds_read_b128 v[196:199], v22 offset:2048
	ds_read_b128 v[200:203], v22 offset:4096
	ds_read_b128 v[204:207], v22 offset:6144
	ds_read_b128 v[176:179], v20 offset:2048
	ds_read_b128 v[180:183], v20 offset:4096
	ds_read_b128 v[184:187], v20 offset:6144
	ds_read_b128 v[188:191], v20 offset:8192
	v_mfma_f32_16x16x32_f16 v[56:59], v[156:159], v[136:139], v[56:59]
	s_add_u32 m0, s28, 0x15000
	s_nop 0
	global_load_lds_dwordx4 v14, s[4:5]
	s_add_u32 s4, s4, s20
	s_addc_u32 s5, s5, 0
	s_waitcnt lgkmcnt(15)
	v_mfma_f32_16x16x32_f16 v[60:63], v[160:163], v[136:139], v[60:63]
	s_waitcnt lgkmcnt(14)
	v_mfma_f32_16x16x32_f16 v[64:67], v[164:167], v[136:139], v[64:67]
	s_waitcnt lgkmcnt(13)
	v_mfma_f32_16x16x32_f16 v[68:71], v[168:171], v[136:139], v[68:71]
	s_waitcnt lgkmcnt(12)
	v_mfma_f32_16x16x32_f16 v[72:75], v[156:159], v[140:143], v[72:75]
	v_mfma_f32_16x16x32_f16 v[76:79], v[160:163], v[140:143], v[76:79]
	v_mfma_f32_16x16x32_f16 v[80:83], v[164:167], v[140:143], v[80:83]
	s_add_u32 m0, s28, 0x16000
	s_nop 0
	global_load_lds_dwordx4 v10, s[6:7]
	v_mfma_f32_16x16x32_f16 v[84:87], v[168:171], v[140:143], v[84:87]
	s_waitcnt lgkmcnt(11)
	v_mfma_f32_16x16x32_f16 v[88:91], v[156:159], v[144:147], v[88:91]
	v_mfma_f32_16x16x32_f16 v[92:95], v[160:163], v[144:147], v[92:95]
	v_mfma_f32_16x16x32_f16 v[96:99], v[164:167], v[144:147], v[96:99]
	v_mfma_f32_16x16x32_f16 v[100:103], v[168:171], v[144:147], v[100:103]
	s_waitcnt lgkmcnt(10)
	v_mfma_f32_16x16x32_f16 v[104:107], v[156:159], v[148:151], v[104:107]
	v_mfma_f32_16x16x32_f16 v[108:111], v[160:163], v[148:151], v[108:111]
	s_add_u32 m0, s28, 0x18000
	s_nop 0
	global_load_lds_dwordx4 v11, s[6:7]
	s_add_u32 s6, s6, s20
	s_addc_u32 s7, s7, 0
	v_mfma_f32_16x16x32_f16 v[112:115], v[164:167], v[148:151], v[112:115]
	v_mfma_f32_16x16x32_f16 v[116:119], v[168:171], v[148:151], v[116:119]
	s_waitcnt lgkmcnt(9)
	v_mfma_f32_16x16x32_f16 v[120:123], v[156:159], v[152:155], v[120:123]
	v_mfma_f32_16x16x32_f16 v[124:127], v[160:163], v[152:155], v[124:127]
	v_mfma_f32_16x16x32_f16 v[128:131], v[164:167], v[152:155], v[128:131]
	v_mfma_f32_16x16x32_f16 v[132:135], v[168:171], v[152:155], v[132:135]
	s_waitcnt vmcnt(7) lgkmcnt(0)
	s_barrier
	s_waitcnt lgkmcnt(6)
	ds_read_b128 v[136:139], v15
	ds_read_b128 v[156:159], v17
	ds_read_b128 v[160:163], v17 offset:2048
	ds_read_b128 v[164:167], v17 offset:4096
	ds_read_b128 v[168:171], v17 offset:6144
	ds_read_b128 v[140:143], v15 offset:2048
	ds_read_b128 v[144:147], v15 offset:4096
	ds_read_b128 v[148:151], v15 offset:6144
	ds_read_b128 v[152:155], v15 offset:8192
	v_mfma_f32_16x16x32_f16 v[56:59], v[192:195], v[172:175], v[56:59]
	s_add_u32 m0, s28, 0x1a000
	s_nop 0
	global_load_lds_dwordx4 v10, s[4:5]
	s_waitcnt lgkmcnt(15)
	v_mfma_f32_16x16x32_f16 v[60:63], v[196:199], v[172:175], v[60:63]
	s_waitcnt lgkmcnt(14)
	v_mfma_f32_16x16x32_f16 v[64:67], v[200:203], v[172:175], v[64:67]
	s_waitcnt lgkmcnt(13)
	v_mfma_f32_16x16x32_f16 v[68:71], v[204:207], v[172:175], v[68:71]
	s_waitcnt lgkmcnt(12)
	v_mfma_f32_16x16x32_f16 v[72:75], v[192:195], v[176:179], v[72:75]
	v_mfma_f32_16x16x32_f16 v[76:79], v[196:199], v[176:179], v[76:79]
	s_add_u32 m0, s28, 0x1c000
	s_nop 0
	global_load_lds_dwordx4 v11, s[4:5]
	v_mfma_f32_16x16x32_f16 v[80:83], v[200:203], v[176:179], v[80:83]
	v_mfma_f32_16x16x32_f16 v[84:87], v[204:207], v[176:179], v[84:87]
	s_waitcnt lgkmcnt(11)
	v_mfma_f32_16x16x32_f16 v[88:91], v[192:195], v[180:183], v[88:91]
	v_mfma_f32_16x16x32_f16 v[92:95], v[196:199], v[180:183], v[92:95]
	v_mfma_f32_16x16x32_f16 v[96:99], v[200:203], v[180:183], v[96:99]
	s_add_u32 m0, s28, 0x1e000
	s_nop 0
	global_load_lds_dwordx4 v12, s[4:5]
	v_mfma_f32_16x16x32_f16 v[100:103], v[204:207], v[180:183], v[100:103]
	s_waitcnt lgkmcnt(10)
	v_mfma_f32_16x16x32_f16 v[104:107], v[192:195], v[184:187], v[104:107]
	v_mfma_f32_16x16x32_f16 v[108:111], v[196:199], v[184:187], v[108:111]
	v_mfma_f32_16x16x32_f16 v[112:115], v[200:203], v[184:187], v[112:115]
	v_mfma_f32_16x16x32_f16 v[116:119], v[204:207], v[184:187], v[116:119]
	s_add_u32 m0, s28, 0x20000
	s_nop 0
	global_load_lds_dwordx4 v13, s[4:5]
	s_waitcnt lgkmcnt(9)
	v_mfma_f32_16x16x32_f16 v[120:123], v[192:195], v[188:191], v[120:123]
	v_mfma_f32_16x16x32_f16 v[124:127], v[196:199], v[188:191], v[124:127]
	v_mfma_f32_16x16x32_f16 v[128:131], v[200:203], v[188:191], v[128:131]
	v_mfma_f32_16x16x32_f16 v[132:135], v[204:207], v[188:191], v[132:135]
	s_waitcnt lgkmcnt(6)
	ds_read_b128 v[172:175], v16
	ds_read_b128 v[192:195], v18
	ds_read_b128 v[196:199], v18 offset:2048
	ds_read_b128 v[200:203], v18 offset:4096
	ds_read_b128 v[204:207], v18 offset:6144
	ds_read_b128 v[176:179], v16 offset:2048
	ds_read_b128 v[180:183], v16 offset:4096
	ds_read_b128 v[184:187], v16 offset:6144
	ds_read_b128 v[188:191], v16 offset:8192
	v_mfma_f32_16x16x32_f16 v[56:59], v[156:159], v[136:139], v[56:59]
	s_add_u32 m0, s28, 0x22000
	s_nop 0
	global_load_lds_dwordx4 v14, s[4:5]
	s_add_u32 s4, s4, s20
	s_addc_u32 s5, s5, 0
	s_waitcnt lgkmcnt(15)
	v_mfma_f32_16x16x32_f16 v[60:63], v[160:163], v[136:139], v[60:63]
	s_waitcnt lgkmcnt(14)
	v_mfma_f32_16x16x32_f16 v[64:67], v[164:167], v[136:139], v[64:67]
	s_waitcnt lgkmcnt(13)
	v_mfma_f32_16x16x32_f16 v[68:71], v[168:171], v[136:139], v[68:71]
	s_waitcnt lgkmcnt(12)
	v_mfma_f32_16x16x32_f16 v[72:75], v[156:159], v[140:143], v[72:75]
	v_mfma_f32_16x16x32_f16 v[76:79], v[160:163], v[140:143], v[76:79]
	v_mfma_f32_16x16x32_f16 v[80:83], v[164:167], v[140:143], v[80:83]
	s_add_u32 m0, s28, 0x23000
	s_nop 0
	global_load_lds_dwordx4 v10, s[6:7]
	v_mfma_f32_16x16x32_f16 v[84:87], v[168:171], v[140:143], v[84:87]
	s_waitcnt lgkmcnt(11)
	v_mfma_f32_16x16x32_f16 v[88:91], v[156:159], v[144:147], v[88:91]
	v_mfma_f32_16x16x32_f16 v[92:95], v[160:163], v[144:147], v[92:95]
	v_mfma_f32_16x16x32_f16 v[96:99], v[164:167], v[144:147], v[96:99]
	v_mfma_f32_16x16x32_f16 v[100:103], v[168:171], v[144:147], v[100:103]
	s_waitcnt lgkmcnt(10)
	v_mfma_f32_16x16x32_f16 v[104:107], v[156:159], v[148:151], v[104:107]
	v_mfma_f32_16x16x32_f16 v[108:111], v[160:163], v[148:151], v[108:111]
	s_add_u32 m0, s28, 0x25000
	s_nop 0
	global_load_lds_dwordx4 v11, s[6:7]
	s_add_u32 s6, s6, s20
	s_addc_u32 s7, s7, 0
	v_mfma_f32_16x16x32_f16 v[112:115], v[164:167], v[148:151], v[112:115]
	v_mfma_f32_16x16x32_f16 v[116:119], v[168:171], v[148:151], v[116:119]
	s_waitcnt lgkmcnt(9)
	v_mfma_f32_16x16x32_f16 v[120:123], v[156:159], v[152:155], v[120:123]
	v_mfma_f32_16x16x32_f16 v[124:127], v[160:163], v[152:155], v[124:127]
	v_mfma_f32_16x16x32_f16 v[128:131], v[164:167], v[152:155], v[128:131]
	v_mfma_f32_16x16x32_f16 v[132:135], v[168:171], v[152:155], v[132:135]
	s_waitcnt vmcnt(7) lgkmcnt(0)
	s_barrier
	s_waitcnt lgkmcnt(6)
	ds_read_b128 v[136:139], v15 offset:53248
	ds_read_b128 v[156:159], v17 offset:53248
	ds_read_b128 v[160:163], v17 offset:55296
	ds_read_b128 v[164:167], v17 offset:57344
	ds_read_b128 v[168:171], v17 offset:59392
	ds_read_b128 v[140:143], v15 offset:55296
	ds_read_b128 v[144:147], v15 offset:57344
	ds_read_b128 v[148:151], v15 offset:59392
	ds_read_b128 v[152:155], v15 offset:61440
	v_mfma_f32_16x16x32_f16 v[56:59], v[192:195], v[172:175], v[56:59]
	s_add_u32 m0, s28, 0x0
	s_nop 0
	global_load_lds_dwordx4 v10, s[4:5]
	s_waitcnt lgkmcnt(15)
	v_mfma_f32_16x16x32_f16 v[60:63], v[196:199], v[172:175], v[60:63]
	s_waitcnt lgkmcnt(14)
	v_mfma_f32_16x16x32_f16 v[64:67], v[200:203], v[172:175], v[64:67]
	s_waitcnt lgkmcnt(13)
	v_mfma_f32_16x16x32_f16 v[68:71], v[204:207], v[172:175], v[68:71]
	s_waitcnt lgkmcnt(12)
	v_mfma_f32_16x16x32_f16 v[72:75], v[192:195], v[176:179], v[72:75]
	v_mfma_f32_16x16x32_f16 v[76:79], v[196:199], v[176:179], v[76:79]
	s_add_u32 m0, s28, 0x2000
	s_nop 0
	global_load_lds_dwordx4 v11, s[4:5]
	v_mfma_f32_16x16x32_f16 v[80:83], v[200:203], v[176:179], v[80:83]
	v_mfma_f32_16x16x32_f16 v[84:87], v[204:207], v[176:179], v[84:87]
	s_waitcnt lgkmcnt(11)
	v_mfma_f32_16x16x32_f16 v[88:91], v[192:195], v[180:183], v[88:91]
	v_mfma_f32_16x16x32_f16 v[92:95], v[196:199], v[180:183], v[92:95]
	v_mfma_f32_16x16x32_f16 v[96:99], v[200:203], v[180:183], v[96:99]
	s_add_u32 m0, s28, 0x4000
	s_nop 0
	global_load_lds_dwordx4 v12, s[4:5]
	v_mfma_f32_16x16x32_f16 v[100:103], v[204:207], v[180:183], v[100:103]
	s_waitcnt lgkmcnt(10)
	v_mfma_f32_16x16x32_f16 v[104:107], v[192:195], v[184:187], v[104:107]
	v_mfma_f32_16x16x32_f16 v[108:111], v[196:199], v[184:187], v[108:111]
	v_mfma_f32_16x16x32_f16 v[112:115], v[200:203], v[184:187], v[112:115]
	v_mfma_f32_16x16x32_f16 v[116:119], v[204:207], v[184:187], v[116:119]
	s_add_u32 m0, s28, 0x6000
	s_nop 0
	global_load_lds_dwordx4 v13, s[4:5]
	s_waitcnt lgkmcnt(9)
	v_mfma_f32_16x16x32_f16 v[120:123], v[192:195], v[188:191], v[120:123]
	v_mfma_f32_16x16x32_f16 v[124:127], v[196:199], v[188:191], v[124:127]
	v_mfma_f32_16x16x32_f16 v[128:131], v[200:203], v[188:191], v[128:131]
	v_mfma_f32_16x16x32_f16 v[132:135], v[204:207], v[188:191], v[132:135]
	s_waitcnt lgkmcnt(6)
	ds_read_b128 v[172:175], v16 offset:53248
	ds_read_b128 v[192:195], v18 offset:53248
	ds_read_b128 v[196:199], v18 offset:55296
	ds_read_b128 v[200:203], v18 offset:57344
	ds_read_b128 v[204:207], v18 offset:59392
	ds_read_b128 v[176:179], v16 offset:55296
	ds_read_b128 v[180:183], v16 offset:57344
	ds_read_b128 v[184:187], v16 offset:59392
	ds_read_b128 v[188:191], v16 offset:61440
	v_mfma_f32_16x16x32_f16 v[56:59], v[156:159], v[136:139], v[56:59]
	s_add_u32 m0, s28, 0x8000
	s_nop 0
	global_load_lds_dwordx4 v14, s[4:5]
	s_add_u32 s4, s4, s20
	s_addc_u32 s5, s5, 0
	s_waitcnt lgkmcnt(15)
	v_mfma_f32_16x16x32_f16 v[60:63], v[160:163], v[136:139], v[60:63]
	s_waitcnt lgkmcnt(14)
	v_mfma_f32_16x16x32_f16 v[64:67], v[164:167], v[136:139], v[64:67]
	s_waitcnt lgkmcnt(13)
	v_mfma_f32_16x16x32_f16 v[68:71], v[168:171], v[136:139], v[68:71]
	s_waitcnt lgkmcnt(12)
	v_mfma_f32_16x16x32_f16 v[72:75], v[156:159], v[140:143], v[72:75]
	v_mfma_f32_16x16x32_f16 v[76:79], v[160:163], v[140:143], v[76:79]
	v_mfma_f32_16x16x32_f16 v[80:83], v[164:167], v[140:143], v[80:83]
	s_add_u32 m0, s28, 0x9000
	s_nop 0
	global_load_lds_dwordx4 v10, s[6:7]
	v_mfma_f32_16x16x32_f16 v[84:87], v[168:171], v[140:143], v[84:87]
	s_waitcnt lgkmcnt(11)
	v_mfma_f32_16x16x32_f16 v[88:91], v[156:159], v[144:147], v[88:91]
	v_mfma_f32_16x16x32_f16 v[92:95], v[160:163], v[144:147], v[92:95]
	v_mfma_f32_16x16x32_f16 v[96:99], v[164:167], v[144:147], v[96:99]
	v_mfma_f32_16x16x32_f16 v[100:103], v[168:171], v[144:147], v[100:103]
	s_waitcnt lgkmcnt(10)
	v_mfma_f32_16x16x32_f16 v[104:107], v[156:159], v[148:151], v[104:107]
	v_mfma_f32_16x16x32_f16 v[108:111], v[160:163], v[148:151], v[108:111]
	s_add_u32 m0, s28, 0xb000
	s_nop 0
	global_load_lds_dwordx4 v11, s[6:7]
	s_add_u32 s6, s6, s20
	s_addc_u32 s7, s7, 0
	v_mfma_f32_16x16x32_f16 v[112:115], v[164:167], v[148:151], v[112:115]
	v_mfma_f32_16x16x32_f16 v[116:119], v[168:171], v[148:151], v[116:119]
	s_waitcnt lgkmcnt(9)
	v_mfma_f32_16x16x32_f16 v[120:123], v[156:159], v[152:155], v[120:123]
	v_mfma_f32_16x16x32_f16 v[124:127], v[160:163], v[152:155], v[124:127]
	v_mfma_f32_16x16x32_f16 v[128:131], v[164:167], v[152:155], v[128:131]
	v_mfma_f32_16x16x32_f16 v[132:135], v[168:171], v[152:155], v[132:135]
	s_waitcnt vmcnt(7) lgkmcnt(0)
	s_barrier
	s_waitcnt lgkmcnt(6)
	ds_read_b128 v[136:139], v19
	ds_read_b128 v[156:159], v21
	ds_read_b128 v[160:163], v21 offset:2048
	ds_read_b128 v[164:167], v21 offset:4096
	ds_read_b128 v[168:171], v21 offset:6144
	ds_read_b128 v[140:143], v19 offset:2048
	ds_read_b128 v[144:147], v19 offset:4096
	ds_read_b128 v[148:151], v19 offset:6144
	ds_read_b128 v[152:155], v19 offset:8192
	v_mfma_f32_16x16x32_f16 v[56:59], v[192:195], v[172:175], v[56:59]
	s_add_u32 m0, s28, 0xd000
	s_nop 0
	global_load_lds_dwordx4 v10, s[4:5]
	s_waitcnt lgkmcnt(15)
	v_mfma_f32_16x16x32_f16 v[60:63], v[196:199], v[172:175], v[60:63]
	s_waitcnt lgkmcnt(14)
	v_mfma_f32_16x16x32_f16 v[64:67], v[200:203], v[172:175], v[64:67]
	s_waitcnt lgkmcnt(13)
	v_mfma_f32_16x16x32_f16 v[68:71], v[204:207], v[172:175], v[68:71]
	s_waitcnt lgkmcnt(12)
	v_mfma_f32_16x16x32_f16 v[72:75], v[192:195], v[176:179], v[72:75]
	v_mfma_f32_16x16x32_f16 v[76:79], v[196:199], v[176:179], v[76:79]
	s_add_u32 m0, s28, 0xf000
	s_nop 0
	global_load_lds_dwordx4 v11, s[4:5]
	v_mfma_f32_16x16x32_f16 v[80:83], v[200:203], v[176:179], v[80:83]
	v_mfma_f32_16x16x32_f16 v[84:87], v[204:207], v[176:179], v[84:87]
	s_waitcnt lgkmcnt(11)
	v_mfma_f32_16x16x32_f16 v[88:91], v[192:195], v[180:183], v[88:91]
	v_mfma_f32_16x16x32_f16 v[92:95], v[196:199], v[180:183], v[92:95]
	v_mfma_f32_16x16x32_f16 v[96:99], v[200:203], v[180:183], v[96:99]
	s_add_u32 m0, s28, 0x11000
	s_nop 0
	global_load_lds_dwordx4 v12, s[4:5]
	v_mfma_f32_16x16x32_f16 v[100:103], v[204:207], v[180:183], v[100:103]
	s_waitcnt lgkmcnt(10)
	v_mfma_f32_16x16x32_f16 v[104:107], v[192:195], v[184:187], v[104:107]
	v_mfma_f32_16x16x32_f16 v[108:111], v[196:199], v[184:187], v[108:111]
	v_mfma_f32_16x16x32_f16 v[112:115], v[200:203], v[184:187], v[112:115]
	v_mfma_f32_16x16x32_f16 v[116:119], v[204:207], v[184:187], v[116:119]
	s_add_u32 m0, s28, 0x13000
	s_nop 0
	global_load_lds_dwordx4 v13, s[4:5]
	s_waitcnt lgkmcnt(9)
	v_mfma_f32_16x16x32_f16 v[120:123], v[192:195], v[188:191], v[120:123]
	v_mfma_f32_16x16x32_f16 v[124:127], v[196:199], v[188:191], v[124:127]
	v_mfma_f32_16x16x32_f16 v[128:131], v[200:203], v[188:191], v[128:131]
	v_mfma_f32_16x16x32_f16 v[132:135], v[204:207], v[188:191], v[132:135]
	s_waitcnt lgkmcnt(6)
	ds_read_b128 v[172:175], v20
	ds_read_b128 v[192:195], v22
	ds_read_b128 v[196:199], v22 offset:2048
	ds_read_b128 v[200:203], v22 offset:4096
	ds_read_b128 v[204:207], v22 offset:6144
	ds_read_b128 v[176:179], v20 offset:2048
	ds_read_b128 v[180:183], v20 offset:4096
	ds_read_b128 v[184:187], v20 offset:6144
	ds_read_b128 v[188:191], v20 offset:8192
	v_mfma_f32_16x16x32_f16 v[56:59], v[156:159], v[136:139], v[56:59]
	s_add_u32 m0, s28, 0x15000
	s_nop 0
	global_load_lds_dwordx4 v14, s[4:5]
	s_add_u32 s4, s4, s20
	s_addc_u32 s5, s5, 0
	s_waitcnt lgkmcnt(15)
	v_mfma_f32_16x16x32_f16 v[60:63], v[160:163], v[136:139], v[60:63]
	s_waitcnt lgkmcnt(14)
	v_mfma_f32_16x16x32_f16 v[64:67], v[164:167], v[136:139], v[64:67]
	s_waitcnt lgkmcnt(13)
	v_mfma_f32_16x16x32_f16 v[68:71], v[168:171], v[136:139], v[68:71]
	s_waitcnt lgkmcnt(12)
	v_mfma_f32_16x16x32_f16 v[72:75], v[156:159], v[140:143], v[72:75]
	v_mfma_f32_16x16x32_f16 v[76:79], v[160:163], v[140:143], v[76:79]
	v_mfma_f32_16x16x32_f16 v[80:83], v[164:167], v[140:143], v[80:83]
	s_add_u32 m0, s28, 0x16000
	s_nop 0
	global_load_lds_dwordx4 v10, s[6:7]
	v_mfma_f32_16x16x32_f16 v[84:87], v[168:171], v[140:143], v[84:87]
	s_waitcnt lgkmcnt(11)
	v_mfma_f32_16x16x32_f16 v[88:91], v[156:159], v[144:147], v[88:91]
	v_mfma_f32_16x16x32_f16 v[92:95], v[160:163], v[144:147], v[92:95]
	v_mfma_f32_16x16x32_f16 v[96:99], v[164:167], v[144:147], v[96:99]
	v_mfma_f32_16x16x32_f16 v[100:103], v[168:171], v[144:147], v[100:103]
	s_waitcnt lgkmcnt(10)
	v_mfma_f32_16x16x32_f16 v[104:107], v[156:159], v[148:151], v[104:107]
	v_mfma_f32_16x16x32_f16 v[108:111], v[160:163], v[148:151], v[108:111]
	s_add_u32 m0, s28, 0x18000
	s_nop 0
	global_load_lds_dwordx4 v11, s[6:7]
	s_add_u32 s6, s6, s20
	s_addc_u32 s7, s7, 0
	v_mfma_f32_16x16x32_f16 v[112:115], v[164:167], v[148:151], v[112:115]
	v_mfma_f32_16x16x32_f16 v[116:119], v[168:171], v[148:151], v[116:119]
	s_waitcnt lgkmcnt(9)
	v_mfma_f32_16x16x32_f16 v[120:123], v[156:159], v[152:155], v[120:123]
	v_mfma_f32_16x16x32_f16 v[124:127], v[160:163], v[152:155], v[124:127]
	v_mfma_f32_16x16x32_f16 v[128:131], v[164:167], v[152:155], v[128:131]
	v_mfma_f32_16x16x32_f16 v[132:135], v[168:171], v[152:155], v[132:135]
	s_waitcnt vmcnt(7) lgkmcnt(0)
	s_barrier
	s_waitcnt lgkmcnt(6)
	ds_read_b128 v[136:139], v15
	ds_read_b128 v[156:159], v17
	ds_read_b128 v[160:163], v17 offset:2048
	ds_read_b128 v[164:167], v17 offset:4096
	ds_read_b128 v[168:171], v17 offset:6144
	ds_read_b128 v[140:143], v15 offset:2048
	ds_read_b128 v[144:147], v15 offset:4096
	ds_read_b128 v[148:151], v15 offset:6144
	ds_read_b128 v[152:155], v15 offset:8192
	v_mfma_f32_16x16x32_f16 v[56:59], v[192:195], v[172:175], v[56:59]
	s_add_u32 m0, s28, 0x1a000
	s_nop 0
	global_load_lds_dwordx4 v10, s[4:5]
	s_waitcnt lgkmcnt(15)
	v_mfma_f32_16x16x32_f16 v[60:63], v[196:199], v[172:175], v[60:63]
	s_waitcnt lgkmcnt(14)
	v_mfma_f32_16x16x32_f16 v[64:67], v[200:203], v[172:175], v[64:67]
	s_waitcnt lgkmcnt(13)
	v_mfma_f32_16x16x32_f16 v[68:71], v[204:207], v[172:175], v[68:71]
	s_waitcnt lgkmcnt(12)
	v_mfma_f32_16x16x32_f16 v[72:75], v[192:195], v[176:179], v[72:75]
	v_mfma_f32_16x16x32_f16 v[76:79], v[196:199], v[176:179], v[76:79]
	s_add_u32 m0, s28, 0x1c000
	s_nop 0
	global_load_lds_dwordx4 v11, s[4:5]
	v_mfma_f32_16x16x32_f16 v[80:83], v[200:203], v[176:179], v[80:83]
	v_mfma_f32_16x16x32_f16 v[84:87], v[204:207], v[176:179], v[84:87]
	s_waitcnt lgkmcnt(11)
	v_mfma_f32_16x16x32_f16 v[88:91], v[192:195], v[180:183], v[88:91]
	v_mfma_f32_16x16x32_f16 v[92:95], v[196:199], v[180:183], v[92:95]
	v_mfma_f32_16x16x32_f16 v[96:99], v[200:203], v[180:183], v[96:99]
	s_add_u32 m0, s28, 0x1e000
	s_nop 0
	global_load_lds_dwordx4 v12, s[4:5]
	v_mfma_f32_16x16x32_f16 v[100:103], v[204:207], v[180:183], v[100:103]
	s_waitcnt lgkmcnt(10)
	v_mfma_f32_16x16x32_f16 v[104:107], v[192:195], v[184:187], v[104:107]
	v_mfma_f32_16x16x32_f16 v[108:111], v[196:199], v[184:187], v[108:111]
	v_mfma_f32_16x16x32_f16 v[112:115], v[200:203], v[184:187], v[112:115]
	v_mfma_f32_16x16x32_f16 v[116:119], v[204:207], v[184:187], v[116:119]
	s_add_u32 m0, s28, 0x20000
	s_nop 0
	global_load_lds_dwordx4 v13, s[4:5]
	s_waitcnt lgkmcnt(9)
	v_mfma_f32_16x16x32_f16 v[120:123], v[192:195], v[188:191], v[120:123]
	v_mfma_f32_16x16x32_f16 v[124:127], v[196:199], v[188:191], v[124:127]
	v_mfma_f32_16x16x32_f16 v[128:131], v[200:203], v[188:191], v[128:131]
	v_mfma_f32_16x16x32_f16 v[132:135], v[204:207], v[188:191], v[132:135]
	s_waitcnt lgkmcnt(6)
	ds_read_b128 v[172:175], v16
	ds_read_b128 v[192:195], v18
	ds_read_b128 v[196:199], v18 offset:2048
	ds_read_b128 v[200:203], v18 offset:4096
	ds_read_b128 v[204:207], v18 offset:6144
	ds_read_b128 v[176:179], v16 offset:2048
	ds_read_b128 v[180:183], v16 offset:4096
	ds_read_b128 v[184:187], v16 offset:6144
	ds_read_b128 v[188:191], v16 offset:8192
	v_mfma_f32_16x16x32_f16 v[56:59], v[156:159], v[136:139], v[56:59]
	s_add_u32 m0, s28, 0x22000
	s_nop 0
	global_load_lds_dwordx4 v14, s[4:5]
	s_add_u32 s4, s4, s20
	s_addc_u32 s5, s5, 0
	s_waitcnt lgkmcnt(15)
	v_mfma_f32_16x16x32_f16 v[60:63], v[160:163], v[136:139], v[60:63]
	s_waitcnt lgkmcnt(14)
	v_mfma_f32_16x16x32_f16 v[64:67], v[164:167], v[136:139], v[64:67]
	s_waitcnt lgkmcnt(13)
	v_mfma_f32_16x16x32_f16 v[68:71], v[168:171], v[136:139], v[68:71]
	s_waitcnt lgkmcnt(12)
	v_mfma_f32_16x16x32_f16 v[72:75], v[156:159], v[140:143], v[72:75]
	v_mfma_f32_16x16x32_f16 v[76:79], v[160:163], v[140:143], v[76:79]
	v_mfma_f32_16x16x32_f16 v[80:83], v[164:167], v[140:143], v[80:83]
	s_add_u32 m0, s28, 0x23000
	s_nop 0
	global_load_lds_dwordx4 v10, s[6:7]
	v_mfma_f32_16x16x32_f16 v[84:87], v[168:171], v[140:143], v[84:87]
	s_waitcnt lgkmcnt(11)
	v_mfma_f32_16x16x32_f16 v[88:91], v[156:159], v[144:147], v[88:91]
	v_mfma_f32_16x16x32_f16 v[92:95], v[160:163], v[144:147], v[92:95]
	v_mfma_f32_16x16x32_f16 v[96:99], v[164:167], v[144:147], v[96:99]
	v_mfma_f32_16x16x32_f16 v[100:103], v[168:171], v[144:147], v[100:103]
	s_waitcnt lgkmcnt(10)
	v_mfma_f32_16x16x32_f16 v[104:107], v[156:159], v[148:151], v[104:107]
	v_mfma_f32_16x16x32_f16 v[108:111], v[160:163], v[148:151], v[108:111]
	s_add_u32 m0, s28, 0x25000
	s_nop 0
	global_load_lds_dwordx4 v11, s[6:7]
	s_add_u32 s6, s6, s20
	s_addc_u32 s7, s7, 0
	v_mfma_f32_16x16x32_f16 v[112:115], v[164:167], v[148:151], v[112:115]
	v_mfma_f32_16x16x32_f16 v[116:119], v[168:171], v[148:151], v[116:119]
	s_waitcnt lgkmcnt(9)
	v_mfma_f32_16x16x32_f16 v[120:123], v[156:159], v[152:155], v[120:123]
	v_mfma_f32_16x16x32_f16 v[124:127], v[160:163], v[152:155], v[124:127]
	v_mfma_f32_16x16x32_f16 v[128:131], v[164:167], v[152:155], v[128:131]
	v_mfma_f32_16x16x32_f16 v[132:135], v[168:171], v[152:155], v[132:135]
	s_waitcnt vmcnt(7) lgkmcnt(0)
	s_barrier
	s_waitcnt lgkmcnt(6)
	ds_read_b128 v[136:139], v15 offset:53248
	ds_read_b128 v[156:159], v17 offset:53248
	ds_read_b128 v[160:163], v17 offset:55296
	ds_read_b128 v[164:167], v17 offset:57344
	ds_read_b128 v[168:171], v17 offset:59392
	ds_read_b128 v[140:143], v15 offset:55296
	ds_read_b128 v[144:147], v15 offset:57344
	ds_read_b128 v[148:151], v15 offset:59392
	ds_read_b128 v[152:155], v15 offset:61440
	v_mfma_f32_16x16x32_f16 v[56:59], v[192:195], v[172:175], v[56:59]
	s_add_u32 m0, s28, 0x0
	s_nop 0
	global_load_lds_dwordx4 v10, s[4:5]
	s_waitcnt lgkmcnt(15)
	v_mfma_f32_16x16x32_f16 v[60:63], v[196:199], v[172:175], v[60:63]
	s_waitcnt lgkmcnt(14)
	v_mfma_f32_16x16x32_f16 v[64:67], v[200:203], v[172:175], v[64:67]
	s_waitcnt lgkmcnt(13)
	v_mfma_f32_16x16x32_f16 v[68:71], v[204:207], v[172:175], v[68:71]
	s_waitcnt lgkmcnt(12)
	v_mfma_f32_16x16x32_f16 v[72:75], v[192:195], v[176:179], v[72:75]
	v_mfma_f32_16x16x32_f16 v[76:79], v[196:199], v[176:179], v[76:79]
	s_add_u32 m0, s28, 0x2000
	s_nop 0
	global_load_lds_dwordx4 v11, s[4:5]
	v_mfma_f32_16x16x32_f16 v[80:83], v[200:203], v[176:179], v[80:83]
	v_mfma_f32_16x16x32_f16 v[84:87], v[204:207], v[176:179], v[84:87]
	s_waitcnt lgkmcnt(11)
	v_mfma_f32_16x16x32_f16 v[88:91], v[192:195], v[180:183], v[88:91]
	v_mfma_f32_16x16x32_f16 v[92:95], v[196:199], v[180:183], v[92:95]
	v_mfma_f32_16x16x32_f16 v[96:99], v[200:203], v[180:183], v[96:99]
	s_add_u32 m0, s28, 0x4000
	s_nop 0
	global_load_lds_dwordx4 v12, s[4:5]
	v_mfma_f32_16x16x32_f16 v[100:103], v[204:207], v[180:183], v[100:103]
	s_waitcnt lgkmcnt(10)
	v_mfma_f32_16x16x32_f16 v[104:107], v[192:195], v[184:187], v[104:107]
	v_mfma_f32_16x16x32_f16 v[108:111], v[196:199], v[184:187], v[108:111]
	v_mfma_f32_16x16x32_f16 v[112:115], v[200:203], v[184:187], v[112:115]
	v_mfma_f32_16x16x32_f16 v[116:119], v[204:207], v[184:187], v[116:119]
	s_add_u32 m0, s28, 0x6000
	s_nop 0
	global_load_lds_dwordx4 v13, s[4:5]
	s_waitcnt lgkmcnt(9)
	v_mfma_f32_16x16x32_f16 v[120:123], v[192:195], v[188:191], v[120:123]
	v_mfma_f32_16x16x32_f16 v[124:127], v[196:199], v[188:191], v[124:127]
	v_mfma_f32_16x16x32_f16 v[128:131], v[200:203], v[188:191], v[128:131]
	v_mfma_f32_16x16x32_f16 v[132:135], v[204:207], v[188:191], v[132:135]
	s_waitcnt lgkmcnt(6)
	ds_read_b128 v[172:175], v16 offset:53248
	ds_read_b128 v[192:195], v18 offset:53248
	ds_read_b128 v[196:199], v18 offset:55296
	ds_read_b128 v[200:203], v18 offset:57344
	ds_read_b128 v[204:207], v18 offset:59392
	ds_read_b128 v[176:179], v16 offset:55296
	ds_read_b128 v[180:183], v16 offset:57344
	ds_read_b128 v[184:187], v16 offset:59392
	ds_read_b128 v[188:191], v16 offset:61440
	v_mfma_f32_16x16x32_f16 v[56:59], v[156:159], v[136:139], v[56:59]
	s_add_u32 m0, s28, 0x8000
	s_nop 0
	global_load_lds_dwordx4 v14, s[4:5]
	s_add_u32 s4, s4, s20
	s_addc_u32 s5, s5, 0
	s_waitcnt lgkmcnt(15)
	v_mfma_f32_16x16x32_f16 v[60:63], v[160:163], v[136:139], v[60:63]
	s_waitcnt lgkmcnt(14)
	v_mfma_f32_16x16x32_f16 v[64:67], v[164:167], v[136:139], v[64:67]
	s_waitcnt lgkmcnt(13)
	v_mfma_f32_16x16x32_f16 v[68:71], v[168:171], v[136:139], v[68:71]
	s_waitcnt lgkmcnt(12)
	v_mfma_f32_16x16x32_f16 v[72:75], v[156:159], v[140:143], v[72:75]
	v_mfma_f32_16x16x32_f16 v[76:79], v[160:163], v[140:143], v[76:79]
	v_mfma_f32_16x16x32_f16 v[80:83], v[164:167], v[140:143], v[80:83]
	s_add_u32 m0, s28, 0x9000
	s_nop 0
	global_load_lds_dwordx4 v10, s[6:7]
	v_mfma_f32_16x16x32_f16 v[84:87], v[168:171], v[140:143], v[84:87]
	s_waitcnt lgkmcnt(11)
	v_mfma_f32_16x16x32_f16 v[88:91], v[156:159], v[144:147], v[88:91]
	v_mfma_f32_16x16x32_f16 v[92:95], v[160:163], v[144:147], v[92:95]
	v_mfma_f32_16x16x32_f16 v[96:99], v[164:167], v[144:147], v[96:99]
	v_mfma_f32_16x16x32_f16 v[100:103], v[168:171], v[144:147], v[100:103]
	s_waitcnt lgkmcnt(10)
	v_mfma_f32_16x16x32_f16 v[104:107], v[156:159], v[148:151], v[104:107]
	v_mfma_f32_16x16x32_f16 v[108:111], v[160:163], v[148:151], v[108:111]
	s_add_u32 m0, s28, 0xb000
	s_nop 0
	global_load_lds_dwordx4 v11, s[6:7]
	s_add_u32 s6, s6, s20
	s_addc_u32 s7, s7, 0
	v_mfma_f32_16x16x32_f16 v[112:115], v[164:167], v[148:151], v[112:115]
	v_mfma_f32_16x16x32_f16 v[116:119], v[168:171], v[148:151], v[116:119]
	s_waitcnt lgkmcnt(9)
	v_mfma_f32_16x16x32_f16 v[120:123], v[156:159], v[152:155], v[120:123]
	v_mfma_f32_16x16x32_f16 v[124:127], v[160:163], v[152:155], v[124:127]
	v_mfma_f32_16x16x32_f16 v[128:131], v[164:167], v[152:155], v[128:131]
	v_mfma_f32_16x16x32_f16 v[132:135], v[168:171], v[152:155], v[132:135]
	s_waitcnt vmcnt(7) lgkmcnt(0)
	s_barrier
	s_waitcnt lgkmcnt(6)
	ds_read_b128 v[136:139], v19
	ds_read_b128 v[156:159], v21
	ds_read_b128 v[160:163], v21 offset:2048
	ds_read_b128 v[164:167], v21 offset:4096
	ds_read_b128 v[168:171], v21 offset:6144
	ds_read_b128 v[140:143], v19 offset:2048
	ds_read_b128 v[144:147], v19 offset:4096
	ds_read_b128 v[148:151], v19 offset:6144
	ds_read_b128 v[152:155], v19 offset:8192
	v_mfma_f32_16x16x32_f16 v[56:59], v[192:195], v[172:175], v[56:59]
	s_add_u32 m0, s28, 0xd000
	s_nop 0
	global_load_lds_dwordx4 v10, s[4:5]
	s_waitcnt lgkmcnt(15)
	v_mfma_f32_16x16x32_f16 v[60:63], v[196:199], v[172:175], v[60:63]
	s_waitcnt lgkmcnt(14)
	v_mfma_f32_16x16x32_f16 v[64:67], v[200:203], v[172:175], v[64:67]
	s_waitcnt lgkmcnt(13)
	v_mfma_f32_16x16x32_f16 v[68:71], v[204:207], v[172:175], v[68:71]
	s_waitcnt lgkmcnt(12)
	v_mfma_f32_16x16x32_f16 v[72:75], v[192:195], v[176:179], v[72:75]
	v_mfma_f32_16x16x32_f16 v[76:79], v[196:199], v[176:179], v[76:79]
	s_add_u32 m0, s28, 0xf000
	s_nop 0
	global_load_lds_dwordx4 v11, s[4:5]
	v_mfma_f32_16x16x32_f16 v[80:83], v[200:203], v[176:179], v[80:83]
	v_mfma_f32_16x16x32_f16 v[84:87], v[204:207], v[176:179], v[84:87]
	s_waitcnt lgkmcnt(11)
	v_mfma_f32_16x16x32_f16 v[88:91], v[192:195], v[180:183], v[88:91]
	v_mfma_f32_16x16x32_f16 v[92:95], v[196:199], v[180:183], v[92:95]
	v_mfma_f32_16x16x32_f16 v[96:99], v[200:203], v[180:183], v[96:99]
	s_add_u32 m0, s28, 0x11000
	s_nop 0
	global_load_lds_dwordx4 v12, s[4:5]
	v_mfma_f32_16x16x32_f16 v[100:103], v[204:207], v[180:183], v[100:103]
	s_waitcnt lgkmcnt(10)
	v_mfma_f32_16x16x32_f16 v[104:107], v[192:195], v[184:187], v[104:107]
	v_mfma_f32_16x16x32_f16 v[108:111], v[196:199], v[184:187], v[108:111]
	v_mfma_f32_16x16x32_f16 v[112:115], v[200:203], v[184:187], v[112:115]
	v_mfma_f32_16x16x32_f16 v[116:119], v[204:207], v[184:187], v[116:119]
	s_add_u32 m0, s28, 0x13000
	s_nop 0
	global_load_lds_dwordx4 v13, s[4:5]
	s_waitcnt lgkmcnt(9)
	v_mfma_f32_16x16x32_f16 v[120:123], v[192:195], v[188:191], v[120:123]
	v_mfma_f32_16x16x32_f16 v[124:127], v[196:199], v[188:191], v[124:127]
	v_mfma_f32_16x16x32_f16 v[128:131], v[200:203], v[188:191], v[128:131]
	v_mfma_f32_16x16x32_f16 v[132:135], v[204:207], v[188:191], v[132:135]
	s_waitcnt lgkmcnt(6)
	ds_read_b128 v[172:175], v20
	ds_read_b128 v[192:195], v22
	ds_read_b128 v[196:199], v22 offset:2048
	ds_read_b128 v[200:203], v22 offset:4096
	ds_read_b128 v[204:207], v22 offset:6144
	ds_read_b128 v[176:179], v20 offset:2048
	ds_read_b128 v[180:183], v20 offset:4096
	ds_read_b128 v[184:187], v20 offset:6144
	ds_read_b128 v[188:191], v20 offset:8192
	v_mfma_f32_16x16x32_f16 v[56:59], v[156:159], v[136:139], v[56:59]
	s_add_u32 m0, s28, 0x15000
	s_nop 0
	global_load_lds_dwordx4 v14, s[4:5]
	s_add_u32 s4, s4, s20
	s_addc_u32 s5, s5, 0
	s_waitcnt lgkmcnt(15)
	v_mfma_f32_16x16x32_f16 v[60:63], v[160:163], v[136:139], v[60:63]
	s_waitcnt lgkmcnt(14)
	v_mfma_f32_16x16x32_f16 v[64:67], v[164:167], v[136:139], v[64:67]
	s_waitcnt lgkmcnt(13)
	v_mfma_f32_16x16x32_f16 v[68:71], v[168:171], v[136:139], v[68:71]
	s_waitcnt lgkmcnt(12)
	v_mfma_f32_16x16x32_f16 v[72:75], v[156:159], v[140:143], v[72:75]
	v_mfma_f32_16x16x32_f16 v[76:79], v[160:163], v[140:143], v[76:79]
	v_mfma_f32_16x16x32_f16 v[80:83], v[164:167], v[140:143], v[80:83]
	s_add_u32 m0, s28, 0x16000
	s_nop 0
	global_load_lds_dwordx4 v10, s[6:7]
	v_mfma_f32_16x16x32_f16 v[84:87], v[168:171], v[140:143], v[84:87]
	s_waitcnt lgkmcnt(11)
	v_mfma_f32_16x16x32_f16 v[88:91], v[156:159], v[144:147], v[88:91]
	v_mfma_f32_16x16x32_f16 v[92:95], v[160:163], v[144:147], v[92:95]
	v_mfma_f32_16x16x32_f16 v[96:99], v[164:167], v[144:147], v[96:99]
	v_mfma_f32_16x16x32_f16 v[100:103], v[168:171], v[144:147], v[100:103]
	s_waitcnt lgkmcnt(10)
	v_mfma_f32_16x16x32_f16 v[104:107], v[156:159], v[148:151], v[104:107]
	v_mfma_f32_16x16x32_f16 v[108:111], v[160:163], v[148:151], v[108:111]
	s_add_u32 m0, s28, 0x18000
	s_nop 0
	global_load_lds_dwordx4 v11, s[6:7]
	s_add_u32 s6, s6, s20
	s_addc_u32 s7, s7, 0
	v_mfma_f32_16x16x32_f16 v[112:115], v[164:167], v[148:151], v[112:115]
	v_mfma_f32_16x16x32_f16 v[116:119], v[168:171], v[148:151], v[116:119]
	s_waitcnt lgkmcnt(9)
	v_mfma_f32_16x16x32_f16 v[120:123], v[156:159], v[152:155], v[120:123]
	v_mfma_f32_16x16x32_f16 v[124:127], v[160:163], v[152:155], v[124:127]
	v_mfma_f32_16x16x32_f16 v[128:131], v[164:167], v[152:155], v[128:131]
	v_mfma_f32_16x16x32_f16 v[132:135], v[168:171], v[152:155], v[132:135]
	s_waitcnt vmcnt(7) lgkmcnt(0)
	s_barrier
	s_waitcnt lgkmcnt(6)
	ds_read_b128 v[136:139], v15
	ds_read_b128 v[156:159], v17
	ds_read_b128 v[160:163], v17 offset:2048
	ds_read_b128 v[164:167], v17 offset:4096
	ds_read_b128 v[168:171], v17 offset:6144
	ds_read_b128 v[140:143], v15 offset:2048
	ds_read_b128 v[144:147], v15 offset:4096
	ds_read_b128 v[148:151], v15 offset:6144
	ds_read_b128 v[152:155], v15 offset:8192
	v_mfma_f32_16x16x32_f16 v[56:59], v[192:195], v[172:175], v[56:59]
	s_add_u32 m0, s28, 0x1a000
	s_nop 0
	global_load_lds_dwordx4 v10, s[4:5]
	s_waitcnt lgkmcnt(15)
	v_mfma_f32_16x16x32_f16 v[60:63], v[196:199], v[172:175], v[60:63]
	s_waitcnt lgkmcnt(14)
	v_mfma_f32_16x16x32_f16 v[64:67], v[200:203], v[172:175], v[64:67]
	s_waitcnt lgkmcnt(13)
	v_mfma_f32_16x16x32_f16 v[68:71], v[204:207], v[172:175], v[68:71]
	s_waitcnt lgkmcnt(12)
	v_mfma_f32_16x16x32_f16 v[72:75], v[192:195], v[176:179], v[72:75]
	v_mfma_f32_16x16x32_f16 v[76:79], v[196:199], v[176:179], v[76:79]
	s_add_u32 m0, s28, 0x1c000
	s_nop 0
	global_load_lds_dwordx4 v11, s[4:5]
	v_mfma_f32_16x16x32_f16 v[80:83], v[200:203], v[176:179], v[80:83]
	v_mfma_f32_16x16x32_f16 v[84:87], v[204:207], v[176:179], v[84:87]
	s_waitcnt lgkmcnt(11)
	v_mfma_f32_16x16x32_f16 v[88:91], v[192:195], v[180:183], v[88:91]
	v_mfma_f32_16x16x32_f16 v[92:95], v[196:199], v[180:183], v[92:95]
	v_mfma_f32_16x16x32_f16 v[96:99], v[200:203], v[180:183], v[96:99]
	s_add_u32 m0, s28, 0x1e000
	s_nop 0
	global_load_lds_dwordx4 v12, s[4:5]
	v_mfma_f32_16x16x32_f16 v[100:103], v[204:207], v[180:183], v[100:103]
	s_waitcnt lgkmcnt(10)
	v_mfma_f32_16x16x32_f16 v[104:107], v[192:195], v[184:187], v[104:107]
	v_mfma_f32_16x16x32_f16 v[108:111], v[196:199], v[184:187], v[108:111]
	v_mfma_f32_16x16x32_f16 v[112:115], v[200:203], v[184:187], v[112:115]
	v_mfma_f32_16x16x32_f16 v[116:119], v[204:207], v[184:187], v[116:119]
	s_add_u32 m0, s28, 0x20000
	s_nop 0
	global_load_lds_dwordx4 v13, s[4:5]
	s_waitcnt lgkmcnt(9)
	v_mfma_f32_16x16x32_f16 v[120:123], v[192:195], v[188:191], v[120:123]
	v_mfma_f32_16x16x32_f16 v[124:127], v[196:199], v[188:191], v[124:127]
	v_mfma_f32_16x16x32_f16 v[128:131], v[200:203], v[188:191], v[128:131]
	v_mfma_f32_16x16x32_f16 v[132:135], v[204:207], v[188:191], v[132:135]
	s_waitcnt lgkmcnt(6)
	ds_read_b128 v[172:175], v16
	ds_read_b128 v[192:195], v18
	ds_read_b128 v[196:199], v18 offset:2048
	ds_read_b128 v[200:203], v18 offset:4096
	ds_read_b128 v[204:207], v18 offset:6144
	ds_read_b128 v[176:179], v16 offset:2048
	ds_read_b128 v[180:183], v16 offset:4096
	ds_read_b128 v[184:187], v16 offset:6144
	ds_read_b128 v[188:191], v16 offset:8192
	v_mfma_f32_16x16x32_f16 v[56:59], v[156:159], v[136:139], v[56:59]
	s_add_u32 m0, s28, 0x22000
	s_nop 0
	global_load_lds_dwordx4 v14, s[4:5]
	s_add_u32 s4, s4, s20
	s_addc_u32 s5, s5, 0
	s_waitcnt lgkmcnt(15)
	v_mfma_f32_16x16x32_f16 v[60:63], v[160:163], v[136:139], v[60:63]
	s_waitcnt lgkmcnt(14)
	v_mfma_f32_16x16x32_f16 v[64:67], v[164:167], v[136:139], v[64:67]
	s_waitcnt lgkmcnt(13)
	v_mfma_f32_16x16x32_f16 v[68:71], v[168:171], v[136:139], v[68:71]
	s_waitcnt lgkmcnt(12)
	v_mfma_f32_16x16x32_f16 v[72:75], v[156:159], v[140:143], v[72:75]
	v_mfma_f32_16x16x32_f16 v[76:79], v[160:163], v[140:143], v[76:79]
	v_mfma_f32_16x16x32_f16 v[80:83], v[164:167], v[140:143], v[80:83]
	s_add_u32 m0, s28, 0x23000
	s_nop 0
	global_load_lds_dwordx4 v10, s[6:7]
	v_mfma_f32_16x16x32_f16 v[84:87], v[168:171], v[140:143], v[84:87]
	s_waitcnt lgkmcnt(11)
	v_mfma_f32_16x16x32_f16 v[88:91], v[156:159], v[144:147], v[88:91]
	v_mfma_f32_16x16x32_f16 v[92:95], v[160:163], v[144:147], v[92:95]
	v_mfma_f32_16x16x32_f16 v[96:99], v[164:167], v[144:147], v[96:99]
	v_mfma_f32_16x16x32_f16 v[100:103], v[168:171], v[144:147], v[100:103]
	s_waitcnt lgkmcnt(10)
	v_mfma_f32_16x16x32_f16 v[104:107], v[156:159], v[148:151], v[104:107]
	v_mfma_f32_16x16x32_f16 v[108:111], v[160:163], v[148:151], v[108:111]
	s_add_u32 m0, s28, 0x25000
	s_nop 0
	global_load_lds_dwordx4 v11, s[6:7]
	s_add_u32 s6, s6, s20
	s_addc_u32 s7, s7, 0
	v_mfma_f32_16x16x32_f16 v[112:115], v[164:167], v[148:151], v[112:115]
	v_mfma_f32_16x16x32_f16 v[116:119], v[168:171], v[148:151], v[116:119]
	s_waitcnt lgkmcnt(9)
	v_mfma_f32_16x16x32_f16 v[120:123], v[156:159], v[152:155], v[120:123]
	v_mfma_f32_16x16x32_f16 v[124:127], v[160:163], v[152:155], v[124:127]
	v_mfma_f32_16x16x32_f16 v[128:131], v[164:167], v[152:155], v[128:131]
	v_mfma_f32_16x16x32_f16 v[132:135], v[168:171], v[152:155], v[132:135]
	s_waitcnt vmcnt(7) lgkmcnt(0)
	s_barrier
	s_waitcnt lgkmcnt(6)
	ds_read_b128 v[136:139], v15 offset:53248
	ds_read_b128 v[156:159], v17 offset:53248
	ds_read_b128 v[160:163], v17 offset:55296
	ds_read_b128 v[164:167], v17 offset:57344
	ds_read_b128 v[168:171], v17 offset:59392
	ds_read_b128 v[140:143], v15 offset:55296
	ds_read_b128 v[144:147], v15 offset:57344
	ds_read_b128 v[148:151], v15 offset:59392
	ds_read_b128 v[152:155], v15 offset:61440
	v_mfma_f32_16x16x32_f16 v[56:59], v[192:195], v[172:175], v[56:59]
	s_add_u32 m0, s28, 0x0
	s_nop 0
	global_load_lds_dwordx4 v10, s[4:5]
	s_waitcnt lgkmcnt(15)
	v_mfma_f32_16x16x32_f16 v[60:63], v[196:199], v[172:175], v[60:63]
	s_waitcnt lgkmcnt(14)
	v_mfma_f32_16x16x32_f16 v[64:67], v[200:203], v[172:175], v[64:67]
	s_waitcnt lgkmcnt(13)
	v_mfma_f32_16x16x32_f16 v[68:71], v[204:207], v[172:175], v[68:71]
	s_waitcnt lgkmcnt(12)
	v_mfma_f32_16x16x32_f16 v[72:75], v[192:195], v[176:179], v[72:75]
	v_mfma_f32_16x16x32_f16 v[76:79], v[196:199], v[176:179], v[76:79]
	s_add_u32 m0, s28, 0x2000
	s_nop 0
	global_load_lds_dwordx4 v11, s[4:5]
	v_mfma_f32_16x16x32_f16 v[80:83], v[200:203], v[176:179], v[80:83]
	v_mfma_f32_16x16x32_f16 v[84:87], v[204:207], v[176:179], v[84:87]
	s_waitcnt lgkmcnt(11)
	v_mfma_f32_16x16x32_f16 v[88:91], v[192:195], v[180:183], v[88:91]
	v_mfma_f32_16x16x32_f16 v[92:95], v[196:199], v[180:183], v[92:95]
	v_mfma_f32_16x16x32_f16 v[96:99], v[200:203], v[180:183], v[96:99]
	s_add_u32 m0, s28, 0x4000
	s_nop 0
	global_load_lds_dwordx4 v12, s[4:5]
	v_mfma_f32_16x16x32_f16 v[100:103], v[204:207], v[180:183], v[100:103]
	s_waitcnt lgkmcnt(10)
	v_mfma_f32_16x16x32_f16 v[104:107], v[192:195], v[184:187], v[104:107]
	v_mfma_f32_16x16x32_f16 v[108:111], v[196:199], v[184:187], v[108:111]
	v_mfma_f32_16x16x32_f16 v[112:115], v[200:203], v[184:187], v[112:115]
	v_mfma_f32_16x16x32_f16 v[116:119], v[204:207], v[184:187], v[116:119]
	s_add_u32 m0, s28, 0x6000
	s_nop 0
	global_load_lds_dwordx4 v13, s[4:5]
	s_waitcnt lgkmcnt(9)
	v_mfma_f32_16x16x32_f16 v[120:123], v[192:195], v[188:191], v[120:123]
	v_mfma_f32_16x16x32_f16 v[124:127], v[196:199], v[188:191], v[124:127]
	v_mfma_f32_16x16x32_f16 v[128:131], v[200:203], v[188:191], v[128:131]
	v_mfma_f32_16x16x32_f16 v[132:135], v[204:207], v[188:191], v[132:135]
	s_waitcnt lgkmcnt(6)
	ds_read_b128 v[172:175], v16 offset:53248
	ds_read_b128 v[192:195], v18 offset:53248
	ds_read_b128 v[196:199], v18 offset:55296
	ds_read_b128 v[200:203], v18 offset:57344
	ds_read_b128 v[204:207], v18 offset:59392
	ds_read_b128 v[176:179], v16 offset:55296
	ds_read_b128 v[180:183], v16 offset:57344
	ds_read_b128 v[184:187], v16 offset:59392
	ds_read_b128 v[188:191], v16 offset:61440
	v_mfma_f32_16x16x32_f16 v[56:59], v[156:159], v[136:139], v[56:59]
	s_add_u32 m0, s28, 0x8000
	s_nop 0
	global_load_lds_dwordx4 v14, s[4:5]
	s_add_u32 s4, s4, s20
	s_addc_u32 s5, s5, 0
	s_waitcnt lgkmcnt(15)
	v_mfma_f32_16x16x32_f16 v[60:63], v[160:163], v[136:139], v[60:63]
	s_waitcnt lgkmcnt(14)
	v_mfma_f32_16x16x32_f16 v[64:67], v[164:167], v[136:139], v[64:67]
	s_waitcnt lgkmcnt(13)
	v_mfma_f32_16x16x32_f16 v[68:71], v[168:171], v[136:139], v[68:71]
	s_waitcnt lgkmcnt(12)
	v_mfma_f32_16x16x32_f16 v[72:75], v[156:159], v[140:143], v[72:75]
	v_mfma_f32_16x16x32_f16 v[76:79], v[160:163], v[140:143], v[76:79]
	v_mfma_f32_16x16x32_f16 v[80:83], v[164:167], v[140:143], v[80:83]
	s_add_u32 m0, s28, 0x9000
	s_nop 0
	global_load_lds_dwordx4 v10, s[6:7]
	v_mfma_f32_16x16x32_f16 v[84:87], v[168:171], v[140:143], v[84:87]
	s_waitcnt lgkmcnt(11)
	v_mfma_f32_16x16x32_f16 v[88:91], v[156:159], v[144:147], v[88:91]
	v_mfma_f32_16x16x32_f16 v[92:95], v[160:163], v[144:147], v[92:95]
	v_mfma_f32_16x16x32_f16 v[96:99], v[164:167], v[144:147], v[96:99]
	v_mfma_f32_16x16x32_f16 v[100:103], v[168:171], v[144:147], v[100:103]
	s_waitcnt lgkmcnt(10)
	v_mfma_f32_16x16x32_f16 v[104:107], v[156:159], v[148:151], v[104:107]
	v_mfma_f32_16x16x32_f16 v[108:111], v[160:163], v[148:151], v[108:111]
	s_add_u32 m0, s28, 0xb000
	s_nop 0
	global_load_lds_dwordx4 v11, s[6:7]
	s_add_u32 s6, s6, s20
	s_addc_u32 s7, s7, 0
	v_mfma_f32_16x16x32_f16 v[112:115], v[164:167], v[148:151], v[112:115]
	v_mfma_f32_16x16x32_f16 v[116:119], v[168:171], v[148:151], v[116:119]
	s_waitcnt lgkmcnt(9)
	v_mfma_f32_16x16x32_f16 v[120:123], v[156:159], v[152:155], v[120:123]
	v_mfma_f32_16x16x32_f16 v[124:127], v[160:163], v[152:155], v[124:127]
	v_mfma_f32_16x16x32_f16 v[128:131], v[164:167], v[152:155], v[128:131]
	v_mfma_f32_16x16x32_f16 v[132:135], v[168:171], v[152:155], v[132:135]
	s_waitcnt vmcnt(7) lgkmcnt(0)
	s_barrier
	s_waitcnt lgkmcnt(6)
	ds_read_b128 v[136:139], v19
	ds_read_b128 v[156:159], v21
	ds_read_b128 v[160:163], v21 offset:2048
	ds_read_b128 v[164:167], v21 offset:4096
	ds_read_b128 v[168:171], v21 offset:6144
	ds_read_b128 v[140:143], v19 offset:2048
	ds_read_b128 v[144:147], v19 offset:4096
	ds_read_b128 v[148:151], v19 offset:6144
	ds_read_b128 v[152:155], v19 offset:8192
	v_mfma_f32_16x16x32_f16 v[56:59], v[192:195], v[172:175], v[56:59]
	s_add_u32 m0, s28, 0xd000
	s_nop 0
	global_load_lds_dwordx4 v10, s[4:5]
	s_waitcnt lgkmcnt(15)
	v_mfma_f32_16x16x32_f16 v[60:63], v[196:199], v[172:175], v[60:63]
	s_waitcnt lgkmcnt(14)
	v_mfma_f32_16x16x32_f16 v[64:67], v[200:203], v[172:175], v[64:67]
	s_waitcnt lgkmcnt(13)
	v_mfma_f32_16x16x32_f16 v[68:71], v[204:207], v[172:175], v[68:71]
	s_waitcnt lgkmcnt(12)
	v_mfma_f32_16x16x32_f16 v[72:75], v[192:195], v[176:179], v[72:75]
	v_mfma_f32_16x16x32_f16 v[76:79], v[196:199], v[176:179], v[76:79]
	s_add_u32 m0, s28, 0xf000
	s_nop 0
	global_load_lds_dwordx4 v11, s[4:5]
	v_mfma_f32_16x16x32_f16 v[80:83], v[200:203], v[176:179], v[80:83]
	v_mfma_f32_16x16x32_f16 v[84:87], v[204:207], v[176:179], v[84:87]
	s_waitcnt lgkmcnt(11)
	v_mfma_f32_16x16x32_f16 v[88:91], v[192:195], v[180:183], v[88:91]
	v_mfma_f32_16x16x32_f16 v[92:95], v[196:199], v[180:183], v[92:95]
	v_mfma_f32_16x16x32_f16 v[96:99], v[200:203], v[180:183], v[96:99]
	s_add_u32 m0, s28, 0x11000
	s_nop 0
	global_load_lds_dwordx4 v12, s[4:5]
	v_mfma_f32_16x16x32_f16 v[100:103], v[204:207], v[180:183], v[100:103]
	s_waitcnt lgkmcnt(10)
	v_mfma_f32_16x16x32_f16 v[104:107], v[192:195], v[184:187], v[104:107]
	v_mfma_f32_16x16x32_f16 v[108:111], v[196:199], v[184:187], v[108:111]
	v_mfma_f32_16x16x32_f16 v[112:115], v[200:203], v[184:187], v[112:115]
	v_mfma_f32_16x16x32_f16 v[116:119], v[204:207], v[184:187], v[116:119]
	s_add_u32 m0, s28, 0x13000
	s_nop 0
	global_load_lds_dwordx4 v13, s[4:5]
	s_waitcnt lgkmcnt(9)
	v_mfma_f32_16x16x32_f16 v[120:123], v[192:195], v[188:191], v[120:123]
	v_mfma_f32_16x16x32_f16 v[124:127], v[196:199], v[188:191], v[124:127]
	v_mfma_f32_16x16x32_f16 v[128:131], v[200:203], v[188:191], v[128:131]
	v_mfma_f32_16x16x32_f16 v[132:135], v[204:207], v[188:191], v[132:135]
	s_waitcnt lgkmcnt(6)
	ds_read_b128 v[172:175], v20
	ds_read_b128 v[192:195], v22
	ds_read_b128 v[196:199], v22 offset:2048
	ds_read_b128 v[200:203], v22 offset:4096
	ds_read_b128 v[204:207], v22 offset:6144
	ds_read_b128 v[176:179], v20 offset:2048
	ds_read_b128 v[180:183], v20 offset:4096
	ds_read_b128 v[184:187], v20 offset:6144
	ds_read_b128 v[188:191], v20 offset:8192
	v_mfma_f32_16x16x32_f16 v[56:59], v[156:159], v[136:139], v[56:59]
	s_add_u32 m0, s28, 0x15000
	s_nop 0
	global_load_lds_dwordx4 v14, s[4:5]
	s_add_u32 s4, s4, s20
	s_addc_u32 s5, s5, 0
	s_waitcnt lgkmcnt(15)
	v_mfma_f32_16x16x32_f16 v[60:63], v[160:163], v[136:139], v[60:63]
	s_waitcnt lgkmcnt(14)
	v_mfma_f32_16x16x32_f16 v[64:67], v[164:167], v[136:139], v[64:67]
	s_waitcnt lgkmcnt(13)
	v_mfma_f32_16x16x32_f16 v[68:71], v[168:171], v[136:139], v[68:71]
	s_waitcnt lgkmcnt(12)
	v_mfma_f32_16x16x32_f16 v[72:75], v[156:159], v[140:143], v[72:75]
	v_mfma_f32_16x16x32_f16 v[76:79], v[160:163], v[140:143], v[76:79]
	v_mfma_f32_16x16x32_f16 v[80:83], v[164:167], v[140:143], v[80:83]
	s_add_u32 m0, s28, 0x16000
	s_nop 0
	global_load_lds_dwordx4 v10, s[6:7]
	v_mfma_f32_16x16x32_f16 v[84:87], v[168:171], v[140:143], v[84:87]
	s_waitcnt lgkmcnt(11)
	v_mfma_f32_16x16x32_f16 v[88:91], v[156:159], v[144:147], v[88:91]
	v_mfma_f32_16x16x32_f16 v[92:95], v[160:163], v[144:147], v[92:95]
	v_mfma_f32_16x16x32_f16 v[96:99], v[164:167], v[144:147], v[96:99]
	v_mfma_f32_16x16x32_f16 v[100:103], v[168:171], v[144:147], v[100:103]
	s_waitcnt lgkmcnt(10)
	v_mfma_f32_16x16x32_f16 v[104:107], v[156:159], v[148:151], v[104:107]
	v_mfma_f32_16x16x32_f16 v[108:111], v[160:163], v[148:151], v[108:111]
	s_add_u32 m0, s28, 0x18000
	s_nop 0
	global_load_lds_dwordx4 v11, s[6:7]
	s_add_u32 s6, s6, s20
	s_addc_u32 s7, s7, 0
	v_mfma_f32_16x16x32_f16 v[112:115], v[164:167], v[148:151], v[112:115]
	v_mfma_f32_16x16x32_f16 v[116:119], v[168:171], v[148:151], v[116:119]
	s_waitcnt lgkmcnt(9)
	v_mfma_f32_16x16x32_f16 v[120:123], v[156:159], v[152:155], v[120:123]
	v_mfma_f32_16x16x32_f16 v[124:127], v[160:163], v[152:155], v[124:127]
	v_mfma_f32_16x16x32_f16 v[128:131], v[164:167], v[152:155], v[128:131]
	v_mfma_f32_16x16x32_f16 v[132:135], v[168:171], v[152:155], v[132:135]
	s_waitcnt vmcnt(7) lgkmcnt(0)
	s_barrier
	s_waitcnt lgkmcnt(6)
	ds_read_b128 v[136:139], v15
	ds_read_b128 v[156:159], v17
	ds_read_b128 v[160:163], v17 offset:2048
	ds_read_b128 v[164:167], v17 offset:4096
	ds_read_b128 v[168:171], v17 offset:6144
	ds_read_b128 v[140:143], v15 offset:2048
	ds_read_b128 v[144:147], v15 offset:4096
	ds_read_b128 v[148:151], v15 offset:6144
	ds_read_b128 v[152:155], v15 offset:8192
	v_mfma_f32_16x16x32_f16 v[56:59], v[192:195], v[172:175], v[56:59]
	s_add_u32 m0, s28, 0x1a000
	s_nop 0
	global_load_lds_dwordx4 v10, s[4:5]
	s_waitcnt lgkmcnt(15)
	v_mfma_f32_16x16x32_f16 v[60:63], v[196:199], v[172:175], v[60:63]
	s_waitcnt lgkmcnt(14)
	v_mfma_f32_16x16x32_f16 v[64:67], v[200:203], v[172:175], v[64:67]
	s_waitcnt lgkmcnt(13)
	v_mfma_f32_16x16x32_f16 v[68:71], v[204:207], v[172:175], v[68:71]
	s_waitcnt lgkmcnt(12)
	v_mfma_f32_16x16x32_f16 v[72:75], v[192:195], v[176:179], v[72:75]
	v_mfma_f32_16x16x32_f16 v[76:79], v[196:199], v[176:179], v[76:79]
	s_add_u32 m0, s28, 0x1c000
	s_nop 0
	global_load_lds_dwordx4 v11, s[4:5]
	v_mfma_f32_16x16x32_f16 v[80:83], v[200:203], v[176:179], v[80:83]
	v_mfma_f32_16x16x32_f16 v[84:87], v[204:207], v[176:179], v[84:87]
	s_waitcnt lgkmcnt(11)
	v_mfma_f32_16x16x32_f16 v[88:91], v[192:195], v[180:183], v[88:91]
	v_mfma_f32_16x16x32_f16 v[92:95], v[196:199], v[180:183], v[92:95]
	v_mfma_f32_16x16x32_f16 v[96:99], v[200:203], v[180:183], v[96:99]
	s_add_u32 m0, s28, 0x1e000
	s_nop 0
	global_load_lds_dwordx4 v12, s[4:5]
	v_mfma_f32_16x16x32_f16 v[100:103], v[204:207], v[180:183], v[100:103]
	s_waitcnt lgkmcnt(10)
	v_mfma_f32_16x16x32_f16 v[104:107], v[192:195], v[184:187], v[104:107]
	v_mfma_f32_16x16x32_f16 v[108:111], v[196:199], v[184:187], v[108:111]
	v_mfma_f32_16x16x32_f16 v[112:115], v[200:203], v[184:187], v[112:115]
	v_mfma_f32_16x16x32_f16 v[116:119], v[204:207], v[184:187], v[116:119]
	s_add_u32 m0, s28, 0x20000
	s_nop 0
	global_load_lds_dwordx4 v13, s[4:5]
	s_waitcnt lgkmcnt(9)
	v_mfma_f32_16x16x32_f16 v[120:123], v[192:195], v[188:191], v[120:123]
	v_mfma_f32_16x16x32_f16 v[124:127], v[196:199], v[188:191], v[124:127]
	v_mfma_f32_16x16x32_f16 v[128:131], v[200:203], v[188:191], v[128:131]
	v_mfma_f32_16x16x32_f16 v[132:135], v[204:207], v[188:191], v[132:135]
	s_waitcnt lgkmcnt(6)
	ds_read_b128 v[172:175], v16
	ds_read_b128 v[192:195], v18
	ds_read_b128 v[196:199], v18 offset:2048
	ds_read_b128 v[200:203], v18 offset:4096
	ds_read_b128 v[204:207], v18 offset:6144
	ds_read_b128 v[176:179], v16 offset:2048
	ds_read_b128 v[180:183], v16 offset:4096
	ds_read_b128 v[184:187], v16 offset:6144
	ds_read_b128 v[188:191], v16 offset:8192
	v_mfma_f32_16x16x32_f16 v[56:59], v[156:159], v[136:139], v[56:59]
	s_add_u32 m0, s28, 0x22000
	s_nop 0
	global_load_lds_dwordx4 v14, s[4:5]
	s_add_u32 s4, s4, s20
	s_addc_u32 s5, s5, 0
	s_waitcnt lgkmcnt(15)
	v_mfma_f32_16x16x32_f16 v[60:63], v[160:163], v[136:139], v[60:63]
	s_waitcnt lgkmcnt(14)
	v_mfma_f32_16x16x32_f16 v[64:67], v[164:167], v[136:139], v[64:67]
	s_waitcnt lgkmcnt(13)
	v_mfma_f32_16x16x32_f16 v[68:71], v[168:171], v[136:139], v[68:71]
	s_waitcnt lgkmcnt(12)
	v_mfma_f32_16x16x32_f16 v[72:75], v[156:159], v[140:143], v[72:75]
	v_mfma_f32_16x16x32_f16 v[76:79], v[160:163], v[140:143], v[76:79]
	v_mfma_f32_16x16x32_f16 v[80:83], v[164:167], v[140:143], v[80:83]
	s_add_u32 m0, s28, 0x23000
	s_nop 0
	global_load_lds_dwordx4 v10, s[6:7]
	v_mfma_f32_16x16x32_f16 v[84:87], v[168:171], v[140:143], v[84:87]
	s_waitcnt lgkmcnt(11)
	v_mfma_f32_16x16x32_f16 v[88:91], v[156:159], v[144:147], v[88:91]
	v_mfma_f32_16x16x32_f16 v[92:95], v[160:163], v[144:147], v[92:95]
	v_mfma_f32_16x16x32_f16 v[96:99], v[164:167], v[144:147], v[96:99]
	v_mfma_f32_16x16x32_f16 v[100:103], v[168:171], v[144:147], v[100:103]
	s_waitcnt lgkmcnt(10)
	v_mfma_f32_16x16x32_f16 v[104:107], v[156:159], v[148:151], v[104:107]
	v_mfma_f32_16x16x32_f16 v[108:111], v[160:163], v[148:151], v[108:111]
	s_add_u32 m0, s28, 0x25000
	s_nop 0
	global_load_lds_dwordx4 v11, s[6:7]
	s_add_u32 s6, s6, s20
	s_addc_u32 s7, s7, 0
	v_mfma_f32_16x16x32_f16 v[112:115], v[164:167], v[148:151], v[112:115]
	v_mfma_f32_16x16x32_f16 v[116:119], v[168:171], v[148:151], v[116:119]
	s_waitcnt lgkmcnt(9)
	v_mfma_f32_16x16x32_f16 v[120:123], v[156:159], v[152:155], v[120:123]
	v_mfma_f32_16x16x32_f16 v[124:127], v[160:163], v[152:155], v[124:127]
	v_mfma_f32_16x16x32_f16 v[128:131], v[164:167], v[152:155], v[128:131]
	v_mfma_f32_16x16x32_f16 v[132:135], v[168:171], v[152:155], v[132:135]
	s_waitcnt vmcnt(7) lgkmcnt(0)
	s_barrier
	s_waitcnt lgkmcnt(6)
	ds_read_b128 v[136:139], v15 offset:53248
	ds_read_b128 v[156:159], v17 offset:53248
	ds_read_b128 v[160:163], v17 offset:55296
	ds_read_b128 v[164:167], v17 offset:57344
	ds_read_b128 v[168:171], v17 offset:59392
	ds_read_b128 v[140:143], v15 offset:55296
	ds_read_b128 v[144:147], v15 offset:57344
	ds_read_b128 v[148:151], v15 offset:59392
	ds_read_b128 v[152:155], v15 offset:61440
	v_mfma_f32_16x16x32_f16 v[56:59], v[192:195], v[172:175], v[56:59]
	s_add_u32 m0, s28, 0x0
	s_nop 0
	global_load_lds_dwordx4 v10, s[4:5]
	s_waitcnt lgkmcnt(15)
	v_mfma_f32_16x16x32_f16 v[60:63], v[196:199], v[172:175], v[60:63]
	s_waitcnt lgkmcnt(14)
	v_mfma_f32_16x16x32_f16 v[64:67], v[200:203], v[172:175], v[64:67]
	s_waitcnt lgkmcnt(13)
	v_mfma_f32_16x16x32_f16 v[68:71], v[204:207], v[172:175], v[68:71]
	s_waitcnt lgkmcnt(12)
	v_mfma_f32_16x16x32_f16 v[72:75], v[192:195], v[176:179], v[72:75]
	v_mfma_f32_16x16x32_f16 v[76:79], v[196:199], v[176:179], v[76:79]
	s_add_u32 m0, s28, 0x2000
	s_nop 0
	global_load_lds_dwordx4 v11, s[4:5]
	v_mfma_f32_16x16x32_f16 v[80:83], v[200:203], v[176:179], v[80:83]
	v_mfma_f32_16x16x32_f16 v[84:87], v[204:207], v[176:179], v[84:87]
	s_waitcnt lgkmcnt(11)
	v_mfma_f32_16x16x32_f16 v[88:91], v[192:195], v[180:183], v[88:91]
	v_mfma_f32_16x16x32_f16 v[92:95], v[196:199], v[180:183], v[92:95]
	v_mfma_f32_16x16x32_f16 v[96:99], v[200:203], v[180:183], v[96:99]
	s_add_u32 m0, s28, 0x4000
	s_nop 0
	global_load_lds_dwordx4 v12, s[4:5]
	v_mfma_f32_16x16x32_f16 v[100:103], v[204:207], v[180:183], v[100:103]
	s_waitcnt lgkmcnt(10)
	v_mfma_f32_16x16x32_f16 v[104:107], v[192:195], v[184:187], v[104:107]
	v_mfma_f32_16x16x32_f16 v[108:111], v[196:199], v[184:187], v[108:111]
	v_mfma_f32_16x16x32_f16 v[112:115], v[200:203], v[184:187], v[112:115]
	v_mfma_f32_16x16x32_f16 v[116:119], v[204:207], v[184:187], v[116:119]
	s_add_u32 m0, s28, 0x6000
	s_nop 0
	global_load_lds_dwordx4 v13, s[4:5]
	s_waitcnt lgkmcnt(9)
	v_mfma_f32_16x16x32_f16 v[120:123], v[192:195], v[188:191], v[120:123]
	v_mfma_f32_16x16x32_f16 v[124:127], v[196:199], v[188:191], v[124:127]
	v_mfma_f32_16x16x32_f16 v[128:131], v[200:203], v[188:191], v[128:131]
	v_mfma_f32_16x16x32_f16 v[132:135], v[204:207], v[188:191], v[132:135]
	s_waitcnt lgkmcnt(6)
	ds_read_b128 v[172:175], v16 offset:53248
	ds_read_b128 v[192:195], v18 offset:53248
	ds_read_b128 v[196:199], v18 offset:55296
	ds_read_b128 v[200:203], v18 offset:57344
	ds_read_b128 v[204:207], v18 offset:59392
	ds_read_b128 v[176:179], v16 offset:55296
	ds_read_b128 v[180:183], v16 offset:57344
	ds_read_b128 v[184:187], v16 offset:59392
	ds_read_b128 v[188:191], v16 offset:61440
	v_mfma_f32_16x16x32_f16 v[56:59], v[156:159], v[136:139], v[56:59]
	s_add_u32 m0, s28, 0x8000
	s_nop 0
	global_load_lds_dwordx4 v14, s[4:5]
	s_add_u32 s4, s4, s20
	s_addc_u32 s5, s5, 0
	s_waitcnt lgkmcnt(15)
	v_mfma_f32_16x16x32_f16 v[60:63], v[160:163], v[136:139], v[60:63]
	s_waitcnt lgkmcnt(14)
	v_mfma_f32_16x16x32_f16 v[64:67], v[164:167], v[136:139], v[64:67]
	s_waitcnt lgkmcnt(13)
	v_mfma_f32_16x16x32_f16 v[68:71], v[168:171], v[136:139], v[68:71]
	s_waitcnt lgkmcnt(12)
	v_mfma_f32_16x16x32_f16 v[72:75], v[156:159], v[140:143], v[72:75]
	v_mfma_f32_16x16x32_f16 v[76:79], v[160:163], v[140:143], v[76:79]
	v_mfma_f32_16x16x32_f16 v[80:83], v[164:167], v[140:143], v[80:83]
	s_add_u32 m0, s28, 0x9000
	s_nop 0
	global_load_lds_dwordx4 v10, s[6:7]
	v_mfma_f32_16x16x32_f16 v[84:87], v[168:171], v[140:143], v[84:87]
	s_waitcnt lgkmcnt(11)
	v_mfma_f32_16x16x32_f16 v[88:91], v[156:159], v[144:147], v[88:91]
	v_mfma_f32_16x16x32_f16 v[92:95], v[160:163], v[144:147], v[92:95]
	v_mfma_f32_16x16x32_f16 v[96:99], v[164:167], v[144:147], v[96:99]
	v_mfma_f32_16x16x32_f16 v[100:103], v[168:171], v[144:147], v[100:103]
	s_waitcnt lgkmcnt(10)
	v_mfma_f32_16x16x32_f16 v[104:107], v[156:159], v[148:151], v[104:107]
	v_mfma_f32_16x16x32_f16 v[108:111], v[160:163], v[148:151], v[108:111]
	s_add_u32 m0, s28, 0xb000
	s_nop 0
	global_load_lds_dwordx4 v11, s[6:7]
	s_add_u32 s6, s6, s20
	s_addc_u32 s7, s7, 0
	v_mfma_f32_16x16x32_f16 v[112:115], v[164:167], v[148:151], v[112:115]
	v_mfma_f32_16x16x32_f16 v[116:119], v[168:171], v[148:151], v[116:119]
	s_waitcnt lgkmcnt(9)
	v_mfma_f32_16x16x32_f16 v[120:123], v[156:159], v[152:155], v[120:123]
	v_mfma_f32_16x16x32_f16 v[124:127], v[160:163], v[152:155], v[124:127]
	v_mfma_f32_16x16x32_f16 v[128:131], v[164:167], v[152:155], v[128:131]
	v_mfma_f32_16x16x32_f16 v[132:135], v[168:171], v[152:155], v[132:135]
	s_waitcnt vmcnt(7) lgkmcnt(0)
	s_barrier
	s_waitcnt lgkmcnt(6)
	ds_read_b128 v[136:139], v19
	ds_read_b128 v[156:159], v21
	ds_read_b128 v[160:163], v21 offset:2048
	ds_read_b128 v[164:167], v21 offset:4096
	ds_read_b128 v[168:171], v21 offset:6144
	ds_read_b128 v[140:143], v19 offset:2048
	ds_read_b128 v[144:147], v19 offset:4096
	ds_read_b128 v[148:151], v19 offset:6144
	ds_read_b128 v[152:155], v19 offset:8192
	v_mfma_f32_16x16x32_f16 v[56:59], v[192:195], v[172:175], v[56:59]
	s_waitcnt lgkmcnt(15)
	v_mfma_f32_16x16x32_f16 v[60:63], v[196:199], v[172:175], v[60:63]
	s_waitcnt lgkmcnt(14)
	v_mfma_f32_16x16x32_f16 v[64:67], v[200:203], v[172:175], v[64:67]
	s_waitcnt lgkmcnt(13)
	v_mfma_f32_16x16x32_f16 v[68:71], v[204:207], v[172:175], v[68:71]
	s_waitcnt lgkmcnt(12)
	v_mfma_f32_16x16x32_f16 v[72:75], v[192:195], v[176:179], v[72:75]
	v_mfma_f32_16x16x32_f16 v[76:79], v[196:199], v[176:179], v[76:79]
	v_mfma_f32_16x16x32_f16 v[80:83], v[200:203], v[176:179], v[80:83]
	v_mfma_f32_16x16x32_f16 v[84:87], v[204:207], v[176:179], v[84:87]
	s_waitcnt lgkmcnt(11)
	v_mfma_f32_16x16x32_f16 v[88:91], v[192:195], v[180:183], v[88:91]
	v_mfma_f32_16x16x32_f16 v[92:95], v[196:199], v[180:183], v[92:95]
	v_mfma_f32_16x16x32_f16 v[96:99], v[200:203], v[180:183], v[96:99]
	v_mfma_f32_16x16x32_f16 v[100:103], v[204:207], v[180:183], v[100:103]
	s_waitcnt lgkmcnt(10)
	v_mfma_f32_16x16x32_f16 v[104:107], v[192:195], v[184:187], v[104:107]
	v_mfma_f32_16x16x32_f16 v[108:111], v[196:199], v[184:187], v[108:111]
	v_mfma_f32_16x16x32_f16 v[112:115], v[200:203], v[184:187], v[112:115]
	v_mfma_f32_16x16x32_f16 v[116:119], v[204:207], v[184:187], v[116:119]
	s_waitcnt lgkmcnt(9)
	v_mfma_f32_16x16x32_f16 v[120:123], v[192:195], v[188:191], v[120:123]
	v_mfma_f32_16x16x32_f16 v[124:127], v[196:199], v[188:191], v[124:127]
	v_mfma_f32_16x16x32_f16 v[128:131], v[200:203], v[188:191], v[128:131]
	v_mfma_f32_16x16x32_f16 v[132:135], v[204:207], v[188:191], v[132:135]
	s_waitcnt lgkmcnt(6)
	ds_read_b128 v[172:175], v20
	ds_read_b128 v[192:195], v22
	ds_read_b128 v[196:199], v22 offset:2048
	ds_read_b128 v[200:203], v22 offset:4096
	ds_read_b128 v[204:207], v22 offset:6144
	ds_read_b128 v[176:179], v20 offset:2048
	ds_read_b128 v[180:183], v20 offset:4096
	ds_read_b128 v[184:187], v20 offset:6144
	ds_read_b128 v[188:191], v20 offset:8192
	v_mfma_f32_16x16x32_f16 v[56:59], v[156:159], v[136:139], v[56:59]
	s_waitcnt lgkmcnt(15)
	v_mfma_f32_16x16x32_f16 v[60:63], v[160:163], v[136:139], v[60:63]
	s_waitcnt lgkmcnt(14)
	v_mfma_f32_16x16x32_f16 v[64:67], v[164:167], v[136:139], v[64:67]
	s_waitcnt lgkmcnt(13)
	v_mfma_f32_16x16x32_f16 v[68:71], v[168:171], v[136:139], v[68:71]
	s_waitcnt lgkmcnt(12)
	v_mfma_f32_16x16x32_f16 v[72:75], v[156:159], v[140:143], v[72:75]
	v_mfma_f32_16x16x32_f16 v[76:79], v[160:163], v[140:143], v[76:79]
	v_mfma_f32_16x16x32_f16 v[80:83], v[164:167], v[140:143], v[80:83]
	v_mfma_f32_16x16x32_f16 v[84:87], v[168:171], v[140:143], v[84:87]
	s_waitcnt lgkmcnt(11)
	v_mfma_f32_16x16x32_f16 v[88:91], v[156:159], v[144:147], v[88:91]
	v_mfma_f32_16x16x32_f16 v[92:95], v[160:163], v[144:147], v[92:95]
	v_mfma_f32_16x16x32_f16 v[96:99], v[164:167], v[144:147], v[96:99]
	v_mfma_f32_16x16x32_f16 v[100:103], v[168:171], v[144:147], v[100:103]
	s_waitcnt lgkmcnt(10)
	v_mfma_f32_16x16x32_f16 v[104:107], v[156:159], v[148:151], v[104:107]
	v_mfma_f32_16x16x32_f16 v[108:111], v[160:163], v[148:151], v[108:111]
	v_mfma_f32_16x16x32_f16 v[112:115], v[164:167], v[148:151], v[112:115]
	v_mfma_f32_16x16x32_f16 v[116:119], v[168:171], v[148:151], v[116:119]
	s_waitcnt lgkmcnt(9)
	v_mfma_f32_16x16x32_f16 v[120:123], v[156:159], v[152:155], v[120:123]
	v_mfma_f32_16x16x32_f16 v[124:127], v[160:163], v[152:155], v[124:127]
	v_mfma_f32_16x16x32_f16 v[128:131], v[164:167], v[152:155], v[128:131]
	v_mfma_f32_16x16x32_f16 v[132:135], v[168:171], v[152:155], v[132:135]
	s_waitcnt vmcnt(0) lgkmcnt(0)
	s_barrier
	s_waitcnt lgkmcnt(6)
	ds_read_b128 v[136:139], v15
	ds_read_b128 v[156:159], v17
	ds_read_b128 v[160:163], v17 offset:2048
	ds_read_b128 v[164:167], v17 offset:4096
	ds_read_b128 v[168:171], v17 offset:6144
	ds_read_b128 v[140:143], v15 offset:2048
	ds_read_b128 v[144:147], v15 offset:4096
	ds_read_b128 v[148:151], v15 offset:6144
	ds_read_b128 v[152:155], v15 offset:8192
	v_mfma_f32_16x16x32_f16 v[56:59], v[192:195], v[172:175], v[56:59]
	s_waitcnt lgkmcnt(15)
	v_mfma_f32_16x16x32_f16 v[60:63], v[196:199], v[172:175], v[60:63]
	s_waitcnt lgkmcnt(14)
	v_mfma_f32_16x16x32_f16 v[64:67], v[200:203], v[172:175], v[64:67]
	s_waitcnt lgkmcnt(13)
	v_mfma_f32_16x16x32_f16 v[68:71], v[204:207], v[172:175], v[68:71]
	s_waitcnt lgkmcnt(12)
	v_mfma_f32_16x16x32_f16 v[72:75], v[192:195], v[176:179], v[72:75]
	v_mfma_f32_16x16x32_f16 v[76:79], v[196:199], v[176:179], v[76:79]
	v_mfma_f32_16x16x32_f16 v[80:83], v[200:203], v[176:179], v[80:83]
	v_mfma_f32_16x16x32_f16 v[84:87], v[204:207], v[176:179], v[84:87]
	s_waitcnt lgkmcnt(11)
	v_mfma_f32_16x16x32_f16 v[88:91], v[192:195], v[180:183], v[88:91]
	v_mfma_f32_16x16x32_f16 v[92:95], v[196:199], v[180:183], v[92:95]
	v_mfma_f32_16x16x32_f16 v[96:99], v[200:203], v[180:183], v[96:99]
	v_mfma_f32_16x16x32_f16 v[100:103], v[204:207], v[180:183], v[100:103]
	s_waitcnt lgkmcnt(10)
	v_mfma_f32_16x16x32_f16 v[104:107], v[192:195], v[184:187], v[104:107]
	v_mfma_f32_16x16x32_f16 v[108:111], v[196:199], v[184:187], v[108:111]
	v_mfma_f32_16x16x32_f16 v[112:115], v[200:203], v[184:187], v[112:115]
	v_mfma_f32_16x16x32_f16 v[116:119], v[204:207], v[184:187], v[116:119]
	s_waitcnt lgkmcnt(9)
	v_mfma_f32_16x16x32_f16 v[120:123], v[192:195], v[188:191], v[120:123]
	v_mfma_f32_16x16x32_f16 v[124:127], v[196:199], v[188:191], v[124:127]
	v_mfma_f32_16x16x32_f16 v[128:131], v[200:203], v[188:191], v[128:131]
	v_mfma_f32_16x16x32_f16 v[132:135], v[204:207], v[188:191], v[132:135]
	s_waitcnt lgkmcnt(6)
	ds_read_b128 v[172:175], v16
	ds_read_b128 v[192:195], v18
	ds_read_b128 v[196:199], v18 offset:2048
	ds_read_b128 v[200:203], v18 offset:4096
	ds_read_b128 v[204:207], v18 offset:6144
	ds_read_b128 v[176:179], v16 offset:2048
	ds_read_b128 v[180:183], v16 offset:4096
	ds_read_b128 v[184:187], v16 offset:6144
	ds_read_b128 v[188:191], v16 offset:8192
	v_mfma_f32_16x16x32_f16 v[56:59], v[156:159], v[136:139], v[56:59]
	s_waitcnt lgkmcnt(15)
	v_mfma_f32_16x16x32_f16 v[60:63], v[160:163], v[136:139], v[60:63]
	s_waitcnt lgkmcnt(14)
	v_mfma_f32_16x16x32_f16 v[64:67], v[164:167], v[136:139], v[64:67]
	s_waitcnt lgkmcnt(13)
	v_mfma_f32_16x16x32_f16 v[68:71], v[168:171], v[136:139], v[68:71]
	s_waitcnt lgkmcnt(12)
	v_mfma_f32_16x16x32_f16 v[72:75], v[156:159], v[140:143], v[72:75]
	v_mfma_f32_16x16x32_f16 v[76:79], v[160:163], v[140:143], v[76:79]
	v_mfma_f32_16x16x32_f16 v[80:83], v[164:167], v[140:143], v[80:83]
	v_mfma_f32_16x16x32_f16 v[84:87], v[168:171], v[140:143], v[84:87]
	s_waitcnt lgkmcnt(11)
	v_mfma_f32_16x16x32_f16 v[88:91], v[156:159], v[144:147], v[88:91]
	v_mfma_f32_16x16x32_f16 v[92:95], v[160:163], v[144:147], v[92:95]
	v_mfma_f32_16x16x32_f16 v[96:99], v[164:167], v[144:147], v[96:99]
	v_mfma_f32_16x16x32_f16 v[100:103], v[168:171], v[144:147], v[100:103]
	s_waitcnt lgkmcnt(10)
	v_mfma_f32_16x16x32_f16 v[104:107], v[156:159], v[148:151], v[104:107]
	v_mfma_f32_16x16x32_f16 v[108:111], v[160:163], v[148:151], v[108:111]
	v_mfma_f32_16x16x32_f16 v[112:115], v[164:167], v[148:151], v[112:115]
	v_mfma_f32_16x16x32_f16 v[116:119], v[168:171], v[148:151], v[116:119]
	s_waitcnt lgkmcnt(9)
	v_mfma_f32_16x16x32_f16 v[120:123], v[156:159], v[152:155], v[120:123]
	v_mfma_f32_16x16x32_f16 v[124:127], v[160:163], v[152:155], v[124:127]
	v_mfma_f32_16x16x32_f16 v[128:131], v[164:167], v[152:155], v[128:131]
	v_mfma_f32_16x16x32_f16 v[132:135], v[168:171], v[152:155], v[132:135]
	s_waitcnt lgkmcnt(7)
	v_mfma_f32_16x16x32_f16 v[56:59], v[192:195], v[172:175], v[56:59]
	s_waitcnt lgkmcnt(6)
	v_mfma_f32_16x16x32_f16 v[60:63], v[196:199], v[172:175], v[60:63]
	s_waitcnt lgkmcnt(5)
	v_mfma_f32_16x16x32_f16 v[64:67], v[200:203], v[172:175], v[64:67]
	s_waitcnt lgkmcnt(4)
	v_mfma_f32_16x16x32_f16 v[68:71], v[204:207], v[172:175], v[68:71]
	s_waitcnt lgkmcnt(3)
	v_mfma_f32_16x16x32_f16 v[72:75], v[192:195], v[176:179], v[72:75]
	v_mfma_f32_16x16x32_f16 v[76:79], v[196:199], v[176:179], v[76:79]
	v_mfma_f32_16x16x32_f16 v[80:83], v[200:203], v[176:179], v[80:83]
	v_mfma_f32_16x16x32_f16 v[84:87], v[204:207], v[176:179], v[84:87]
	s_waitcnt lgkmcnt(2)
	v_mfma_f32_16x16x32_f16 v[88:91], v[192:195], v[180:183], v[88:91]
	v_mfma_f32_16x16x32_f16 v[92:95], v[196:199], v[180:183], v[92:95]
	v_mfma_f32_16x16x32_f16 v[96:99], v[200:203], v[180:183], v[96:99]
	v_mfma_f32_16x16x32_f16 v[100:103], v[204:207], v[180:183], v[100:103]
	s_waitcnt lgkmcnt(1)
	v_mfma_f32_16x16x32_f16 v[104:107], v[192:195], v[184:187], v[104:107]
	v_mfma_f32_16x16x32_f16 v[108:111], v[196:199], v[184:187], v[108:111]
	v_mfma_f32_16x16x32_f16 v[112:115], v[200:203], v[184:187], v[112:115]
	v_mfma_f32_16x16x32_f16 v[116:119], v[204:207], v[184:187], v[116:119]
	s_waitcnt lgkmcnt(0)
	v_mfma_f32_16x16x32_f16 v[120:123], v[192:195], v[188:191], v[120:123]
	v_mfma_f32_16x16x32_f16 v[124:127], v[196:199], v[188:191], v[124:127]
	v_mfma_f32_16x16x32_f16 v[128:131], v[200:203], v[188:191], v[128:131]
	v_mfma_f32_16x16x32_f16 v[132:135], v[204:207], v[188:191], v[132:135]
	s_nop 7
	s_nop 1
	v_mov_b32_e32 v213, s19
	v_pk_add_f32 v[56:57], v[56:57], v[24:25]
	v_pk_add_f32 v[58:59], v[58:59], v[26:27]
	v_pk_add_f32 v[60:61], v[60:61], v[28:29]
	v_pk_add_f32 v[62:63], v[62:63], v[30:31]
	v_pk_add_f32 v[64:65], v[64:65], v[32:33]
	v_pk_add_f32 v[66:67], v[66:67], v[34:35]
	v_pk_add_f32 v[68:69], v[68:69], v[36:37]
	v_pk_add_f32 v[70:71], v[70:71], v[38:39]
	v_pk_mul_f32 v[208:209], v[56:57], v[56:57]
	v_pk_fma_f32 v[208:209], v[58:59], v[58:59], v[208:209]
	v_pk_fma_f32 v[208:209], v[60:61], v[60:61], v[208:209]
	v_pk_fma_f32 v[208:209], v[62:63], v[62:63], v[208:209]
	v_pk_fma_f32 v[208:209], v[64:65], v[64:65], v[208:209]
	v_pk_fma_f32 v[208:209], v[66:67], v[66:67], v[208:209]
	v_pk_fma_f32 v[208:209], v[68:69], v[68:69], v[208:209]
	v_pk_fma_f32 v[208:209], v[70:71], v[70:71], v[208:209]
	v_add_f32_e32 v208, v208, v209
	v_mov_b32_e32 v209, v208
	s_nop 1
	v_permlane16_swap_b32_e32 v208, v209
	v_add_f32_e32 v208, v208, v209
	v_mov_b32_e32 v209, v208
	s_nop 1
	v_permlane32_swap_b32_e32 v208, v209
	v_add_f32_e32 v208, v208, v209
	v_mov_b32_e32 v210, 0x358637bd
	v_fmac_f32_e32 v210, 0x3c800000, v208
	v_rsq_f32_e32 v210, v210
	s_add_u32 s24, s29, 0
	s_lshr_b32 s8, s24, 1
	s_lshl_b32 s8, s8, 12
	s_and_b32 s24, s24, 1
	s_lshl_b32 s24, s24, 8
	s_add_u32 s8, s8, s24
	v_mul_f32_e32 v210, v213, v210
	v_add_u32_e32 v212, s8, v23
	v_pk_mul_f32 v[56:57], v[56:57], v[210:211] op_sel_hi:[1,0]
	v_pk_mul_f32 v[58:59], v[58:59], v[210:211] op_sel_hi:[1,0]
	v_pk_mul_f32 v[56:57], v[56:57], v[40:41]
	v_pk_mul_f32 v[58:59], v[58:59], v[42:43]
	v_cvt_pk_f16_f32 v56, v56, v57
	v_cvt_pk_f16_f32 v57, v58, v59
	global_store_dwordx2 v212, v[56:57], s[22:23] offset:0 sc0 sc1
	v_pk_mul_f32 v[60:61], v[60:61], v[210:211] op_sel_hi:[1,0]
	v_pk_mul_f32 v[62:63], v[62:63], v[210:211] op_sel_hi:[1,0]
	v_pk_mul_f32 v[60:61], v[60:61], v[44:45]
	v_pk_mul_f32 v[62:63], v[62:63], v[46:47]
	v_cvt_pk_f16_f32 v60, v60, v61
	v_cvt_pk_f16_f32 v61, v62, v63
	global_store_dwordx2 v212, v[60:61], s[22:23] offset:1024 sc0 sc1
	v_pk_mul_f32 v[64:65], v[64:65], v[210:211] op_sel_hi:[1,0]
	v_pk_mul_f32 v[66:67], v[66:67], v[210:211] op_sel_hi:[1,0]
	v_pk_mul_f32 v[64:65], v[64:65], v[48:49]
	v_pk_mul_f32 v[66:67], v[66:67], v[50:51]
	v_cvt_pk_f16_f32 v64, v64, v65
	v_cvt_pk_f16_f32 v65, v66, v67
	global_store_dwordx2 v212, v[64:65], s[22:23] offset:2048 sc0 sc1
	v_pk_mul_f32 v[68:69], v[68:69], v[210:211] op_sel_hi:[1,0]
	v_pk_mul_f32 v[70:71], v[70:71], v[210:211] op_sel_hi:[1,0]
	v_pk_mul_f32 v[68:69], v[68:69], v[52:53]
	v_pk_mul_f32 v[70:71], v[70:71], v[54:55]
	v_cvt_pk_f16_f32 v68, v68, v69
	v_cvt_pk_f16_f32 v69, v70, v71
	global_store_dwordx2 v212, v[68:69], s[22:23] offset:3072 sc0 sc1
	v_pk_add_f32 v[72:73], v[72:73], v[24:25]
	v_pk_add_f32 v[74:75], v[74:75], v[26:27]
	v_pk_add_f32 v[76:77], v[76:77], v[28:29]
	v_pk_add_f32 v[78:79], v[78:79], v[30:31]
	v_pk_add_f32 v[80:81], v[80:81], v[32:33]
	v_pk_add_f32 v[82:83], v[82:83], v[34:35]
	v_pk_add_f32 v[84:85], v[84:85], v[36:37]
	v_pk_add_f32 v[86:87], v[86:87], v[38:39]
	v_pk_mul_f32 v[208:209], v[72:73], v[72:73]
	v_pk_fma_f32 v[208:209], v[74:75], v[74:75], v[208:209]
	v_pk_fma_f32 v[208:209], v[76:77], v[76:77], v[208:209]
	v_pk_fma_f32 v[208:209], v[78:79], v[78:79], v[208:209]
	v_pk_fma_f32 v[208:209], v[80:81], v[80:81], v[208:209]
	v_pk_fma_f32 v[208:209], v[82:83], v[82:83], v[208:209]
	v_pk_fma_f32 v[208:209], v[84:85], v[84:85], v[208:209]
	v_pk_fma_f32 v[208:209], v[86:87], v[86:87], v[208:209]
	v_add_f32_e32 v208, v208, v209
	v_mov_b32_e32 v209, v208
	s_nop 1
	v_permlane16_swap_b32_e32 v208, v209
	v_add_f32_e32 v208, v208, v209
	v_mov_b32_e32 v209, v208
	s_nop 1
	v_permlane32_swap_b32_e32 v208, v209
	v_add_f32_e32 v208, v208, v209
	v_mov_b32_e32 v210, 0x358637bd
	v_fmac_f32_e32 v210, 0x3c800000, v208
	v_rsq_f32_e32 v210, v210
	s_add_u32 s24, s29, 1
	s_lshr_b32 s8, s24, 1
	s_lshl_b32 s8, s8, 12
	s_and_b32 s24, s24, 1
	s_lshl_b32 s24, s24, 8
	s_add_u32 s8, s8, s24
	v_mul_f32_e32 v210, v213, v210
	v_add_u32_e32 v212, s8, v23
	v_pk_mul_f32 v[72:73], v[72:73], v[210:211] op_sel_hi:[1,0]
	v_pk_mul_f32 v[74:75], v[74:75], v[210:211] op_sel_hi:[1,0]
	v_pk_mul_f32 v[72:73], v[72:73], v[40:41]
	v_pk_mul_f32 v[74:75], v[74:75], v[42:43]
	v_cvt_pk_f16_f32 v72, v72, v73
	v_cvt_pk_f16_f32 v73, v74, v75
	global_store_dwordx2 v212, v[72:73], s[22:23] offset:0 sc0 sc1
	v_pk_mul_f32 v[76:77], v[76:77], v[210:211] op_sel_hi:[1,0]
	v_pk_mul_f32 v[78:79], v[78:79], v[210:211] op_sel_hi:[1,0]
	v_pk_mul_f32 v[76:77], v[76:77], v[44:45]
	v_pk_mul_f32 v[78:79], v[78:79], v[46:47]
	v_cvt_pk_f16_f32 v76, v76, v77
	v_cvt_pk_f16_f32 v77, v78, v79
	global_store_dwordx2 v212, v[76:77], s[22:23] offset:1024 sc0 sc1
	v_pk_mul_f32 v[80:81], v[80:81], v[210:211] op_sel_hi:[1,0]
	v_pk_mul_f32 v[82:83], v[82:83], v[210:211] op_sel_hi:[1,0]
	v_pk_mul_f32 v[80:81], v[80:81], v[48:49]
	v_pk_mul_f32 v[82:83], v[82:83], v[50:51]
	v_cvt_pk_f16_f32 v80, v80, v81
	v_cvt_pk_f16_f32 v81, v82, v83
	global_store_dwordx2 v212, v[80:81], s[22:23] offset:2048 sc0 sc1
	v_pk_mul_f32 v[84:85], v[84:85], v[210:211] op_sel_hi:[1,0]
	v_pk_mul_f32 v[86:87], v[86:87], v[210:211] op_sel_hi:[1,0]
	v_pk_mul_f32 v[84:85], v[84:85], v[52:53]
	v_pk_mul_f32 v[86:87], v[86:87], v[54:55]
	v_cvt_pk_f16_f32 v84, v84, v85
	v_cvt_pk_f16_f32 v85, v86, v87
	global_store_dwordx2 v212, v[84:85], s[22:23] offset:3072 sc0 sc1
	v_pk_add_f32 v[88:89], v[88:89], v[24:25]
	v_pk_add_f32 v[90:91], v[90:91], v[26:27]
	v_pk_add_f32 v[92:93], v[92:93], v[28:29]
	v_pk_add_f32 v[94:95], v[94:95], v[30:31]
	v_pk_add_f32 v[96:97], v[96:97], v[32:33]
	v_pk_add_f32 v[98:99], v[98:99], v[34:35]
	v_pk_add_f32 v[100:101], v[100:101], v[36:37]
	v_pk_add_f32 v[102:103], v[102:103], v[38:39]
	v_pk_mul_f32 v[208:209], v[88:89], v[88:89]
	v_pk_fma_f32 v[208:209], v[90:91], v[90:91], v[208:209]
	v_pk_fma_f32 v[208:209], v[92:93], v[92:93], v[208:209]
	v_pk_fma_f32 v[208:209], v[94:95], v[94:95], v[208:209]
	v_pk_fma_f32 v[208:209], v[96:97], v[96:97], v[208:209]
	v_pk_fma_f32 v[208:209], v[98:99], v[98:99], v[208:209]
	v_pk_fma_f32 v[208:209], v[100:101], v[100:101], v[208:209]
	v_pk_fma_f32 v[208:209], v[102:103], v[102:103], v[208:209]
	v_add_f32_e32 v208, v208, v209
	v_mov_b32_e32 v209, v208
	s_nop 1
	v_permlane16_swap_b32_e32 v208, v209
	v_add_f32_e32 v208, v208, v209
	v_mov_b32_e32 v209, v208
	s_nop 1
	v_permlane32_swap_b32_e32 v208, v209
	v_add_f32_e32 v208, v208, v209
	v_mov_b32_e32 v210, 0x358637bd
	v_fmac_f32_e32 v210, 0x3c800000, v208
	v_rsq_f32_e32 v210, v210
	s_add_u32 s24, s29, 2
	s_lshr_b32 s8, s24, 1
	s_lshl_b32 s8, s8, 12
	s_and_b32 s24, s24, 1
	s_lshl_b32 s24, s24, 8
	s_add_u32 s8, s8, s24
	v_mul_f32_e32 v210, v213, v210
	v_add_u32_e32 v212, s8, v23
	v_pk_mul_f32 v[88:89], v[88:89], v[210:211] op_sel_hi:[1,0]
	v_pk_mul_f32 v[90:91], v[90:91], v[210:211] op_sel_hi:[1,0]
	v_pk_mul_f32 v[88:89], v[88:89], v[40:41]
	v_pk_mul_f32 v[90:91], v[90:91], v[42:43]
	v_cvt_pk_f16_f32 v88, v88, v89
	v_cvt_pk_f16_f32 v89, v90, v91
	global_store_dwordx2 v212, v[88:89], s[22:23] offset:0 sc0 sc1
	v_pk_mul_f32 v[92:93], v[92:93], v[210:211] op_sel_hi:[1,0]
	v_pk_mul_f32 v[94:95], v[94:95], v[210:211] op_sel_hi:[1,0]
	v_pk_mul_f32 v[92:93], v[92:93], v[44:45]
	v_pk_mul_f32 v[94:95], v[94:95], v[46:47]
	v_cvt_pk_f16_f32 v92, v92, v93
	v_cvt_pk_f16_f32 v93, v94, v95
	global_store_dwordx2 v212, v[92:93], s[22:23] offset:1024 sc0 sc1
	v_pk_mul_f32 v[96:97], v[96:97], v[210:211] op_sel_hi:[1,0]
	v_pk_mul_f32 v[98:99], v[98:99], v[210:211] op_sel_hi:[1,0]
	v_pk_mul_f32 v[96:97], v[96:97], v[48:49]
	v_pk_mul_f32 v[98:99], v[98:99], v[50:51]
	v_cvt_pk_f16_f32 v96, v96, v97
	v_cvt_pk_f16_f32 v97, v98, v99
	global_store_dwordx2 v212, v[96:97], s[22:23] offset:2048 sc0 sc1
	v_pk_mul_f32 v[100:101], v[100:101], v[210:211] op_sel_hi:[1,0]
	v_pk_mul_f32 v[102:103], v[102:103], v[210:211] op_sel_hi:[1,0]
	v_pk_mul_f32 v[100:101], v[100:101], v[52:53]
	v_pk_mul_f32 v[102:103], v[102:103], v[54:55]
	v_cvt_pk_f16_f32 v100, v100, v101
	v_cvt_pk_f16_f32 v101, v102, v103
	global_store_dwordx2 v212, v[100:101], s[22:23] offset:3072 sc0 sc1
	v_pk_add_f32 v[104:105], v[104:105], v[24:25]
	v_pk_add_f32 v[106:107], v[106:107], v[26:27]
	v_pk_add_f32 v[108:109], v[108:109], v[28:29]
	v_pk_add_f32 v[110:111], v[110:111], v[30:31]
	v_pk_add_f32 v[112:113], v[112:113], v[32:33]
	v_pk_add_f32 v[114:115], v[114:115], v[34:35]
	v_pk_add_f32 v[116:117], v[116:117], v[36:37]
	v_pk_add_f32 v[118:119], v[118:119], v[38:39]
	v_pk_mul_f32 v[208:209], v[104:105], v[104:105]
	v_pk_fma_f32 v[208:209], v[106:107], v[106:107], v[208:209]
	v_pk_fma_f32 v[208:209], v[108:109], v[108:109], v[208:209]
	v_pk_fma_f32 v[208:209], v[110:111], v[110:111], v[208:209]
	v_pk_fma_f32 v[208:209], v[112:113], v[112:113], v[208:209]
	v_pk_fma_f32 v[208:209], v[114:115], v[114:115], v[208:209]
	v_pk_fma_f32 v[208:209], v[116:117], v[116:117], v[208:209]
	v_pk_fma_f32 v[208:209], v[118:119], v[118:119], v[208:209]
	v_add_f32_e32 v208, v208, v209
	v_mov_b32_e32 v209, v208
	s_nop 1
	v_permlane16_swap_b32_e32 v208, v209
	v_add_f32_e32 v208, v208, v209
	v_mov_b32_e32 v209, v208
	s_nop 1
	v_permlane32_swap_b32_e32 v208, v209
	v_add_f32_e32 v208, v208, v209
	v_mov_b32_e32 v210, 0x358637bd
	v_fmac_f32_e32 v210, 0x3c800000, v208
	v_rsq_f32_e32 v210, v210
	s_add_u32 s24, s29, 3
	s_lshr_b32 s8, s24, 1
	s_lshl_b32 s8, s8, 12
	s_and_b32 s24, s24, 1
	s_lshl_b32 s24, s24, 8
	s_add_u32 s8, s8, s24
	v_mul_f32_e32 v210, v213, v210
	v_add_u32_e32 v212, s8, v23
	v_pk_mul_f32 v[104:105], v[104:105], v[210:211] op_sel_hi:[1,0]
	v_pk_mul_f32 v[106:107], v[106:107], v[210:211] op_sel_hi:[1,0]
	v_pk_mul_f32 v[104:105], v[104:105], v[40:41]
	v_pk_mul_f32 v[106:107], v[106:107], v[42:43]
	v_cvt_pk_f16_f32 v104, v104, v105
	v_cvt_pk_f16_f32 v105, v106, v107
	global_store_dwordx2 v212, v[104:105], s[22:23] offset:0 sc0 sc1
	v_pk_mul_f32 v[108:109], v[108:109], v[210:211] op_sel_hi:[1,0]
	v_pk_mul_f32 v[110:111], v[110:111], v[210:211] op_sel_hi:[1,0]
	v_pk_mul_f32 v[108:109], v[108:109], v[44:45]
	v_pk_mul_f32 v[110:111], v[110:111], v[46:47]
	v_cvt_pk_f16_f32 v108, v108, v109
	v_cvt_pk_f16_f32 v109, v110, v111
	global_store_dwordx2 v212, v[108:109], s[22:23] offset:1024 sc0 sc1
	v_pk_mul_f32 v[112:113], v[112:113], v[210:211] op_sel_hi:[1,0]
	v_pk_mul_f32 v[114:115], v[114:115], v[210:211] op_sel_hi:[1,0]
	v_pk_mul_f32 v[112:113], v[112:113], v[48:49]
	v_pk_mul_f32 v[114:115], v[114:115], v[50:51]
	v_cvt_pk_f16_f32 v112, v112, v113
	v_cvt_pk_f16_f32 v113, v114, v115
	global_store_dwordx2 v212, v[112:113], s[22:23] offset:2048 sc0 sc1
	v_pk_mul_f32 v[116:117], v[116:117], v[210:211] op_sel_hi:[1,0]
	v_pk_mul_f32 v[118:119], v[118:119], v[210:211] op_sel_hi:[1,0]
	v_pk_mul_f32 v[116:117], v[116:117], v[52:53]
	v_pk_mul_f32 v[118:119], v[118:119], v[54:55]
	v_cvt_pk_f16_f32 v116, v116, v117
	v_cvt_pk_f16_f32 v117, v118, v119
	global_store_dwordx2 v212, v[116:117], s[22:23] offset:3072 sc0 sc1
	v_pk_add_f32 v[120:121], v[120:121], v[24:25]
	v_pk_add_f32 v[122:123], v[122:123], v[26:27]
	v_pk_add_f32 v[124:125], v[124:125], v[28:29]
	v_pk_add_f32 v[126:127], v[126:127], v[30:31]
	v_pk_add_f32 v[128:129], v[128:129], v[32:33]
	v_pk_add_f32 v[130:131], v[130:131], v[34:35]
	v_pk_add_f32 v[132:133], v[132:133], v[36:37]
	v_pk_add_f32 v[134:135], v[134:135], v[38:39]
	v_pk_mul_f32 v[208:209], v[120:121], v[120:121]
	v_pk_fma_f32 v[208:209], v[122:123], v[122:123], v[208:209]
	v_pk_fma_f32 v[208:209], v[124:125], v[124:125], v[208:209]
	v_pk_fma_f32 v[208:209], v[126:127], v[126:127], v[208:209]
	v_pk_fma_f32 v[208:209], v[128:129], v[128:129], v[208:209]
	v_pk_fma_f32 v[208:209], v[130:131], v[130:131], v[208:209]
	v_pk_fma_f32 v[208:209], v[132:133], v[132:133], v[208:209]
	v_pk_fma_f32 v[208:209], v[134:135], v[134:135], v[208:209]
	v_add_f32_e32 v208, v208, v209
	v_mov_b32_e32 v209, v208
	s_nop 1
	v_permlane16_swap_b32_e32 v208, v209
	v_add_f32_e32 v208, v208, v209
	v_mov_b32_e32 v209, v208
	s_nop 1
	v_permlane32_swap_b32_e32 v208, v209
	v_add_f32_e32 v208, v208, v209
	v_mov_b32_e32 v210, 0x358637bd
	v_fmac_f32_e32 v210, 0x3c800000, v208
	v_rsq_f32_e32 v210, v210
	s_add_u32 s24, s29, 4
	s_lshr_b32 s8, s24, 1
	s_lshl_b32 s8, s8, 12
	s_and_b32 s24, s24, 1
	s_lshl_b32 s24, s24, 8
	s_add_u32 s8, s8, s24
	v_mul_f32_e32 v210, v213, v210
	v_add_u32_e32 v212, s8, v23
	v_pk_mul_f32 v[120:121], v[120:121], v[210:211] op_sel_hi:[1,0]
	v_pk_mul_f32 v[122:123], v[122:123], v[210:211] op_sel_hi:[1,0]
	v_pk_mul_f32 v[120:121], v[120:121], v[40:41]
	v_pk_mul_f32 v[122:123], v[122:123], v[42:43]
	v_cvt_pk_f16_f32 v120, v120, v121
	v_cvt_pk_f16_f32 v121, v122, v123
	global_store_dwordx2 v212, v[120:121], s[22:23] offset:0 sc0 sc1
	v_pk_mul_f32 v[124:125], v[124:125], v[210:211] op_sel_hi:[1,0]
	v_pk_mul_f32 v[126:127], v[126:127], v[210:211] op_sel_hi:[1,0]
	v_pk_mul_f32 v[124:125], v[124:125], v[44:45]
	v_pk_mul_f32 v[126:127], v[126:127], v[46:47]
	v_cvt_pk_f16_f32 v124, v124, v125
	v_cvt_pk_f16_f32 v125, v126, v127
	global_store_dwordx2 v212, v[124:125], s[22:23] offset:1024 sc0 sc1
	v_pk_mul_f32 v[128:129], v[128:129], v[210:211] op_sel_hi:[1,0]
	v_pk_mul_f32 v[130:131], v[130:131], v[210:211] op_sel_hi:[1,0]
	v_pk_mul_f32 v[128:129], v[128:129], v[48:49]
	v_pk_mul_f32 v[130:131], v[130:131], v[50:51]
	v_cvt_pk_f16_f32 v128, v128, v129
	v_cvt_pk_f16_f32 v129, v130, v131
	global_store_dwordx2 v212, v[128:129], s[22:23] offset:2048 sc0 sc1
	v_pk_mul_f32 v[132:133], v[132:133], v[210:211] op_sel_hi:[1,0]
	v_pk_mul_f32 v[134:135], v[134:135], v[210:211] op_sel_hi:[1,0]
	v_pk_mul_f32 v[132:133], v[132:133], v[52:53]
	v_pk_mul_f32 v[134:135], v[134:135], v[54:55]
	v_cvt_pk_f16_f32 v132, v132, v133
	v_cvt_pk_f16_f32 v133, v134, v135
	global_store_dwordx2 v212, v[132:133], s[22:23] offset:3072 sc0 sc1
	s_branch .Lpf_done
.Lpf_vKB:
	s_lshl_b32 s25, s25, 6
	s_add_u32 s25, s25, 32
	s_add_u32 s29, s10, s25
	s_lshr_b32 s29, s29, 4
	v_add_u32_e32 v5, s25, v3
	v_lshlrev_b32_e32 v5, 7, v5
	v_add_u32_e32 v15, v5, v6
	v_add_u32_e32 v16, v5, v7
	v_add_u32_e32 v5, 0x9000, v9
	v_add_u32_e32 v17, v5, v6
	v_add_u32_e32 v18, v5, v7
	v_add_u32_e32 v19, 0x1a000, v15
	v_add_u32_e32 v20, 0x1a000, v16
	v_add_u32_e32 v21, 0x1a000, v17
	v_add_u32_e32 v22, 0x1a000, v18
	v_lshlrev_b32_e32 v5, 4, v4
	global_load_dwordx4 v[24:27], v5, s[14:15] offset:0
	global_load_dwordx4 v[28:31], v5, s[14:15] offset:64
	global_load_dwordx4 v[32:35], v5, s[14:15] offset:128
	global_load_dwordx4 v[36:39], v5, s[14:15] offset:192
	global_load_dwordx4 v[40:43], v5, s[16:17] offset:0
	global_load_dwordx4 v[44:47], v5, s[16:17] offset:64
	global_load_dwordx4 v[48:51], v5, s[16:17] offset:128
	global_load_dwordx4 v[52:55], v5, s[16:17] offset:192
	s_add_u32 m0, s28, 0x0
	s_nop 0
	global_load_lds_dwordx4 v10, s[4:5]
	s_add_u32 m0, s28, 0x2000
	s_nop 0
	global_load_lds_dwordx4 v11, s[4:5]
	s_add_u32 m0, s28, 0x4000
	s_nop 0
	global_load_lds_dwordx4 v12, s[4:5]
	s_add_u32 m0, s28, 0x6000
	s_nop 0
	global_load_lds_dwordx4 v13, s[4:5]
	s_add_u32 s4, s4, s20
	s_addc_u32 s5, s5, 0
	s_add_u32 m0, s28, 0x9000
	s_nop 0
	global_load_lds_dwordx4 v10, s[6:7]
	s_add_u32 m0, s28, 0xb000
	s_nop 0
	global_load_lds_dwordx4 v11, s[6:7]
	s_add_u32 s6, s6, s20
	s_addc_u32 s7, s7, 0
	s_add_u32 m0, s28, 0xd000
	s_nop 0
	global_load_lds_dwordx4 v10, s[4:5]
	s_add_u32 m0, s28, 0xf000
	s_nop 0
	global_load_lds_dwordx4 v11, s[4:5]
	s_add_u32 m0, s28, 0x11000
	s_nop 0
	global_load_lds_dwordx4 v12, s[4:5]
	s_add_u32 m0, s28, 0x13000
	s_nop 0
	global_load_lds_dwordx4 v13, s[4:5]
	s_add_u32 s4, s4, s20
	s_addc_u32 s5, s5, 0
	s_add_u32 m0, s28, 0x16000
	s_nop 0
	global_load_lds_dwordx4 v10, s[6:7]
	s_add_u32 m0, s28, 0x18000
	s_nop 0
	global_load_lds_dwordx4 v11, s[6:7]
	s_add_u32 s6, s6, s20
	s_addc_u32 s7, s7, 0
	s_add_u32 m0, s28, 0x1a000
	s_nop 0
	global_load_lds_dwordx4 v10, s[4:5]
	s_add_u32 m0, s28, 0x1c000
	s_nop 0
	global_load_lds_dwordx4 v11, s[4:5]
	s_add_u32 m0, s28, 0x1e000
	s_nop 0
	global_load_lds_dwordx4 v12, s[4:5]
	s_add_u32 m0, s28, 0x20000
	s_nop 0
	global_load_lds_dwordx4 v13, s[4:5]
	s_add_u32 s4, s4, s20
	s_addc_u32 s5, s5, 0
	s_add_u32 m0, s28, 0x23000
	s_nop 0
	global_load_lds_dwordx4 v10, s[6:7]
	s_add_u32 m0, s28, 0x25000
	s_nop 0
	global_load_lds_dwordx4 v11, s[6:7]
	s_add_u32 s6, s6, s20
	s_addc_u32 s7, s7, 0
	s_waitcnt vmcnt(12) lgkmcnt(0)
	s_barrier
	s_waitcnt lgkmcnt(7)
	ds_read_b128 v[136:139], v15
	ds_read_b128 v[156:159], v17
	ds_read_b128 v[160:163], v17 offset:2048
	ds_read_b128 v[164:167], v17 offset:4096
	ds_read_b128 v[168:171], v17 offset:6144
	ds_read_b128 v[140:143], v15 offset:2048
	ds_read_b128 v[144:147], v15 offset:4096
	ds_read_b128 v[148:151], v15 offset:6144
	s_waitcnt lgkmcnt(7)
	ds_read_b128 v[172:175], v16
	ds_read_b128 v[192:195], v18
	ds_read_b128 v[196:199], v18 offset:2048
	ds_read_b128 v[200:203], v18 offset:4096
	ds_read_b128 v[204:207], v18 offset:6144
	ds_read_b128 v[176:179], v16 offset:2048
	ds_read_b128 v[180:183], v16 offset:4096
	ds_read_b128 v[184:187], v16 offset:6144
	s_waitcnt lgkmcnt(14)
	v_mfma_f32_16x16x32_f16 v[56:59], v[156:159], v[136:139], 0
	s_waitcnt lgkmcnt(13)
	v_mfma_f32_16x16x32_f16 v[60:63], v[160:163], v[136:139], 0
	s_waitcnt lgkmcnt(12)
	v_mfma_f32_16x16x32_f16 v[64:67], v[164:167], v[136:139], 0
	s_waitcnt lgkmcnt(11)
	v_mfma_f32_16x16x32_f16 v[68:71], v[168:171], v[136:139], 0
	s_waitcnt lgkmcnt(10)
	v_mfma_f32_16x16x32_f16 v[72:75], v[156:159], v[140:143], 0
	v_mfma_f32_16x16x32_f16 v[76:79], v[160:163], v[140:143], 0
	v_mfma_f32_16x16x32_f16 v[80:83], v[164:167], v[140:143], 0
	v_mfma_f32_16x16x32_f16 v[84:87], v[168:171], v[140:143], 0
	s_waitcnt lgkmcnt(9)
	v_mfma_f32_16x16x32_f16 v[88:91], v[156:159], v[144:147], 0
	v_mfma_f32_16x16x32_f16 v[92:95], v[160:163], v[144:147], 0
	v_mfma_f32_16x16x32_f16 v[96:99], v[164:167], v[144:147], 0
	v_mfma_f32_16x16x32_f16 v[100:103], v[168:171], v[144:147], 0
	s_waitcnt lgkmcnt(8)
	v_mfma_f32_16x16x32_f16 v[104:107], v[156:159], v[148:151], 0
	v_mfma_f32_16x16x32_f16 v[108:111], v[160:163], v[148:151], 0
	v_mfma_f32_16x16x32_f16 v[112:115], v[164:167], v[148:151], 0
	v_mfma_f32_16x16x32_f16 v[116:119], v[168:171], v[148:151], 0
	s_waitcnt vmcnt(6) lgkmcnt(0)
	s_barrier
	s_waitcnt lgkmcnt(7)
	ds_read_b128 v[136:139], v15 offset:53248
	ds_read_b128 v[156:159], v17 offset:53248
	ds_read_b128 v[160:163], v17 offset:55296
	ds_read_b128 v[164:167], v17 offset:57344
	ds_read_b128 v[168:171], v17 offset:59392
	ds_read_b128 v[140:143], v15 offset:55296
	ds_read_b128 v[144:147], v15 offset:57344
	ds_read_b128 v[148:151], v15 offset:59392
	s_waitcnt lgkmcnt(14)
	v_mfma_f32_16x16x32_f16 v[56:59], v[192:195], v[172:175], v[56:59]
	s_add_u32 m0, s28, 0x0
	s_nop 0
	global_load_lds_dwordx4 v10, s[4:5]
	s_waitcnt lgkmcnt(13)
	v_mfma_f32_16x16x32_f16 v[60:63], v[196:199], v[172:175], v[60:63]
	s_waitcnt lgkmcnt(12)
	v_mfma_f32_16x16x32_f16 v[64:67], v[200:203], v[172:175], v[64:67]
	s_waitcnt lgkmcnt(11)
	v_mfma_f32_16x16x32_f16 v[68:71], v[204:207], v[172:175], v[68:71]
	s_waitcnt lgkmcnt(10)
	v_mfma_f32_16x16x32_f16 v[72:75], v[192:195], v[176:179], v[72:75]
	v_mfma_f32_16x16x32_f16 v[76:79], v[196:199], v[176:179], v[76:79]
	s_add_u32 m0, s28, 0x2000
	s_nop 0
	global_load_lds_dwordx4 v11, s[4:5]
	v_mfma_f32_16x16x32_f16 v[80:83], v[200:203], v[176:179], v[80:83]
	v_mfma_f32_16x16x32_f16 v[84:87], v[204:207], v[176:179], v[84:87]
	s_waitcnt lgkmcnt(9)
	v_mfma_f32_16x16x32_f16 v[88:91], v[192:195], v[180:183], v[88:91]
	v_mfma_f32_16x16x32_f16 v[92:95], v[196:199], v[180:183], v[92:95]
	v_mfma_f32_16x16x32_f16 v[96:99], v[200:203], v[180:183], v[96:99]
	s_add_u32 m0, s28, 0x4000
	s_nop 0
	global_load_lds_dwordx4 v12, s[4:5]
	v_mfma_f32_16x16x32_f16 v[100:103], v[204:207], v[180:183], v[100:103]
	s_waitcnt lgkmcnt(8)
	v_mfma_f32_16x16x32_f16 v[104:107], v[192:195], v[184:187], v[104:107]
	v_mfma_f32_16x16x32_f16 v[108:111], v[196:199], v[184:187], v[108:111]
	v_mfma_f32_16x16x32_f16 v[112:115], v[200:203], v[184:187], v[112:115]
	v_mfma_f32_16x16x32_f16 v[116:119], v[204:207], v[184:187], v[116:119]
	s_waitcnt lgkmcnt(7)
	ds_read_b128 v[172:175], v16 offset:53248
	ds_read_b128 v[192:195], v18 offset:53248
	ds_read_b128 v[196:199], v18 offset:55296
	ds_read_b128 v[200:203], v18 offset:57344
	ds_read_b128 v[204:207], v18 offset:59392
	ds_read_b128 v[176:179], v16 offset:55296
	ds_read_b128 v[180:183], v16 offset:57344
	ds_read_b128 v[184:187], v16 offset:59392
	s_waitcnt lgkmcnt(14)
	v_mfma_f32_16x16x32_f16 v[56:59], v[156:159], v[136:139], v[56:59]
	s_add_u32 m0, s28, 0x6000
	s_nop 0
	global_load_lds_dwordx4 v13, s[4:5]
	s_add_u32 s4, s4, s20
	s_addc_u32 s5, s5, 0
	s_waitcnt lgkmcnt(13)
	v_mfma_f32_16x16x32_f16 v[60:63], v[160:163], v[136:139], v[60:63]
	s_waitcnt lgkmcnt(12)
	v_mfma_f32_16x16x32_f16 v[64:67], v[164:167], v[136:139], v[64:67]
	s_waitcnt lgkmcnt(11)
	v_mfma_f32_16x16x32_f16 v[68:71], v[168:171], v[136:139], v[68:71]
	s_waitcnt lgkmcnt(10)
	v_mfma_f32_16x16x32_f16 v[72:75], v[156:159], v[140:143], v[72:75]
	v_mfma_f32_16x16x32_f16 v[76:79], v[160:163], v[140:143], v[76:79]
	s_add_u32 m0, s28, 0x9000
	s_nop 0
	global_load_lds_dwordx4 v10, s[6:7]
	v_mfma_f32_16x16x32_f16 v[80:83], v[164:167], v[140:143], v[80:83]
	v_mfma_f32_16x16x32_f16 v[84:87], v[168:171], v[140:143], v[84:87]
	s_waitcnt lgkmcnt(9)
	v_mfma_f32_16x16x32_f16 v[88:91], v[156:159], v[144:147], v[88:91]
	v_mfma_f32_16x16x32_f16 v[92:95], v[160:163], v[144:147], v[92:95]
	v_mfma_f32_16x16x32_f16 v[96:99], v[164:167], v[144:147], v[96:99]
	s_add_u32 m0, s28, 0xb000
	s_nop 0
	global_load_lds_dwordx4 v11, s[6:7]
	s_add_u32 s6, s6, s20
	s_addc_u32 s7, s7, 0
	v_mfma_f32_16x16x32_f16 v[100:103], v[168:171], v[144:147], v[100:103]
	s_waitcnt lgkmcnt(8)
	v_mfma_f32_16x16x32_f16 v[104:107], v[156:159], v[148:151], v[104:107]
	v_mfma_f32_16x16x32_f16 v[108:111], v[160:163], v[148:151], v[108:111]
	v_mfma_f32_16x16x32_f16 v[112:115], v[164:167], v[148:151], v[112:115]
	v_mfma_f32_16x16x32_f16 v[116:119], v[168:171], v[148:151], v[116:119]
	s_waitcnt vmcnt(6) lgkmcnt(0)
	s_barrier
	s_waitcnt lgkmcnt(7)
	ds_read_b128 v[136:139], v19
	ds_read_b128 v[156:159], v21
	ds_read_b128 v[160:163], v21 offset:2048
	ds_read_b128 v[164:167], v21 offset:4096
	ds_read_b128 v[168:171], v21 offset:6144
	ds_read_b128 v[140:143], v19 offset:2048
	ds_read_b128 v[144:147], v19 offset:4096
	ds_read_b128 v[148:151], v19 offset:6144
	s_waitcnt lgkmcnt(14)
	v_mfma_f32_16x16x32_f16 v[56:59], v[192:195], v[172:175], v[56:59]
	s_add_u32 m0, s28, 0xd000
	s_nop 0
	global_load_lds_dwordx4 v10, s[4:5]
	s_waitcnt lgkmcnt(13)
	v_mfma_f32_16x16x32_f16 v[60:63], v[196:199], v[172:175], v[60:63]
	s_waitcnt lgkmcnt(12)
	v_mfma_f32_16x16x32_f16 v[64:67], v[200:203], v[172:175], v[64:67]
	s_waitcnt lgkmcnt(11)
	v_mfma_f32_16x16x32_f16 v[68:71], v[204:207], v[172:175], v[68:71]
	s_waitcnt lgkmcnt(10)
	v_mfma_f32_16x16x32_f16 v[72:75], v[192:195], v[176:179], v[72:75]
	v_mfma_f32_16x16x32_f16 v[76:79], v[196:199], v[176:179], v[76:79]
	s_add_u32 m0, s28, 0xf000
	s_nop 0
	global_load_lds_dwordx4 v11, s[4:5]
	v_mfma_f32_16x16x32_f16 v[80:83], v[200:203], v[176:179], v[80:83]
	v_mfma_f32_16x16x32_f16 v[84:87], v[204:207], v[176:179], v[84:87]
	s_waitcnt lgkmcnt(9)
	v_mfma_f32_16x16x32_f16 v[88:91], v[192:195], v[180:183], v[88:91]
	v_mfma_f32_16x16x32_f16 v[92:95], v[196:199], v[180:183], v[92:95]
	v_mfma_f32_16x16x32_f16 v[96:99], v[200:203], v[180:183], v[96:99]
	s_add_u32 m0, s28, 0x11000
	s_nop 0
	global_load_lds_dwordx4 v12, s[4:5]
	v_mfma_f32_16x16x32_f16 v[100:103], v[204:207], v[180:183], v[100:103]
	s_waitcnt lgkmcnt(8)
	v_mfma_f32_16x16x32_f16 v[104:107], v[192:195], v[184:187], v[104:107]
	v_mfma_f32_16x16x32_f16 v[108:111], v[196:199], v[184:187], v[108:111]
	v_mfma_f32_16x16x32_f16 v[112:115], v[200:203], v[184:187], v[112:115]
	v_mfma_f32_16x16x32_f16 v[116:119], v[204:207], v[184:187], v[116:119]
	s_waitcnt lgkmcnt(7)
	ds_read_b128 v[172:175], v20
	ds_read_b128 v[192:195], v22
	ds_read_b128 v[196:199], v22 offset:2048
	ds_read_b128 v[200:203], v22 offset:4096
	ds_read_b128 v[204:207], v22 offset:6144
	ds_read_b128 v[176:179], v20 offset:2048
	ds_read_b128 v[180:183], v20 offset:4096
	ds_read_b128 v[184:187], v20 offset:6144
	s_waitcnt lgkmcnt(14)
	v_mfma_f32_16x16x32_f16 v[56:59], v[156:159], v[136:139], v[56:59]
	s_add_u32 m0, s28, 0x13000
	s_nop 0
	global_load_lds_dwordx4 v13, s[4:5]
	s_add_u32 s4, s4, s20
	s_addc_u32 s5, s5, 0
	s_waitcnt lgkmcnt(13)
	v_mfma_f32_16x16x32_f16 v[60:63], v[160:163], v[136:139], v[60:63]
	s_waitcnt lgkmcnt(12)
	v_mfma_f32_16x16x32_f16 v[64:67], v[164:167], v[136:139], v[64:67]
	s_waitcnt lgkmcnt(11)
	v_mfma_f32_16x16x32_f16 v[68:71], v[168:171], v[136:139], v[68:71]
	s_waitcnt lgkmcnt(10)
	v_mfma_f32_16x16x32_f16 v[72:75], v[156:159], v[140:143], v[72:75]
	v_mfma_f32_16x16x32_f16 v[76:79], v[160:163], v[140:143], v[76:79]
	s_add_u32 m0, s28, 0x16000
	s_nop 0
	global_load_lds_dwordx4 v10, s[6:7]
	v_mfma_f32_16x16x32_f16 v[80:83], v[164:167], v[140:143], v[80:83]
	v_mfma_f32_16x16x32_f16 v[84:87], v[168:171], v[140:143], v[84:87]
	s_waitcnt lgkmcnt(9)
	v_mfma_f32_16x16x32_f16 v[88:91], v[156:159], v[144:147], v[88:91]
	v_mfma_f32_16x16x32_f16 v[92:95], v[160:163], v[144:147], v[92:95]
	v_mfma_f32_16x16x32_f16 v[96:99], v[164:167], v[144:147], v[96:99]
	s_add_u32 m0, s28, 0x18000
	s_nop 0
	global_load_lds_dwordx4 v11, s[6:7]
	s_add_u32 s6, s6, s20
	s_addc_u32 s7, s7, 0
	v_mfma_f32_16x16x32_f16 v[100:103], v[168:171], v[144:147], v[100:103]
	s_waitcnt lgkmcnt(8)
	v_mfma_f32_16x16x32_f16 v[104:107], v[156:159], v[148:151], v[104:107]
	v_mfma_f32_16x16x32_f16 v[108:111], v[160:163], v[148:151], v[108:111]
	v_mfma_f32_16x16x32_f16 v[112:115], v[164:167], v[148:151], v[112:115]
	v_mfma_f32_16x16x32_f16 v[116:119], v[168:171], v[148:151], v[116:119]
	s_waitcnt vmcnt(6) lgkmcnt(0)
	s_barrier
	s_waitcnt lgkmcnt(7)
	ds_read_b128 v[136:139], v15
	ds_read_b128 v[156:159], v17
	ds_read_b128 v[160:163], v17 offset:2048
	ds_read_b128 v[164:167], v17 offset:4096
	ds_read_b128 v[168:171], v17 offset:6144
	ds_read_b128 v[140:143], v15 offset:2048
	ds_read_b128 v[144:147], v15 offset:4096
	ds_read_b128 v[148:151], v15 offset:6144
	s_waitcnt lgkmcnt(14)
	v_mfma_f32_16x16x32_f16 v[56:59], v[192:195], v[172:175], v[56:59]
	s_add_u32 m0, s28, 0x1a000
	s_nop 0
	global_load_lds_dwordx4 v10, s[4:5]
	s_waitcnt lgkmcnt(13)
	v_mfma_f32_16x16x32_f16 v[60:63], v[196:199], v[172:175], v[60:63]
	s_waitcnt lgkmcnt(12)
	v_mfma_f32_16x16x32_f16 v[64:67], v[200:203], v[172:175], v[64:67]
	s_waitcnt lgkmcnt(11)
	v_mfma_f32_16x16x32_f16 v[68:71], v[204:207], v[172:175], v[68:71]
	s_waitcnt lgkmcnt(10)
	v_mfma_f32_16x16x32_f16 v[72:75], v[192:195], v[176:179], v[72:75]
	v_mfma_f32_16x16x32_f16 v[76:79], v[196:199], v[176:179], v[76:79]
	s_add_u32 m0, s28, 0x1c000
	s_nop 0
	global_load_lds_dwordx4 v11, s[4:5]
	v_mfma_f32_16x16x32_f16 v[80:83], v[200:203], v[176:179], v[80:83]
	v_mfma_f32_16x16x32_f16 v[84:87], v[204:207], v[176:179], v[84:87]
	s_waitcnt lgkmcnt(9)
	v_mfma_f32_16x16x32_f16 v[88:91], v[192:195], v[180:183], v[88:91]
	v_mfma_f32_16x16x32_f16 v[92:95], v[196:199], v[180:183], v[92:95]
	v_mfma_f32_16x16x32_f16 v[96:99], v[200:203], v[180:183], v[96:99]
	s_add_u32 m0, s28, 0x1e000
	s_nop 0
	global_load_lds_dwordx4 v12, s[4:5]
	v_mfma_f32_16x16x32_f16 v[100:103], v[204:207], v[180:183], v[100:103]
	s_waitcnt lgkmcnt(8)
	v_mfma_f32_16x16x32_f16 v[104:107], v[192:195], v[184:187], v[104:107]
	v_mfma_f32_16x16x32_f16 v[108:111], v[196:199], v[184:187], v[108:111]
	v_mfma_f32_16x16x32_f16 v[112:115], v[200:203], v[184:187], v[112:115]
	v_mfma_f32_16x16x32_f16 v[116:119], v[204:207], v[184:187], v[116:119]
	s_waitcnt lgkmcnt(7)
	ds_read_b128 v[172:175], v16
	ds_read_b128 v[192:195], v18
	ds_read_b128 v[196:199], v18 offset:2048
	ds_read_b128 v[200:203], v18 offset:4096
	ds_read_b128 v[204:207], v18 offset:6144
	ds_read_b128 v[176:179], v16 offset:2048
	ds_read_b128 v[180:183], v16 offset:4096
	ds_read_b128 v[184:187], v16 offset:6144
	s_waitcnt lgkmcnt(14)
	v_mfma_f32_16x16x32_f16 v[56:59], v[156:159], v[136:139], v[56:59]
	s_add_u32 m0, s28, 0x20000
	s_nop 0
	global_load_lds_dwordx4 v13, s[4:5]
	s_add_u32 s4, s4, s20
	s_addc_u32 s5, s5, 0
	s_waitcnt lgkmcnt(13)
	v_mfma_f32_16x16x32_f16 v[60:63], v[160:163], v[136:139], v[60:63]
	s_waitcnt lgkmcnt(12)
	v_mfma_f32_16x16x32_f16 v[64:67], v[164:167], v[136:139], v[64:67]
	s_waitcnt lgkmcnt(11)
	v_mfma_f32_16x16x32_f16 v[68:71], v[168:171], v[136:139], v[68:71]
	s_waitcnt lgkmcnt(10)
	v_mfma_f32_16x16x32_f16 v[72:75], v[156:159], v[140:143], v[72:75]
	v_mfma_f32_16x16x32_f16 v[76:79], v[160:163], v[140:143], v[76:79]
	s_add_u32 m0, s28, 0x23000
	s_nop 0
	global_load_lds_dwordx4 v10, s[6:7]
	v_mfma_f32_16x16x32_f16 v[80:83], v[164:167], v[140:143], v[80:83]
	v_mfma_f32_16x16x32_f16 v[84:87], v[168:171], v[140:143], v[84:87]
	s_waitcnt lgkmcnt(9)
	v_mfma_f32_16x16x32_f16 v[88:91], v[156:159], v[144:147], v[88:91]
	v_mfma_f32_16x16x32_f16 v[92:95], v[160:163], v[144:147], v[92:95]
	v_mfma_f32_16x16x32_f16 v[96:99], v[164:167], v[144:147], v[96:99]
	s_add_u32 m0, s28, 0x25000
	s_nop 0
	global_load_lds_dwordx4 v11, s[6:7]
	s_add_u32 s6, s6, s20
	s_addc_u32 s7, s7, 0
	v_mfma_f32_16x16x32_f16 v[100:103], v[168:171], v[144:147], v[100:103]
	s_waitcnt lgkmcnt(8)
	v_mfma_f32_16x16x32_f16 v[104:107], v[156:159], v[148:151], v[104:107]
	v_mfma_f32_16x16x32_f16 v[108:111], v[160:163], v[148:151], v[108:111]
	v_mfma_f32_16x16x32_f16 v[112:115], v[164:167], v[148:151], v[112:115]
	v_mfma_f32_16x16x32_f16 v[116:119], v[168:171], v[148:151], v[116:119]
	s_waitcnt vmcnt(6) lgkmcnt(0)
	s_barrier
	s_waitcnt lgkmcnt(7)
	ds_read_b128 v[136:139], v15 offset:53248
	ds_read_b128 v[156:159], v17 offset:53248
	ds_read_b128 v[160:163], v17 offset:55296
	ds_read_b128 v[164:167], v17 offset:57344
	ds_read_b128 v[168:171], v17 offset:59392
	ds_read_b128 v[140:143], v15 offset:55296
	ds_read_b128 v[144:147], v15 offset:57344
	ds_read_b128 v[148:151], v15 offset:59392
	s_waitcnt lgkmcnt(14)
	v_mfma_f32_16x16x32_f16 v[56:59], v[192:195], v[172:175], v[56:59]
	s_add_u32 m0, s28, 0x0
	s_nop 0
	global_load_lds_dwordx4 v10, s[4:5]
	s_waitcnt lgkmcnt(13)
	v_mfma_f32_16x16x32_f16 v[60:63], v[196:199], v[172:175], v[60:63]
	s_waitcnt lgkmcnt(12)
	v_mfma_f32_16x16x32_f16 v[64:67], v[200:203], v[172:175], v[64:67]
	s_waitcnt lgkmcnt(11)
	v_mfma_f32_16x16x32_f16 v[68:71], v[204:207], v[172:175], v[68:71]
	s_waitcnt lgkmcnt(10)
	v_mfma_f32_16x16x32_f16 v[72:75], v[192:195], v[176:179], v[72:75]
	v_mfma_f32_16x16x32_f16 v[76:79], v[196:199], v[176:179], v[76:79]
	s_add_u32 m0, s28, 0x2000
	s_nop 0
	global_load_lds_dwordx4 v11, s[4:5]
	v_mfma_f32_16x16x32_f16 v[80:83], v[200:203], v[176:179], v[80:83]
	v_mfma_f32_16x16x32_f16 v[84:87], v[204:207], v[176:179], v[84:87]
	s_waitcnt lgkmcnt(9)
	v_mfma_f32_16x16x32_f16 v[88:91], v[192:195], v[180:183], v[88:91]
	v_mfma_f32_16x16x32_f16 v[92:95], v[196:199], v[180:183], v[92:95]
	v_mfma_f32_16x16x32_f16 v[96:99], v[200:203], v[180:183], v[96:99]
	s_add_u32 m0, s28, 0x4000
	s_nop 0
	global_load_lds_dwordx4 v12, s[4:5]
	v_mfma_f32_16x16x32_f16 v[100:103], v[204:207], v[180:183], v[100:103]
	s_waitcnt lgkmcnt(8)
	v_mfma_f32_16x16x32_f16 v[104:107], v[192:195], v[184:187], v[104:107]
	v_mfma_f32_16x16x32_f16 v[108:111], v[196:199], v[184:187], v[108:111]
	v_mfma_f32_16x16x32_f16 v[112:115], v[200:203], v[184:187], v[112:115]
	v_mfma_f32_16x16x32_f16 v[116:119], v[204:207], v[184:187], v[116:119]
	s_waitcnt lgkmcnt(7)
	ds_read_b128 v[172:175], v16 offset:53248
	ds_read_b128 v[192:195], v18 offset:53248
	ds_read_b128 v[196:199], v18 offset:55296
	ds_read_b128 v[200:203], v18 offset:57344
	ds_read_b128 v[204:207], v18 offset:59392
	ds_read_b128 v[176:179], v16 offset:55296
	ds_read_b128 v[180:183], v16 offset:57344
	ds_read_b128 v[184:187], v16 offset:59392
	s_waitcnt lgkmcnt(14)
	v_mfma_f32_16x16x32_f16 v[56:59], v[156:159], v[136:139], v[56:59]
	s_add_u32 m0, s28, 0x6000
	s_nop 0
	global_load_lds_dwordx4 v13, s[4:5]
	s_add_u32 s4, s4, s20
	s_addc_u32 s5, s5, 0
	s_waitcnt lgkmcnt(13)
	v_mfma_f32_16x16x32_f16 v[60:63], v[160:163], v[136:139], v[60:63]
	s_waitcnt lgkmcnt(12)
	v_mfma_f32_16x16x32_f16 v[64:67], v[164:167], v[136:139], v[64:67]
	s_waitcnt lgkmcnt(11)
	v_mfma_f32_16x16x32_f16 v[68:71], v[168:171], v[136:139], v[68:71]
	s_waitcnt lgkmcnt(10)
	v_mfma_f32_16x16x32_f16 v[72:75], v[156:159], v[140:143], v[72:75]
	v_mfma_f32_16x16x32_f16 v[76:79], v[160:163], v[140:143], v[76:79]
	s_add_u32 m0, s28, 0x9000
	s_nop 0
	global_load_lds_dwordx4 v10, s[6:7]
	v_mfma_f32_16x16x32_f16 v[80:83], v[164:167], v[140:143], v[80:83]
	v_mfma_f32_16x16x32_f16 v[84:87], v[168:171], v[140:143], v[84:87]
	s_waitcnt lgkmcnt(9)
	v_mfma_f32_16x16x32_f16 v[88:91], v[156:159], v[144:147], v[88:91]
	v_mfma_f32_16x16x32_f16 v[92:95], v[160:163], v[144:147], v[92:95]
	v_mfma_f32_16x16x32_f16 v[96:99], v[164:167], v[144:147], v[96:99]
	s_add_u32 m0, s28, 0xb000
	s_nop 0
	global_load_lds_dwordx4 v11, s[6:7]
	s_add_u32 s6, s6, s20
	s_addc_u32 s7, s7, 0
	v_mfma_f32_16x16x32_f16 v[100:103], v[168:171], v[144:147], v[100:103]
	s_waitcnt lgkmcnt(8)
	v_mfma_f32_16x16x32_f16 v[104:107], v[156:159], v[148:151], v[104:107]
	v_mfma_f32_16x16x32_f16 v[108:111], v[160:163], v[148:151], v[108:111]
	v_mfma_f32_16x16x32_f16 v[112:115], v[164:167], v[148:151], v[112:115]
	v_mfma_f32_16x16x32_f16 v[116:119], v[168:171], v[148:151], v[116:119]
	s_waitcnt vmcnt(6) lgkmcnt(0)
	s_barrier
	s_waitcnt lgkmcnt(7)
	ds_read_b128 v[136:139], v19
	ds_read_b128 v[156:159], v21
	ds_read_b128 v[160:163], v21 offset:2048
	ds_read_b128 v[164:167], v21 offset:4096
	ds_read_b128 v[168:171], v21 offset:6144
	ds_read_b128 v[140:143], v19 offset:2048
	ds_read_b128 v[144:147], v19 offset:4096
	ds_read_b128 v[148:151], v19 offset:6144
	s_waitcnt lgkmcnt(14)
	v_mfma_f32_16x16x32_f16 v[56:59], v[192:195], v[172:175], v[56:59]
	s_add_u32 m0, s28, 0xd000
	s_nop 0
	global_load_lds_dwordx4 v10, s[4:5]
	s_waitcnt lgkmcnt(13)
	v_mfma_f32_16x16x32_f16 v[60:63], v[196:199], v[172:175], v[60:63]
	s_waitcnt lgkmcnt(12)
	v_mfma_f32_16x16x32_f16 v[64:67], v[200:203], v[172:175], v[64:67]
	s_waitcnt lgkmcnt(11)
	v_mfma_f32_16x16x32_f16 v[68:71], v[204:207], v[172:175], v[68:71]
	s_waitcnt lgkmcnt(10)
	v_mfma_f32_16x16x32_f16 v[72:75], v[192:195], v[176:179], v[72:75]
	v_mfma_f32_16x16x32_f16 v[76:79], v[196:199], v[176:179], v[76:79]
	s_add_u32 m0, s28, 0xf000
	s_nop 0
	global_load_lds_dwordx4 v11, s[4:5]
	v_mfma_f32_16x16x32_f16 v[80:83], v[200:203], v[176:179], v[80:83]
	v_mfma_f32_16x16x32_f16 v[84:87], v[204:207], v[176:179], v[84:87]
	s_waitcnt lgkmcnt(9)
	v_mfma_f32_16x16x32_f16 v[88:91], v[192:195], v[180:183], v[88:91]
	v_mfma_f32_16x16x32_f16 v[92:95], v[196:199], v[180:183], v[92:95]
	v_mfma_f32_16x16x32_f16 v[96:99], v[200:203], v[180:183], v[96:99]
	s_add_u32 m0, s28, 0x11000
	s_nop 0
	global_load_lds_dwordx4 v12, s[4:5]
	v_mfma_f32_16x16x32_f16 v[100:103], v[204:207], v[180:183], v[100:103]
	s_waitcnt lgkmcnt(8)
	v_mfma_f32_16x16x32_f16 v[104:107], v[192:195], v[184:187], v[104:107]
	v_mfma_f32_16x16x32_f16 v[108:111], v[196:199], v[184:187], v[108:111]
	v_mfma_f32_16x16x32_f16 v[112:115], v[200:203], v[184:187], v[112:115]
	v_mfma_f32_16x16x32_f16 v[116:119], v[204:207], v[184:187], v[116:119]
	s_waitcnt lgkmcnt(7)
	ds_read_b128 v[172:175], v20
	ds_read_b128 v[192:195], v22
	ds_read_b128 v[196:199], v22 offset:2048
	ds_read_b128 v[200:203], v22 offset:4096
	ds_read_b128 v[204:207], v22 offset:6144
	ds_read_b128 v[176:179], v20 offset:2048
	ds_read_b128 v[180:183], v20 offset:4096
	ds_read_b128 v[184:187], v20 offset:6144
	s_waitcnt lgkmcnt(14)
	v_mfma_f32_16x16x32_f16 v[56:59], v[156:159], v[136:139], v[56:59]
	s_add_u32 m0, s28, 0x13000
	s_nop 0
	global_load_lds_dwordx4 v13, s[4:5]
	s_add_u32 s4, s4, s20
	s_addc_u32 s5, s5, 0
	s_waitcnt lgkmcnt(13)
	v_mfma_f32_16x16x32_f16 v[60:63], v[160:163], v[136:139], v[60:63]
	s_waitcnt lgkmcnt(12)
	v_mfma_f32_16x16x32_f16 v[64:67], v[164:167], v[136:139], v[64:67]
	s_waitcnt lgkmcnt(11)
	v_mfma_f32_16x16x32_f16 v[68:71], v[168:171], v[136:139], v[68:71]
	s_waitcnt lgkmcnt(10)
	v_mfma_f32_16x16x32_f16 v[72:75], v[156:159], v[140:143], v[72:75]
	v_mfma_f32_16x16x32_f16 v[76:79], v[160:163], v[140:143], v[76:79]
	s_add_u32 m0, s28, 0x16000
	s_nop 0
	global_load_lds_dwordx4 v10, s[6:7]
	v_mfma_f32_16x16x32_f16 v[80:83], v[164:167], v[140:143], v[80:83]
	v_mfma_f32_16x16x32_f16 v[84:87], v[168:171], v[140:143], v[84:87]
	s_waitcnt lgkmcnt(9)
	v_mfma_f32_16x16x32_f16 v[88:91], v[156:159], v[144:147], v[88:91]
	v_mfma_f32_16x16x32_f16 v[92:95], v[160:163], v[144:147], v[92:95]
	v_mfma_f32_16x16x32_f16 v[96:99], v[164:167], v[144:147], v[96:99]
	s_add_u32 m0, s28, 0x18000
	s_nop 0
	global_load_lds_dwordx4 v11, s[6:7]
	s_add_u32 s6, s6, s20
	s_addc_u32 s7, s7, 0
	v_mfma_f32_16x16x32_f16 v[100:103], v[168:171], v[144:147], v[100:103]
	s_waitcnt lgkmcnt(8)
	v_mfma_f32_16x16x32_f16 v[104:107], v[156:159], v[148:151], v[104:107]
	v_mfma_f32_16x16x32_f16 v[108:111], v[160:163], v[148:151], v[108:111]
	v_mfma_f32_16x16x32_f16 v[112:115], v[164:167], v[148:151], v[112:115]
	v_mfma_f32_16x16x32_f16 v[116:119], v[168:171], v[148:151], v[116:119]
	s_waitcnt vmcnt(6) lgkmcnt(0)
	s_barrier
	s_waitcnt lgkmcnt(7)
	ds_read_b128 v[136:139], v15
	ds_read_b128 v[156:159], v17
	ds_read_b128 v[160:163], v17 offset:2048
	ds_read_b128 v[164:167], v17 offset:4096
	ds_read_b128 v[168:171], v17 offset:6144
	ds_read_b128 v[140:143], v15 offset:2048
	ds_read_b128 v[144:147], v15 offset:4096
	ds_read_b128 v[148:151], v15 offset:6144
	s_waitcnt lgkmcnt(14)
	v_mfma_f32_16x16x32_f16 v[56:59], v[192:195], v[172:175], v[56:59]
	s_add_u32 m0, s28, 0x1a000
	s_nop 0
	global_load_lds_dwordx4 v10, s[4:5]
	s_waitcnt lgkmcnt(13)
	v_mfma_f32_16x16x32_f16 v[60:63], v[196:199], v[172:175], v[60:63]
	s_waitcnt lgkmcnt(12)
	v_mfma_f32_16x16x32_f16 v[64:67], v[200:203], v[172:175], v[64:67]
	s_waitcnt lgkmcnt(11)
	v_mfma_f32_16x16x32_f16 v[68:71], v[204:207], v[172:175], v[68:71]
	s_waitcnt lgkmcnt(10)
	v_mfma_f32_16x16x32_f16 v[72:75], v[192:195], v[176:179], v[72:75]
	v_mfma_f32_16x16x32_f16 v[76:79], v[196:199], v[176:179], v[76:79]
	s_add_u32 m0, s28, 0x1c000
	s_nop 0
	global_load_lds_dwordx4 v11, s[4:5]
	v_mfma_f32_16x16x32_f16 v[80:83], v[200:203], v[176:179], v[80:83]
	v_mfma_f32_16x16x32_f16 v[84:87], v[204:207], v[176:179], v[84:87]
	s_waitcnt lgkmcnt(9)
	v_mfma_f32_16x16x32_f16 v[88:91], v[192:195], v[180:183], v[88:91]
	v_mfma_f32_16x16x32_f16 v[92:95], v[196:199], v[180:183], v[92:95]
	v_mfma_f32_16x16x32_f16 v[96:99], v[200:203], v[180:183], v[96:99]
	s_add_u32 m0, s28, 0x1e000
	s_nop 0
	global_load_lds_dwordx4 v12, s[4:5]
	v_mfma_f32_16x16x32_f16 v[100:103], v[204:207], v[180:183], v[100:103]
	s_waitcnt lgkmcnt(8)
	v_mfma_f32_16x16x32_f16 v[104:107], v[192:195], v[184:187], v[104:107]
	v_mfma_f32_16x16x32_f16 v[108:111], v[196:199], v[184:187], v[108:111]
	v_mfma_f32_16x16x32_f16 v[112:115], v[200:203], v[184:187], v[112:115]
	v_mfma_f32_16x16x32_f16 v[116:119], v[204:207], v[184:187], v[116:119]
	s_waitcnt lgkmcnt(7)
	ds_read_b128 v[172:175], v16
	ds_read_b128 v[192:195], v18
	ds_read_b128 v[196:199], v18 offset:2048
	ds_read_b128 v[200:203], v18 offset:4096
	ds_read_b128 v[204:207], v18 offset:6144
	ds_read_b128 v[176:179], v16 offset:2048
	ds_read_b128 v[180:183], v16 offset:4096
	ds_read_b128 v[184:187], v16 offset:6144
	s_waitcnt lgkmcnt(14)
	v_mfma_f32_16x16x32_f16 v[56:59], v[156:159], v[136:139], v[56:59]
	s_add_u32 m0, s28, 0x20000
	s_nop 0
	global_load_lds_dwordx4 v13, s[4:5]
	s_add_u32 s4, s4, s20
	s_addc_u32 s5, s5, 0
	s_waitcnt lgkmcnt(13)
	v_mfma_f32_16x16x32_f16 v[60:63], v[160:163], v[136:139], v[60:63]
	s_waitcnt lgkmcnt(12)
	v_mfma_f32_16x16x32_f16 v[64:67], v[164:167], v[136:139], v[64:67]
	s_waitcnt lgkmcnt(11)
	v_mfma_f32_16x16x32_f16 v[68:71], v[168:171], v[136:139], v[68:71]
	s_waitcnt lgkmcnt(10)
	v_mfma_f32_16x16x32_f16 v[72:75], v[156:159], v[140:143], v[72:75]
	v_mfma_f32_16x16x32_f16 v[76:79], v[160:163], v[140:143], v[76:79]
	s_add_u32 m0, s28, 0x23000
	s_nop 0
	global_load_lds_dwordx4 v10, s[6:7]
	v_mfma_f32_16x16x32_f16 v[80:83], v[164:167], v[140:143], v[80:83]
	v_mfma_f32_16x16x32_f16 v[84:87], v[168:171], v[140:143], v[84:87]
	s_waitcnt lgkmcnt(9)
	v_mfma_f32_16x16x32_f16 v[88:91], v[156:159], v[144:147], v[88:91]
	v_mfma_f32_16x16x32_f16 v[92:95], v[160:163], v[144:147], v[92:95]
	v_mfma_f32_16x16x32_f16 v[96:99], v[164:167], v[144:147], v[96:99]
	s_add_u32 m0, s28, 0x25000
	s_nop 0
	global_load_lds_dwordx4 v11, s[6:7]
	s_add_u32 s6, s6, s20
	s_addc_u32 s7, s7, 0
	v_mfma_f32_16x16x32_f16 v[100:103], v[168:171], v[144:147], v[100:103]
	s_waitcnt lgkmcnt(8)
	v_mfma_f32_16x16x32_f16 v[104:107], v[156:159], v[148:151], v[104:107]
	v_mfma_f32_16x16x32_f16 v[108:111], v[160:163], v[148:151], v[108:111]
	v_mfma_f32_16x16x32_f16 v[112:115], v[164:167], v[148:151], v[112:115]
	v_mfma_f32_16x16x32_f16 v[116:119], v[168:171], v[148:151], v[116:119]
	s_waitcnt vmcnt(6) lgkmcnt(0)
	s_barrier
	s_waitcnt lgkmcnt(7)
	ds_read_b128 v[136:139], v15 offset:53248
	ds_read_b128 v[156:159], v17 offset:53248
	ds_read_b128 v[160:163], v17 offset:55296
	ds_read_b128 v[164:167], v17 offset:57344
	ds_read_b128 v[168:171], v17 offset:59392
	ds_read_b128 v[140:143], v15 offset:55296
	ds_read_b128 v[144:147], v15 offset:57344
	ds_read_b128 v[148:151], v15 offset:59392
	s_waitcnt lgkmcnt(14)
	v_mfma_f32_16x16x32_f16 v[56:59], v[192:195], v[172:175], v[56:59]
	s_add_u32 m0, s28, 0x0
	s_nop 0
	global_load_lds_dwordx4 v10, s[4:5]
	s_waitcnt lgkmcnt(13)
	v_mfma_f32_16x16x32_f16 v[60:63], v[196:199], v[172:175], v[60:63]
	s_waitcnt lgkmcnt(12)
	v_mfma_f32_16x16x32_f16 v[64:67], v[200:203], v[172:175], v[64:67]
	s_waitcnt lgkmcnt(11)
	v_mfma_f32_16x16x32_f16 v[68:71], v[204:207], v[172:175], v[68:71]
	s_waitcnt lgkmcnt(10)
	v_mfma_f32_16x16x32_f16 v[72:75], v[192:195], v[176:179], v[72:75]
	v_mfma_f32_16x16x32_f16 v[76:79], v[196:199], v[176:179], v[76:79]
	s_add_u32 m0, s28, 0x2000
	s_nop 0
	global_load_lds_dwordx4 v11, s[4:5]
	v_mfma_f32_16x16x32_f16 v[80:83], v[200:203], v[176:179], v[80:83]
	v_mfma_f32_16x16x32_f16 v[84:87], v[204:207], v[176:179], v[84:87]
	s_waitcnt lgkmcnt(9)
	v_mfma_f32_16x16x32_f16 v[88:91], v[192:195], v[180:183], v[88:91]
	v_mfma_f32_16x16x32_f16 v[92:95], v[196:199], v[180:183], v[92:95]
	v_mfma_f32_16x16x32_f16 v[96:99], v[200:203], v[180:183], v[96:99]
	s_add_u32 m0, s28, 0x4000
	s_nop 0
	global_load_lds_dwordx4 v12, s[4:5]
	v_mfma_f32_16x16x32_f16 v[100:103], v[204:207], v[180:183], v[100:103]
	s_waitcnt lgkmcnt(8)
	v_mfma_f32_16x16x32_f16 v[104:107], v[192:195], v[184:187], v[104:107]
	v_mfma_f32_16x16x32_f16 v[108:111], v[196:199], v[184:187], v[108:111]
	v_mfma_f32_16x16x32_f16 v[112:115], v[200:203], v[184:187], v[112:115]
	v_mfma_f32_16x16x32_f16 v[116:119], v[204:207], v[184:187], v[116:119]
	s_waitcnt lgkmcnt(7)
	ds_read_b128 v[172:175], v16 offset:53248
	ds_read_b128 v[192:195], v18 offset:53248
	ds_read_b128 v[196:199], v18 offset:55296
	ds_read_b128 v[200:203], v18 offset:57344
	ds_read_b128 v[204:207], v18 offset:59392
	ds_read_b128 v[176:179], v16 offset:55296
	ds_read_b128 v[180:183], v16 offset:57344
	ds_read_b128 v[184:187], v16 offset:59392
	s_waitcnt lgkmcnt(14)
	v_mfma_f32_16x16x32_f16 v[56:59], v[156:159], v[136:139], v[56:59]
	s_add_u32 m0, s28, 0x6000
	s_nop 0
	global_load_lds_dwordx4 v13, s[4:5]
	s_add_u32 s4, s4, s20
	s_addc_u32 s5, s5, 0
	s_waitcnt lgkmcnt(13)
	v_mfma_f32_16x16x32_f16 v[60:63], v[160:163], v[136:139], v[60:63]
	s_waitcnt lgkmcnt(12)
	v_mfma_f32_16x16x32_f16 v[64:67], v[164:167], v[136:139], v[64:67]
	s_waitcnt lgkmcnt(11)
	v_mfma_f32_16x16x32_f16 v[68:71], v[168:171], v[136:139], v[68:71]
	s_waitcnt lgkmcnt(10)
	v_mfma_f32_16x16x32_f16 v[72:75], v[156:159], v[140:143], v[72:75]
	v_mfma_f32_16x16x32_f16 v[76:79], v[160:163], v[140:143], v[76:79]
	s_add_u32 m0, s28, 0x9000
	s_nop 0
	global_load_lds_dwordx4 v10, s[6:7]
	v_mfma_f32_16x16x32_f16 v[80:83], v[164:167], v[140:143], v[80:83]
	v_mfma_f32_16x16x32_f16 v[84:87], v[168:171], v[140:143], v[84:87]
	s_waitcnt lgkmcnt(9)
	v_mfma_f32_16x16x32_f16 v[88:91], v[156:159], v[144:147], v[88:91]
	v_mfma_f32_16x16x32_f16 v[92:95], v[160:163], v[144:147], v[92:95]
	v_mfma_f32_16x16x32_f16 v[96:99], v[164:167], v[144:147], v[96:99]
	s_add_u32 m0, s28, 0xb000
	s_nop 0
	global_load_lds_dwordx4 v11, s[6:7]
	s_add_u32 s6, s6, s20
	s_addc_u32 s7, s7, 0
	v_mfma_f32_16x16x32_f16 v[100:103], v[168:171], v[144:147], v[100:103]
	s_waitcnt lgkmcnt(8)
	v_mfma_f32_16x16x32_f16 v[104:107], v[156:159], v[148:151], v[104:107]
	v_mfma_f32_16x16x32_f16 v[108:111], v[160:163], v[148:151], v[108:111]
	v_mfma_f32_16x16x32_f16 v[112:115], v[164:167], v[148:151], v[112:115]
	v_mfma_f32_16x16x32_f16 v[116:119], v[168:171], v[148:151], v[116:119]
	s_waitcnt vmcnt(6) lgkmcnt(0)
	s_barrier
	s_waitcnt lgkmcnt(7)
	ds_read_b128 v[136:139], v19
	ds_read_b128 v[156:159], v21
	ds_read_b128 v[160:163], v21 offset:2048
	ds_read_b128 v[164:167], v21 offset:4096
	ds_read_b128 v[168:171], v21 offset:6144
	ds_read_b128 v[140:143], v19 offset:2048
	ds_read_b128 v[144:147], v19 offset:4096
	ds_read_b128 v[148:151], v19 offset:6144
	s_waitcnt lgkmcnt(14)
	v_mfma_f32_16x16x32_f16 v[56:59], v[192:195], v[172:175], v[56:59]
	s_add_u32 m0, s28, 0xd000
	s_nop 0
	global_load_lds_dwordx4 v10, s[4:5]
	s_waitcnt lgkmcnt(13)
	v_mfma_f32_16x16x32_f16 v[60:63], v[196:199], v[172:175], v[60:63]
	s_waitcnt lgkmcnt(12)
	v_mfma_f32_16x16x32_f16 v[64:67], v[200:203], v[172:175], v[64:67]
	s_waitcnt lgkmcnt(11)
	v_mfma_f32_16x16x32_f16 v[68:71], v[204:207], v[172:175], v[68:71]
	s_waitcnt lgkmcnt(10)
	v_mfma_f32_16x16x32_f16 v[72:75], v[192:195], v[176:179], v[72:75]
	v_mfma_f32_16x16x32_f16 v[76:79], v[196:199], v[176:179], v[76:79]
	s_add_u32 m0, s28, 0xf000
	s_nop 0
	global_load_lds_dwordx4 v11, s[4:5]
	v_mfma_f32_16x16x32_f16 v[80:83], v[200:203], v[176:179], v[80:83]
	v_mfma_f32_16x16x32_f16 v[84:87], v[204:207], v[176:179], v[84:87]
	s_waitcnt lgkmcnt(9)
	v_mfma_f32_16x16x32_f16 v[88:91], v[192:195], v[180:183], v[88:91]
	v_mfma_f32_16x16x32_f16 v[92:95], v[196:199], v[180:183], v[92:95]
	v_mfma_f32_16x16x32_f16 v[96:99], v[200:203], v[180:183], v[96:99]
	s_add_u32 m0, s28, 0x11000
	s_nop 0
	global_load_lds_dwordx4 v12, s[4:5]
	v_mfma_f32_16x16x32_f16 v[100:103], v[204:207], v[180:183], v[100:103]
	s_waitcnt lgkmcnt(8)
	v_mfma_f32_16x16x32_f16 v[104:107], v[192:195], v[184:187], v[104:107]
	v_mfma_f32_16x16x32_f16 v[108:111], v[196:199], v[184:187], v[108:111]
	v_mfma_f32_16x16x32_f16 v[112:115], v[200:203], v[184:187], v[112:115]
	v_mfma_f32_16x16x32_f16 v[116:119], v[204:207], v[184:187], v[116:119]
	s_waitcnt lgkmcnt(7)
	ds_read_b128 v[172:175], v20
	ds_read_b128 v[192:195], v22
	ds_read_b128 v[196:199], v22 offset:2048
	ds_read_b128 v[200:203], v22 offset:4096
	ds_read_b128 v[204:207], v22 offset:6144
	ds_read_b128 v[176:179], v20 offset:2048
	ds_read_b128 v[180:183], v20 offset:4096
	ds_read_b128 v[184:187], v20 offset:6144
	s_waitcnt lgkmcnt(14)
	v_mfma_f32_16x16x32_f16 v[56:59], v[156:159], v[136:139], v[56:59]
	s_add_u32 m0, s28, 0x13000
	s_nop 0
	global_load_lds_dwordx4 v13, s[4:5]
	s_add_u32 s4, s4, s20
	s_addc_u32 s5, s5, 0
	s_waitcnt lgkmcnt(13)
	v_mfma_f32_16x16x32_f16 v[60:63], v[160:163], v[136:139], v[60:63]
	s_waitcnt lgkmcnt(12)
	v_mfma_f32_16x16x32_f16 v[64:67], v[164:167], v[136:139], v[64:67]
	s_waitcnt lgkmcnt(11)
	v_mfma_f32_16x16x32_f16 v[68:71], v[168:171], v[136:139], v[68:71]
	s_waitcnt lgkmcnt(10)
	v_mfma_f32_16x16x32_f16 v[72:75], v[156:159], v[140:143], v[72:75]
	v_mfma_f32_16x16x32_f16 v[76:79], v[160:163], v[140:143], v[76:79]
	s_add_u32 m0, s28, 0x16000
	s_nop 0
	global_load_lds_dwordx4 v10, s[6:7]
	v_mfma_f32_16x16x32_f16 v[80:83], v[164:167], v[140:143], v[80:83]
	v_mfma_f32_16x16x32_f16 v[84:87], v[168:171], v[140:143], v[84:87]
	s_waitcnt lgkmcnt(9)
	v_mfma_f32_16x16x32_f16 v[88:91], v[156:159], v[144:147], v[88:91]
	v_mfma_f32_16x16x32_f16 v[92:95], v[160:163], v[144:147], v[92:95]
	v_mfma_f32_16x16x32_f16 v[96:99], v[164:167], v[144:147], v[96:99]
	s_add_u32 m0, s28, 0x18000
	s_nop 0
	global_load_lds_dwordx4 v11, s[6:7]
	s_add_u32 s6, s6, s20
	s_addc_u32 s7, s7, 0
	v_mfma_f32_16x16x32_f16 v[100:103], v[168:171], v[144:147], v[100:103]
	s_waitcnt lgkmcnt(8)
	v_mfma_f32_16x16x32_f16 v[104:107], v[156:159], v[148:151], v[104:107]
	v_mfma_f32_16x16x32_f16 v[108:111], v[160:163], v[148:151], v[108:111]
	v_mfma_f32_16x16x32_f16 v[112:115], v[164:167], v[148:151], v[112:115]
	v_mfma_f32_16x16x32_f16 v[116:119], v[168:171], v[148:151], v[116:119]
	s_waitcnt vmcnt(6) lgkmcnt(0)
	s_barrier
	s_waitcnt lgkmcnt(7)
	ds_read_b128 v[136:139], v15
	ds_read_b128 v[156:159], v17
	ds_read_b128 v[160:163], v17 offset:2048
	ds_read_b128 v[164:167], v17 offset:4096
	ds_read_b128 v[168:171], v17 offset:6144
	ds_read_b128 v[140:143], v15 offset:2048
	ds_read_b128 v[144:147], v15 offset:4096
	ds_read_b128 v[148:151], v15 offset:6144
	s_waitcnt lgkmcnt(14)
	v_mfma_f32_16x16x32_f16 v[56:59], v[192:195], v[172:175], v[56:59]
	s_add_u32 m0, s28, 0x1a000
	s_nop 0
	global_load_lds_dwordx4 v10, s[4:5]
	s_waitcnt lgkmcnt(13)
	v_mfma_f32_16x16x32_f16 v[60:63], v[196:199], v[172:175], v[60:63]
	s_waitcnt lgkmcnt(12)
	v_mfma_f32_16x16x32_f16 v[64:67], v[200:203], v[172:175], v[64:67]
	s_waitcnt lgkmcnt(11)
	v_mfma_f32_16x16x32_f16 v[68:71], v[204:207], v[172:175], v[68:71]
	s_waitcnt lgkmcnt(10)
	v_mfma_f32_16x16x32_f16 v[72:75], v[192:195], v[176:179], v[72:75]
	v_mfma_f32_16x16x32_f16 v[76:79], v[196:199], v[176:179], v[76:79]
	s_add_u32 m0, s28, 0x1c000
	s_nop 0
	global_load_lds_dwordx4 v11, s[4:5]
	v_mfma_f32_16x16x32_f16 v[80:83], v[200:203], v[176:179], v[80:83]
	v_mfma_f32_16x16x32_f16 v[84:87], v[204:207], v[176:179], v[84:87]
	s_waitcnt lgkmcnt(9)
	v_mfma_f32_16x16x32_f16 v[88:91], v[192:195], v[180:183], v[88:91]
	v_mfma_f32_16x16x32_f16 v[92:95], v[196:199], v[180:183], v[92:95]
	v_mfma_f32_16x16x32_f16 v[96:99], v[200:203], v[180:183], v[96:99]
	s_add_u32 m0, s28, 0x1e000
	s_nop 0
	global_load_lds_dwordx4 v12, s[4:5]
	v_mfma_f32_16x16x32_f16 v[100:103], v[204:207], v[180:183], v[100:103]
	s_waitcnt lgkmcnt(8)
	v_mfma_f32_16x16x32_f16 v[104:107], v[192:195], v[184:187], v[104:107]
	v_mfma_f32_16x16x32_f16 v[108:111], v[196:199], v[184:187], v[108:111]
	v_mfma_f32_16x16x32_f16 v[112:115], v[200:203], v[184:187], v[112:115]
	v_mfma_f32_16x16x32_f16 v[116:119], v[204:207], v[184:187], v[116:119]
	s_waitcnt lgkmcnt(7)
	ds_read_b128 v[172:175], v16
	ds_read_b128 v[192:195], v18
	ds_read_b128 v[196:199], v18 offset:2048
	ds_read_b128 v[200:203], v18 offset:4096
	ds_read_b128 v[204:207], v18 offset:6144
	ds_read_b128 v[176:179], v16 offset:2048
	ds_read_b128 v[180:183], v16 offset:4096
	ds_read_b128 v[184:187], v16 offset:6144
	s_waitcnt lgkmcnt(14)
	v_mfma_f32_16x16x32_f16 v[56:59], v[156:159], v[136:139], v[56:59]
	s_add_u32 m0, s28, 0x20000
	s_nop 0
	global_load_lds_dwordx4 v13, s[4:5]
	s_add_u32 s4, s4, s20
	s_addc_u32 s5, s5, 0
	s_waitcnt lgkmcnt(13)
	v_mfma_f32_16x16x32_f16 v[60:63], v[160:163], v[136:139], v[60:63]
	s_waitcnt lgkmcnt(12)
	v_mfma_f32_16x16x32_f16 v[64:67], v[164:167], v[136:139], v[64:67]
	s_waitcnt lgkmcnt(11)
	v_mfma_f32_16x16x32_f16 v[68:71], v[168:171], v[136:139], v[68:71]
	s_waitcnt lgkmcnt(10)
	v_mfma_f32_16x16x32_f16 v[72:75], v[156:159], v[140:143], v[72:75]
	v_mfma_f32_16x16x32_f16 v[76:79], v[160:163], v[140:143], v[76:79]
	s_add_u32 m0, s28, 0x23000
	s_nop 0
	global_load_lds_dwordx4 v10, s[6:7]
	v_mfma_f32_16x16x32_f16 v[80:83], v[164:167], v[140:143], v[80:83]
	v_mfma_f32_16x16x32_f16 v[84:87], v[168:171], v[140:143], v[84:87]
	s_waitcnt lgkmcnt(9)
	v_mfma_f32_16x16x32_f16 v[88:91], v[156:159], v[144:147], v[88:91]
	v_mfma_f32_16x16x32_f16 v[92:95], v[160:163], v[144:147], v[92:95]
	v_mfma_f32_16x16x32_f16 v[96:99], v[164:167], v[144:147], v[96:99]
	s_add_u32 m0, s28, 0x25000
	s_nop 0
	global_load_lds_dwordx4 v11, s[6:7]
	s_add_u32 s6, s6, s20
	s_addc_u32 s7, s7, 0
	v_mfma_f32_16x16x32_f16 v[100:103], v[168:171], v[144:147], v[100:103]
	s_waitcnt lgkmcnt(8)
	v_mfma_f32_16x16x32_f16 v[104:107], v[156:159], v[148:151], v[104:107]
	v_mfma_f32_16x16x32_f16 v[108:111], v[160:163], v[148:151], v[108:111]
	v_mfma_f32_16x16x32_f16 v[112:115], v[164:167], v[148:151], v[112:115]
	v_mfma_f32_16x16x32_f16 v[116:119], v[168:171], v[148:151], v[116:119]
	s_waitcnt vmcnt(6) lgkmcnt(0)
	s_barrier
	s_waitcnt lgkmcnt(7)
	ds_read_b128 v[136:139], v15 offset:53248
	ds_read_b128 v[156:159], v17 offset:53248
	ds_read_b128 v[160:163], v17 offset:55296
	ds_read_b128 v[164:167], v17 offset:57344
	ds_read_b128 v[168:171], v17 offset:59392
	ds_read_b128 v[140:143], v15 offset:55296
	ds_read_b128 v[144:147], v15 offset:57344
	ds_read_b128 v[148:151], v15 offset:59392
	s_waitcnt lgkmcnt(14)
	v_mfma_f32_16x16x32_f16 v[56:59], v[192:195], v[172:175], v[56:59]
	s_add_u32 m0, s28, 0x0
	s_nop 0
	global_load_lds_dwordx4 v10, s[4:5]
	s_waitcnt lgkmcnt(13)
	v_mfma_f32_16x16x32_f16 v[60:63], v[196:199], v[172:175], v[60:63]
	s_waitcnt lgkmcnt(12)
	v_mfma_f32_16x16x32_f16 v[64:67], v[200:203], v[172:175], v[64:67]
	s_waitcnt lgkmcnt(11)
	v_mfma_f32_16x16x32_f16 v[68:71], v[204:207], v[172:175], v[68:71]
	s_waitcnt lgkmcnt(10)
	v_mfma_f32_16x16x32_f16 v[72:75], v[192:195], v[176:179], v[72:75]
	v_mfma_f32_16x16x32_f16 v[76:79], v[196:199], v[176:179], v[76:79]
	s_add_u32 m0, s28, 0x2000
	s_nop 0
	global_load_lds_dwordx4 v11, s[4:5]
	v_mfma_f32_16x16x32_f16 v[80:83], v[200:203], v[176:179], v[80:83]
	v_mfma_f32_16x16x32_f16 v[84:87], v[204:207], v[176:179], v[84:87]
	s_waitcnt lgkmcnt(9)
	v_mfma_f32_16x16x32_f16 v[88:91], v[192:195], v[180:183], v[88:91]
	v_mfma_f32_16x16x32_f16 v[92:95], v[196:199], v[180:183], v[92:95]
	v_mfma_f32_16x16x32_f16 v[96:99], v[200:203], v[180:183], v[96:99]
	s_add_u32 m0, s28, 0x4000
	s_nop 0
	global_load_lds_dwordx4 v12, s[4:5]
	v_mfma_f32_16x16x32_f16 v[100:103], v[204:207], v[180:183], v[100:103]
	s_waitcnt lgkmcnt(8)
	v_mfma_f32_16x16x32_f16 v[104:107], v[192:195], v[184:187], v[104:107]
	v_mfma_f32_16x16x32_f16 v[108:111], v[196:199], v[184:187], v[108:111]
	v_mfma_f32_16x16x32_f16 v[112:115], v[200:203], v[184:187], v[112:115]
	v_mfma_f32_16x16x32_f16 v[116:119], v[204:207], v[184:187], v[116:119]
	s_waitcnt lgkmcnt(7)
	ds_read_b128 v[172:175], v16 offset:53248
	ds_read_b128 v[192:195], v18 offset:53248
	ds_read_b128 v[196:199], v18 offset:55296
	ds_read_b128 v[200:203], v18 offset:57344
	ds_read_b128 v[204:207], v18 offset:59392
	ds_read_b128 v[176:179], v16 offset:55296
	ds_read_b128 v[180:183], v16 offset:57344
	ds_read_b128 v[184:187], v16 offset:59392
	s_waitcnt lgkmcnt(14)
	v_mfma_f32_16x16x32_f16 v[56:59], v[156:159], v[136:139], v[56:59]
	s_add_u32 m0, s28, 0x6000
	s_nop 0
	global_load_lds_dwordx4 v13, s[4:5]
	s_add_u32 s4, s4, s20
	s_addc_u32 s5, s5, 0
	s_waitcnt lgkmcnt(13)
	v_mfma_f32_16x16x32_f16 v[60:63], v[160:163], v[136:139], v[60:63]
	s_waitcnt lgkmcnt(12)
	v_mfma_f32_16x16x32_f16 v[64:67], v[164:167], v[136:139], v[64:67]
	s_waitcnt lgkmcnt(11)
	v_mfma_f32_16x16x32_f16 v[68:71], v[168:171], v[136:139], v[68:71]
	s_waitcnt lgkmcnt(10)
	v_mfma_f32_16x16x32_f16 v[72:75], v[156:159], v[140:143], v[72:75]
	v_mfma_f32_16x16x32_f16 v[76:79], v[160:163], v[140:143], v[76:79]
	s_add_u32 m0, s28, 0x9000
	s_nop 0
	global_load_lds_dwordx4 v10, s[6:7]
	v_mfma_f32_16x16x32_f16 v[80:83], v[164:167], v[140:143], v[80:83]
	v_mfma_f32_16x16x32_f16 v[84:87], v[168:171], v[140:143], v[84:87]
	s_waitcnt lgkmcnt(9)
	v_mfma_f32_16x16x32_f16 v[88:91], v[156:159], v[144:147], v[88:91]
	v_mfma_f32_16x16x32_f16 v[92:95], v[160:163], v[144:147], v[92:95]
	v_mfma_f32_16x16x32_f16 v[96:99], v[164:167], v[144:147], v[96:99]
	s_add_u32 m0, s28, 0xb000
	s_nop 0
	global_load_lds_dwordx4 v11, s[6:7]
	s_add_u32 s6, s6, s20
	s_addc_u32 s7, s7, 0
	v_mfma_f32_16x16x32_f16 v[100:103], v[168:171], v[144:147], v[100:103]
	s_waitcnt lgkmcnt(8)
	v_mfma_f32_16x16x32_f16 v[104:107], v[156:159], v[148:151], v[104:107]
	v_mfma_f32_16x16x32_f16 v[108:111], v[160:163], v[148:151], v[108:111]
	v_mfma_f32_16x16x32_f16 v[112:115], v[164:167], v[148:151], v[112:115]
	v_mfma_f32_16x16x32_f16 v[116:119], v[168:171], v[148:151], v[116:119]
	s_waitcnt vmcnt(6) lgkmcnt(0)
	s_barrier
	s_waitcnt lgkmcnt(7)
	ds_read_b128 v[136:139], v19
	ds_read_b128 v[156:159], v21
	ds_read_b128 v[160:163], v21 offset:2048
	ds_read_b128 v[164:167], v21 offset:4096
	ds_read_b128 v[168:171], v21 offset:6144
	ds_read_b128 v[140:143], v19 offset:2048
	ds_read_b128 v[144:147], v19 offset:4096
	ds_read_b128 v[148:151], v19 offset:6144
	s_waitcnt lgkmcnt(14)
	v_mfma_f32_16x16x32_f16 v[56:59], v[192:195], v[172:175], v[56:59]
	s_add_u32 m0, s28, 0xd000
	s_nop 0
	global_load_lds_dwordx4 v10, s[4:5]
	s_waitcnt lgkmcnt(13)
	v_mfma_f32_16x16x32_f16 v[60:63], v[196:199], v[172:175], v[60:63]
	s_waitcnt lgkmcnt(12)
	v_mfma_f32_16x16x32_f16 v[64:67], v[200:203], v[172:175], v[64:67]
	s_waitcnt lgkmcnt(11)
	v_mfma_f32_16x16x32_f16 v[68:71], v[204:207], v[172:175], v[68:71]
	s_waitcnt lgkmcnt(10)
	v_mfma_f32_16x16x32_f16 v[72:75], v[192:195], v[176:179], v[72:75]
	v_mfma_f32_16x16x32_f16 v[76:79], v[196:199], v[176:179], v[76:79]
	s_add_u32 m0, s28, 0xf000
	s_nop 0
	global_load_lds_dwordx4 v11, s[4:5]
	v_mfma_f32_16x16x32_f16 v[80:83], v[200:203], v[176:179], v[80:83]
	v_mfma_f32_16x16x32_f16 v[84:87], v[204:207], v[176:179], v[84:87]
	s_waitcnt lgkmcnt(9)
	v_mfma_f32_16x16x32_f16 v[88:91], v[192:195], v[180:183], v[88:91]
	v_mfma_f32_16x16x32_f16 v[92:95], v[196:199], v[180:183], v[92:95]
	v_mfma_f32_16x16x32_f16 v[96:99], v[200:203], v[180:183], v[96:99]
	s_add_u32 m0, s28, 0x11000
	s_nop 0
	global_load_lds_dwordx4 v12, s[4:5]
	v_mfma_f32_16x16x32_f16 v[100:103], v[204:207], v[180:183], v[100:103]
	s_waitcnt lgkmcnt(8)
	v_mfma_f32_16x16x32_f16 v[104:107], v[192:195], v[184:187], v[104:107]
	v_mfma_f32_16x16x32_f16 v[108:111], v[196:199], v[184:187], v[108:111]
	v_mfma_f32_16x16x32_f16 v[112:115], v[200:203], v[184:187], v[112:115]
	v_mfma_f32_16x16x32_f16 v[116:119], v[204:207], v[184:187], v[116:119]
	s_waitcnt lgkmcnt(7)
	ds_read_b128 v[172:175], v20
	ds_read_b128 v[192:195], v22
	ds_read_b128 v[196:199], v22 offset:2048
	ds_read_b128 v[200:203], v22 offset:4096
	ds_read_b128 v[204:207], v22 offset:6144
	ds_read_b128 v[176:179], v20 offset:2048
	ds_read_b128 v[180:183], v20 offset:4096
	ds_read_b128 v[184:187], v20 offset:6144
	s_waitcnt lgkmcnt(14)
	v_mfma_f32_16x16x32_f16 v[56:59], v[156:159], v[136:139], v[56:59]
	s_add_u32 m0, s28, 0x13000
	s_nop 0
	global_load_lds_dwordx4 v13, s[4:5]
	s_add_u32 s4, s4, s20
	s_addc_u32 s5, s5, 0
	s_waitcnt lgkmcnt(13)
	v_mfma_f32_16x16x32_f16 v[60:63], v[160:163], v[136:139], v[60:63]
	s_waitcnt lgkmcnt(12)
	v_mfma_f32_16x16x32_f16 v[64:67], v[164:167], v[136:139], v[64:67]
	s_waitcnt lgkmcnt(11)
	v_mfma_f32_16x16x32_f16 v[68:71], v[168:171], v[136:139], v[68:71]
	s_waitcnt lgkmcnt(10)
	v_mfma_f32_16x16x32_f16 v[72:75], v[156:159], v[140:143], v[72:75]
	v_mfma_f32_16x16x32_f16 v[76:79], v[160:163], v[140:143], v[76:79]
	s_add_u32 m0, s28, 0x16000
	s_nop 0
	global_load_lds_dwordx4 v10, s[6:7]
	v_mfma_f32_16x16x32_f16 v[80:83], v[164:167], v[140:143], v[80:83]
	v_mfma_f32_16x16x32_f16 v[84:87], v[168:171], v[140:143], v[84:87]
	s_waitcnt lgkmcnt(9)
	v_mfma_f32_16x16x32_f16 v[88:91], v[156:159], v[144:147], v[88:91]
	v_mfma_f32_16x16x32_f16 v[92:95], v[160:163], v[144:147], v[92:95]
	v_mfma_f32_16x16x32_f16 v[96:99], v[164:167], v[144:147], v[96:99]
	s_add_u32 m0, s28, 0x18000
	s_nop 0
	global_load_lds_dwordx4 v11, s[6:7]
	s_add_u32 s6, s6, s20
	s_addc_u32 s7, s7, 0
	v_mfma_f32_16x16x32_f16 v[100:103], v[168:171], v[144:147], v[100:103]
	s_waitcnt lgkmcnt(8)
	v_mfma_f32_16x16x32_f16 v[104:107], v[156:159], v[148:151], v[104:107]
	v_mfma_f32_16x16x32_f16 v[108:111], v[160:163], v[148:151], v[108:111]
	v_mfma_f32_16x16x32_f16 v[112:115], v[164:167], v[148:151], v[112:115]
	v_mfma_f32_16x16x32_f16 v[116:119], v[168:171], v[148:151], v[116:119]
	s_waitcnt vmcnt(6) lgkmcnt(0)
	s_barrier
	s_waitcnt lgkmcnt(7)
	ds_read_b128 v[136:139], v15
	ds_read_b128 v[156:159], v17
	ds_read_b128 v[160:163], v17 offset:2048
	ds_read_b128 v[164:167], v17 offset:4096
	ds_read_b128 v[168:171], v17 offset:6144
	ds_read_b128 v[140:143], v15 offset:2048
	ds_read_b128 v[144:147], v15 offset:4096
	ds_read_b128 v[148:151], v15 offset:6144
	s_waitcnt lgkmcnt(14)
	v_mfma_f32_16x16x32_f16 v[56:59], v[192:195], v[172:175], v[56:59]
	s_add_u32 m0, s28, 0x1a000
	s_nop 0
	global_load_lds_dwordx4 v10, s[4:5]
	s_waitcnt lgkmcnt(13)
	v_mfma_f32_16x16x32_f16 v[60:63], v[196:199], v[172:175], v[60:63]
	s_waitcnt lgkmcnt(12)
	v_mfma_f32_16x16x32_f16 v[64:67], v[200:203], v[172:175], v[64:67]
	s_waitcnt lgkmcnt(11)
	v_mfma_f32_16x16x32_f16 v[68:71], v[204:207], v[172:175], v[68:71]
	s_waitcnt lgkmcnt(10)
	v_mfma_f32_16x16x32_f16 v[72:75], v[192:195], v[176:179], v[72:75]
	v_mfma_f32_16x16x32_f16 v[76:79], v[196:199], v[176:179], v[76:79]
	s_add_u32 m0, s28, 0x1c000
	s_nop 0
	global_load_lds_dwordx4 v11, s[4:5]
	v_mfma_f32_16x16x32_f16 v[80:83], v[200:203], v[176:179], v[80:83]
	v_mfma_f32_16x16x32_f16 v[84:87], v[204:207], v[176:179], v[84:87]
	s_waitcnt lgkmcnt(9)
	v_mfma_f32_16x16x32_f16 v[88:91], v[192:195], v[180:183], v[88:91]
	v_mfma_f32_16x16x32_f16 v[92:95], v[196:199], v[180:183], v[92:95]
	v_mfma_f32_16x16x32_f16 v[96:99], v[200:203], v[180:183], v[96:99]
	s_add_u32 m0, s28, 0x1e000
	s_nop 0
	global_load_lds_dwordx4 v12, s[4:5]
	v_mfma_f32_16x16x32_f16 v[100:103], v[204:207], v[180:183], v[100:103]
	s_waitcnt lgkmcnt(8)
	v_mfma_f32_16x16x32_f16 v[104:107], v[192:195], v[184:187], v[104:107]
	v_mfma_f32_16x16x32_f16 v[108:111], v[196:199], v[184:187], v[108:111]
	v_mfma_f32_16x16x32_f16 v[112:115], v[200:203], v[184:187], v[112:115]
	v_mfma_f32_16x16x32_f16 v[116:119], v[204:207], v[184:187], v[116:119]
	s_waitcnt lgkmcnt(7)
	ds_read_b128 v[172:175], v16
	ds_read_b128 v[192:195], v18
	ds_read_b128 v[196:199], v18 offset:2048
	ds_read_b128 v[200:203], v18 offset:4096
	ds_read_b128 v[204:207], v18 offset:6144
	ds_read_b128 v[176:179], v16 offset:2048
	ds_read_b128 v[180:183], v16 offset:4096
	ds_read_b128 v[184:187], v16 offset:6144
	s_waitcnt lgkmcnt(14)
	v_mfma_f32_16x16x32_f16 v[56:59], v[156:159], v[136:139], v[56:59]
	s_add_u32 m0, s28, 0x20000
	s_nop 0
	global_load_lds_dwordx4 v13, s[4:5]
	s_add_u32 s4, s4, s20
	s_addc_u32 s5, s5, 0
	s_waitcnt lgkmcnt(13)
	v_mfma_f32_16x16x32_f16 v[60:63], v[160:163], v[136:139], v[60:63]
	s_waitcnt lgkmcnt(12)
	v_mfma_f32_16x16x32_f16 v[64:67], v[164:167], v[136:139], v[64:67]
	s_waitcnt lgkmcnt(11)
	v_mfma_f32_16x16x32_f16 v[68:71], v[168:171], v[136:139], v[68:71]
	s_waitcnt lgkmcnt(10)
	v_mfma_f32_16x16x32_f16 v[72:75], v[156:159], v[140:143], v[72:75]
	v_mfma_f32_16x16x32_f16 v[76:79], v[160:163], v[140:143], v[76:79]
	s_add_u32 m0, s28, 0x23000
	s_nop 0
	global_load_lds_dwordx4 v10, s[6:7]
	v_mfma_f32_16x16x32_f16 v[80:83], v[164:167], v[140:143], v[80:83]
	v_mfma_f32_16x16x32_f16 v[84:87], v[168:171], v[140:143], v[84:87]
	s_waitcnt lgkmcnt(9)
	v_mfma_f32_16x16x32_f16 v[88:91], v[156:159], v[144:147], v[88:91]
	v_mfma_f32_16x16x32_f16 v[92:95], v[160:163], v[144:147], v[92:95]
	v_mfma_f32_16x16x32_f16 v[96:99], v[164:167], v[144:147], v[96:99]
	s_add_u32 m0, s28, 0x25000
	s_nop 0
	global_load_lds_dwordx4 v11, s[6:7]
	s_add_u32 s6, s6, s20
	s_addc_u32 s7, s7, 0
	v_mfma_f32_16x16x32_f16 v[100:103], v[168:171], v[144:147], v[100:103]
	s_waitcnt lgkmcnt(8)
	v_mfma_f32_16x16x32_f16 v[104:107], v[156:159], v[148:151], v[104:107]
	v_mfma_f32_16x16x32_f16 v[108:111], v[160:163], v[148:151], v[108:111]
	v_mfma_f32_16x16x32_f16 v[112:115], v[164:167], v[148:151], v[112:115]
	v_mfma_f32_16x16x32_f16 v[116:119], v[168:171], v[148:151], v[116:119]
	s_waitcnt vmcnt(6) lgkmcnt(0)
	s_barrier
	s_waitcnt lgkmcnt(7)
	ds_read_b128 v[136:139], v15 offset:53248
	ds_read_b128 v[156:159], v17 offset:53248
	ds_read_b128 v[160:163], v17 offset:55296
	ds_read_b128 v[164:167], v17 offset:57344
	ds_read_b128 v[168:171], v17 offset:59392
	ds_read_b128 v[140:143], v15 offset:55296
	ds_read_b128 v[144:147], v15 offset:57344
	ds_read_b128 v[148:151], v15 offset:59392
	s_waitcnt lgkmcnt(14)
	v_mfma_f32_16x16x32_f16 v[56:59], v[192:195], v[172:175], v[56:59]
	s_add_u32 m0, s28, 0x0
	s_nop 0
	global_load_lds_dwordx4 v10, s[4:5]
	s_waitcnt lgkmcnt(13)
	v_mfma_f32_16x16x32_f16 v[60:63], v[196:199], v[172:175], v[60:63]
	s_waitcnt lgkmcnt(12)
	v_mfma_f32_16x16x32_f16 v[64:67], v[200:203], v[172:175], v[64:67]
	s_waitcnt lgkmcnt(11)
	v_mfma_f32_16x16x32_f16 v[68:71], v[204:207], v[172:175], v[68:71]
	s_waitcnt lgkmcnt(10)
	v_mfma_f32_16x16x32_f16 v[72:75], v[192:195], v[176:179], v[72:75]
	v_mfma_f32_16x16x32_f16 v[76:79], v[196:199], v[176:179], v[76:79]
	s_add_u32 m0, s28, 0x2000
	s_nop 0
	global_load_lds_dwordx4 v11, s[4:5]
	v_mfma_f32_16x16x32_f16 v[80:83], v[200:203], v[176:179], v[80:83]
	v_mfma_f32_16x16x32_f16 v[84:87], v[204:207], v[176:179], v[84:87]
	s_waitcnt lgkmcnt(9)
	v_mfma_f32_16x16x32_f16 v[88:91], v[192:195], v[180:183], v[88:91]
	v_mfma_f32_16x16x32_f16 v[92:95], v[196:199], v[180:183], v[92:95]
	v_mfma_f32_16x16x32_f16 v[96:99], v[200:203], v[180:183], v[96:99]
	s_add_u32 m0, s28, 0x4000
	s_nop 0
	global_load_lds_dwordx4 v12, s[4:5]
	v_mfma_f32_16x16x32_f16 v[100:103], v[204:207], v[180:183], v[100:103]
	s_waitcnt lgkmcnt(8)
	v_mfma_f32_16x16x32_f16 v[104:107], v[192:195], v[184:187], v[104:107]
	v_mfma_f32_16x16x32_f16 v[108:111], v[196:199], v[184:187], v[108:111]
	v_mfma_f32_16x16x32_f16 v[112:115], v[200:203], v[184:187], v[112:115]
	v_mfma_f32_16x16x32_f16 v[116:119], v[204:207], v[184:187], v[116:119]
	s_waitcnt lgkmcnt(7)
	ds_read_b128 v[172:175], v16 offset:53248
	ds_read_b128 v[192:195], v18 offset:53248
	ds_read_b128 v[196:199], v18 offset:55296
	ds_read_b128 v[200:203], v18 offset:57344
	ds_read_b128 v[204:207], v18 offset:59392
	ds_read_b128 v[176:179], v16 offset:55296
	ds_read_b128 v[180:183], v16 offset:57344
	ds_read_b128 v[184:187], v16 offset:59392
	s_waitcnt lgkmcnt(14)
	v_mfma_f32_16x16x32_f16 v[56:59], v[156:159], v[136:139], v[56:59]
	s_add_u32 m0, s28, 0x6000
	s_nop 0
	global_load_lds_dwordx4 v13, s[4:5]
	s_add_u32 s4, s4, s20
	s_addc_u32 s5, s5, 0
	s_waitcnt lgkmcnt(13)
	v_mfma_f32_16x16x32_f16 v[60:63], v[160:163], v[136:139], v[60:63]
	s_waitcnt lgkmcnt(12)
	v_mfma_f32_16x16x32_f16 v[64:67], v[164:167], v[136:139], v[64:67]
	s_waitcnt lgkmcnt(11)
	v_mfma_f32_16x16x32_f16 v[68:71], v[168:171], v[136:139], v[68:71]
	s_waitcnt lgkmcnt(10)
	v_mfma_f32_16x16x32_f16 v[72:75], v[156:159], v[140:143], v[72:75]
	v_mfma_f32_16x16x32_f16 v[76:79], v[160:163], v[140:143], v[76:79]
	s_add_u32 m0, s28, 0x9000
	s_nop 0
	global_load_lds_dwordx4 v10, s[6:7]
	v_mfma_f32_16x16x32_f16 v[80:83], v[164:167], v[140:143], v[80:83]
	v_mfma_f32_16x16x32_f16 v[84:87], v[168:171], v[140:143], v[84:87]
	s_waitcnt lgkmcnt(9)
	v_mfma_f32_16x16x32_f16 v[88:91], v[156:159], v[144:147], v[88:91]
	v_mfma_f32_16x16x32_f16 v[92:95], v[160:163], v[144:147], v[92:95]
	v_mfma_f32_16x16x32_f16 v[96:99], v[164:167], v[144:147], v[96:99]
	s_add_u32 m0, s28, 0xb000
	s_nop 0
	global_load_lds_dwordx4 v11, s[6:7]
	s_add_u32 s6, s6, s20
	s_addc_u32 s7, s7, 0
	v_mfma_f32_16x16x32_f16 v[100:103], v[168:171], v[144:147], v[100:103]
	s_waitcnt lgkmcnt(8)
	v_mfma_f32_16x16x32_f16 v[104:107], v[156:159], v[148:151], v[104:107]
	v_mfma_f32_16x16x32_f16 v[108:111], v[160:163], v[148:151], v[108:111]
	v_mfma_f32_16x16x32_f16 v[112:115], v[164:167], v[148:151], v[112:115]
	v_mfma_f32_16x16x32_f16 v[116:119], v[168:171], v[148:151], v[116:119]
	s_waitcnt vmcnt(6) lgkmcnt(0)
	s_barrier
	s_waitcnt lgkmcnt(7)
	ds_read_b128 v[136:139], v19
	ds_read_b128 v[156:159], v21
	ds_read_b128 v[160:163], v21 offset:2048
	ds_read_b128 v[164:167], v21 offset:4096
	ds_read_b128 v[168:171], v21 offset:6144
	ds_read_b128 v[140:143], v19 offset:2048
	ds_read_b128 v[144:147], v19 offset:4096
	ds_read_b128 v[148:151], v19 offset:6144
	s_waitcnt lgkmcnt(14)
	v_mfma_f32_16x16x32_f16 v[56:59], v[192:195], v[172:175], v[56:59]
	s_waitcnt lgkmcnt(13)
	v_mfma_f32_16x16x32_f16 v[60:63], v[196:199], v[172:175], v[60:63]
	s_waitcnt lgkmcnt(12)
	v_mfma_f32_16x16x32_f16 v[64:67], v[200:203], v[172:175], v[64:67]
	s_waitcnt lgkmcnt(11)
	v_mfma_f32_16x16x32_f16 v[68:71], v[204:207], v[172:175], v[68:71]
	s_waitcnt lgkmcnt(10)
	v_mfma_f32_16x16x32_f16 v[72:75], v[192:195], v[176:179], v[72:75]
	v_mfma_f32_16x16x32_f16 v[76:79], v[196:199], v[176:179], v[76:79]
	v_mfma_f32_16x16x32_f16 v[80:83], v[200:203], v[176:179], v[80:83]
	v_mfma_f32_16x16x32_f16 v[84:87], v[204:207], v[176:179], v[84:87]
	s_waitcnt lgkmcnt(9)
	v_mfma_f32_16x16x32_f16 v[88:91], v[192:195], v[180:183], v[88:91]
	v_mfma_f32_16x16x32_f16 v[92:95], v[196:199], v[180:183], v[92:95]
	v_mfma_f32_16x16x32_f16 v[96:99], v[200:203], v[180:183], v[96:99]
	v_mfma_f32_16x16x32_f16 v[100:103], v[204:207], v[180:183], v[100:103]
	s_waitcnt lgkmcnt(8)
	v_mfma_f32_16x16x32_f16 v[104:107], v[192:195], v[184:187], v[104:107]
	v_mfma_f32_16x16x32_f16 v[108:111], v[196:199], v[184:187], v[108:111]
	v_mfma_f32_16x16x32_f16 v[112:115], v[200:203], v[184:187], v[112:115]
	v_mfma_f32_16x16x32_f16 v[116:119], v[204:207], v[184:187], v[116:119]
	s_waitcnt lgkmcnt(7)
	ds_read_b128 v[172:175], v20
	ds_read_b128 v[192:195], v22
	ds_read_b128 v[196:199], v22 offset:2048
	ds_read_b128 v[200:203], v22 offset:4096
	ds_read_b128 v[204:207], v22 offset:6144
	ds_read_b128 v[176:179], v20 offset:2048
	ds_read_b128 v[180:183], v20 offset:4096
	ds_read_b128 v[184:187], v20 offset:6144
	s_waitcnt lgkmcnt(14)
	v_mfma_f32_16x16x32_f16 v[56:59], v[156:159], v[136:139], v[56:59]
	s_waitcnt lgkmcnt(13)
	v_mfma_f32_16x16x32_f16 v[60:63], v[160:163], v[136:139], v[60:63]
	s_waitcnt lgkmcnt(12)
	v_mfma_f32_16x16x32_f16 v[64:67], v[164:167], v[136:139], v[64:67]
	s_waitcnt lgkmcnt(11)
	v_mfma_f32_16x16x32_f16 v[68:71], v[168:171], v[136:139], v[68:71]
	s_waitcnt lgkmcnt(10)
	v_mfma_f32_16x16x32_f16 v[72:75], v[156:159], v[140:143], v[72:75]
	v_mfma_f32_16x16x32_f16 v[76:79], v[160:163], v[140:143], v[76:79]
	v_mfma_f32_16x16x32_f16 v[80:83], v[164:167], v[140:143], v[80:83]
	v_mfma_f32_16x16x32_f16 v[84:87], v[168:171], v[140:143], v[84:87]
	s_waitcnt lgkmcnt(9)
	v_mfma_f32_16x16x32_f16 v[88:91], v[156:159], v[144:147], v[88:91]
	v_mfma_f32_16x16x32_f16 v[92:95], v[160:163], v[144:147], v[92:95]
	v_mfma_f32_16x16x32_f16 v[96:99], v[164:167], v[144:147], v[96:99]
	v_mfma_f32_16x16x32_f16 v[100:103], v[168:171], v[144:147], v[100:103]
	s_waitcnt lgkmcnt(8)
	v_mfma_f32_16x16x32_f16 v[104:107], v[156:159], v[148:151], v[104:107]
	v_mfma_f32_16x16x32_f16 v[108:111], v[160:163], v[148:151], v[108:111]
	v_mfma_f32_16x16x32_f16 v[112:115], v[164:167], v[148:151], v[112:115]
	v_mfma_f32_16x16x32_f16 v[116:119], v[168:171], v[148:151], v[116:119]
	s_waitcnt vmcnt(0) lgkmcnt(0)
	s_barrier
	s_waitcnt lgkmcnt(7)
	ds_read_b128 v[136:139], v15
	ds_read_b128 v[156:159], v17
	ds_read_b128 v[160:163], v17 offset:2048
	ds_read_b128 v[164:167], v17 offset:4096
	ds_read_b128 v[168:171], v17 offset:6144
	ds_read_b128 v[140:143], v15 offset:2048
	ds_read_b128 v[144:147], v15 offset:4096
	ds_read_b128 v[148:151], v15 offset:6144
	s_waitcnt lgkmcnt(14)
	v_mfma_f32_16x16x32_f16 v[56:59], v[192:195], v[172:175], v[56:59]
	s_waitcnt lgkmcnt(13)
	v_mfma_f32_16x16x32_f16 v[60:63], v[196:199], v[172:175], v[60:63]
	s_waitcnt lgkmcnt(12)
	v_mfma_f32_16x16x32_f16 v[64:67], v[200:203], v[172:175], v[64:67]
	s_waitcnt lgkmcnt(11)
	v_mfma_f32_16x16x32_f16 v[68:71], v[204:207], v[172:175], v[68:71]
	s_waitcnt lgkmcnt(10)
	v_mfma_f32_16x16x32_f16 v[72:75], v[192:195], v[176:179], v[72:75]
	v_mfma_f32_16x16x32_f16 v[76:79], v[196:199], v[176:179], v[76:79]
	v_mfma_f32_16x16x32_f16 v[80:83], v[200:203], v[176:179], v[80:83]
	v_mfma_f32_16x16x32_f16 v[84:87], v[204:207], v[176:179], v[84:87]
	s_waitcnt lgkmcnt(9)
	v_mfma_f32_16x16x32_f16 v[88:91], v[192:195], v[180:183], v[88:91]
	v_mfma_f32_16x16x32_f16 v[92:95], v[196:199], v[180:183], v[92:95]
	v_mfma_f32_16x16x32_f16 v[96:99], v[200:203], v[180:183], v[96:99]
	v_mfma_f32_16x16x32_f16 v[100:103], v[204:207], v[180:183], v[100:103]
	s_waitcnt lgkmcnt(8)
	v_mfma_f32_16x16x32_f16 v[104:107], v[192:195], v[184:187], v[104:107]
	v_mfma_f32_16x16x32_f16 v[108:111], v[196:199], v[184:187], v[108:111]
	v_mfma_f32_16x16x32_f16 v[112:115], v[200:203], v[184:187], v[112:115]
	v_mfma_f32_16x16x32_f16 v[116:119], v[204:207], v[184:187], v[116:119]
	s_waitcnt lgkmcnt(7)
	ds_read_b128 v[172:175], v16
	ds_read_b128 v[192:195], v18
	ds_read_b128 v[196:199], v18 offset:2048
	ds_read_b128 v[200:203], v18 offset:4096
	ds_read_b128 v[204:207], v18 offset:6144
	ds_read_b128 v[176:179], v16 offset:2048
	ds_read_b128 v[180:183], v16 offset:4096
	ds_read_b128 v[184:187], v16 offset:6144
	s_waitcnt lgkmcnt(14)
	v_mfma_f32_16x16x32_f16 v[56:59], v[156:159], v[136:139], v[56:59]
	s_waitcnt lgkmcnt(13)
	v_mfma_f32_16x16x32_f16 v[60:63], v[160:163], v[136:139], v[60:63]
	s_waitcnt lgkmcnt(12)
	v_mfma_f32_16x16x32_f16 v[64:67], v[164:167], v[136:139], v[64:67]
	s_waitcnt lgkmcnt(11)
	v_mfma_f32_16x16x32_f16 v[68:71], v[168:171], v[136:139], v[68:71]
	s_waitcnt lgkmcnt(10)
	v_mfma_f32_16x16x32_f16 v[72:75], v[156:159], v[140:143], v[72:75]
	v_mfma_f32_16x16x32_f16 v[76:79], v[160:163], v[140:143], v[76:79]
	v_mfma_f32_16x16x32_f16 v[80:83], v[164:167], v[140:143], v[80:83]
	v_mfma_f32_16x16x32_f16 v[84:87], v[168:171], v[140:143], v[84:87]
	s_waitcnt lgkmcnt(9)
	v_mfma_f32_16x16x32_f16 v[88:91], v[156:159], v[144:147], v[88:91]
	v_mfma_f32_16x16x32_f16 v[92:95], v[160:163], v[144:147], v[92:95]
	v_mfma_f32_16x16x32_f16 v[96:99], v[164:167], v[144:147], v[96:99]
	v_mfma_f32_16x16x32_f16 v[100:103], v[168:171], v[144:147], v[100:103]
	s_waitcnt lgkmcnt(8)
	v_mfma_f32_16x16x32_f16 v[104:107], v[156:159], v[148:151], v[104:107]
	v_mfma_f32_16x16x32_f16 v[108:111], v[160:163], v[148:151], v[108:111]
	v_mfma_f32_16x16x32_f16 v[112:115], v[164:167], v[148:151], v[112:115]
	v_mfma_f32_16x16x32_f16 v[116:119], v[168:171], v[148:151], v[116:119]
	s_waitcnt lgkmcnt(6)
	v_mfma_f32_16x16x32_f16 v[56:59], v[192:195], v[172:175], v[56:59]
	s_waitcnt lgkmcnt(5)
	v_mfma_f32_16x16x32_f16 v[60:63], v[196:199], v[172:175], v[60:63]
	s_waitcnt lgkmcnt(4)
	v_mfma_f32_16x16x32_f16 v[64:67], v[200:203], v[172:175], v[64:67]
	s_waitcnt lgkmcnt(3)
	v_mfma_f32_16x16x32_f16 v[68:71], v[204:207], v[172:175], v[68:71]
	s_waitcnt lgkmcnt(2)
	v_mfma_f32_16x16x32_f16 v[72:75], v[192:195], v[176:179], v[72:75]
	v_mfma_f32_16x16x32_f16 v[76:79], v[196:199], v[176:179], v[76:79]
	v_mfma_f32_16x16x32_f16 v[80:83], v[200:203], v[176:179], v[80:83]
	v_mfma_f32_16x16x32_f16 v[84:87], v[204:207], v[176:179], v[84:87]
	s_waitcnt lgkmcnt(1)
	v_mfma_f32_16x16x32_f16 v[88:91], v[192:195], v[180:183], v[88:91]
	v_mfma_f32_16x16x32_f16 v[92:95], v[196:199], v[180:183], v[92:95]
	v_mfma_f32_16x16x32_f16 v[96:99], v[200:203], v[180:183], v[96:99]
	v_mfma_f32_16x16x32_f16 v[100:103], v[204:207], v[180:183], v[100:103]
	s_waitcnt lgkmcnt(0)
	v_mfma_f32_16x16x32_f16 v[104:107], v[192:195], v[184:187], v[104:107]
	v_mfma_f32_16x16x32_f16 v[108:111], v[196:199], v[184:187], v[108:111]
	v_mfma_f32_16x16x32_f16 v[112:115], v[200:203], v[184:187], v[112:115]
	v_mfma_f32_16x16x32_f16 v[116:119], v[204:207], v[184:187], v[116:119]
	s_nop 7
	s_nop 1
	v_mov_b32_e32 v213, s19
	v_pk_add_f32 v[56:57], v[56:57], v[24:25]
	v_pk_add_f32 v[58:59], v[58:59], v[26:27]
	v_pk_add_f32 v[60:61], v[60:61], v[28:29]
	v_pk_add_f32 v[62:63], v[62:63], v[30:31]
	v_pk_add_f32 v[64:65], v[64:65], v[32:33]
	v_pk_add_f32 v[66:67], v[66:67], v[34:35]
	v_pk_add_f32 v[68:69], v[68:69], v[36:37]
	v_pk_add_f32 v[70:71], v[70:71], v[38:39]
	v_pk_mul_f32 v[208:209], v[56:57], v[56:57]
	v_pk_fma_f32 v[208:209], v[58:59], v[58:59], v[208:209]
	v_pk_fma_f32 v[208:209], v[60:61], v[60:61], v[208:209]
	v_pk_fma_f32 v[208:209], v[62:63], v[62:63], v[208:209]
	v_pk_fma_f32 v[208:209], v[64:65], v[64:65], v[208:209]
	v_pk_fma_f32 v[208:209], v[66:67], v[66:67], v[208:209]
	v_pk_fma_f32 v[208:209], v[68:69], v[68:69], v[208:209]
	v_pk_fma_f32 v[208:209], v[70:71], v[70:71], v[208:209]
	v_add_f32_e32 v208, v208, v209
	v_mov_b32_e32 v209, v208
	s_nop 1
	v_permlane16_swap_b32_e32 v208, v209
	v_add_f32_e32 v208, v208, v209
	v_mov_b32_e32 v209, v208
	s_nop 1
	v_permlane32_swap_b32_e32 v208, v209
	v_add_f32_e32 v208, v208, v209
	v_mov_b32_e32 v210, 0x358637bd
	v_fmac_f32_e32 v210, 0x3c800000, v208
	v_rsq_f32_e32 v210, v210
	s_add_u32 s24, s29, 0
	s_lshr_b32 s8, s24, 1
	s_lshl_b32 s8, s8, 12
	s_and_b32 s24, s24, 1
	s_lshl_b32 s24, s24, 8
	s_add_u32 s8, s8, s24
	v_mul_f32_e32 v210, v213, v210
	v_add_u32_e32 v212, s8, v23
	v_pk_mul_f32 v[56:57], v[56:57], v[210:211] op_sel_hi:[1,0]
	v_pk_mul_f32 v[58:59], v[58:59], v[210:211] op_sel_hi:[1,0]
	v_pk_mul_f32 v[56:57], v[56:57], v[40:41]
	v_pk_mul_f32 v[58:59], v[58:59], v[42:43]
	v_cvt_pk_f16_f32 v56, v56, v57
	v_cvt_pk_f16_f32 v57, v58, v59
	global_store_dwordx2 v212, v[56:57], s[22:23] offset:0 sc0 sc1
	v_pk_mul_f32 v[60:61], v[60:61], v[210:211] op_sel_hi:[1,0]
	v_pk_mul_f32 v[62:63], v[62:63], v[210:211] op_sel_hi:[1,0]
	v_pk_mul_f32 v[60:61], v[60:61], v[44:45]
	v_pk_mul_f32 v[62:63], v[62:63], v[46:47]
	v_cvt_pk_f16_f32 v60, v60, v61
	v_cvt_pk_f16_f32 v61, v62, v63
	global_store_dwordx2 v212, v[60:61], s[22:23] offset:1024 sc0 sc1
	v_pk_mul_f32 v[64:65], v[64:65], v[210:211] op_sel_hi:[1,0]
	v_pk_mul_f32 v[66:67], v[66:67], v[210:211] op_sel_hi:[1,0]
	v_pk_mul_f32 v[64:65], v[64:65], v[48:49]
	v_pk_mul_f32 v[66:67], v[66:67], v[50:51]
	v_cvt_pk_f16_f32 v64, v64, v65
	v_cvt_pk_f16_f32 v65, v66, v67
	global_store_dwordx2 v212, v[64:65], s[22:23] offset:2048 sc0 sc1
	v_pk_mul_f32 v[68:69], v[68:69], v[210:211] op_sel_hi:[1,0]
	v_pk_mul_f32 v[70:71], v[70:71], v[210:211] op_sel_hi:[1,0]
	v_pk_mul_f32 v[68:69], v[68:69], v[52:53]
	v_pk_mul_f32 v[70:71], v[70:71], v[54:55]
	v_cvt_pk_f16_f32 v68, v68, v69
	v_cvt_pk_f16_f32 v69, v70, v71
	global_store_dwordx2 v212, v[68:69], s[22:23] offset:3072 sc0 sc1
	v_pk_add_f32 v[72:73], v[72:73], v[24:25]
	v_pk_add_f32 v[74:75], v[74:75], v[26:27]
	v_pk_add_f32 v[76:77], v[76:77], v[28:29]
	v_pk_add_f32 v[78:79], v[78:79], v[30:31]
	v_pk_add_f32 v[80:81], v[80:81], v[32:33]
	v_pk_add_f32 v[82:83], v[82:83], v[34:35]
	v_pk_add_f32 v[84:85], v[84:85], v[36:37]
	v_pk_add_f32 v[86:87], v[86:87], v[38:39]
	v_pk_mul_f32 v[208:209], v[72:73], v[72:73]
	v_pk_fma_f32 v[208:209], v[74:75], v[74:75], v[208:209]
	v_pk_fma_f32 v[208:209], v[76:77], v[76:77], v[208:209]
	v_pk_fma_f32 v[208:209], v[78:79], v[78:79], v[208:209]
	v_pk_fma_f32 v[208:209], v[80:81], v[80:81], v[208:209]
	v_pk_fma_f32 v[208:209], v[82:83], v[82:83], v[208:209]
	v_pk_fma_f32 v[208:209], v[84:85], v[84:85], v[208:209]
	v_pk_fma_f32 v[208:209], v[86:87], v[86:87], v[208:209]
	v_add_f32_e32 v208, v208, v209
	v_mov_b32_e32 v209, v208
	s_nop 1
	v_permlane16_swap_b32_e32 v208, v209
	v_add_f32_e32 v208, v208, v209
	v_mov_b32_e32 v209, v208
	s_nop 1
	v_permlane32_swap_b32_e32 v208, v209
	v_add_f32_e32 v208, v208, v209
	v_mov_b32_e32 v210, 0x358637bd
	v_fmac_f32_e32 v210, 0x3c800000, v208
	v_rsq_f32_e32 v210, v210
	s_add_u32 s24, s29, 1
	s_lshr_b32 s8, s24, 1
	s_lshl_b32 s8, s8, 12
	s_and_b32 s24, s24, 1
	s_lshl_b32 s24, s24, 8
	s_add_u32 s8, s8, s24
	v_mul_f32_e32 v210, v213, v210
	v_add_u32_e32 v212, s8, v23
	v_pk_mul_f32 v[72:73], v[72:73], v[210:211] op_sel_hi:[1,0]
	v_pk_mul_f32 v[74:75], v[74:75], v[210:211] op_sel_hi:[1,0]
	v_pk_mul_f32 v[72:73], v[72:73], v[40:41]
	v_pk_mul_f32 v[74:75], v[74:75], v[42:43]
	v_cvt_pk_f16_f32 v72, v72, v73
	v_cvt_pk_f16_f32 v73, v74, v75
	global_store_dwordx2 v212, v[72:73], s[22:23] offset:0 sc0 sc1
	v_pk_mul_f32 v[76:77], v[76:77], v[210:211] op_sel_hi:[1,0]
	v_pk_mul_f32 v[78:79], v[78:79], v[210:211] op_sel_hi:[1,0]
	v_pk_mul_f32 v[76:77], v[76:77], v[44:45]
	v_pk_mul_f32 v[78:79], v[78:79], v[46:47]
	v_cvt_pk_f16_f32 v76, v76, v77
	v_cvt_pk_f16_f32 v77, v78, v79
	global_store_dwordx2 v212, v[76:77], s[22:23] offset:1024 sc0 sc1
	v_pk_mul_f32 v[80:81], v[80:81], v[210:211] op_sel_hi:[1,0]
	v_pk_mul_f32 v[82:83], v[82:83], v[210:211] op_sel_hi:[1,0]
	v_pk_mul_f32 v[80:81], v[80:81], v[48:49]
	v_pk_mul_f32 v[82:83], v[82:83], v[50:51]
	v_cvt_pk_f16_f32 v80, v80, v81
	v_cvt_pk_f16_f32 v81, v82, v83
	global_store_dwordx2 v212, v[80:81], s[22:23] offset:2048 sc0 sc1
	v_pk_mul_f32 v[84:85], v[84:85], v[210:211] op_sel_hi:[1,0]
	v_pk_mul_f32 v[86:87], v[86:87], v[210:211] op_sel_hi:[1,0]
	v_pk_mul_f32 v[84:85], v[84:85], v[52:53]
	v_pk_mul_f32 v[86:87], v[86:87], v[54:55]
	v_cvt_pk_f16_f32 v84, v84, v85
	v_cvt_pk_f16_f32 v85, v86, v87
	global_store_dwordx2 v212, v[84:85], s[22:23] offset:3072 sc0 sc1
	v_pk_add_f32 v[88:89], v[88:89], v[24:25]
	v_pk_add_f32 v[90:91], v[90:91], v[26:27]
	v_pk_add_f32 v[92:93], v[92:93], v[28:29]
	v_pk_add_f32 v[94:95], v[94:95], v[30:31]
	v_pk_add_f32 v[96:97], v[96:97], v[32:33]
	v_pk_add_f32 v[98:99], v[98:99], v[34:35]
	v_pk_add_f32 v[100:101], v[100:101], v[36:37]
	v_pk_add_f32 v[102:103], v[102:103], v[38:39]
	v_pk_mul_f32 v[208:209], v[88:89], v[88:89]
	v_pk_fma_f32 v[208:209], v[90:91], v[90:91], v[208:209]
	v_pk_fma_f32 v[208:209], v[92:93], v[92:93], v[208:209]
	v_pk_fma_f32 v[208:209], v[94:95], v[94:95], v[208:209]
	v_pk_fma_f32 v[208:209], v[96:97], v[96:97], v[208:209]
	v_pk_fma_f32 v[208:209], v[98:99], v[98:99], v[208:209]
	v_pk_fma_f32 v[208:209], v[100:101], v[100:101], v[208:209]
	v_pk_fma_f32 v[208:209], v[102:103], v[102:103], v[208:209]
	v_add_f32_e32 v208, v208, v209
	v_mov_b32_e32 v209, v208
	s_nop 1
	v_permlane16_swap_b32_e32 v208, v209
	v_add_f32_e32 v208, v208, v209
	v_mov_b32_e32 v209, v208
	s_nop 1
	v_permlane32_swap_b32_e32 v208, v209
	v_add_f32_e32 v208, v208, v209
	v_mov_b32_e32 v210, 0x358637bd
	v_fmac_f32_e32 v210, 0x3c800000, v208
	v_rsq_f32_e32 v210, v210
	s_add_u32 s24, s29, 2
	s_lshr_b32 s8, s24, 1
	s_lshl_b32 s8, s8, 12
	s_and_b32 s24, s24, 1
	s_lshl_b32 s24, s24, 8
	s_add_u32 s8, s8, s24
	v_mul_f32_e32 v210, v213, v210
	v_add_u32_e32 v212, s8, v23
	v_pk_mul_f32 v[88:89], v[88:89], v[210:211] op_sel_hi:[1,0]
	v_pk_mul_f32 v[90:91], v[90:91], v[210:211] op_sel_hi:[1,0]
	v_pk_mul_f32 v[88:89], v[88:89], v[40:41]
	v_pk_mul_f32 v[90:91], v[90:91], v[42:43]
	v_cvt_pk_f16_f32 v88, v88, v89
	v_cvt_pk_f16_f32 v89, v90, v91
	global_store_dwordx2 v212, v[88:89], s[22:23] offset:0 sc0 sc1
	v_pk_mul_f32 v[92:93], v[92:93], v[210:211] op_sel_hi:[1,0]
	v_pk_mul_f32 v[94:95], v[94:95], v[210:211] op_sel_hi:[1,0]
	v_pk_mul_f32 v[92:93], v[92:93], v[44:45]
	v_pk_mul_f32 v[94:95], v[94:95], v[46:47]
	v_cvt_pk_f16_f32 v92, v92, v93
	v_cvt_pk_f16_f32 v93, v94, v95
	global_store_dwordx2 v212, v[92:93], s[22:23] offset:1024 sc0 sc1
	v_pk_mul_f32 v[96:97], v[96:97], v[210:211] op_sel_hi:[1,0]
	v_pk_mul_f32 v[98:99], v[98:99], v[210:211] op_sel_hi:[1,0]
	v_pk_mul_f32 v[96:97], v[96:97], v[48:49]
	v_pk_mul_f32 v[98:99], v[98:99], v[50:51]
	v_cvt_pk_f16_f32 v96, v96, v97
	v_cvt_pk_f16_f32 v97, v98, v99
	global_store_dwordx2 v212, v[96:97], s[22:23] offset:2048 sc0 sc1
	v_pk_mul_f32 v[100:101], v[100:101], v[210:211] op_sel_hi:[1,0]
	v_pk_mul_f32 v[102:103], v[102:103], v[210:211] op_sel_hi:[1,0]
	v_pk_mul_f32 v[100:101], v[100:101], v[52:53]
	v_pk_mul_f32 v[102:103], v[102:103], v[54:55]
	v_cvt_pk_f16_f32 v100, v100, v101
	v_cvt_pk_f16_f32 v101, v102, v103
	global_store_dwordx2 v212, v[100:101], s[22:23] offset:3072 sc0 sc1
	v_pk_add_f32 v[104:105], v[104:105], v[24:25]
	v_pk_add_f32 v[106:107], v[106:107], v[26:27]
	v_pk_add_f32 v[108:109], v[108:109], v[28:29]
	v_pk_add_f32 v[110:111], v[110:111], v[30:31]
	v_pk_add_f32 v[112:113], v[112:113], v[32:33]
	v_pk_add_f32 v[114:115], v[114:115], v[34:35]
	v_pk_add_f32 v[116:117], v[116:117], v[36:37]
	v_pk_add_f32 v[118:119], v[118:119], v[38:39]
	v_pk_mul_f32 v[208:209], v[104:105], v[104:105]
	v_pk_fma_f32 v[208:209], v[106:107], v[106:107], v[208:209]
	v_pk_fma_f32 v[208:209], v[108:109], v[108:109], v[208:209]
	v_pk_fma_f32 v[208:209], v[110:111], v[110:111], v[208:209]
	v_pk_fma_f32 v[208:209], v[112:113], v[112:113], v[208:209]
	v_pk_fma_f32 v[208:209], v[114:115], v[114:115], v[208:209]
	v_pk_fma_f32 v[208:209], v[116:117], v[116:117], v[208:209]
	v_pk_fma_f32 v[208:209], v[118:119], v[118:119], v[208:209]
	v_add_f32_e32 v208, v208, v209
	v_mov_b32_e32 v209, v208
	s_nop 1
	v_permlane16_swap_b32_e32 v208, v209
	v_add_f32_e32 v208, v208, v209
	v_mov_b32_e32 v209, v208
	s_nop 1
	v_permlane32_swap_b32_e32 v208, v209
	v_add_f32_e32 v208, v208, v209
	v_mov_b32_e32 v210, 0x358637bd
	v_fmac_f32_e32 v210, 0x3c800000, v208
	v_rsq_f32_e32 v210, v210
	s_add_u32 s24, s29, 3
	s_lshr_b32 s8, s24, 1
	s_lshl_b32 s8, s8, 12
	s_and_b32 s24, s24, 1
	s_lshl_b32 s24, s24, 8
	s_add_u32 s8, s8, s24
	v_mul_f32_e32 v210, v213, v210
	v_add_u32_e32 v212, s8, v23
	v_pk_mul_f32 v[104:105], v[104:105], v[210:211] op_sel_hi:[1,0]
	v_pk_mul_f32 v[106:107], v[106:107], v[210:211] op_sel_hi:[1,0]
	v_pk_mul_f32 v[104:105], v[104:105], v[40:41]
	v_pk_mul_f32 v[106:107], v[106:107], v[42:43]
	v_cvt_pk_f16_f32 v104, v104, v105
	v_cvt_pk_f16_f32 v105, v106, v107
	global_store_dwordx2 v212, v[104:105], s[22:23] offset:0 sc0 sc1
	v_pk_mul_f32 v[108:109], v[108:109], v[210:211] op_sel_hi:[1,0]
	v_pk_mul_f32 v[110:111], v[110:111], v[210:211] op_sel_hi:[1,0]
	v_pk_mul_f32 v[108:109], v[108:109], v[44:45]
	v_pk_mul_f32 v[110:111], v[110:111], v[46:47]
	v_cvt_pk_f16_f32 v108, v108, v109
	v_cvt_pk_f16_f32 v109, v110, v111
	global_store_dwordx2 v212, v[108:109], s[22:23] offset:1024 sc0 sc1
	v_pk_mul_f32 v[112:113], v[112:113], v[210:211] op_sel_hi:[1,0]
	v_pk_mul_f32 v[114:115], v[114:115], v[210:211] op_sel_hi:[1,0]
	v_pk_mul_f32 v[112:113], v[112:113], v[48:49]
	v_pk_mul_f32 v[114:115], v[114:115], v[50:51]
	v_cvt_pk_f16_f32 v112, v112, v113
	v_cvt_pk_f16_f32 v113, v114, v115
	global_store_dwordx2 v212, v[112:113], s[22:23] offset:2048 sc0 sc1
	v_pk_mul_f32 v[116:117], v[116:117], v[210:211] op_sel_hi:[1,0]
	v_pk_mul_f32 v[118:119], v[118:119], v[210:211] op_sel_hi:[1,0]
	v_pk_mul_f32 v[116:117], v[116:117], v[52:53]
	v_pk_mul_f32 v[118:119], v[118:119], v[54:55]
	v_cvt_pk_f16_f32 v116, v116, v117
	v_cvt_pk_f16_f32 v117, v118, v119
	global_store_dwordx2 v212, v[116:117], s[22:23] offset:3072 sc0 sc1
	s_branch .Lpf_done
.Lpf_vVA:
	s_mul_i32 s25, s25, 0x50
	s_add_u32 s29, s10, s25
	s_lshr_b32 s29, s29, 4
	v_add_u32_e32 v5, s25, v3
	v_lshlrev_b32_e32 v5, 7, v5
	v_add_u32_e32 v15, v5, v6
	v_add_u32_e32 v16, v5, v7
	v_add_u32_e32 v5, 0x9000, v9
	v_add_u32_e32 v17, v5, v6
	v_add_u32_e32 v18, v5, v7
	v_add_u32_e32 v19, 0x1a000, v15
	v_add_u32_e32 v20, 0x1a000, v16
	v_add_u32_e32 v21, 0x1a000, v17
	v_add_u32_e32 v22, 0x1a000, v18
	v_lshlrev_b32_e32 v5, 2, v3
	global_load_dword v24, v5, s[14:15] offset:0
	global_load_dword v26, v5, s[14:15] offset:64
	global_load_dword v28, v5, s[14:15] offset:128
	global_load_dword v30, v5, s[14:15] offset:192
	s_add_u32 m0, s28, 0x0
	s_nop 0
	global_load_lds_dwordx4 v10, s[4:5]
	s_add_u32 m0, s28, 0x2000
	s_nop 0
	global_load_lds_dwordx4 v11, s[4:5]
	s_add_u32 m0, s28, 0x4000
	s_nop 0
	global_load_lds_dwordx4 v12, s[4:5]
	s_add_u32 m0, s28, 0x6000
	s_nop 0
	global_load_lds_dwordx4 v13, s[4:5]
	s_add_u32 m0, s28, 0x8000
	s_nop 0
	global_load_lds_dwordx4 v14, s[4:5]
	s_add_u32 s4, s4, s20
	s_addc_u32 s5, s5, 0
	s_add_u32 m0, s28, 0x9000
	s_nop 0
	global_load_lds_dwordx4 v10, s[6:7]
	s_add_u32 m0, s28, 0xb000
	s_nop 0
	global_load_lds_dwordx4 v11, s[6:7]
	s_add_u32 s6, s6, s20
	s_addc_u32 s7, s7, 0
	s_add_u32 m0, s28, 0xd000
	s_nop 0
	global_load_lds_dwordx4 v10, s[4:5]
	s_add_u32 m0, s28, 0xf000
	s_nop 0
	global_load_lds_dwordx4 v11, s[4:5]
	s_add_u32 m0, s28, 0x11000
	s_nop 0
	global_load_lds_dwordx4 v12, s[4:5]
	s_add_u32 m0, s28, 0x13000
	s_nop 0
	global_load_lds_dwordx4 v13, s[4:5]
	s_add_u32 m0, s28, 0x15000
	s_nop 0
	global_load_lds_dwordx4 v14, s[4:5]
	s_add_u32 s4, s4, s20
	s_addc_u32 s5, s5, 0
	s_add_u32 m0, s28, 0x16000
	s_nop 0
	global_load_lds_dwordx4 v10, s[6:7]
	s_add_u32 m0, s28, 0x18000
	s_nop 0
	global_load_lds_dwordx4 v11, s[6:7]
	s_add_u32 s6, s6, s20
	s_addc_u32 s7, s7, 0
	s_add_u32 m0, s28, 0x1a000
	s_nop 0
	global_load_lds_dwordx4 v10, s[4:5]
	s_add_u32 m0, s28, 0x1c000
	s_nop 0
	global_load_lds_dwordx4 v11, s[4:5]
	s_add_u32 m0, s28, 0x1e000
	s_nop 0
	global_load_lds_dwordx4 v12, s[4:5]
	s_add_u32 m0, s28, 0x20000
	s_nop 0
	global_load_lds_dwordx4 v13, s[4:5]
	s_add_u32 m0, s28, 0x22000
	s_nop 0
	global_load_lds_dwordx4 v14, s[4:5]
	s_add_u32 s4, s4, s20
	s_addc_u32 s5, s5, 0
	s_add_u32 m0, s28, 0x23000
	s_nop 0
	global_load_lds_dwordx4 v10, s[6:7]
	s_add_u32 m0, s28, 0x25000
	s_nop 0
	global_load_lds_dwordx4 v11, s[6:7]
	s_add_u32 s6, s6, s20
	s_addc_u32 s7, s7, 0
	s_waitcnt vmcnt(14) lgkmcnt(0)
	s_barrier
	s_waitcnt lgkmcnt(6)
	ds_read_b128 v[136:139], v15
	ds_read_b128 v[156:159], v17
	ds_read_b128 v[160:163], v17 offset:2048
	ds_read_b128 v[164:167], v17 offset:4096
	ds_read_b128 v[168:171], v17 offset:6144
	ds_read_b128 v[140:143], v15 offset:2048
	ds_read_b128 v[144:147], v15 offset:4096
	ds_read_b128 v[148:151], v15 offset:6144
	ds_read_b128 v[152:155], v15 offset:8192
	s_waitcnt lgkmcnt(6)
	ds_read_b128 v[172:175], v16
	ds_read_b128 v[192:195], v18
	ds_read_b128 v[196:199], v18 offset:2048
	ds_read_b128 v[200:203], v18 offset:4096
	ds_read_b128 v[204:207], v18 offset:6144
	ds_read_b128 v[176:179], v16 offset:2048
	ds_read_b128 v[180:183], v16 offset:4096
	ds_read_b128 v[184:187], v16 offset:6144
	ds_read_b128 v[188:191], v16 offset:8192
	v_mfma_f32_16x16x32_f16 v[56:59], v[136:139], v[156:159], 0
	s_waitcnt lgkmcnt(15)
	v_mfma_f32_16x16x32_f16 v[60:63], v[136:139], v[160:163], 0
	s_waitcnt lgkmcnt(14)
	v_mfma_f32_16x16x32_f16 v[64:67], v[136:139], v[164:167], 0
	s_waitcnt lgkmcnt(13)
	v_mfma_f32_16x16x32_f16 v[68:71], v[136:139], v[168:171], 0
	s_waitcnt lgkmcnt(12)
	v_mfma_f32_16x16x32_f16 v[72:75], v[140:143], v[156:159], 0
	v_mfma_f32_16x16x32_f16 v[76:79], v[140:143], v[160:163], 0
	v_mfma_f32_16x16x32_f16 v[80:83], v[140:143], v[164:167], 0
	v_mfma_f32_16x16x32_f16 v[84:87], v[140:143], v[168:171], 0
	s_waitcnt lgkmcnt(11)
	v_mfma_f32_16x16x32_f16 v[88:91], v[144:147], v[156:159], 0
	v_mfma_f32_16x16x32_f16 v[92:95], v[144:147], v[160:163], 0
	v_mfma_f32_16x16x32_f16 v[96:99], v[144:147], v[164:167], 0
	v_mfma_f32_16x16x32_f16 v[100:103], v[144:147], v[168:171], 0
	s_waitcnt lgkmcnt(10)
	v_mfma_f32_16x16x32_f16 v[104:107], v[148:151], v[156:159], 0
	v_mfma_f32_16x16x32_f16 v[108:111], v[148:151], v[160:163], 0
	v_mfma_f32_16x16x32_f16 v[112:115], v[148:151], v[164:167], 0
	v_mfma_f32_16x16x32_f16 v[116:119], v[148:151], v[168:171], 0
	s_waitcnt lgkmcnt(9)
	v_mfma_f32_16x16x32_f16 v[120:123], v[152:155], v[156:159], 0
	v_mfma_f32_16x16x32_f16 v[124:127], v[152:155], v[160:163], 0
	v_mfma_f32_16x16x32_f16 v[128:131], v[152:155], v[164:167], 0
	v_mfma_f32_16x16x32_f16 v[132:135], v[152:155], v[168:171], 0
	s_waitcnt vmcnt(7) lgkmcnt(0)
	s_barrier
	s_waitcnt lgkmcnt(6)
	ds_read_b128 v[136:139], v15 offset:53248
	ds_read_b128 v[156:159], v17 offset:53248
	ds_read_b128 v[160:163], v17 offset:55296
	ds_read_b128 v[164:167], v17 offset:57344
	ds_read_b128 v[168:171], v17 offset:59392
	ds_read_b128 v[140:143], v15 offset:55296
	ds_read_b128 v[144:147], v15 offset:57344
	ds_read_b128 v[148:151], v15 offset:59392
	ds_read_b128 v[152:155], v15 offset:61440
	v_mfma_f32_16x16x32_f16 v[56:59], v[172:175], v[192:195], v[56:59]
	s_add_u32 m0, s28, 0x0
	s_nop 0
	global_load_lds_dwordx4 v10, s[4:5]
	s_waitcnt lgkmcnt(15)
	v_mfma_f32_16x16x32_f16 v[60:63], v[172:175], v[196:199], v[60:63]
	s_waitcnt lgkmcnt(14)
	v_mfma_f32_16x16x32_f16 v[64:67], v[172:175], v[200:203], v[64:67]
	s_waitcnt lgkmcnt(13)
	v_mfma_f32_16x16x32_f16 v[68:71], v[172:175], v[204:207], v[68:71]
	s_waitcnt lgkmcnt(12)
	v_mfma_f32_16x16x32_f16 v[72:75], v[176:179], v[192:195], v[72:75]
	v_mfma_f32_16x16x32_f16 v[76:79], v[176:179], v[196:199], v[76:79]
	s_add_u32 m0, s28, 0x2000
	s_nop 0
	global_load_lds_dwordx4 v11, s[4:5]
	v_mfma_f32_16x16x32_f16 v[80:83], v[176:179], v[200:203], v[80:83]
	v_mfma_f32_16x16x32_f16 v[84:87], v[176:179], v[204:207], v[84:87]
	s_waitcnt lgkmcnt(11)
	v_mfma_f32_16x16x32_f16 v[88:91], v[180:183], v[192:195], v[88:91]
	v_mfma_f32_16x16x32_f16 v[92:95], v[180:183], v[196:199], v[92:95]
	v_mfma_f32_16x16x32_f16 v[96:99], v[180:183], v[200:203], v[96:99]
	s_add_u32 m0, s28, 0x4000
	s_nop 0
	global_load_lds_dwordx4 v12, s[4:5]
	v_mfma_f32_16x16x32_f16 v[100:103], v[180:183], v[204:207], v[100:103]
	s_waitcnt lgkmcnt(10)
	v_mfma_f32_16x16x32_f16 v[104:107], v[184:187], v[192:195], v[104:107]
	v_mfma_f32_16x16x32_f16 v[108:111], v[184:187], v[196:199], v[108:111]
	v_mfma_f32_16x16x32_f16 v[112:115], v[184:187], v[200:203], v[112:115]
	v_mfma_f32_16x16x32_f16 v[116:119], v[184:187], v[204:207], v[116:119]
	s_add_u32 m0, s28, 0x6000
	s_nop 0
	global_load_lds_dwordx4 v13, s[4:5]
	s_waitcnt lgkmcnt(9)
	v_mfma_f32_16x16x32_f16 v[120:123], v[188:191], v[192:195], v[120:123]
	v_mfma_f32_16x16x32_f16 v[124:127], v[188:191], v[196:199], v[124:127]
	v_mfma_f32_16x16x32_f16 v[128:131], v[188:191], v[200:203], v[128:131]
	v_mfma_f32_16x16x32_f16 v[132:135], v[188:191], v[204:207], v[132:135]
	s_waitcnt lgkmcnt(6)
	ds_read_b128 v[172:175], v16 offset:53248
	ds_read_b128 v[192:195], v18 offset:53248
	ds_read_b128 v[196:199], v18 offset:55296
	ds_read_b128 v[200:203], v18 offset:57344
	ds_read_b128 v[204:207], v18 offset:59392
	ds_read_b128 v[176:179], v16 offset:55296
	ds_read_b128 v[180:183], v16 offset:57344
	ds_read_b128 v[184:187], v16 offset:59392
	ds_read_b128 v[188:191], v16 offset:61440
	v_mfma_f32_16x16x32_f16 v[56:59], v[136:139], v[156:159], v[56:59]
	s_add_u32 m0, s28, 0x8000
	s_nop 0
	global_load_lds_dwordx4 v14, s[4:5]
	s_add_u32 s4, s4, s20
	s_addc_u32 s5, s5, 0
	s_waitcnt lgkmcnt(15)
	v_mfma_f32_16x16x32_f16 v[60:63], v[136:139], v[160:163], v[60:63]
	s_waitcnt lgkmcnt(14)
	v_mfma_f32_16x16x32_f16 v[64:67], v[136:139], v[164:167], v[64:67]
	s_waitcnt lgkmcnt(13)
	v_mfma_f32_16x16x32_f16 v[68:71], v[136:139], v[168:171], v[68:71]
	s_waitcnt lgkmcnt(12)
	v_mfma_f32_16x16x32_f16 v[72:75], v[140:143], v[156:159], v[72:75]
	v_mfma_f32_16x16x32_f16 v[76:79], v[140:143], v[160:163], v[76:79]
	v_mfma_f32_16x16x32_f16 v[80:83], v[140:143], v[164:167], v[80:83]
	s_add_u32 m0, s28, 0x9000
	s_nop 0
	global_load_lds_dwordx4 v10, s[6:7]
	v_mfma_f32_16x16x32_f16 v[84:87], v[140:143], v[168:171], v[84:87]
	s_waitcnt lgkmcnt(11)
	v_mfma_f32_16x16x32_f16 v[88:91], v[144:147], v[156:159], v[88:91]
	v_mfma_f32_16x16x32_f16 v[92:95], v[144:147], v[160:163], v[92:95]
	v_mfma_f32_16x16x32_f16 v[96:99], v[144:147], v[164:167], v[96:99]
	v_mfma_f32_16x16x32_f16 v[100:103], v[144:147], v[168:171], v[100:103]
	s_waitcnt lgkmcnt(10)
	v_mfma_f32_16x16x32_f16 v[104:107], v[148:151], v[156:159], v[104:107]
	v_mfma_f32_16x16x32_f16 v[108:111], v[148:151], v[160:163], v[108:111]
	s_add_u32 m0, s28, 0xb000
	s_nop 0
	global_load_lds_dwordx4 v11, s[6:7]
	s_add_u32 s6, s6, s20
	s_addc_u32 s7, s7, 0
	v_mfma_f32_16x16x32_f16 v[112:115], v[148:151], v[164:167], v[112:115]
	v_mfma_f32_16x16x32_f16 v[116:119], v[148:151], v[168:171], v[116:119]
	s_waitcnt lgkmcnt(9)
	v_mfma_f32_16x16x32_f16 v[120:123], v[152:155], v[156:159], v[120:123]
	v_mfma_f32_16x16x32_f16 v[124:127], v[152:155], v[160:163], v[124:127]
	v_mfma_f32_16x16x32_f16 v[128:131], v[152:155], v[164:167], v[128:131]
	v_mfma_f32_16x16x32_f16 v[132:135], v[152:155], v[168:171], v[132:135]
	s_waitcnt vmcnt(7) lgkmcnt(0)
	s_barrier
	s_waitcnt lgkmcnt(6)
	ds_read_b128 v[136:139], v19
	ds_read_b128 v[156:159], v21
	ds_read_b128 v[160:163], v21 offset:2048
	ds_read_b128 v[164:167], v21 offset:4096
	ds_read_b128 v[168:171], v21 offset:6144
	ds_read_b128 v[140:143], v19 offset:2048
	ds_read_b128 v[144:147], v19 offset:4096
	ds_read_b128 v[148:151], v19 offset:6144
	ds_read_b128 v[152:155], v19 offset:8192
	v_mfma_f32_16x16x32_f16 v[56:59], v[172:175], v[192:195], v[56:59]
	s_add_u32 m0, s28, 0xd000
	s_nop 0
	global_load_lds_dwordx4 v10, s[4:5]
	s_waitcnt lgkmcnt(15)
	v_mfma_f32_16x16x32_f16 v[60:63], v[172:175], v[196:199], v[60:63]
	s_waitcnt lgkmcnt(14)
	v_mfma_f32_16x16x32_f16 v[64:67], v[172:175], v[200:203], v[64:67]
	s_waitcnt lgkmcnt(13)
	v_mfma_f32_16x16x32_f16 v[68:71], v[172:175], v[204:207], v[68:71]
	s_waitcnt lgkmcnt(12)
	v_mfma_f32_16x16x32_f16 v[72:75], v[176:179], v[192:195], v[72:75]
	v_mfma_f32_16x16x32_f16 v[76:79], v[176:179], v[196:199], v[76:79]
	s_add_u32 m0, s28, 0xf000
	s_nop 0
	global_load_lds_dwordx4 v11, s[4:5]
	v_mfma_f32_16x16x32_f16 v[80:83], v[176:179], v[200:203], v[80:83]
	v_mfma_f32_16x16x32_f16 v[84:87], v[176:179], v[204:207], v[84:87]
	s_waitcnt lgkmcnt(11)
	v_mfma_f32_16x16x32_f16 v[88:91], v[180:183], v[192:195], v[88:91]
	v_mfma_f32_16x16x32_f16 v[92:95], v[180:183], v[196:199], v[92:95]
	v_mfma_f32_16x16x32_f16 v[96:99], v[180:183], v[200:203], v[96:99]
	s_add_u32 m0, s28, 0x11000
	s_nop 0
	global_load_lds_dwordx4 v12, s[4:5]
	v_mfma_f32_16x16x32_f16 v[100:103], v[180:183], v[204:207], v[100:103]
	s_waitcnt lgkmcnt(10)
	v_mfma_f32_16x16x32_f16 v[104:107], v[184:187], v[192:195], v[104:107]
	v_mfma_f32_16x16x32_f16 v[108:111], v[184:187], v[196:199], v[108:111]
	v_mfma_f32_16x16x32_f16 v[112:115], v[184:187], v[200:203], v[112:115]
	v_mfma_f32_16x16x32_f16 v[116:119], v[184:187], v[204:207], v[116:119]
	s_add_u32 m0, s28, 0x13000
	s_nop 0
	global_load_lds_dwordx4 v13, s[4:5]
	s_waitcnt lgkmcnt(9)
	v_mfma_f32_16x16x32_f16 v[120:123], v[188:191], v[192:195], v[120:123]
	v_mfma_f32_16x16x32_f16 v[124:127], v[188:191], v[196:199], v[124:127]
	v_mfma_f32_16x16x32_f16 v[128:131], v[188:191], v[200:203], v[128:131]
	v_mfma_f32_16x16x32_f16 v[132:135], v[188:191], v[204:207], v[132:135]
	s_waitcnt lgkmcnt(6)
	ds_read_b128 v[172:175], v20
	ds_read_b128 v[192:195], v22
	ds_read_b128 v[196:199], v22 offset:2048
	ds_read_b128 v[200:203], v22 offset:4096
	ds_read_b128 v[204:207], v22 offset:6144
	ds_read_b128 v[176:179], v20 offset:2048
	ds_read_b128 v[180:183], v20 offset:4096
	ds_read_b128 v[184:187], v20 offset:6144
	ds_read_b128 v[188:191], v20 offset:8192
	v_mfma_f32_16x16x32_f16 v[56:59], v[136:139], v[156:159], v[56:59]
	s_add_u32 m0, s28, 0x15000
	s_nop 0
	global_load_lds_dwordx4 v14, s[4:5]
	s_add_u32 s4, s4, s20
	s_addc_u32 s5, s5, 0
	s_waitcnt lgkmcnt(15)
	v_mfma_f32_16x16x32_f16 v[60:63], v[136:139], v[160:163], v[60:63]
	s_waitcnt lgkmcnt(14)
	v_mfma_f32_16x16x32_f16 v[64:67], v[136:139], v[164:167], v[64:67]
	s_waitcnt lgkmcnt(13)
	v_mfma_f32_16x16x32_f16 v[68:71], v[136:139], v[168:171], v[68:71]
	s_waitcnt lgkmcnt(12)
	v_mfma_f32_16x16x32_f16 v[72:75], v[140:143], v[156:159], v[72:75]
	v_mfma_f32_16x16x32_f16 v[76:79], v[140:143], v[160:163], v[76:79]
	v_mfma_f32_16x16x32_f16 v[80:83], v[140:143], v[164:167], v[80:83]
	s_add_u32 m0, s28, 0x16000
	s_nop 0
	global_load_lds_dwordx4 v10, s[6:7]
	v_mfma_f32_16x16x32_f16 v[84:87], v[140:143], v[168:171], v[84:87]
	s_waitcnt lgkmcnt(11)
	v_mfma_f32_16x16x32_f16 v[88:91], v[144:147], v[156:159], v[88:91]
	v_mfma_f32_16x16x32_f16 v[92:95], v[144:147], v[160:163], v[92:95]
	v_mfma_f32_16x16x32_f16 v[96:99], v[144:147], v[164:167], v[96:99]
	v_mfma_f32_16x16x32_f16 v[100:103], v[144:147], v[168:171], v[100:103]
	s_waitcnt lgkmcnt(10)
	v_mfma_f32_16x16x32_f16 v[104:107], v[148:151], v[156:159], v[104:107]
	v_mfma_f32_16x16x32_f16 v[108:111], v[148:151], v[160:163], v[108:111]
	s_add_u32 m0, s28, 0x18000
	s_nop 0
	global_load_lds_dwordx4 v11, s[6:7]
	s_add_u32 s6, s6, s20
	s_addc_u32 s7, s7, 0
	v_mfma_f32_16x16x32_f16 v[112:115], v[148:151], v[164:167], v[112:115]
	v_mfma_f32_16x16x32_f16 v[116:119], v[148:151], v[168:171], v[116:119]
	s_waitcnt lgkmcnt(9)
	v_mfma_f32_16x16x32_f16 v[120:123], v[152:155], v[156:159], v[120:123]
	v_mfma_f32_16x16x32_f16 v[124:127], v[152:155], v[160:163], v[124:127]
	v_mfma_f32_16x16x32_f16 v[128:131], v[152:155], v[164:167], v[128:131]
	v_mfma_f32_16x16x32_f16 v[132:135], v[152:155], v[168:171], v[132:135]
	s_waitcnt vmcnt(7) lgkmcnt(0)
	s_barrier
	s_waitcnt lgkmcnt(6)
	ds_read_b128 v[136:139], v15
	ds_read_b128 v[156:159], v17
	ds_read_b128 v[160:163], v17 offset:2048
	ds_read_b128 v[164:167], v17 offset:4096
	ds_read_b128 v[168:171], v17 offset:6144
	ds_read_b128 v[140:143], v15 offset:2048
	ds_read_b128 v[144:147], v15 offset:4096
	ds_read_b128 v[148:151], v15 offset:6144
	ds_read_b128 v[152:155], v15 offset:8192
	v_mfma_f32_16x16x32_f16 v[56:59], v[172:175], v[192:195], v[56:59]
	s_add_u32 m0, s28, 0x1a000
	s_nop 0
	global_load_lds_dwordx4 v10, s[4:5]
	s_waitcnt lgkmcnt(15)
	v_mfma_f32_16x16x32_f16 v[60:63], v[172:175], v[196:199], v[60:63]
	s_waitcnt lgkmcnt(14)
	v_mfma_f32_16x16x32_f16 v[64:67], v[172:175], v[200:203], v[64:67]
	s_waitcnt lgkmcnt(13)
	v_mfma_f32_16x16x32_f16 v[68:71], v[172:175], v[204:207], v[68:71]
	s_waitcnt lgkmcnt(12)
	v_mfma_f32_16x16x32_f16 v[72:75], v[176:179], v[192:195], v[72:75]
	v_mfma_f32_16x16x32_f16 v[76:79], v[176:179], v[196:199], v[76:79]
	s_add_u32 m0, s28, 0x1c000
	s_nop 0
	global_load_lds_dwordx4 v11, s[4:5]
	v_mfma_f32_16x16x32_f16 v[80:83], v[176:179], v[200:203], v[80:83]
	v_mfma_f32_16x16x32_f16 v[84:87], v[176:179], v[204:207], v[84:87]
	s_waitcnt lgkmcnt(11)
	v_mfma_f32_16x16x32_f16 v[88:91], v[180:183], v[192:195], v[88:91]
	v_mfma_f32_16x16x32_f16 v[92:95], v[180:183], v[196:199], v[92:95]
	v_mfma_f32_16x16x32_f16 v[96:99], v[180:183], v[200:203], v[96:99]
	s_add_u32 m0, s28, 0x1e000
	s_nop 0
	global_load_lds_dwordx4 v12, s[4:5]
	v_mfma_f32_16x16x32_f16 v[100:103], v[180:183], v[204:207], v[100:103]
	s_waitcnt lgkmcnt(10)
	v_mfma_f32_16x16x32_f16 v[104:107], v[184:187], v[192:195], v[104:107]
	v_mfma_f32_16x16x32_f16 v[108:111], v[184:187], v[196:199], v[108:111]
	v_mfma_f32_16x16x32_f16 v[112:115], v[184:187], v[200:203], v[112:115]
	v_mfma_f32_16x16x32_f16 v[116:119], v[184:187], v[204:207], v[116:119]
	s_add_u32 m0, s28, 0x20000
	s_nop 0
	global_load_lds_dwordx4 v13, s[4:5]
	s_waitcnt lgkmcnt(9)
	v_mfma_f32_16x16x32_f16 v[120:123], v[188:191], v[192:195], v[120:123]
	v_mfma_f32_16x16x32_f16 v[124:127], v[188:191], v[196:199], v[124:127]
	v_mfma_f32_16x16x32_f16 v[128:131], v[188:191], v[200:203], v[128:131]
	v_mfma_f32_16x16x32_f16 v[132:135], v[188:191], v[204:207], v[132:135]
	s_waitcnt lgkmcnt(6)
	ds_read_b128 v[172:175], v16
	ds_read_b128 v[192:195], v18
	ds_read_b128 v[196:199], v18 offset:2048
	ds_read_b128 v[200:203], v18 offset:4096
	ds_read_b128 v[204:207], v18 offset:6144
	ds_read_b128 v[176:179], v16 offset:2048
	ds_read_b128 v[180:183], v16 offset:4096
	ds_read_b128 v[184:187], v16 offset:6144
	ds_read_b128 v[188:191], v16 offset:8192
	v_mfma_f32_16x16x32_f16 v[56:59], v[136:139], v[156:159], v[56:59]
	s_add_u32 m0, s28, 0x22000
	s_nop 0
	global_load_lds_dwordx4 v14, s[4:5]
	s_add_u32 s4, s4, s20
	s_addc_u32 s5, s5, 0
	s_waitcnt lgkmcnt(15)
	v_mfma_f32_16x16x32_f16 v[60:63], v[136:139], v[160:163], v[60:63]
	s_waitcnt lgkmcnt(14)
	v_mfma_f32_16x16x32_f16 v[64:67], v[136:139], v[164:167], v[64:67]
	s_waitcnt lgkmcnt(13)
	v_mfma_f32_16x16x32_f16 v[68:71], v[136:139], v[168:171], v[68:71]
	s_waitcnt lgkmcnt(12)
	v_mfma_f32_16x16x32_f16 v[72:75], v[140:143], v[156:159], v[72:75]
	v_mfma_f32_16x16x32_f16 v[76:79], v[140:143], v[160:163], v[76:79]
	v_mfma_f32_16x16x32_f16 v[80:83], v[140:143], v[164:167], v[80:83]
	s_add_u32 m0, s28, 0x23000
	s_nop 0
	global_load_lds_dwordx4 v10, s[6:7]
	v_mfma_f32_16x16x32_f16 v[84:87], v[140:143], v[168:171], v[84:87]
	s_waitcnt lgkmcnt(11)
	v_mfma_f32_16x16x32_f16 v[88:91], v[144:147], v[156:159], v[88:91]
	v_mfma_f32_16x16x32_f16 v[92:95], v[144:147], v[160:163], v[92:95]
	v_mfma_f32_16x16x32_f16 v[96:99], v[144:147], v[164:167], v[96:99]
	v_mfma_f32_16x16x32_f16 v[100:103], v[144:147], v[168:171], v[100:103]
	s_waitcnt lgkmcnt(10)
	v_mfma_f32_16x16x32_f16 v[104:107], v[148:151], v[156:159], v[104:107]
	v_mfma_f32_16x16x32_f16 v[108:111], v[148:151], v[160:163], v[108:111]
	s_add_u32 m0, s28, 0x25000
	s_nop 0
	global_load_lds_dwordx4 v11, s[6:7]
	s_add_u32 s6, s6, s20
	s_addc_u32 s7, s7, 0
	v_mfma_f32_16x16x32_f16 v[112:115], v[148:151], v[164:167], v[112:115]
	v_mfma_f32_16x16x32_f16 v[116:119], v[148:151], v[168:171], v[116:119]
	s_waitcnt lgkmcnt(9)
	v_mfma_f32_16x16x32_f16 v[120:123], v[152:155], v[156:159], v[120:123]
	v_mfma_f32_16x16x32_f16 v[124:127], v[152:155], v[160:163], v[124:127]
	v_mfma_f32_16x16x32_f16 v[128:131], v[152:155], v[164:167], v[128:131]
	v_mfma_f32_16x16x32_f16 v[132:135], v[152:155], v[168:171], v[132:135]
	s_waitcnt vmcnt(7) lgkmcnt(0)
	s_barrier
	s_waitcnt lgkmcnt(6)
	ds_read_b128 v[136:139], v15 offset:53248
	ds_read_b128 v[156:159], v17 offset:53248
	ds_read_b128 v[160:163], v17 offset:55296
	ds_read_b128 v[164:167], v17 offset:57344
	ds_read_b128 v[168:171], v17 offset:59392
	ds_read_b128 v[140:143], v15 offset:55296
	ds_read_b128 v[144:147], v15 offset:57344
	ds_read_b128 v[148:151], v15 offset:59392
	ds_read_b128 v[152:155], v15 offset:61440
	v_mfma_f32_16x16x32_f16 v[56:59], v[172:175], v[192:195], v[56:59]
	s_add_u32 m0, s28, 0x0
	s_nop 0
	global_load_lds_dwordx4 v10, s[4:5]
	s_waitcnt lgkmcnt(15)
	v_mfma_f32_16x16x32_f16 v[60:63], v[172:175], v[196:199], v[60:63]
	s_waitcnt lgkmcnt(14)
	v_mfma_f32_16x16x32_f16 v[64:67], v[172:175], v[200:203], v[64:67]
	s_waitcnt lgkmcnt(13)
	v_mfma_f32_16x16x32_f16 v[68:71], v[172:175], v[204:207], v[68:71]
	s_waitcnt lgkmcnt(12)
	v_mfma_f32_16x16x32_f16 v[72:75], v[176:179], v[192:195], v[72:75]
	v_mfma_f32_16x16x32_f16 v[76:79], v[176:179], v[196:199], v[76:79]
	s_add_u32 m0, s28, 0x2000
	s_nop 0
	global_load_lds_dwordx4 v11, s[4:5]
	v_mfma_f32_16x16x32_f16 v[80:83], v[176:179], v[200:203], v[80:83]
	v_mfma_f32_16x16x32_f16 v[84:87], v[176:179], v[204:207], v[84:87]
	s_waitcnt lgkmcnt(11)
	v_mfma_f32_16x16x32_f16 v[88:91], v[180:183], v[192:195], v[88:91]
	v_mfma_f32_16x16x32_f16 v[92:95], v[180:183], v[196:199], v[92:95]
	v_mfma_f32_16x16x32_f16 v[96:99], v[180:183], v[200:203], v[96:99]
	s_add_u32 m0, s28, 0x4000
	s_nop 0
	global_load_lds_dwordx4 v12, s[4:5]
	v_mfma_f32_16x16x32_f16 v[100:103], v[180:183], v[204:207], v[100:103]
	s_waitcnt lgkmcnt(10)
	v_mfma_f32_16x16x32_f16 v[104:107], v[184:187], v[192:195], v[104:107]
	v_mfma_f32_16x16x32_f16 v[108:111], v[184:187], v[196:199], v[108:111]
	v_mfma_f32_16x16x32_f16 v[112:115], v[184:187], v[200:203], v[112:115]
	v_mfma_f32_16x16x32_f16 v[116:119], v[184:187], v[204:207], v[116:119]
	s_add_u32 m0, s28, 0x6000
	s_nop 0
	global_load_lds_dwordx4 v13, s[4:5]
	s_waitcnt lgkmcnt(9)
	v_mfma_f32_16x16x32_f16 v[120:123], v[188:191], v[192:195], v[120:123]
	v_mfma_f32_16x16x32_f16 v[124:127], v[188:191], v[196:199], v[124:127]
	v_mfma_f32_16x16x32_f16 v[128:131], v[188:191], v[200:203], v[128:131]
	v_mfma_f32_16x16x32_f16 v[132:135], v[188:191], v[204:207], v[132:135]
	s_waitcnt lgkmcnt(6)
	ds_read_b128 v[172:175], v16 offset:53248
	ds_read_b128 v[192:195], v18 offset:53248
	ds_read_b128 v[196:199], v18 offset:55296
	ds_read_b128 v[200:203], v18 offset:57344
	ds_read_b128 v[204:207], v18 offset:59392
	ds_read_b128 v[176:179], v16 offset:55296
	ds_read_b128 v[180:183], v16 offset:57344
	ds_read_b128 v[184:187], v16 offset:59392
	ds_read_b128 v[188:191], v16 offset:61440
	v_mfma_f32_16x16x32_f16 v[56:59], v[136:139], v[156:159], v[56:59]
	s_add_u32 m0, s28, 0x8000
	s_nop 0
	global_load_lds_dwordx4 v14, s[4:5]
	s_add_u32 s4, s4, s20
	s_addc_u32 s5, s5, 0
	s_waitcnt lgkmcnt(15)
	v_mfma_f32_16x16x32_f16 v[60:63], v[136:139], v[160:163], v[60:63]
	s_waitcnt lgkmcnt(14)
	v_mfma_f32_16x16x32_f16 v[64:67], v[136:139], v[164:167], v[64:67]
	s_waitcnt lgkmcnt(13)
	v_mfma_f32_16x16x32_f16 v[68:71], v[136:139], v[168:171], v[68:71]
	s_waitcnt lgkmcnt(12)
	v_mfma_f32_16x16x32_f16 v[72:75], v[140:143], v[156:159], v[72:75]
	v_mfma_f32_16x16x32_f16 v[76:79], v[140:143], v[160:163], v[76:79]
	v_mfma_f32_16x16x32_f16 v[80:83], v[140:143], v[164:167], v[80:83]
	s_add_u32 m0, s28, 0x9000
	s_nop 0
	global_load_lds_dwordx4 v10, s[6:7]
	v_mfma_f32_16x16x32_f16 v[84:87], v[140:143], v[168:171], v[84:87]
	s_waitcnt lgkmcnt(11)
	v_mfma_f32_16x16x32_f16 v[88:91], v[144:147], v[156:159], v[88:91]
	v_mfma_f32_16x16x32_f16 v[92:95], v[144:147], v[160:163], v[92:95]
	v_mfma_f32_16x16x32_f16 v[96:99], v[144:147], v[164:167], v[96:99]
	v_mfma_f32_16x16x32_f16 v[100:103], v[144:147], v[168:171], v[100:103]
	s_waitcnt lgkmcnt(10)
	v_mfma_f32_16x16x32_f16 v[104:107], v[148:151], v[156:159], v[104:107]
	v_mfma_f32_16x16x32_f16 v[108:111], v[148:151], v[160:163], v[108:111]
	s_add_u32 m0, s28, 0xb000
	s_nop 0
	global_load_lds_dwordx4 v11, s[6:7]
	s_add_u32 s6, s6, s20
	s_addc_u32 s7, s7, 0
	v_mfma_f32_16x16x32_f16 v[112:115], v[148:151], v[164:167], v[112:115]
	v_mfma_f32_16x16x32_f16 v[116:119], v[148:151], v[168:171], v[116:119]
	s_waitcnt lgkmcnt(9)
	v_mfma_f32_16x16x32_f16 v[120:123], v[152:155], v[156:159], v[120:123]
	v_mfma_f32_16x16x32_f16 v[124:127], v[152:155], v[160:163], v[124:127]
	v_mfma_f32_16x16x32_f16 v[128:131], v[152:155], v[164:167], v[128:131]
	v_mfma_f32_16x16x32_f16 v[132:135], v[152:155], v[168:171], v[132:135]
	s_waitcnt vmcnt(7) lgkmcnt(0)
	s_barrier
	s_waitcnt lgkmcnt(6)
	ds_read_b128 v[136:139], v19
	ds_read_b128 v[156:159], v21
	ds_read_b128 v[160:163], v21 offset:2048
	ds_read_b128 v[164:167], v21 offset:4096
	ds_read_b128 v[168:171], v21 offset:6144
	ds_read_b128 v[140:143], v19 offset:2048
	ds_read_b128 v[144:147], v19 offset:4096
	ds_read_b128 v[148:151], v19 offset:6144
	ds_read_b128 v[152:155], v19 offset:8192
	v_mfma_f32_16x16x32_f16 v[56:59], v[172:175], v[192:195], v[56:59]
	s_add_u32 m0, s28, 0xd000
	s_nop 0
	global_load_lds_dwordx4 v10, s[4:5]
	s_waitcnt lgkmcnt(15)
	v_mfma_f32_16x16x32_f16 v[60:63], v[172:175], v[196:199], v[60:63]
	s_waitcnt lgkmcnt(14)
	v_mfma_f32_16x16x32_f16 v[64:67], v[172:175], v[200:203], v[64:67]
	s_waitcnt lgkmcnt(13)
	v_mfma_f32_16x16x32_f16 v[68:71], v[172:175], v[204:207], v[68:71]
	s_waitcnt lgkmcnt(12)
	v_mfma_f32_16x16x32_f16 v[72:75], v[176:179], v[192:195], v[72:75]
	v_mfma_f32_16x16x32_f16 v[76:79], v[176:179], v[196:199], v[76:79]
	s_add_u32 m0, s28, 0xf000
	s_nop 0
	global_load_lds_dwordx4 v11, s[4:5]
	v_mfma_f32_16x16x32_f16 v[80:83], v[176:179], v[200:203], v[80:83]
	v_mfma_f32_16x16x32_f16 v[84:87], v[176:179], v[204:207], v[84:87]
	s_waitcnt lgkmcnt(11)
	v_mfma_f32_16x16x32_f16 v[88:91], v[180:183], v[192:195], v[88:91]
	v_mfma_f32_16x16x32_f16 v[92:95], v[180:183], v[196:199], v[92:95]
	v_mfma_f32_16x16x32_f16 v[96:99], v[180:183], v[200:203], v[96:99]
	s_add_u32 m0, s28, 0x11000
	s_nop 0
	global_load_lds_dwordx4 v12, s[4:5]
	v_mfma_f32_16x16x32_f16 v[100:103], v[180:183], v[204:207], v[100:103]
	s_waitcnt lgkmcnt(10)
	v_mfma_f32_16x16x32_f16 v[104:107], v[184:187], v[192:195], v[104:107]
	v_mfma_f32_16x16x32_f16 v[108:111], v[184:187], v[196:199], v[108:111]
	v_mfma_f32_16x16x32_f16 v[112:115], v[184:187], v[200:203], v[112:115]
	v_mfma_f32_16x16x32_f16 v[116:119], v[184:187], v[204:207], v[116:119]
	s_add_u32 m0, s28, 0x13000
	s_nop 0
	global_load_lds_dwordx4 v13, s[4:5]
	s_waitcnt lgkmcnt(9)
	v_mfma_f32_16x16x32_f16 v[120:123], v[188:191], v[192:195], v[120:123]
	v_mfma_f32_16x16x32_f16 v[124:127], v[188:191], v[196:199], v[124:127]
	v_mfma_f32_16x16x32_f16 v[128:131], v[188:191], v[200:203], v[128:131]
	v_mfma_f32_16x16x32_f16 v[132:135], v[188:191], v[204:207], v[132:135]
	s_waitcnt lgkmcnt(6)
	ds_read_b128 v[172:175], v20
	ds_read_b128 v[192:195], v22
	ds_read_b128 v[196:199], v22 offset:2048
	ds_read_b128 v[200:203], v22 offset:4096
	ds_read_b128 v[204:207], v22 offset:6144
	ds_read_b128 v[176:179], v20 offset:2048
	ds_read_b128 v[180:183], v20 offset:4096
	ds_read_b128 v[184:187], v20 offset:6144
	ds_read_b128 v[188:191], v20 offset:8192
	v_mfma_f32_16x16x32_f16 v[56:59], v[136:139], v[156:159], v[56:59]
	s_add_u32 m0, s28, 0x15000
	s_nop 0
	global_load_lds_dwordx4 v14, s[4:5]
	s_add_u32 s4, s4, s20
	s_addc_u32 s5, s5, 0
	s_waitcnt lgkmcnt(15)
	v_mfma_f32_16x16x32_f16 v[60:63], v[136:139], v[160:163], v[60:63]
	s_waitcnt lgkmcnt(14)
	v_mfma_f32_16x16x32_f16 v[64:67], v[136:139], v[164:167], v[64:67]
	s_waitcnt lgkmcnt(13)
	v_mfma_f32_16x16x32_f16 v[68:71], v[136:139], v[168:171], v[68:71]
	s_waitcnt lgkmcnt(12)
	v_mfma_f32_16x16x32_f16 v[72:75], v[140:143], v[156:159], v[72:75]
	v_mfma_f32_16x16x32_f16 v[76:79], v[140:143], v[160:163], v[76:79]
	v_mfma_f32_16x16x32_f16 v[80:83], v[140:143], v[164:167], v[80:83]
	s_add_u32 m0, s28, 0x16000
	s_nop 0
	global_load_lds_dwordx4 v10, s[6:7]
	v_mfma_f32_16x16x32_f16 v[84:87], v[140:143], v[168:171], v[84:87]
	s_waitcnt lgkmcnt(11)
	v_mfma_f32_16x16x32_f16 v[88:91], v[144:147], v[156:159], v[88:91]
	v_mfma_f32_16x16x32_f16 v[92:95], v[144:147], v[160:163], v[92:95]
	v_mfma_f32_16x16x32_f16 v[96:99], v[144:147], v[164:167], v[96:99]
	v_mfma_f32_16x16x32_f16 v[100:103], v[144:147], v[168:171], v[100:103]
	s_waitcnt lgkmcnt(10)
	v_mfma_f32_16x16x32_f16 v[104:107], v[148:151], v[156:159], v[104:107]
	v_mfma_f32_16x16x32_f16 v[108:111], v[148:151], v[160:163], v[108:111]
	s_add_u32 m0, s28, 0x18000
	s_nop 0
	global_load_lds_dwordx4 v11, s[6:7]
	s_add_u32 s6, s6, s20
	s_addc_u32 s7, s7, 0
	v_mfma_f32_16x16x32_f16 v[112:115], v[148:151], v[164:167], v[112:115]
	v_mfma_f32_16x16x32_f16 v[116:119], v[148:151], v[168:171], v[116:119]
	s_waitcnt lgkmcnt(9)
	v_mfma_f32_16x16x32_f16 v[120:123], v[152:155], v[156:159], v[120:123]
	v_mfma_f32_16x16x32_f16 v[124:127], v[152:155], v[160:163], v[124:127]
	v_mfma_f32_16x16x32_f16 v[128:131], v[152:155], v[164:167], v[128:131]
	v_mfma_f32_16x16x32_f16 v[132:135], v[152:155], v[168:171], v[132:135]
	s_waitcnt vmcnt(7) lgkmcnt(0)
	s_barrier
	s_waitcnt lgkmcnt(6)
	ds_read_b128 v[136:139], v15
	ds_read_b128 v[156:159], v17
	ds_read_b128 v[160:163], v17 offset:2048
	ds_read_b128 v[164:167], v17 offset:4096
	ds_read_b128 v[168:171], v17 offset:6144
	ds_read_b128 v[140:143], v15 offset:2048
	ds_read_b128 v[144:147], v15 offset:4096
	ds_read_b128 v[148:151], v15 offset:6144
	ds_read_b128 v[152:155], v15 offset:8192
	v_mfma_f32_16x16x32_f16 v[56:59], v[172:175], v[192:195], v[56:59]
	s_add_u32 m0, s28, 0x1a000
	s_nop 0
	global_load_lds_dwordx4 v10, s[4:5]
	s_waitcnt lgkmcnt(15)
	v_mfma_f32_16x16x32_f16 v[60:63], v[172:175], v[196:199], v[60:63]
	s_waitcnt lgkmcnt(14)
	v_mfma_f32_16x16x32_f16 v[64:67], v[172:175], v[200:203], v[64:67]
	s_waitcnt lgkmcnt(13)
	v_mfma_f32_16x16x32_f16 v[68:71], v[172:175], v[204:207], v[68:71]
	s_waitcnt lgkmcnt(12)
	v_mfma_f32_16x16x32_f16 v[72:75], v[176:179], v[192:195], v[72:75]
	v_mfma_f32_16x16x32_f16 v[76:79], v[176:179], v[196:199], v[76:79]
	s_add_u32 m0, s28, 0x1c000
	s_nop 0
	global_load_lds_dwordx4 v11, s[4:5]
	v_mfma_f32_16x16x32_f16 v[80:83], v[176:179], v[200:203], v[80:83]
	v_mfma_f32_16x16x32_f16 v[84:87], v[176:179], v[204:207], v[84:87]
	s_waitcnt lgkmcnt(11)
	v_mfma_f32_16x16x32_f16 v[88:91], v[180:183], v[192:195], v[88:91]
	v_mfma_f32_16x16x32_f16 v[92:95], v[180:183], v[196:199], v[92:95]
	v_mfma_f32_16x16x32_f16 v[96:99], v[180:183], v[200:203], v[96:99]
	s_add_u32 m0, s28, 0x1e000
	s_nop 0
	global_load_lds_dwordx4 v12, s[4:5]
	v_mfma_f32_16x16x32_f16 v[100:103], v[180:183], v[204:207], v[100:103]
	s_waitcnt lgkmcnt(10)
	v_mfma_f32_16x16x32_f16 v[104:107], v[184:187], v[192:195], v[104:107]
	v_mfma_f32_16x16x32_f16 v[108:111], v[184:187], v[196:199], v[108:111]
	v_mfma_f32_16x16x32_f16 v[112:115], v[184:187], v[200:203], v[112:115]
	v_mfma_f32_16x16x32_f16 v[116:119], v[184:187], v[204:207], v[116:119]
	s_add_u32 m0, s28, 0x20000
	s_nop 0
	global_load_lds_dwordx4 v13, s[4:5]
	s_waitcnt lgkmcnt(9)
	v_mfma_f32_16x16x32_f16 v[120:123], v[188:191], v[192:195], v[120:123]
	v_mfma_f32_16x16x32_f16 v[124:127], v[188:191], v[196:199], v[124:127]
	v_mfma_f32_16x16x32_f16 v[128:131], v[188:191], v[200:203], v[128:131]
	v_mfma_f32_16x16x32_f16 v[132:135], v[188:191], v[204:207], v[132:135]
	s_waitcnt lgkmcnt(6)
	ds_read_b128 v[172:175], v16
	ds_read_b128 v[192:195], v18
	ds_read_b128 v[196:199], v18 offset:2048
	ds_read_b128 v[200:203], v18 offset:4096
	ds_read_b128 v[204:207], v18 offset:6144
	ds_read_b128 v[176:179], v16 offset:2048
	ds_read_b128 v[180:183], v16 offset:4096
	ds_read_b128 v[184:187], v16 offset:6144
	ds_read_b128 v[188:191], v16 offset:8192
	v_mfma_f32_16x16x32_f16 v[56:59], v[136:139], v[156:159], v[56:59]
	s_add_u32 m0, s28, 0x22000
	s_nop 0
	global_load_lds_dwordx4 v14, s[4:5]
	s_add_u32 s4, s4, s20
	s_addc_u32 s5, s5, 0
	s_waitcnt lgkmcnt(15)
	v_mfma_f32_16x16x32_f16 v[60:63], v[136:139], v[160:163], v[60:63]
	s_waitcnt lgkmcnt(14)
	v_mfma_f32_16x16x32_f16 v[64:67], v[136:139], v[164:167], v[64:67]
	s_waitcnt lgkmcnt(13)
	v_mfma_f32_16x16x32_f16 v[68:71], v[136:139], v[168:171], v[68:71]
	s_waitcnt lgkmcnt(12)
	v_mfma_f32_16x16x32_f16 v[72:75], v[140:143], v[156:159], v[72:75]
	v_mfma_f32_16x16x32_f16 v[76:79], v[140:143], v[160:163], v[76:79]
	v_mfma_f32_16x16x32_f16 v[80:83], v[140:143], v[164:167], v[80:83]
	s_add_u32 m0, s28, 0x23000
	s_nop 0
	global_load_lds_dwordx4 v10, s[6:7]
	v_mfma_f32_16x16x32_f16 v[84:87], v[140:143], v[168:171], v[84:87]
	s_waitcnt lgkmcnt(11)
	v_mfma_f32_16x16x32_f16 v[88:91], v[144:147], v[156:159], v[88:91]
	v_mfma_f32_16x16x32_f16 v[92:95], v[144:147], v[160:163], v[92:95]
	v_mfma_f32_16x16x32_f16 v[96:99], v[144:147], v[164:167], v[96:99]
	v_mfma_f32_16x16x32_f16 v[100:103], v[144:147], v[168:171], v[100:103]
	s_waitcnt lgkmcnt(10)
	v_mfma_f32_16x16x32_f16 v[104:107], v[148:151], v[156:159], v[104:107]
	v_mfma_f32_16x16x32_f16 v[108:111], v[148:151], v[160:163], v[108:111]
	s_add_u32 m0, s28, 0x25000
	s_nop 0
	global_load_lds_dwordx4 v11, s[6:7]
	s_add_u32 s6, s6, s20
	s_addc_u32 s7, s7, 0
	v_mfma_f32_16x16x32_f16 v[112:115], v[148:151], v[164:167], v[112:115]
	v_mfma_f32_16x16x32_f16 v[116:119], v[148:151], v[168:171], v[116:119]
	s_waitcnt lgkmcnt(9)
	v_mfma_f32_16x16x32_f16 v[120:123], v[152:155], v[156:159], v[120:123]
	v_mfma_f32_16x16x32_f16 v[124:127], v[152:155], v[160:163], v[124:127]
	v_mfma_f32_16x16x32_f16 v[128:131], v[152:155], v[164:167], v[128:131]
	v_mfma_f32_16x16x32_f16 v[132:135], v[152:155], v[168:171], v[132:135]
	s_waitcnt vmcnt(7) lgkmcnt(0)
	s_barrier
	s_waitcnt lgkmcnt(6)
	ds_read_b128 v[136:139], v15 offset:53248
	ds_read_b128 v[156:159], v17 offset:53248
	ds_read_b128 v[160:163], v17 offset:55296
	ds_read_b128 v[164:167], v17 offset:57344
	ds_read_b128 v[168:171], v17 offset:59392
	ds_read_b128 v[140:143], v15 offset:55296
	ds_read_b128 v[144:147], v15 offset:57344
	ds_read_b128 v[148:151], v15 offset:59392
	ds_read_b128 v[152:155], v15 offset:61440
	v_mfma_f32_16x16x32_f16 v[56:59], v[172:175], v[192:195], v[56:59]
	s_add_u32 m0, s28, 0x0
	s_nop 0
	global_load_lds_dwordx4 v10, s[4:5]
	s_waitcnt lgkmcnt(15)
	v_mfma_f32_16x16x32_f16 v[60:63], v[172:175], v[196:199], v[60:63]
	s_waitcnt lgkmcnt(14)
	v_mfma_f32_16x16x32_f16 v[64:67], v[172:175], v[200:203], v[64:67]
	s_waitcnt lgkmcnt(13)
	v_mfma_f32_16x16x32_f16 v[68:71], v[172:175], v[204:207], v[68:71]
	s_waitcnt lgkmcnt(12)
	v_mfma_f32_16x16x32_f16 v[72:75], v[176:179], v[192:195], v[72:75]
	v_mfma_f32_16x16x32_f16 v[76:79], v[176:179], v[196:199], v[76:79]
	s_add_u32 m0, s28, 0x2000
	s_nop 0
	global_load_lds_dwordx4 v11, s[4:5]
	v_mfma_f32_16x16x32_f16 v[80:83], v[176:179], v[200:203], v[80:83]
	v_mfma_f32_16x16x32_f16 v[84:87], v[176:179], v[204:207], v[84:87]
	s_waitcnt lgkmcnt(11)
	v_mfma_f32_16x16x32_f16 v[88:91], v[180:183], v[192:195], v[88:91]
	v_mfma_f32_16x16x32_f16 v[92:95], v[180:183], v[196:199], v[92:95]
	v_mfma_f32_16x16x32_f16 v[96:99], v[180:183], v[200:203], v[96:99]
	s_add_u32 m0, s28, 0x4000
	s_nop 0
	global_load_lds_dwordx4 v12, s[4:5]
	v_mfma_f32_16x16x32_f16 v[100:103], v[180:183], v[204:207], v[100:103]
	s_waitcnt lgkmcnt(10)
	v_mfma_f32_16x16x32_f16 v[104:107], v[184:187], v[192:195], v[104:107]
	v_mfma_f32_16x16x32_f16 v[108:111], v[184:187], v[196:199], v[108:111]
	v_mfma_f32_16x16x32_f16 v[112:115], v[184:187], v[200:203], v[112:115]
	v_mfma_f32_16x16x32_f16 v[116:119], v[184:187], v[204:207], v[116:119]
	s_add_u32 m0, s28, 0x6000
	s_nop 0
	global_load_lds_dwordx4 v13, s[4:5]
	s_waitcnt lgkmcnt(9)
	v_mfma_f32_16x16x32_f16 v[120:123], v[188:191], v[192:195], v[120:123]
	v_mfma_f32_16x16x32_f16 v[124:127], v[188:191], v[196:199], v[124:127]
	v_mfma_f32_16x16x32_f16 v[128:131], v[188:191], v[200:203], v[128:131]
	v_mfma_f32_16x16x32_f16 v[132:135], v[188:191], v[204:207], v[132:135]
	s_waitcnt lgkmcnt(6)
	ds_read_b128 v[172:175], v16 offset:53248
	ds_read_b128 v[192:195], v18 offset:53248
	ds_read_b128 v[196:199], v18 offset:55296
	ds_read_b128 v[200:203], v18 offset:57344
	ds_read_b128 v[204:207], v18 offset:59392
	ds_read_b128 v[176:179], v16 offset:55296
	ds_read_b128 v[180:183], v16 offset:57344
	ds_read_b128 v[184:187], v16 offset:59392
	ds_read_b128 v[188:191], v16 offset:61440
	v_mfma_f32_16x16x32_f16 v[56:59], v[136:139], v[156:159], v[56:59]
	s_add_u32 m0, s28, 0x8000
	s_nop 0
	global_load_lds_dwordx4 v14, s[4:5]
	s_add_u32 s4, s4, s20
	s_addc_u32 s5, s5, 0
	s_waitcnt lgkmcnt(15)
	v_mfma_f32_16x16x32_f16 v[60:63], v[136:139], v[160:163], v[60:63]
	s_waitcnt lgkmcnt(14)
	v_mfma_f32_16x16x32_f16 v[64:67], v[136:139], v[164:167], v[64:67]
	s_waitcnt lgkmcnt(13)
	v_mfma_f32_16x16x32_f16 v[68:71], v[136:139], v[168:171], v[68:71]
	s_waitcnt lgkmcnt(12)
	v_mfma_f32_16x16x32_f16 v[72:75], v[140:143], v[156:159], v[72:75]
	v_mfma_f32_16x16x32_f16 v[76:79], v[140:143], v[160:163], v[76:79]
	v_mfma_f32_16x16x32_f16 v[80:83], v[140:143], v[164:167], v[80:83]
	s_add_u32 m0, s28, 0x9000
	s_nop 0
	global_load_lds_dwordx4 v10, s[6:7]
	v_mfma_f32_16x16x32_f16 v[84:87], v[140:143], v[168:171], v[84:87]
	s_waitcnt lgkmcnt(11)
	v_mfma_f32_16x16x32_f16 v[88:91], v[144:147], v[156:159], v[88:91]
	v_mfma_f32_16x16x32_f16 v[92:95], v[144:147], v[160:163], v[92:95]
	v_mfma_f32_16x16x32_f16 v[96:99], v[144:147], v[164:167], v[96:99]
	v_mfma_f32_16x16x32_f16 v[100:103], v[144:147], v[168:171], v[100:103]
	s_waitcnt lgkmcnt(10)
	v_mfma_f32_16x16x32_f16 v[104:107], v[148:151], v[156:159], v[104:107]
	v_mfma_f32_16x16x32_f16 v[108:111], v[148:151], v[160:163], v[108:111]
	s_add_u32 m0, s28, 0xb000
	s_nop 0
	global_load_lds_dwordx4 v11, s[6:7]
	s_add_u32 s6, s6, s20
	s_addc_u32 s7, s7, 0
	v_mfma_f32_16x16x32_f16 v[112:115], v[148:151], v[164:167], v[112:115]
	v_mfma_f32_16x16x32_f16 v[116:119], v[148:151], v[168:171], v[116:119]
	s_waitcnt lgkmcnt(9)
	v_mfma_f32_16x16x32_f16 v[120:123], v[152:155], v[156:159], v[120:123]
	v_mfma_f32_16x16x32_f16 v[124:127], v[152:155], v[160:163], v[124:127]
	v_mfma_f32_16x16x32_f16 v[128:131], v[152:155], v[164:167], v[128:131]
	v_mfma_f32_16x16x32_f16 v[132:135], v[152:155], v[168:171], v[132:135]
	s_waitcnt vmcnt(7) lgkmcnt(0)
	s_barrier
	s_waitcnt lgkmcnt(6)
	ds_read_b128 v[136:139], v19
	ds_read_b128 v[156:159], v21
	ds_read_b128 v[160:163], v21 offset:2048
	ds_read_b128 v[164:167], v21 offset:4096
	ds_read_b128 v[168:171], v21 offset:6144
	ds_read_b128 v[140:143], v19 offset:2048
	ds_read_b128 v[144:147], v19 offset:4096
	ds_read_b128 v[148:151], v19 offset:6144
	ds_read_b128 v[152:155], v19 offset:8192
	v_mfma_f32_16x16x32_f16 v[56:59], v[172:175], v[192:195], v[56:59]
	s_add_u32 m0, s28, 0xd000
	s_nop 0
	global_load_lds_dwordx4 v10, s[4:5]
	s_waitcnt lgkmcnt(15)
	v_mfma_f32_16x16x32_f16 v[60:63], v[172:175], v[196:199], v[60:63]
	s_waitcnt lgkmcnt(14)
	v_mfma_f32_16x16x32_f16 v[64:67], v[172:175], v[200:203], v[64:67]
	s_waitcnt lgkmcnt(13)
	v_mfma_f32_16x16x32_f16 v[68:71], v[172:175], v[204:207], v[68:71]
	s_waitcnt lgkmcnt(12)
	v_mfma_f32_16x16x32_f16 v[72:75], v[176:179], v[192:195], v[72:75]
	v_mfma_f32_16x16x32_f16 v[76:79], v[176:179], v[196:199], v[76:79]
	s_add_u32 m0, s28, 0xf000
	s_nop 0
	global_load_lds_dwordx4 v11, s[4:5]
	v_mfma_f32_16x16x32_f16 v[80:83], v[176:179], v[200:203], v[80:83]
	v_mfma_f32_16x16x32_f16 v[84:87], v[176:179], v[204:207], v[84:87]
	s_waitcnt lgkmcnt(11)
	v_mfma_f32_16x16x32_f16 v[88:91], v[180:183], v[192:195], v[88:91]
	v_mfma_f32_16x16x32_f16 v[92:95], v[180:183], v[196:199], v[92:95]
	v_mfma_f32_16x16x32_f16 v[96:99], v[180:183], v[200:203], v[96:99]
	s_add_u32 m0, s28, 0x11000
	s_nop 0
	global_load_lds_dwordx4 v12, s[4:5]
	v_mfma_f32_16x16x32_f16 v[100:103], v[180:183], v[204:207], v[100:103]
	s_waitcnt lgkmcnt(10)
	v_mfma_f32_16x16x32_f16 v[104:107], v[184:187], v[192:195], v[104:107]
	v_mfma_f32_16x16x32_f16 v[108:111], v[184:187], v[196:199], v[108:111]
	v_mfma_f32_16x16x32_f16 v[112:115], v[184:187], v[200:203], v[112:115]
	v_mfma_f32_16x16x32_f16 v[116:119], v[184:187], v[204:207], v[116:119]
	s_add_u32 m0, s28, 0x13000
	s_nop 0
	global_load_lds_dwordx4 v13, s[4:5]
	s_waitcnt lgkmcnt(9)
	v_mfma_f32_16x16x32_f16 v[120:123], v[188:191], v[192:195], v[120:123]
	v_mfma_f32_16x16x32_f16 v[124:127], v[188:191], v[196:199], v[124:127]
	v_mfma_f32_16x16x32_f16 v[128:131], v[188:191], v[200:203], v[128:131]
	v_mfma_f32_16x16x32_f16 v[132:135], v[188:191], v[204:207], v[132:135]
	s_waitcnt lgkmcnt(6)
	ds_read_b128 v[172:175], v20
	ds_read_b128 v[192:195], v22
	ds_read_b128 v[196:199], v22 offset:2048
	ds_read_b128 v[200:203], v22 offset:4096
	ds_read_b128 v[204:207], v22 offset:6144
	ds_read_b128 v[176:179], v20 offset:2048
	ds_read_b128 v[180:183], v20 offset:4096
	ds_read_b128 v[184:187], v20 offset:6144
	ds_read_b128 v[188:191], v20 offset:8192
	v_mfma_f32_16x16x32_f16 v[56:59], v[136:139], v[156:159], v[56:59]
	s_add_u32 m0, s28, 0x15000
	s_nop 0
	global_load_lds_dwordx4 v14, s[4:5]
	s_add_u32 s4, s4, s20
	s_addc_u32 s5, s5, 0
	s_waitcnt lgkmcnt(15)
	v_mfma_f32_16x16x32_f16 v[60:63], v[136:139], v[160:163], v[60:63]
	s_waitcnt lgkmcnt(14)
	v_mfma_f32_16x16x32_f16 v[64:67], v[136:139], v[164:167], v[64:67]
	s_waitcnt lgkmcnt(13)
	v_mfma_f32_16x16x32_f16 v[68:71], v[136:139], v[168:171], v[68:71]
	s_waitcnt lgkmcnt(12)
	v_mfma_f32_16x16x32_f16 v[72:75], v[140:143], v[156:159], v[72:75]
	v_mfma_f32_16x16x32_f16 v[76:79], v[140:143], v[160:163], v[76:79]
	v_mfma_f32_16x16x32_f16 v[80:83], v[140:143], v[164:167], v[80:83]
	s_add_u32 m0, s28, 0x16000
	s_nop 0
	global_load_lds_dwordx4 v10, s[6:7]
	v_mfma_f32_16x16x32_f16 v[84:87], v[140:143], v[168:171], v[84:87]
	s_waitcnt lgkmcnt(11)
	v_mfma_f32_16x16x32_f16 v[88:91], v[144:147], v[156:159], v[88:91]
	v_mfma_f32_16x16x32_f16 v[92:95], v[144:147], v[160:163], v[92:95]
	v_mfma_f32_16x16x32_f16 v[96:99], v[144:147], v[164:167], v[96:99]
	v_mfma_f32_16x16x32_f16 v[100:103], v[144:147], v[168:171], v[100:103]
	s_waitcnt lgkmcnt(10)
	v_mfma_f32_16x16x32_f16 v[104:107], v[148:151], v[156:159], v[104:107]
	v_mfma_f32_16x16x32_f16 v[108:111], v[148:151], v[160:163], v[108:111]
	s_add_u32 m0, s28, 0x18000
	s_nop 0
	global_load_lds_dwordx4 v11, s[6:7]
	s_add_u32 s6, s6, s20
	s_addc_u32 s7, s7, 0
	v_mfma_f32_16x16x32_f16 v[112:115], v[148:151], v[164:167], v[112:115]
	v_mfma_f32_16x16x32_f16 v[116:119], v[148:151], v[168:171], v[116:119]
	s_waitcnt lgkmcnt(9)
	v_mfma_f32_16x16x32_f16 v[120:123], v[152:155], v[156:159], v[120:123]
	v_mfma_f32_16x16x32_f16 v[124:127], v[152:155], v[160:163], v[124:127]
	v_mfma_f32_16x16x32_f16 v[128:131], v[152:155], v[164:167], v[128:131]
	v_mfma_f32_16x16x32_f16 v[132:135], v[152:155], v[168:171], v[132:135]
	s_waitcnt vmcnt(7) lgkmcnt(0)
	s_barrier
	s_waitcnt lgkmcnt(6)
	ds_read_b128 v[136:139], v15
	ds_read_b128 v[156:159], v17
	ds_read_b128 v[160:163], v17 offset:2048
	ds_read_b128 v[164:167], v17 offset:4096
	ds_read_b128 v[168:171], v17 offset:6144
	ds_read_b128 v[140:143], v15 offset:2048
	ds_read_b128 v[144:147], v15 offset:4096
	ds_read_b128 v[148:151], v15 offset:6144
	ds_read_b128 v[152:155], v15 offset:8192
	v_mfma_f32_16x16x32_f16 v[56:59], v[172:175], v[192:195], v[56:59]
	s_add_u32 m0, s28, 0x1a000
	s_nop 0
	global_load_lds_dwordx4 v10, s[4:5]
	s_waitcnt lgkmcnt(15)
	v_mfma_f32_16x16x32_f16 v[60:63], v[172:175], v[196:199], v[60:63]
	s_waitcnt lgkmcnt(14)
	v_mfma_f32_16x16x32_f16 v[64:67], v[172:175], v[200:203], v[64:67]
	s_waitcnt lgkmcnt(13)
	v_mfma_f32_16x16x32_f16 v[68:71], v[172:175], v[204:207], v[68:71]
	s_waitcnt lgkmcnt(12)
	v_mfma_f32_16x16x32_f16 v[72:75], v[176:179], v[192:195], v[72:75]
	v_mfma_f32_16x16x32_f16 v[76:79], v[176:179], v[196:199], v[76:79]
	s_add_u32 m0, s28, 0x1c000
	s_nop 0
	global_load_lds_dwordx4 v11, s[4:5]
	v_mfma_f32_16x16x32_f16 v[80:83], v[176:179], v[200:203], v[80:83]
	v_mfma_f32_16x16x32_f16 v[84:87], v[176:179], v[204:207], v[84:87]
	s_waitcnt lgkmcnt(11)
	v_mfma_f32_16x16x32_f16 v[88:91], v[180:183], v[192:195], v[88:91]
	v_mfma_f32_16x16x32_f16 v[92:95], v[180:183], v[196:199], v[92:95]
	v_mfma_f32_16x16x32_f16 v[96:99], v[180:183], v[200:203], v[96:99]
	s_add_u32 m0, s28, 0x1e000
	s_nop 0
	global_load_lds_dwordx4 v12, s[4:5]
	v_mfma_f32_16x16x32_f16 v[100:103], v[180:183], v[204:207], v[100:103]
	s_waitcnt lgkmcnt(10)
	v_mfma_f32_16x16x32_f16 v[104:107], v[184:187], v[192:195], v[104:107]
	v_mfma_f32_16x16x32_f16 v[108:111], v[184:187], v[196:199], v[108:111]
	v_mfma_f32_16x16x32_f16 v[112:115], v[184:187], v[200:203], v[112:115]
	v_mfma_f32_16x16x32_f16 v[116:119], v[184:187], v[204:207], v[116:119]
	s_add_u32 m0, s28, 0x20000
	s_nop 0
	global_load_lds_dwordx4 v13, s[4:5]
	s_waitcnt lgkmcnt(9)
	v_mfma_f32_16x16x32_f16 v[120:123], v[188:191], v[192:195], v[120:123]
	v_mfma_f32_16x16x32_f16 v[124:127], v[188:191], v[196:199], v[124:127]
	v_mfma_f32_16x16x32_f16 v[128:131], v[188:191], v[200:203], v[128:131]
	v_mfma_f32_16x16x32_f16 v[132:135], v[188:191], v[204:207], v[132:135]
	s_waitcnt lgkmcnt(6)
	ds_read_b128 v[172:175], v16
	ds_read_b128 v[192:195], v18
	ds_read_b128 v[196:199], v18 offset:2048
	ds_read_b128 v[200:203], v18 offset:4096
	ds_read_b128 v[204:207], v18 offset:6144
	ds_read_b128 v[176:179], v16 offset:2048
	ds_read_b128 v[180:183], v16 offset:4096
	ds_read_b128 v[184:187], v16 offset:6144
	ds_read_b128 v[188:191], v16 offset:8192
	v_mfma_f32_16x16x32_f16 v[56:59], v[136:139], v[156:159], v[56:59]
	s_add_u32 m0, s28, 0x22000
	s_nop 0
	global_load_lds_dwordx4 v14, s[4:5]
	s_add_u32 s4, s4, s20
	s_addc_u32 s5, s5, 0
	s_waitcnt lgkmcnt(15)
	v_mfma_f32_16x16x32_f16 v[60:63], v[136:139], v[160:163], v[60:63]
	s_waitcnt lgkmcnt(14)
	v_mfma_f32_16x16x32_f16 v[64:67], v[136:139], v[164:167], v[64:67]
	s_waitcnt lgkmcnt(13)
	v_mfma_f32_16x16x32_f16 v[68:71], v[136:139], v[168:171], v[68:71]
	s_waitcnt lgkmcnt(12)
	v_mfma_f32_16x16x32_f16 v[72:75], v[140:143], v[156:159], v[72:75]
	v_mfma_f32_16x16x32_f16 v[76:79], v[140:143], v[160:163], v[76:79]
	v_mfma_f32_16x16x32_f16 v[80:83], v[140:143], v[164:167], v[80:83]
	s_add_u32 m0, s28, 0x23000
	s_nop 0
	global_load_lds_dwordx4 v10, s[6:7]
	v_mfma_f32_16x16x32_f16 v[84:87], v[140:143], v[168:171], v[84:87]
	s_waitcnt lgkmcnt(11)
	v_mfma_f32_16x16x32_f16 v[88:91], v[144:147], v[156:159], v[88:91]
	v_mfma_f32_16x16x32_f16 v[92:95], v[144:147], v[160:163], v[92:95]
	v_mfma_f32_16x16x32_f16 v[96:99], v[144:147], v[164:167], v[96:99]
	v_mfma_f32_16x16x32_f16 v[100:103], v[144:147], v[168:171], v[100:103]
	s_waitcnt lgkmcnt(10)
	v_mfma_f32_16x16x32_f16 v[104:107], v[148:151], v[156:159], v[104:107]
	v_mfma_f32_16x16x32_f16 v[108:111], v[148:151], v[160:163], v[108:111]
	s_add_u32 m0, s28, 0x25000
	s_nop 0
	global_load_lds_dwordx4 v11, s[6:7]
	s_add_u32 s6, s6, s20
	s_addc_u32 s7, s7, 0
	v_mfma_f32_16x16x32_f16 v[112:115], v[148:151], v[164:167], v[112:115]
	v_mfma_f32_16x16x32_f16 v[116:119], v[148:151], v[168:171], v[116:119]
	s_waitcnt lgkmcnt(9)
	v_mfma_f32_16x16x32_f16 v[120:123], v[152:155], v[156:159], v[120:123]
	v_mfma_f32_16x16x32_f16 v[124:127], v[152:155], v[160:163], v[124:127]
	v_mfma_f32_16x16x32_f16 v[128:131], v[152:155], v[164:167], v[128:131]
	v_mfma_f32_16x16x32_f16 v[132:135], v[152:155], v[168:171], v[132:135]
	s_waitcnt vmcnt(7) lgkmcnt(0)
	s_barrier
	s_waitcnt lgkmcnt(6)
	ds_read_b128 v[136:139], v15 offset:53248
	ds_read_b128 v[156:159], v17 offset:53248
	ds_read_b128 v[160:163], v17 offset:55296
	ds_read_b128 v[164:167], v17 offset:57344
	ds_read_b128 v[168:171], v17 offset:59392
	ds_read_b128 v[140:143], v15 offset:55296
	ds_read_b128 v[144:147], v15 offset:57344
	ds_read_b128 v[148:151], v15 offset:59392
	ds_read_b128 v[152:155], v15 offset:61440
	v_mfma_f32_16x16x32_f16 v[56:59], v[172:175], v[192:195], v[56:59]
	s_add_u32 m0, s28, 0x0
	s_nop 0
	global_load_lds_dwordx4 v10, s[4:5]
	s_waitcnt lgkmcnt(15)
	v_mfma_f32_16x16x32_f16 v[60:63], v[172:175], v[196:199], v[60:63]
	s_waitcnt lgkmcnt(14)
	v_mfma_f32_16x16x32_f16 v[64:67], v[172:175], v[200:203], v[64:67]
	s_waitcnt lgkmcnt(13)
	v_mfma_f32_16x16x32_f16 v[68:71], v[172:175], v[204:207], v[68:71]
	s_waitcnt lgkmcnt(12)
	v_mfma_f32_16x16x32_f16 v[72:75], v[176:179], v[192:195], v[72:75]
	v_mfma_f32_16x16x32_f16 v[76:79], v[176:179], v[196:199], v[76:79]
	s_add_u32 m0, s28, 0x2000
	s_nop 0
	global_load_lds_dwordx4 v11, s[4:5]
	v_mfma_f32_16x16x32_f16 v[80:83], v[176:179], v[200:203], v[80:83]
	v_mfma_f32_16x16x32_f16 v[84:87], v[176:179], v[204:207], v[84:87]
	s_waitcnt lgkmcnt(11)
	v_mfma_f32_16x16x32_f16 v[88:91], v[180:183], v[192:195], v[88:91]
	v_mfma_f32_16x16x32_f16 v[92:95], v[180:183], v[196:199], v[92:95]
	v_mfma_f32_16x16x32_f16 v[96:99], v[180:183], v[200:203], v[96:99]
	s_add_u32 m0, s28, 0x4000
	s_nop 0
	global_load_lds_dwordx4 v12, s[4:5]
	v_mfma_f32_16x16x32_f16 v[100:103], v[180:183], v[204:207], v[100:103]
	s_waitcnt lgkmcnt(10)
	v_mfma_f32_16x16x32_f16 v[104:107], v[184:187], v[192:195], v[104:107]
	v_mfma_f32_16x16x32_f16 v[108:111], v[184:187], v[196:199], v[108:111]
	v_mfma_f32_16x16x32_f16 v[112:115], v[184:187], v[200:203], v[112:115]
	v_mfma_f32_16x16x32_f16 v[116:119], v[184:187], v[204:207], v[116:119]
	s_add_u32 m0, s28, 0x6000
	s_nop 0
	global_load_lds_dwordx4 v13, s[4:5]
	s_waitcnt lgkmcnt(9)
	v_mfma_f32_16x16x32_f16 v[120:123], v[188:191], v[192:195], v[120:123]
	v_mfma_f32_16x16x32_f16 v[124:127], v[188:191], v[196:199], v[124:127]
	v_mfma_f32_16x16x32_f16 v[128:131], v[188:191], v[200:203], v[128:131]
	v_mfma_f32_16x16x32_f16 v[132:135], v[188:191], v[204:207], v[132:135]
	s_waitcnt lgkmcnt(6)
	ds_read_b128 v[172:175], v16 offset:53248
	ds_read_b128 v[192:195], v18 offset:53248
	ds_read_b128 v[196:199], v18 offset:55296
	ds_read_b128 v[200:203], v18 offset:57344
	ds_read_b128 v[204:207], v18 offset:59392
	ds_read_b128 v[176:179], v16 offset:55296
	ds_read_b128 v[180:183], v16 offset:57344
	ds_read_b128 v[184:187], v16 offset:59392
	ds_read_b128 v[188:191], v16 offset:61440
	v_mfma_f32_16x16x32_f16 v[56:59], v[136:139], v[156:159], v[56:59]
	s_add_u32 m0, s28, 0x8000
	s_nop 0
	global_load_lds_dwordx4 v14, s[4:5]
	s_add_u32 s4, s4, s20
	s_addc_u32 s5, s5, 0
	s_waitcnt lgkmcnt(15)
	v_mfma_f32_16x16x32_f16 v[60:63], v[136:139], v[160:163], v[60:63]
	s_waitcnt lgkmcnt(14)
	v_mfma_f32_16x16x32_f16 v[64:67], v[136:139], v[164:167], v[64:67]
	s_waitcnt lgkmcnt(13)
	v_mfma_f32_16x16x32_f16 v[68:71], v[136:139], v[168:171], v[68:71]
	s_waitcnt lgkmcnt(12)
	v_mfma_f32_16x16x32_f16 v[72:75], v[140:143], v[156:159], v[72:75]
	v_mfma_f32_16x16x32_f16 v[76:79], v[140:143], v[160:163], v[76:79]
	v_mfma_f32_16x16x32_f16 v[80:83], v[140:143], v[164:167], v[80:83]
	s_add_u32 m0, s28, 0x9000
	s_nop 0
	global_load_lds_dwordx4 v10, s[6:7]
	v_mfma_f32_16x16x32_f16 v[84:87], v[140:143], v[168:171], v[84:87]
	s_waitcnt lgkmcnt(11)
	v_mfma_f32_16x16x32_f16 v[88:91], v[144:147], v[156:159], v[88:91]
	v_mfma_f32_16x16x32_f16 v[92:95], v[144:147], v[160:163], v[92:95]
	v_mfma_f32_16x16x32_f16 v[96:99], v[144:147], v[164:167], v[96:99]
	v_mfma_f32_16x16x32_f16 v[100:103], v[144:147], v[168:171], v[100:103]
	s_waitcnt lgkmcnt(10)
	v_mfma_f32_16x16x32_f16 v[104:107], v[148:151], v[156:159], v[104:107]
	v_mfma_f32_16x16x32_f16 v[108:111], v[148:151], v[160:163], v[108:111]
	s_add_u32 m0, s28, 0xb000
	s_nop 0
	global_load_lds_dwordx4 v11, s[6:7]
	s_add_u32 s6, s6, s20
	s_addc_u32 s7, s7, 0
	v_mfma_f32_16x16x32_f16 v[112:115], v[148:151], v[164:167], v[112:115]
	v_mfma_f32_16x16x32_f16 v[116:119], v[148:151], v[168:171], v[116:119]
	s_waitcnt lgkmcnt(9)
	v_mfma_f32_16x16x32_f16 v[120:123], v[152:155], v[156:159], v[120:123]
	v_mfma_f32_16x16x32_f16 v[124:127], v[152:155], v[160:163], v[124:127]
	v_mfma_f32_16x16x32_f16 v[128:131], v[152:155], v[164:167], v[128:131]
	v_mfma_f32_16x16x32_f16 v[132:135], v[152:155], v[168:171], v[132:135]
	s_waitcnt vmcnt(7) lgkmcnt(0)
	s_barrier
	s_waitcnt lgkmcnt(6)
	ds_read_b128 v[136:139], v19
	ds_read_b128 v[156:159], v21
	ds_read_b128 v[160:163], v21 offset:2048
	ds_read_b128 v[164:167], v21 offset:4096
	ds_read_b128 v[168:171], v21 offset:6144
	ds_read_b128 v[140:143], v19 offset:2048
	ds_read_b128 v[144:147], v19 offset:4096
	ds_read_b128 v[148:151], v19 offset:6144
	ds_read_b128 v[152:155], v19 offset:8192
	v_mfma_f32_16x16x32_f16 v[56:59], v[172:175], v[192:195], v[56:59]
	s_add_u32 m0, s28, 0xd000
	s_nop 0
	global_load_lds_dwordx4 v10, s[4:5]
	s_waitcnt lgkmcnt(15)
	v_mfma_f32_16x16x32_f16 v[60:63], v[172:175], v[196:199], v[60:63]
	s_waitcnt lgkmcnt(14)
	v_mfma_f32_16x16x32_f16 v[64:67], v[172:175], v[200:203], v[64:67]
	s_waitcnt lgkmcnt(13)
	v_mfma_f32_16x16x32_f16 v[68:71], v[172:175], v[204:207], v[68:71]
	s_waitcnt lgkmcnt(12)
	v_mfma_f32_16x16x32_f16 v[72:75], v[176:179], v[192:195], v[72:75]
	v_mfma_f32_16x16x32_f16 v[76:79], v[176:179], v[196:199], v[76:79]
	s_add_u32 m0, s28, 0xf000
	s_nop 0
	global_load_lds_dwordx4 v11, s[4:5]
	v_mfma_f32_16x16x32_f16 v[80:83], v[176:179], v[200:203], v[80:83]
	v_mfma_f32_16x16x32_f16 v[84:87], v[176:179], v[204:207], v[84:87]
	s_waitcnt lgkmcnt(11)
	v_mfma_f32_16x16x32_f16 v[88:91], v[180:183], v[192:195], v[88:91]
	v_mfma_f32_16x16x32_f16 v[92:95], v[180:183], v[196:199], v[92:95]
	v_mfma_f32_16x16x32_f16 v[96:99], v[180:183], v[200:203], v[96:99]
	s_add_u32 m0, s28, 0x11000
	s_nop 0
	global_load_lds_dwordx4 v12, s[4:5]
	v_mfma_f32_16x16x32_f16 v[100:103], v[180:183], v[204:207], v[100:103]
	s_waitcnt lgkmcnt(10)
	v_mfma_f32_16x16x32_f16 v[104:107], v[184:187], v[192:195], v[104:107]
	v_mfma_f32_16x16x32_f16 v[108:111], v[184:187], v[196:199], v[108:111]
	v_mfma_f32_16x16x32_f16 v[112:115], v[184:187], v[200:203], v[112:115]
	v_mfma_f32_16x16x32_f16 v[116:119], v[184:187], v[204:207], v[116:119]
	s_add_u32 m0, s28, 0x13000
	s_nop 0
	global_load_lds_dwordx4 v13, s[4:5]
	s_waitcnt lgkmcnt(9)
	v_mfma_f32_16x16x32_f16 v[120:123], v[188:191], v[192:195], v[120:123]
	v_mfma_f32_16x16x32_f16 v[124:127], v[188:191], v[196:199], v[124:127]
	v_mfma_f32_16x16x32_f16 v[128:131], v[188:191], v[200:203], v[128:131]
	v_mfma_f32_16x16x32_f16 v[132:135], v[188:191], v[204:207], v[132:135]
	s_waitcnt lgkmcnt(6)
	ds_read_b128 v[172:175], v20
	ds_read_b128 v[192:195], v22
	ds_read_b128 v[196:199], v22 offset:2048
	ds_read_b128 v[200:203], v22 offset:4096
	ds_read_b128 v[204:207], v22 offset:6144
	ds_read_b128 v[176:179], v20 offset:2048
	ds_read_b128 v[180:183], v20 offset:4096
	ds_read_b128 v[184:187], v20 offset:6144
	ds_read_b128 v[188:191], v20 offset:8192
	v_mfma_f32_16x16x32_f16 v[56:59], v[136:139], v[156:159], v[56:59]
	s_add_u32 m0, s28, 0x15000
	s_nop 0
	global_load_lds_dwordx4 v14, s[4:5]
	s_add_u32 s4, s4, s20
	s_addc_u32 s5, s5, 0
	s_waitcnt lgkmcnt(15)
	v_mfma_f32_16x16x32_f16 v[60:63], v[136:139], v[160:163], v[60:63]
	s_waitcnt lgkmcnt(14)
	v_mfma_f32_16x16x32_f16 v[64:67], v[136:139], v[164:167], v[64:67]
	s_waitcnt lgkmcnt(13)
	v_mfma_f32_16x16x32_f16 v[68:71], v[136:139], v[168:171], v[68:71]
	s_waitcnt lgkmcnt(12)
	v_mfma_f32_16x16x32_f16 v[72:75], v[140:143], v[156:159], v[72:75]
	v_mfma_f32_16x16x32_f16 v[76:79], v[140:143], v[160:163], v[76:79]
	v_mfma_f32_16x16x32_f16 v[80:83], v[140:143], v[164:167], v[80:83]
	s_add_u32 m0, s28, 0x16000
	s_nop 0
	global_load_lds_dwordx4 v10, s[6:7]
	v_mfma_f32_16x16x32_f16 v[84:87], v[140:143], v[168:171], v[84:87]
	s_waitcnt lgkmcnt(11)
	v_mfma_f32_16x16x32_f16 v[88:91], v[144:147], v[156:159], v[88:91]
	v_mfma_f32_16x16x32_f16 v[92:95], v[144:147], v[160:163], v[92:95]
	v_mfma_f32_16x16x32_f16 v[96:99], v[144:147], v[164:167], v[96:99]
	v_mfma_f32_16x16x32_f16 v[100:103], v[144:147], v[168:171], v[100:103]
	s_waitcnt lgkmcnt(10)
	v_mfma_f32_16x16x32_f16 v[104:107], v[148:151], v[156:159], v[104:107]
	v_mfma_f32_16x16x32_f16 v[108:111], v[148:151], v[160:163], v[108:111]
	s_add_u32 m0, s28, 0x18000
	s_nop 0
	global_load_lds_dwordx4 v11, s[6:7]
	s_add_u32 s6, s6, s20
	s_addc_u32 s7, s7, 0
	v_mfma_f32_16x16x32_f16 v[112:115], v[148:151], v[164:167], v[112:115]
	v_mfma_f32_16x16x32_f16 v[116:119], v[148:151], v[168:171], v[116:119]
	s_waitcnt lgkmcnt(9)
	v_mfma_f32_16x16x32_f16 v[120:123], v[152:155], v[156:159], v[120:123]
	v_mfma_f32_16x16x32_f16 v[124:127], v[152:155], v[160:163], v[124:127]
	v_mfma_f32_16x16x32_f16 v[128:131], v[152:155], v[164:167], v[128:131]
	v_mfma_f32_16x16x32_f16 v[132:135], v[152:155], v[168:171], v[132:135]
	s_waitcnt vmcnt(7) lgkmcnt(0)
	s_barrier
	s_waitcnt lgkmcnt(6)
	ds_read_b128 v[136:139], v15
	ds_read_b128 v[156:159], v17
	ds_read_b128 v[160:163], v17 offset:2048
	ds_read_b128 v[164:167], v17 offset:4096
	ds_read_b128 v[168:171], v17 offset:6144
	ds_read_b128 v[140:143], v15 offset:2048
	ds_read_b128 v[144:147], v15 offset:4096
	ds_read_b128 v[148:151], v15 offset:6144
	ds_read_b128 v[152:155], v15 offset:8192
	v_mfma_f32_16x16x32_f16 v[56:59], v[172:175], v[192:195], v[56:59]
	s_add_u32 m0, s28, 0x1a000
	s_nop 0
	global_load_lds_dwordx4 v10, s[4:5]
	s_waitcnt lgkmcnt(15)
	v_mfma_f32_16x16x32_f16 v[60:63], v[172:175], v[196:199], v[60:63]
	s_waitcnt lgkmcnt(14)
	v_mfma_f32_16x16x32_f16 v[64:67], v[172:175], v[200:203], v[64:67]
	s_waitcnt lgkmcnt(13)
	v_mfma_f32_16x16x32_f16 v[68:71], v[172:175], v[204:207], v[68:71]
	s_waitcnt lgkmcnt(12)
	v_mfma_f32_16x16x32_f16 v[72:75], v[176:179], v[192:195], v[72:75]
	v_mfma_f32_16x16x32_f16 v[76:79], v[176:179], v[196:199], v[76:79]
	s_add_u32 m0, s28, 0x1c000
	s_nop 0
	global_load_lds_dwordx4 v11, s[4:5]
	v_mfma_f32_16x16x32_f16 v[80:83], v[176:179], v[200:203], v[80:83]
	v_mfma_f32_16x16x32_f16 v[84:87], v[176:179], v[204:207], v[84:87]
	s_waitcnt lgkmcnt(11)
	v_mfma_f32_16x16x32_f16 v[88:91], v[180:183], v[192:195], v[88:91]
	v_mfma_f32_16x16x32_f16 v[92:95], v[180:183], v[196:199], v[92:95]
	v_mfma_f32_16x16x32_f16 v[96:99], v[180:183], v[200:203], v[96:99]
	s_add_u32 m0, s28, 0x1e000
	s_nop 0
	global_load_lds_dwordx4 v12, s[4:5]
	v_mfma_f32_16x16x32_f16 v[100:103], v[180:183], v[204:207], v[100:103]
	s_waitcnt lgkmcnt(10)
	v_mfma_f32_16x16x32_f16 v[104:107], v[184:187], v[192:195], v[104:107]
	v_mfma_f32_16x16x32_f16 v[108:111], v[184:187], v[196:199], v[108:111]
	v_mfma_f32_16x16x32_f16 v[112:115], v[184:187], v[200:203], v[112:115]
	v_mfma_f32_16x16x32_f16 v[116:119], v[184:187], v[204:207], v[116:119]
	s_add_u32 m0, s28, 0x20000
	s_nop 0
	global_load_lds_dwordx4 v13, s[4:5]
	s_waitcnt lgkmcnt(9)
	v_mfma_f32_16x16x32_f16 v[120:123], v[188:191], v[192:195], v[120:123]
	v_mfma_f32_16x16x32_f16 v[124:127], v[188:191], v[196:199], v[124:127]
	v_mfma_f32_16x16x32_f16 v[128:131], v[188:191], v[200:203], v[128:131]
	v_mfma_f32_16x16x32_f16 v[132:135], v[188:191], v[204:207], v[132:135]
	s_waitcnt lgkmcnt(6)
	ds_read_b128 v[172:175], v16
	ds_read_b128 v[192:195], v18
	ds_read_b128 v[196:199], v18 offset:2048
	ds_read_b128 v[200:203], v18 offset:4096
	ds_read_b128 v[204:207], v18 offset:6144
	ds_read_b128 v[176:179], v16 offset:2048
	ds_read_b128 v[180:183], v16 offset:4096
	ds_read_b128 v[184:187], v16 offset:6144
	ds_read_b128 v[188:191], v16 offset:8192
	v_mfma_f32_16x16x32_f16 v[56:59], v[136:139], v[156:159], v[56:59]
	s_add_u32 m0, s28, 0x22000
	s_nop 0
	global_load_lds_dwordx4 v14, s[4:5]
	s_add_u32 s4, s4, s20
	s_addc_u32 s5, s5, 0
	s_waitcnt lgkmcnt(15)
	v_mfma_f32_16x16x32_f16 v[60:63], v[136:139], v[160:163], v[60:63]
	s_waitcnt lgkmcnt(14)
	v_mfma_f32_16x16x32_f16 v[64:67], v[136:139], v[164:167], v[64:67]
	s_waitcnt lgkmcnt(13)
	v_mfma_f32_16x16x32_f16 v[68:71], v[136:139], v[168:171], v[68:71]
	s_waitcnt lgkmcnt(12)
	v_mfma_f32_16x16x32_f16 v[72:75], v[140:143], v[156:159], v[72:75]
	v_mfma_f32_16x16x32_f16 v[76:79], v[140:143], v[160:163], v[76:79]
	v_mfma_f32_16x16x32_f16 v[80:83], v[140:143], v[164:167], v[80:83]
	s_add_u32 m0, s28, 0x23000
	s_nop 0
	global_load_lds_dwordx4 v10, s[6:7]
	v_mfma_f32_16x16x32_f16 v[84:87], v[140:143], v[168:171], v[84:87]
	s_waitcnt lgkmcnt(11)
	v_mfma_f32_16x16x32_f16 v[88:91], v[144:147], v[156:159], v[88:91]
	v_mfma_f32_16x16x32_f16 v[92:95], v[144:147], v[160:163], v[92:95]
	v_mfma_f32_16x16x32_f16 v[96:99], v[144:147], v[164:167], v[96:99]
	v_mfma_f32_16x16x32_f16 v[100:103], v[144:147], v[168:171], v[100:103]
	s_waitcnt lgkmcnt(10)
	v_mfma_f32_16x16x32_f16 v[104:107], v[148:151], v[156:159], v[104:107]
	v_mfma_f32_16x16x32_f16 v[108:111], v[148:151], v[160:163], v[108:111]
	s_add_u32 m0, s28, 0x25000
	s_nop 0
	global_load_lds_dwordx4 v11, s[6:7]
	s_add_u32 s6, s6, s20
	s_addc_u32 s7, s7, 0
	v_mfma_f32_16x16x32_f16 v[112:115], v[148:151], v[164:167], v[112:115]
	v_mfma_f32_16x16x32_f16 v[116:119], v[148:151], v[168:171], v[116:119]
	s_waitcnt lgkmcnt(9)
	v_mfma_f32_16x16x32_f16 v[120:123], v[152:155], v[156:159], v[120:123]
	v_mfma_f32_16x16x32_f16 v[124:127], v[152:155], v[160:163], v[124:127]
	v_mfma_f32_16x16x32_f16 v[128:131], v[152:155], v[164:167], v[128:131]
	v_mfma_f32_16x16x32_f16 v[132:135], v[152:155], v[168:171], v[132:135]
	s_waitcnt vmcnt(7) lgkmcnt(0)
	s_barrier
	s_waitcnt lgkmcnt(6)
	ds_read_b128 v[136:139], v15 offset:53248
	ds_read_b128 v[156:159], v17 offset:53248
	ds_read_b128 v[160:163], v17 offset:55296
	ds_read_b128 v[164:167], v17 offset:57344
	ds_read_b128 v[168:171], v17 offset:59392
	ds_read_b128 v[140:143], v15 offset:55296
	ds_read_b128 v[144:147], v15 offset:57344
	ds_read_b128 v[148:151], v15 offset:59392
	ds_read_b128 v[152:155], v15 offset:61440
	v_mfma_f32_16x16x32_f16 v[56:59], v[172:175], v[192:195], v[56:59]
	s_add_u32 m0, s28, 0x0
	s_nop 0
	global_load_lds_dwordx4 v10, s[4:5]
	s_waitcnt lgkmcnt(15)
	v_mfma_f32_16x16x32_f16 v[60:63], v[172:175], v[196:199], v[60:63]
	s_waitcnt lgkmcnt(14)
	v_mfma_f32_16x16x32_f16 v[64:67], v[172:175], v[200:203], v[64:67]
	s_waitcnt lgkmcnt(13)
	v_mfma_f32_16x16x32_f16 v[68:71], v[172:175], v[204:207], v[68:71]
	s_waitcnt lgkmcnt(12)
	v_mfma_f32_16x16x32_f16 v[72:75], v[176:179], v[192:195], v[72:75]
	v_mfma_f32_16x16x32_f16 v[76:79], v[176:179], v[196:199], v[76:79]
	s_add_u32 m0, s28, 0x2000
	s_nop 0
	global_load_lds_dwordx4 v11, s[4:5]
	v_mfma_f32_16x16x32_f16 v[80:83], v[176:179], v[200:203], v[80:83]
	v_mfma_f32_16x16x32_f16 v[84:87], v[176:179], v[204:207], v[84:87]
	s_waitcnt lgkmcnt(11)
	v_mfma_f32_16x16x32_f16 v[88:91], v[180:183], v[192:195], v[88:91]
	v_mfma_f32_16x16x32_f16 v[92:95], v[180:183], v[196:199], v[92:95]
	v_mfma_f32_16x16x32_f16 v[96:99], v[180:183], v[200:203], v[96:99]
	s_add_u32 m0, s28, 0x4000
	s_nop 0
	global_load_lds_dwordx4 v12, s[4:5]
	v_mfma_f32_16x16x32_f16 v[100:103], v[180:183], v[204:207], v[100:103]
	s_waitcnt lgkmcnt(10)
	v_mfma_f32_16x16x32_f16 v[104:107], v[184:187], v[192:195], v[104:107]
	v_mfma_f32_16x16x32_f16 v[108:111], v[184:187], v[196:199], v[108:111]
	v_mfma_f32_16x16x32_f16 v[112:115], v[184:187], v[200:203], v[112:115]
	v_mfma_f32_16x16x32_f16 v[116:119], v[184:187], v[204:207], v[116:119]
	s_add_u32 m0, s28, 0x6000
	s_nop 0
	global_load_lds_dwordx4 v13, s[4:5]
	s_waitcnt lgkmcnt(9)
	v_mfma_f32_16x16x32_f16 v[120:123], v[188:191], v[192:195], v[120:123]
	v_mfma_f32_16x16x32_f16 v[124:127], v[188:191], v[196:199], v[124:127]
	v_mfma_f32_16x16x32_f16 v[128:131], v[188:191], v[200:203], v[128:131]
	v_mfma_f32_16x16x32_f16 v[132:135], v[188:191], v[204:207], v[132:135]
	s_waitcnt lgkmcnt(6)
	ds_read_b128 v[172:175], v16 offset:53248
	ds_read_b128 v[192:195], v18 offset:53248
	ds_read_b128 v[196:199], v18 offset:55296
	ds_read_b128 v[200:203], v18 offset:57344
	ds_read_b128 v[204:207], v18 offset:59392
	ds_read_b128 v[176:179], v16 offset:55296
	ds_read_b128 v[180:183], v16 offset:57344
	ds_read_b128 v[184:187], v16 offset:59392
	ds_read_b128 v[188:191], v16 offset:61440
	v_mfma_f32_16x16x32_f16 v[56:59], v[136:139], v[156:159], v[56:59]
	s_add_u32 m0, s28, 0x8000
	s_nop 0
	global_load_lds_dwordx4 v14, s[4:5]
	s_add_u32 s4, s4, s20
	s_addc_u32 s5, s5, 0
	s_waitcnt lgkmcnt(15)
	v_mfma_f32_16x16x32_f16 v[60:63], v[136:139], v[160:163], v[60:63]
	s_waitcnt lgkmcnt(14)
	v_mfma_f32_16x16x32_f16 v[64:67], v[136:139], v[164:167], v[64:67]
	s_waitcnt lgkmcnt(13)
	v_mfma_f32_16x16x32_f16 v[68:71], v[136:139], v[168:171], v[68:71]
	s_waitcnt lgkmcnt(12)
	v_mfma_f32_16x16x32_f16 v[72:75], v[140:143], v[156:159], v[72:75]
	v_mfma_f32_16x16x32_f16 v[76:79], v[140:143], v[160:163], v[76:79]
	v_mfma_f32_16x16x32_f16 v[80:83], v[140:143], v[164:167], v[80:83]
	s_add_u32 m0, s28, 0x9000
	s_nop 0
	global_load_lds_dwordx4 v10, s[6:7]
	v_mfma_f32_16x16x32_f16 v[84:87], v[140:143], v[168:171], v[84:87]
	s_waitcnt lgkmcnt(11)
	v_mfma_f32_16x16x32_f16 v[88:91], v[144:147], v[156:159], v[88:91]
	v_mfma_f32_16x16x32_f16 v[92:95], v[144:147], v[160:163], v[92:95]
	v_mfma_f32_16x16x32_f16 v[96:99], v[144:147], v[164:167], v[96:99]
	v_mfma_f32_16x16x32_f16 v[100:103], v[144:147], v[168:171], v[100:103]
	s_waitcnt lgkmcnt(10)
	v_mfma_f32_16x16x32_f16 v[104:107], v[148:151], v[156:159], v[104:107]
	v_mfma_f32_16x16x32_f16 v[108:111], v[148:151], v[160:163], v[108:111]
	s_add_u32 m0, s28, 0xb000
	s_nop 0
	global_load_lds_dwordx4 v11, s[6:7]
	s_add_u32 s6, s6, s20
	s_addc_u32 s7, s7, 0
	v_mfma_f32_16x16x32_f16 v[112:115], v[148:151], v[164:167], v[112:115]
	v_mfma_f32_16x16x32_f16 v[116:119], v[148:151], v[168:171], v[116:119]
	s_waitcnt lgkmcnt(9)
	v_mfma_f32_16x16x32_f16 v[120:123], v[152:155], v[156:159], v[120:123]
	v_mfma_f32_16x16x32_f16 v[124:127], v[152:155], v[160:163], v[124:127]
	v_mfma_f32_16x16x32_f16 v[128:131], v[152:155], v[164:167], v[128:131]
	v_mfma_f32_16x16x32_f16 v[132:135], v[152:155], v[168:171], v[132:135]
	s_waitcnt vmcnt(7) lgkmcnt(0)
	s_barrier
	s_waitcnt lgkmcnt(6)
	ds_read_b128 v[136:139], v19
	ds_read_b128 v[156:159], v21
	ds_read_b128 v[160:163], v21 offset:2048
	ds_read_b128 v[164:167], v21 offset:4096
	ds_read_b128 v[168:171], v21 offset:6144
	ds_read_b128 v[140:143], v19 offset:2048
	ds_read_b128 v[144:147], v19 offset:4096
	ds_read_b128 v[148:151], v19 offset:6144
	ds_read_b128 v[152:155], v19 offset:8192
	v_mfma_f32_16x16x32_f16 v[56:59], v[172:175], v[192:195], v[56:59]
	s_waitcnt lgkmcnt(15)
	v_mfma_f32_16x16x32_f16 v[60:63], v[172:175], v[196:199], v[60:63]
	s_waitcnt lgkmcnt(14)
	v_mfma_f32_16x16x32_f16 v[64:67], v[172:175], v[200:203], v[64:67]
	s_waitcnt lgkmcnt(13)
	v_mfma_f32_16x16x32_f16 v[68:71], v[172:175], v[204:207], v[68:71]
	s_waitcnt lgkmcnt(12)
	v_mfma_f32_16x16x32_f16 v[72:75], v[176:179], v[192:195], v[72:75]
	v_mfma_f32_16x16x32_f16 v[76:79], v[176:179], v[196:199], v[76:79]
	v_mfma_f32_16x16x32_f16 v[80:83], v[176:179], v[200:203], v[80:83]
	v_mfma_f32_16x16x32_f16 v[84:87], v[176:179], v[204:207], v[84:87]
	s_waitcnt lgkmcnt(11)
	v_mfma_f32_16x16x32_f16 v[88:91], v[180:183], v[192:195], v[88:91]
	v_mfma_f32_16x16x32_f16 v[92:95], v[180:183], v[196:199], v[92:95]
	v_mfma_f32_16x16x32_f16 v[96:99], v[180:183], v[200:203], v[96:99]
	v_mfma_f32_16x16x32_f16 v[100:103], v[180:183], v[204:207], v[100:103]
	s_waitcnt lgkmcnt(10)
	v_mfma_f32_16x16x32_f16 v[104:107], v[184:187], v[192:195], v[104:107]
	v_mfma_f32_16x16x32_f16 v[108:111], v[184:187], v[196:199], v[108:111]
	v_mfma_f32_16x16x32_f16 v[112:115], v[184:187], v[200:203], v[112:115]
	v_mfma_f32_16x16x32_f16 v[116:119], v[184:187], v[204:207], v[116:119]
	s_waitcnt lgkmcnt(9)
	v_mfma_f32_16x16x32_f16 v[120:123], v[188:191], v[192:195], v[120:123]
	v_mfma_f32_16x16x32_f16 v[124:127], v[188:191], v[196:199], v[124:127]
	v_mfma_f32_16x16x32_f16 v[128:131], v[188:191], v[200:203], v[128:131]
	v_mfma_f32_16x16x32_f16 v[132:135], v[188:191], v[204:207], v[132:135]
	s_waitcnt lgkmcnt(6)
	ds_read_b128 v[172:175], v20
	ds_read_b128 v[192:195], v22
	ds_read_b128 v[196:199], v22 offset:2048
	ds_read_b128 v[200:203], v22 offset:4096
	ds_read_b128 v[204:207], v22 offset:6144
	ds_read_b128 v[176:179], v20 offset:2048
	ds_read_b128 v[180:183], v20 offset:4096
	ds_read_b128 v[184:187], v20 offset:6144
	ds_read_b128 v[188:191], v20 offset:8192
	v_mfma_f32_16x16x32_f16 v[56:59], v[136:139], v[156:159], v[56:59]
	s_waitcnt lgkmcnt(15)
	v_mfma_f32_16x16x32_f16 v[60:63], v[136:139], v[160:163], v[60:63]
	s_waitcnt lgkmcnt(14)
	v_mfma_f32_16x16x32_f16 v[64:67], v[136:139], v[164:167], v[64:67]
	s_waitcnt lgkmcnt(13)
	v_mfma_f32_16x16x32_f16 v[68:71], v[136:139], v[168:171], v[68:71]
	s_waitcnt lgkmcnt(12)
	v_mfma_f32_16x16x32_f16 v[72:75], v[140:143], v[156:159], v[72:75]
	v_mfma_f32_16x16x32_f16 v[76:79], v[140:143], v[160:163], v[76:79]
	v_mfma_f32_16x16x32_f16 v[80:83], v[140:143], v[164:167], v[80:83]
	v_mfma_f32_16x16x32_f16 v[84:87], v[140:143], v[168:171], v[84:87]
	s_waitcnt lgkmcnt(11)
	v_mfma_f32_16x16x32_f16 v[88:91], v[144:147], v[156:159], v[88:91]
	v_mfma_f32_16x16x32_f16 v[92:95], v[144:147], v[160:163], v[92:95]
	v_mfma_f32_16x16x32_f16 v[96:99], v[144:147], v[164:167], v[96:99]
	v_mfma_f32_16x16x32_f16 v[100:103], v[144:147], v[168:171], v[100:103]
	s_waitcnt lgkmcnt(10)
	v_mfma_f32_16x16x32_f16 v[104:107], v[148:151], v[156:159], v[104:107]
	v_mfma_f32_16x16x32_f16 v[108:111], v[148:151], v[160:163], v[108:111]
	v_mfma_f32_16x16x32_f16 v[112:115], v[148:151], v[164:167], v[112:115]
	v_mfma_f32_16x16x32_f16 v[116:119], v[148:151], v[168:171], v[116:119]
	s_waitcnt lgkmcnt(9)
	v_mfma_f32_16x16x32_f16 v[120:123], v[152:155], v[156:159], v[120:123]
	v_mfma_f32_16x16x32_f16 v[124:127], v[152:155], v[160:163], v[124:127]
	v_mfma_f32_16x16x32_f16 v[128:131], v[152:155], v[164:167], v[128:131]
	v_mfma_f32_16x16x32_f16 v[132:135], v[152:155], v[168:171], v[132:135]
	s_waitcnt vmcnt(0) lgkmcnt(0)
	s_barrier
	s_waitcnt lgkmcnt(6)
	ds_read_b128 v[136:139], v15
	ds_read_b128 v[156:159], v17
	ds_read_b128 v[160:163], v17 offset:2048
	ds_read_b128 v[164:167], v17 offset:4096
	ds_read_b128 v[168:171], v17 offset:6144
	ds_read_b128 v[140:143], v15 offset:2048
	ds_read_b128 v[144:147], v15 offset:4096
	ds_read_b128 v[148:151], v15 offset:6144
	ds_read_b128 v[152:155], v15 offset:8192
	v_mfma_f32_16x16x32_f16 v[56:59], v[172:175], v[192:195], v[56:59]
	s_waitcnt lgkmcnt(15)
	v_mfma_f32_16x16x32_f16 v[60:63], v[172:175], v[196:199], v[60:63]
	s_waitcnt lgkmcnt(14)
	v_mfma_f32_16x16x32_f16 v[64:67], v[172:175], v[200:203], v[64:67]
	s_waitcnt lgkmcnt(13)
	v_mfma_f32_16x16x32_f16 v[68:71], v[172:175], v[204:207], v[68:71]
	s_waitcnt lgkmcnt(12)
	v_mfma_f32_16x16x32_f16 v[72:75], v[176:179], v[192:195], v[72:75]
	v_mfma_f32_16x16x32_f16 v[76:79], v[176:179], v[196:199], v[76:79]
	v_mfma_f32_16x16x32_f16 v[80:83], v[176:179], v[200:203], v[80:83]
	v_mfma_f32_16x16x32_f16 v[84:87], v[176:179], v[204:207], v[84:87]
	s_waitcnt lgkmcnt(11)
	v_mfma_f32_16x16x32_f16 v[88:91], v[180:183], v[192:195], v[88:91]
	v_mfma_f32_16x16x32_f16 v[92:95], v[180:183], v[196:199], v[92:95]
	v_mfma_f32_16x16x32_f16 v[96:99], v[180:183], v[200:203], v[96:99]
	v_mfma_f32_16x16x32_f16 v[100:103], v[180:183], v[204:207], v[100:103]
	s_waitcnt lgkmcnt(10)
	v_mfma_f32_16x16x32_f16 v[104:107], v[184:187], v[192:195], v[104:107]
	v_mfma_f32_16x16x32_f16 v[108:111], v[184:187], v[196:199], v[108:111]
	v_mfma_f32_16x16x32_f16 v[112:115], v[184:187], v[200:203], v[112:115]
	v_mfma_f32_16x16x32_f16 v[116:119], v[184:187], v[204:207], v[116:119]
	s_waitcnt lgkmcnt(9)
	v_mfma_f32_16x16x32_f16 v[120:123], v[188:191], v[192:195], v[120:123]
	v_mfma_f32_16x16x32_f16 v[124:127], v[188:191], v[196:199], v[124:127]
	v_mfma_f32_16x16x32_f16 v[128:131], v[188:191], v[200:203], v[128:131]
	v_mfma_f32_16x16x32_f16 v[132:135], v[188:191], v[204:207], v[132:135]
	s_waitcnt lgkmcnt(6)
	ds_read_b128 v[172:175], v16
	ds_read_b128 v[192:195], v18
	ds_read_b128 v[196:199], v18 offset:2048
	ds_read_b128 v[200:203], v18 offset:4096
	ds_read_b128 v[204:207], v18 offset:6144
	ds_read_b128 v[176:179], v16 offset:2048
	ds_read_b128 v[180:183], v16 offset:4096
	ds_read_b128 v[184:187], v16 offset:6144
	ds_read_b128 v[188:191], v16 offset:8192
	v_mfma_f32_16x16x32_f16 v[56:59], v[136:139], v[156:159], v[56:59]
	s_waitcnt lgkmcnt(15)
	v_mfma_f32_16x16x32_f16 v[60:63], v[136:139], v[160:163], v[60:63]
	s_waitcnt lgkmcnt(14)
	v_mfma_f32_16x16x32_f16 v[64:67], v[136:139], v[164:167], v[64:67]
	s_waitcnt lgkmcnt(13)
	v_mfma_f32_16x16x32_f16 v[68:71], v[136:139], v[168:171], v[68:71]
	s_waitcnt lgkmcnt(12)
	v_mfma_f32_16x16x32_f16 v[72:75], v[140:143], v[156:159], v[72:75]
	v_mfma_f32_16x16x32_f16 v[76:79], v[140:143], v[160:163], v[76:79]
	v_mfma_f32_16x16x32_f16 v[80:83], v[140:143], v[164:167], v[80:83]
	v_mfma_f32_16x16x32_f16 v[84:87], v[140:143], v[168:171], v[84:87]
	s_waitcnt lgkmcnt(11)
	v_mfma_f32_16x16x32_f16 v[88:91], v[144:147], v[156:159], v[88:91]
	v_mfma_f32_16x16x32_f16 v[92:95], v[144:147], v[160:163], v[92:95]
	v_mfma_f32_16x16x32_f16 v[96:99], v[144:147], v[164:167], v[96:99]
	v_mfma_f32_16x16x32_f16 v[100:103], v[144:147], v[168:171], v[100:103]
	s_waitcnt lgkmcnt(10)
	v_mfma_f32_16x16x32_f16 v[104:107], v[148:151], v[156:159], v[104:107]
	v_mfma_f32_16x16x32_f16 v[108:111], v[148:151], v[160:163], v[108:111]
	v_mfma_f32_16x16x32_f16 v[112:115], v[148:151], v[164:167], v[112:115]
	v_mfma_f32_16x16x32_f16 v[116:119], v[148:151], v[168:171], v[116:119]
	s_waitcnt lgkmcnt(9)
	v_mfma_f32_16x16x32_f16 v[120:123], v[152:155], v[156:159], v[120:123]
	v_mfma_f32_16x16x32_f16 v[124:127], v[152:155], v[160:163], v[124:127]
	v_mfma_f32_16x16x32_f16 v[128:131], v[152:155], v[164:167], v[128:131]
	v_mfma_f32_16x16x32_f16 v[132:135], v[152:155], v[168:171], v[132:135]
	s_waitcnt lgkmcnt(7)
	v_mfma_f32_16x16x32_f16 v[56:59], v[172:175], v[192:195], v[56:59]
	s_waitcnt lgkmcnt(6)
	v_mfma_f32_16x16x32_f16 v[60:63], v[172:175], v[196:199], v[60:63]
	s_waitcnt lgkmcnt(5)
	v_mfma_f32_16x16x32_f16 v[64:67], v[172:175], v[200:203], v[64:67]
	s_waitcnt lgkmcnt(4)
	v_mfma_f32_16x16x32_f16 v[68:71], v[172:175], v[204:207], v[68:71]
	s_waitcnt lgkmcnt(3)
	v_mfma_f32_16x16x32_f16 v[72:75], v[176:179], v[192:195], v[72:75]
	v_mfma_f32_16x16x32_f16 v[76:79], v[176:179], v[196:199], v[76:79]
	v_mfma_f32_16x16x32_f16 v[80:83], v[176:179], v[200:203], v[80:83]
	v_mfma_f32_16x16x32_f16 v[84:87], v[176:179], v[204:207], v[84:87]
	s_waitcnt lgkmcnt(2)
	v_mfma_f32_16x16x32_f16 v[88:91], v[180:183], v[192:195], v[88:91]
	v_mfma_f32_16x16x32_f16 v[92:95], v[180:183], v[196:199], v[92:95]
	v_mfma_f32_16x16x32_f16 v[96:99], v[180:183], v[200:203], v[96:99]
	v_mfma_f32_16x16x32_f16 v[100:103], v[180:183], v[204:207], v[100:103]
	s_waitcnt lgkmcnt(1)
	v_mfma_f32_16x16x32_f16 v[104:107], v[184:187], v[192:195], v[104:107]
	v_mfma_f32_16x16x32_f16 v[108:111], v[184:187], v[196:199], v[108:111]
	v_mfma_f32_16x16x32_f16 v[112:115], v[184:187], v[200:203], v[112:115]
	v_mfma_f32_16x16x32_f16 v[116:119], v[184:187], v[204:207], v[116:119]
	s_waitcnt lgkmcnt(0)
	v_mfma_f32_16x16x32_f16 v[120:123], v[188:191], v[192:195], v[120:123]
	v_mfma_f32_16x16x32_f16 v[124:127], v[188:191], v[196:199], v[124:127]
	v_mfma_f32_16x16x32_f16 v[128:131], v[188:191], v[200:203], v[128:131]
	v_mfma_f32_16x16x32_f16 v[132:135], v[188:191], v[204:207], v[132:135]
	s_nop 7
	s_nop 1
	s_add_u32 s24, s29, 0
	s_lshl_b32 s8, s24, 11
	v_add_u32_e32 v212, s8, v23
	v_pk_add_f32 v[56:57], v[56:57], v[24:25] op_sel_hi:[1,0]
	v_pk_add_f32 v[58:59], v[58:59], v[24:25] op_sel_hi:[1,0]
	v_cvt_pk_f16_f32 v56, v56, v57
	v_cvt_pk_f16_f32 v57, v58, v59
	global_store_dwordx2 v212, v[56:57], s[22:23] offset:0 sc0 sc1
	v_pk_add_f32 v[60:61], v[60:61], v[26:27] op_sel_hi:[1,0]
	v_pk_add_f32 v[62:63], v[62:63], v[26:27] op_sel_hi:[1,0]
	v_cvt_pk_f16_f32 v60, v60, v61
	v_cvt_pk_f16_f32 v61, v62, v63
	global_store_dwordx2 v212, v[60:61], s[22:23] offset:256 sc0 sc1
	v_pk_add_f32 v[64:65], v[64:65], v[28:29] op_sel_hi:[1,0]
	v_pk_add_f32 v[66:67], v[66:67], v[28:29] op_sel_hi:[1,0]
	v_cvt_pk_f16_f32 v64, v64, v65
	v_cvt_pk_f16_f32 v65, v66, v67
	global_store_dwordx2 v212, v[64:65], s[22:23] offset:1024 sc0 sc1
	v_pk_add_f32 v[68:69], v[68:69], v[30:31] op_sel_hi:[1,0]
	v_pk_add_f32 v[70:71], v[70:71], v[30:31] op_sel_hi:[1,0]
	v_cvt_pk_f16_f32 v68, v68, v69
	v_cvt_pk_f16_f32 v69, v70, v71
	global_store_dwordx2 v212, v[68:69], s[22:23] offset:1280 sc0 sc1
	s_add_u32 s24, s29, 1
	s_lshl_b32 s8, s24, 11
	v_add_u32_e32 v212, s8, v23
	v_pk_add_f32 v[72:73], v[72:73], v[24:25] op_sel_hi:[1,0]
	v_pk_add_f32 v[74:75], v[74:75], v[24:25] op_sel_hi:[1,0]
	v_cvt_pk_f16_f32 v72, v72, v73
	v_cvt_pk_f16_f32 v73, v74, v75
	global_store_dwordx2 v212, v[72:73], s[22:23] offset:0 sc0 sc1
	v_pk_add_f32 v[76:77], v[76:77], v[26:27] op_sel_hi:[1,0]
	v_pk_add_f32 v[78:79], v[78:79], v[26:27] op_sel_hi:[1,0]
	v_cvt_pk_f16_f32 v76, v76, v77
	v_cvt_pk_f16_f32 v77, v78, v79
	global_store_dwordx2 v212, v[76:77], s[22:23] offset:256 sc0 sc1
	v_pk_add_f32 v[80:81], v[80:81], v[28:29] op_sel_hi:[1,0]
	v_pk_add_f32 v[82:83], v[82:83], v[28:29] op_sel_hi:[1,0]
	v_cvt_pk_f16_f32 v80, v80, v81
	v_cvt_pk_f16_f32 v81, v82, v83
	global_store_dwordx2 v212, v[80:81], s[22:23] offset:1024 sc0 sc1
	v_pk_add_f32 v[84:85], v[84:85], v[30:31] op_sel_hi:[1,0]
	v_pk_add_f32 v[86:87], v[86:87], v[30:31] op_sel_hi:[1,0]
	v_cvt_pk_f16_f32 v84, v84, v85
	v_cvt_pk_f16_f32 v85, v86, v87
	global_store_dwordx2 v212, v[84:85], s[22:23] offset:1280 sc0 sc1
	s_add_u32 s24, s29, 2
	s_lshl_b32 s8, s24, 11
	v_add_u32_e32 v212, s8, v23
	v_pk_add_f32 v[88:89], v[88:89], v[24:25] op_sel_hi:[1,0]
	v_pk_add_f32 v[90:91], v[90:91], v[24:25] op_sel_hi:[1,0]
	v_cvt_pk_f16_f32 v88, v88, v89
	v_cvt_pk_f16_f32 v89, v90, v91
	global_store_dwordx2 v212, v[88:89], s[22:23] offset:0 sc0 sc1
	v_pk_add_f32 v[92:93], v[92:93], v[26:27] op_sel_hi:[1,0]
	v_pk_add_f32 v[94:95], v[94:95], v[26:27] op_sel_hi:[1,0]
	v_cvt_pk_f16_f32 v92, v92, v93
	v_cvt_pk_f16_f32 v93, v94, v95
	global_store_dwordx2 v212, v[92:93], s[22:23] offset:256 sc0 sc1
	v_pk_add_f32 v[96:97], v[96:97], v[28:29] op_sel_hi:[1,0]
	v_pk_add_f32 v[98:99], v[98:99], v[28:29] op_sel_hi:[1,0]
	v_cvt_pk_f16_f32 v96, v96, v97
	v_cvt_pk_f16_f32 v97, v98, v99
	global_store_dwordx2 v212, v[96:97], s[22:23] offset:1024 sc0 sc1
	v_pk_add_f32 v[100:101], v[100:101], v[30:31] op_sel_hi:[1,0]
	v_pk_add_f32 v[102:103], v[102:103], v[30:31] op_sel_hi:[1,0]
	v_cvt_pk_f16_f32 v100, v100, v101
	v_cvt_pk_f16_f32 v101, v102, v103
	global_store_dwordx2 v212, v[100:101], s[22:23] offset:1280 sc0 sc1
	s_add_u32 s24, s29, 3
	s_lshl_b32 s8, s24, 11
	v_add_u32_e32 v212, s8, v23
	v_pk_add_f32 v[104:105], v[104:105], v[24:25] op_sel_hi:[1,0]
	v_pk_add_f32 v[106:107], v[106:107], v[24:25] op_sel_hi:[1,0]
	v_cvt_pk_f16_f32 v104, v104, v105
	v_cvt_pk_f16_f32 v105, v106, v107
	global_store_dwordx2 v212, v[104:105], s[22:23] offset:0 sc0 sc1
	v_pk_add_f32 v[108:109], v[108:109], v[26:27] op_sel_hi:[1,0]
	v_pk_add_f32 v[110:111], v[110:111], v[26:27] op_sel_hi:[1,0]
	v_cvt_pk_f16_f32 v108, v108, v109
	v_cvt_pk_f16_f32 v109, v110, v111
	global_store_dwordx2 v212, v[108:109], s[22:23] offset:256 sc0 sc1
	v_pk_add_f32 v[112:113], v[112:113], v[28:29] op_sel_hi:[1,0]
	v_pk_add_f32 v[114:115], v[114:115], v[28:29] op_sel_hi:[1,0]
	v_cvt_pk_f16_f32 v112, v112, v113
	v_cvt_pk_f16_f32 v113, v114, v115
	global_store_dwordx2 v212, v[112:113], s[22:23] offset:1024 sc0 sc1
	v_pk_add_f32 v[116:117], v[116:117], v[30:31] op_sel_hi:[1,0]
	v_pk_add_f32 v[118:119], v[118:119], v[30:31] op_sel_hi:[1,0]
	v_cvt_pk_f16_f32 v116, v116, v117
	v_cvt_pk_f16_f32 v117, v118, v119
	global_store_dwordx2 v212, v[116:117], s[22:23] offset:1280 sc0 sc1
	s_add_u32 s24, s29, 4
	s_lshl_b32 s8, s24, 11
	v_add_u32_e32 v212, s8, v23
	v_pk_add_f32 v[120:121], v[120:121], v[24:25] op_sel_hi:[1,0]
	v_pk_add_f32 v[122:123], v[122:123], v[24:25] op_sel_hi:[1,0]
	v_cvt_pk_f16_f32 v120, v120, v121
	v_cvt_pk_f16_f32 v121, v122, v123
	global_store_dwordx2 v212, v[120:121], s[22:23] offset:0 sc0 sc1
	v_pk_add_f32 v[124:125], v[124:125], v[26:27] op_sel_hi:[1,0]
	v_pk_add_f32 v[126:127], v[126:127], v[26:27] op_sel_hi:[1,0]
	v_cvt_pk_f16_f32 v124, v124, v125
	v_cvt_pk_f16_f32 v125, v126, v127
	global_store_dwordx2 v212, v[124:125], s[22:23] offset:256 sc0 sc1
	v_pk_add_f32 v[128:129], v[128:129], v[28:29] op_sel_hi:[1,0]
	v_pk_add_f32 v[130:131], v[130:131], v[28:29] op_sel_hi:[1,0]
	v_cvt_pk_f16_f32 v128, v128, v129
	v_cvt_pk_f16_f32 v129, v130, v131
	global_store_dwordx2 v212, v[128:129], s[22:23] offset:1024 sc0 sc1
	v_pk_add_f32 v[132:133], v[132:133], v[30:31] op_sel_hi:[1,0]
	v_pk_add_f32 v[134:135], v[134:135], v[30:31] op_sel_hi:[1,0]
	v_cvt_pk_f16_f32 v132, v132, v133
	v_cvt_pk_f16_f32 v133, v134, v135
	global_store_dwordx2 v212, v[132:133], s[22:23] offset:1280 sc0 sc1
	s_branch .Lpf_done
.Lpf_vVB:
	s_lshl_b32 s25, s25, 6
	s_add_u32 s25, s25, 32
	s_add_u32 s29, s10, s25
	s_lshr_b32 s29, s29, 4
	v_add_u32_e32 v5, s25, v3
	v_lshlrev_b32_e32 v5, 7, v5
	v_add_u32_e32 v15, v5, v6
	v_add_u32_e32 v16, v5, v7
	v_add_u32_e32 v5, 0x9000, v9
	v_add_u32_e32 v17, v5, v6
	v_add_u32_e32 v18, v5, v7
	v_add_u32_e32 v19, 0x1a000, v15
	v_add_u32_e32 v20, 0x1a000, v16
	v_add_u32_e32 v21, 0x1a000, v17
	v_add_u32_e32 v22, 0x1a000, v18
	v_lshlrev_b32_e32 v5, 2, v3
	global_load_dword v24, v5, s[14:15] offset:0
	global_load_dword v26, v5, s[14:15] offset:64
	global_load_dword v28, v5, s[14:15] offset:128
	global_load_dword v30, v5, s[14:15] offset:192
	s_add_u32 m0, s28, 0x0
	s_nop 0
	global_load_lds_dwordx4 v10, s[4:5]
	s_add_u32 m0, s28, 0x2000
	s_nop 0
	global_load_lds_dwordx4 v11, s[4:5]
	s_add_u32 m0, s28, 0x4000
	s_nop 0
	global_load_lds_dwordx4 v12, s[4:5]
	s_add_u32 m0, s28, 0x6000
	s_nop 0
	global_load_lds_dwordx4 v13, s[4:5]
	s_add_u32 s4, s4, s20
	s_addc_u32 s5, s5, 0
	s_add_u32 m0, s28, 0x9000
	s_nop 0
	global_load_lds_dwordx4 v10, s[6:7]
	s_add_u32 m0, s28, 0xb000
	s_nop 0
	global_load_lds_dwordx4 v11, s[6:7]
	s_add_u32 s6, s6, s20
	s_addc_u32 s7, s7, 0
	s_add_u32 m0, s28, 0xd000
	s_nop 0
	global_load_lds_dwordx4 v10, s[4:5]
	s_add_u32 m0, s28, 0xf000
	s_nop 0
	global_load_lds_dwordx4 v11, s[4:5]
	s_add_u32 m0, s28, 0x11000
	s_nop 0
	global_load_lds_dwordx4 v12, s[4:5]
	s_add_u32 m0, s28, 0x13000
	s_nop 0
	global_load_lds_dwordx4 v13, s[4:5]
	s_add_u32 s4, s4, s20
	s_addc_u32 s5, s5, 0
	s_add_u32 m0, s28, 0x16000
	s_nop 0
	global_load_lds_dwordx4 v10, s[6:7]
	s_add_u32 m0, s28, 0x18000
	s_nop 0
	global_load_lds_dwordx4 v11, s[6:7]
	s_add_u32 s6, s6, s20
	s_addc_u32 s7, s7, 0
	s_add_u32 m0, s28, 0x1a000
	s_nop 0
	global_load_lds_dwordx4 v10, s[4:5]
	s_add_u32 m0, s28, 0x1c000
	s_nop 0
	global_load_lds_dwordx4 v11, s[4:5]
	s_add_u32 m0, s28, 0x1e000
	s_nop 0
	global_load_lds_dwordx4 v12, s[4:5]
	s_add_u32 m0, s28, 0x20000
	s_nop 0
	global_load_lds_dwordx4 v13, s[4:5]
	s_add_u32 s4, s4, s20
	s_addc_u32 s5, s5, 0
	s_add_u32 m0, s28, 0x23000
	s_nop 0
	global_load_lds_dwordx4 v10, s[6:7]
	s_add_u32 m0, s28, 0x25000
	s_nop 0
	global_load_lds_dwordx4 v11, s[6:7]
	s_add_u32 s6, s6, s20
	s_addc_u32 s7, s7, 0
	s_waitcnt vmcnt(12) lgkmcnt(0)
	s_barrier
	s_waitcnt lgkmcnt(7)
	ds_read_b128 v[136:139], v15
	ds_read_b128 v[156:159], v17
	ds_read_b128 v[160:163], v17 offset:2048
	ds_read_b128 v[164:167], v17 offset:4096
	ds_read_b128 v[168:171], v17 offset:6144
	ds_read_b128 v[140:143], v15 offset:2048
	ds_read_b128 v[144:147], v15 offset:4096
	ds_read_b128 v[148:151], v15 offset:6144
	s_waitcnt lgkmcnt(7)
	ds_read_b128 v[172:175], v16
	ds_read_b128 v[192:195], v18
	ds_read_b128 v[196:199], v18 offset:2048
	ds_read_b128 v[200:203], v18 offset:4096
	ds_read_b128 v[204:207], v18 offset:6144
	ds_read_b128 v[176:179], v16 offset:2048
	ds_read_b128 v[180:183], v16 offset:4096
	ds_read_b128 v[184:187], v16 offset:6144
	s_waitcnt lgkmcnt(14)
	v_mfma_f32_16x16x32_f16 v[56:59], v[136:139], v[156:159], 0
	s_waitcnt lgkmcnt(13)
	v_mfma_f32_16x16x32_f16 v[60:63], v[136:139], v[160:163], 0
	s_waitcnt lgkmcnt(12)
	v_mfma_f32_16x16x32_f16 v[64:67], v[136:139], v[164:167], 0
	s_waitcnt lgkmcnt(11)
	v_mfma_f32_16x16x32_f16 v[68:71], v[136:139], v[168:171], 0
	s_waitcnt lgkmcnt(10)
	v_mfma_f32_16x16x32_f16 v[72:75], v[140:143], v[156:159], 0
	v_mfma_f32_16x16x32_f16 v[76:79], v[140:143], v[160:163], 0
	v_mfma_f32_16x16x32_f16 v[80:83], v[140:143], v[164:167], 0
	v_mfma_f32_16x16x32_f16 v[84:87], v[140:143], v[168:171], 0
	s_waitcnt lgkmcnt(9)
	v_mfma_f32_16x16x32_f16 v[88:91], v[144:147], v[156:159], 0
	v_mfma_f32_16x16x32_f16 v[92:95], v[144:147], v[160:163], 0
	v_mfma_f32_16x16x32_f16 v[96:99], v[144:147], v[164:167], 0
	v_mfma_f32_16x16x32_f16 v[100:103], v[144:147], v[168:171], 0
	s_waitcnt lgkmcnt(8)
	v_mfma_f32_16x16x32_f16 v[104:107], v[148:151], v[156:159], 0
	v_mfma_f32_16x16x32_f16 v[108:111], v[148:151], v[160:163], 0
	v_mfma_f32_16x16x32_f16 v[112:115], v[148:151], v[164:167], 0
	v_mfma_f32_16x16x32_f16 v[116:119], v[148:151], v[168:171], 0
	s_waitcnt vmcnt(6) lgkmcnt(0)
	s_barrier
	s_waitcnt lgkmcnt(7)
	ds_read_b128 v[136:139], v15 offset:53248
	ds_read_b128 v[156:159], v17 offset:53248
	ds_read_b128 v[160:163], v17 offset:55296
	ds_read_b128 v[164:167], v17 offset:57344
	ds_read_b128 v[168:171], v17 offset:59392
	ds_read_b128 v[140:143], v15 offset:55296
	ds_read_b128 v[144:147], v15 offset:57344
	ds_read_b128 v[148:151], v15 offset:59392
	s_waitcnt lgkmcnt(14)
	v_mfma_f32_16x16x32_f16 v[56:59], v[172:175], v[192:195], v[56:59]
	s_add_u32 m0, s28, 0x0
	s_nop 0
	global_load_lds_dwordx4 v10, s[4:5]
	s_waitcnt lgkmcnt(13)
	v_mfma_f32_16x16x32_f16 v[60:63], v[172:175], v[196:199], v[60:63]
	s_waitcnt lgkmcnt(12)
	v_mfma_f32_16x16x32_f16 v[64:67], v[172:175], v[200:203], v[64:67]
	s_waitcnt lgkmcnt(11)
	v_mfma_f32_16x16x32_f16 v[68:71], v[172:175], v[204:207], v[68:71]
	s_waitcnt lgkmcnt(10)
	v_mfma_f32_16x16x32_f16 v[72:75], v[176:179], v[192:195], v[72:75]
	v_mfma_f32_16x16x32_f16 v[76:79], v[176:179], v[196:199], v[76:79]
	s_add_u32 m0, s28, 0x2000
	s_nop 0
	global_load_lds_dwordx4 v11, s[4:5]
	v_mfma_f32_16x16x32_f16 v[80:83], v[176:179], v[200:203], v[80:83]
	v_mfma_f32_16x16x32_f16 v[84:87], v[176:179], v[204:207], v[84:87]
	s_waitcnt lgkmcnt(9)
	v_mfma_f32_16x16x32_f16 v[88:91], v[180:183], v[192:195], v[88:91]
	v_mfma_f32_16x16x32_f16 v[92:95], v[180:183], v[196:199], v[92:95]
	v_mfma_f32_16x16x32_f16 v[96:99], v[180:183], v[200:203], v[96:99]
	s_add_u32 m0, s28, 0x4000
	s_nop 0
	global_load_lds_dwordx4 v12, s[4:5]
	v_mfma_f32_16x16x32_f16 v[100:103], v[180:183], v[204:207], v[100:103]
	s_waitcnt lgkmcnt(8)
	v_mfma_f32_16x16x32_f16 v[104:107], v[184:187], v[192:195], v[104:107]
	v_mfma_f32_16x16x32_f16 v[108:111], v[184:187], v[196:199], v[108:111]
	v_mfma_f32_16x16x32_f16 v[112:115], v[184:187], v[200:203], v[112:115]
	v_mfma_f32_16x16x32_f16 v[116:119], v[184:187], v[204:207], v[116:119]
	s_waitcnt lgkmcnt(7)
	ds_read_b128 v[172:175], v16 offset:53248
	ds_read_b128 v[192:195], v18 offset:53248
	ds_read_b128 v[196:199], v18 offset:55296
	ds_read_b128 v[200:203], v18 offset:57344
	ds_read_b128 v[204:207], v18 offset:59392
	ds_read_b128 v[176:179], v16 offset:55296
	ds_read_b128 v[180:183], v16 offset:57344
	ds_read_b128 v[184:187], v16 offset:59392
	s_waitcnt lgkmcnt(14)
	v_mfma_f32_16x16x32_f16 v[56:59], v[136:139], v[156:159], v[56:59]
	s_add_u32 m0, s28, 0x6000
	s_nop 0
	global_load_lds_dwordx4 v13, s[4:5]
	s_add_u32 s4, s4, s20
	s_addc_u32 s5, s5, 0
	s_waitcnt lgkmcnt(13)
	v_mfma_f32_16x16x32_f16 v[60:63], v[136:139], v[160:163], v[60:63]
	s_waitcnt lgkmcnt(12)
	v_mfma_f32_16x16x32_f16 v[64:67], v[136:139], v[164:167], v[64:67]
	s_waitcnt lgkmcnt(11)
	v_mfma_f32_16x16x32_f16 v[68:71], v[136:139], v[168:171], v[68:71]
	s_waitcnt lgkmcnt(10)
	v_mfma_f32_16x16x32_f16 v[72:75], v[140:143], v[156:159], v[72:75]
	v_mfma_f32_16x16x32_f16 v[76:79], v[140:143], v[160:163], v[76:79]
	s_add_u32 m0, s28, 0x9000
	s_nop 0
	global_load_lds_dwordx4 v10, s[6:7]
	v_mfma_f32_16x16x32_f16 v[80:83], v[140:143], v[164:167], v[80:83]
	v_mfma_f32_16x16x32_f16 v[84:87], v[140:143], v[168:171], v[84:87]
	s_waitcnt lgkmcnt(9)
	v_mfma_f32_16x16x32_f16 v[88:91], v[144:147], v[156:159], v[88:91]
	v_mfma_f32_16x16x32_f16 v[92:95], v[144:147], v[160:163], v[92:95]
	v_mfma_f32_16x16x32_f16 v[96:99], v[144:147], v[164:167], v[96:99]
	s_add_u32 m0, s28, 0xb000
	s_nop 0
	global_load_lds_dwordx4 v11, s[6:7]
	s_add_u32 s6, s6, s20
	s_addc_u32 s7, s7, 0
	v_mfma_f32_16x16x32_f16 v[100:103], v[144:147], v[168:171], v[100:103]
	s_waitcnt lgkmcnt(8)
	v_mfma_f32_16x16x32_f16 v[104:107], v[148:151], v[156:159], v[104:107]
	v_mfma_f32_16x16x32_f16 v[108:111], v[148:151], v[160:163], v[108:111]
	v_mfma_f32_16x16x32_f16 v[112:115], v[148:151], v[164:167], v[112:115]
	v_mfma_f32_16x16x32_f16 v[116:119], v[148:151], v[168:171], v[116:119]
	s_waitcnt vmcnt(6) lgkmcnt(0)
	s_barrier
	s_waitcnt lgkmcnt(7)
	ds_read_b128 v[136:139], v19
	ds_read_b128 v[156:159], v21
	ds_read_b128 v[160:163], v21 offset:2048
	ds_read_b128 v[164:167], v21 offset:4096
	ds_read_b128 v[168:171], v21 offset:6144
	ds_read_b128 v[140:143], v19 offset:2048
	ds_read_b128 v[144:147], v19 offset:4096
	ds_read_b128 v[148:151], v19 offset:6144
	s_waitcnt lgkmcnt(14)
	v_mfma_f32_16x16x32_f16 v[56:59], v[172:175], v[192:195], v[56:59]
	s_add_u32 m0, s28, 0xd000
	s_nop 0
	global_load_lds_dwordx4 v10, s[4:5]
	s_waitcnt lgkmcnt(13)
	v_mfma_f32_16x16x32_f16 v[60:63], v[172:175], v[196:199], v[60:63]
	s_waitcnt lgkmcnt(12)
	v_mfma_f32_16x16x32_f16 v[64:67], v[172:175], v[200:203], v[64:67]
	s_waitcnt lgkmcnt(11)
	v_mfma_f32_16x16x32_f16 v[68:71], v[172:175], v[204:207], v[68:71]
	s_waitcnt lgkmcnt(10)
	v_mfma_f32_16x16x32_f16 v[72:75], v[176:179], v[192:195], v[72:75]
	v_mfma_f32_16x16x32_f16 v[76:79], v[176:179], v[196:199], v[76:79]
	s_add_u32 m0, s28, 0xf000
	s_nop 0
	global_load_lds_dwordx4 v11, s[4:5]
	v_mfma_f32_16x16x32_f16 v[80:83], v[176:179], v[200:203], v[80:83]
	v_mfma_f32_16x16x32_f16 v[84:87], v[176:179], v[204:207], v[84:87]
	s_waitcnt lgkmcnt(9)
	v_mfma_f32_16x16x32_f16 v[88:91], v[180:183], v[192:195], v[88:91]
	v_mfma_f32_16x16x32_f16 v[92:95], v[180:183], v[196:199], v[92:95]
	v_mfma_f32_16x16x32_f16 v[96:99], v[180:183], v[200:203], v[96:99]
	s_add_u32 m0, s28, 0x11000
	s_nop 0
	global_load_lds_dwordx4 v12, s[4:5]
	v_mfma_f32_16x16x32_f16 v[100:103], v[180:183], v[204:207], v[100:103]
	s_waitcnt lgkmcnt(8)
	v_mfma_f32_16x16x32_f16 v[104:107], v[184:187], v[192:195], v[104:107]
	v_mfma_f32_16x16x32_f16 v[108:111], v[184:187], v[196:199], v[108:111]
	v_mfma_f32_16x16x32_f16 v[112:115], v[184:187], v[200:203], v[112:115]
	v_mfma_f32_16x16x32_f16 v[116:119], v[184:187], v[204:207], v[116:119]
	s_waitcnt lgkmcnt(7)
	ds_read_b128 v[172:175], v20
	ds_read_b128 v[192:195], v22
	ds_read_b128 v[196:199], v22 offset:2048
	ds_read_b128 v[200:203], v22 offset:4096
	ds_read_b128 v[204:207], v22 offset:6144
	ds_read_b128 v[176:179], v20 offset:2048
	ds_read_b128 v[180:183], v20 offset:4096
	ds_read_b128 v[184:187], v20 offset:6144
	s_waitcnt lgkmcnt(14)
	v_mfma_f32_16x16x32_f16 v[56:59], v[136:139], v[156:159], v[56:59]
	s_add_u32 m0, s28, 0x13000
	s_nop 0
	global_load_lds_dwordx4 v13, s[4:5]
	s_add_u32 s4, s4, s20
	s_addc_u32 s5, s5, 0
	s_waitcnt lgkmcnt(13)
	v_mfma_f32_16x16x32_f16 v[60:63], v[136:139], v[160:163], v[60:63]
	s_waitcnt lgkmcnt(12)
	v_mfma_f32_16x16x32_f16 v[64:67], v[136:139], v[164:167], v[64:67]
	s_waitcnt lgkmcnt(11)
	v_mfma_f32_16x16x32_f16 v[68:71], v[136:139], v[168:171], v[68:71]
	s_waitcnt lgkmcnt(10)
	v_mfma_f32_16x16x32_f16 v[72:75], v[140:143], v[156:159], v[72:75]
	v_mfma_f32_16x16x32_f16 v[76:79], v[140:143], v[160:163], v[76:79]
	s_add_u32 m0, s28, 0x16000
	s_nop 0
	global_load_lds_dwordx4 v10, s[6:7]
	v_mfma_f32_16x16x32_f16 v[80:83], v[140:143], v[164:167], v[80:83]
	v_mfma_f32_16x16x32_f16 v[84:87], v[140:143], v[168:171], v[84:87]
	s_waitcnt lgkmcnt(9)
	v_mfma_f32_16x16x32_f16 v[88:91], v[144:147], v[156:159], v[88:91]
	v_mfma_f32_16x16x32_f16 v[92:95], v[144:147], v[160:163], v[92:95]
	v_mfma_f32_16x16x32_f16 v[96:99], v[144:147], v[164:167], v[96:99]
	s_add_u32 m0, s28, 0x18000
	s_nop 0
	global_load_lds_dwordx4 v11, s[6:7]
	s_add_u32 s6, s6, s20
	s_addc_u32 s7, s7, 0
	v_mfma_f32_16x16x32_f16 v[100:103], v[144:147], v[168:171], v[100:103]
	s_waitcnt lgkmcnt(8)
	v_mfma_f32_16x16x32_f16 v[104:107], v[148:151], v[156:159], v[104:107]
	v_mfma_f32_16x16x32_f16 v[108:111], v[148:151], v[160:163], v[108:111]
	v_mfma_f32_16x16x32_f16 v[112:115], v[148:151], v[164:167], v[112:115]
	v_mfma_f32_16x16x32_f16 v[116:119], v[148:151], v[168:171], v[116:119]
	s_waitcnt vmcnt(6) lgkmcnt(0)
	s_barrier
	s_waitcnt lgkmcnt(7)
	ds_read_b128 v[136:139], v15
	ds_read_b128 v[156:159], v17
	ds_read_b128 v[160:163], v17 offset:2048
	ds_read_b128 v[164:167], v17 offset:4096
	ds_read_b128 v[168:171], v17 offset:6144
	ds_read_b128 v[140:143], v15 offset:2048
	ds_read_b128 v[144:147], v15 offset:4096
	ds_read_b128 v[148:151], v15 offset:6144
	s_waitcnt lgkmcnt(14)
	v_mfma_f32_16x16x32_f16 v[56:59], v[172:175], v[192:195], v[56:59]
	s_add_u32 m0, s28, 0x1a000
	s_nop 0
	global_load_lds_dwordx4 v10, s[4:5]
	s_waitcnt lgkmcnt(13)
	v_mfma_f32_16x16x32_f16 v[60:63], v[172:175], v[196:199], v[60:63]
	s_waitcnt lgkmcnt(12)
	v_mfma_f32_16x16x32_f16 v[64:67], v[172:175], v[200:203], v[64:67]
	s_waitcnt lgkmcnt(11)
	v_mfma_f32_16x16x32_f16 v[68:71], v[172:175], v[204:207], v[68:71]
	s_waitcnt lgkmcnt(10)
	v_mfma_f32_16x16x32_f16 v[72:75], v[176:179], v[192:195], v[72:75]
	v_mfma_f32_16x16x32_f16 v[76:79], v[176:179], v[196:199], v[76:79]
	s_add_u32 m0, s28, 0x1c000
	s_nop 0
	global_load_lds_dwordx4 v11, s[4:5]
	v_mfma_f32_16x16x32_f16 v[80:83], v[176:179], v[200:203], v[80:83]
	v_mfma_f32_16x16x32_f16 v[84:87], v[176:179], v[204:207], v[84:87]
	s_waitcnt lgkmcnt(9)
	v_mfma_f32_16x16x32_f16 v[88:91], v[180:183], v[192:195], v[88:91]
	v_mfma_f32_16x16x32_f16 v[92:95], v[180:183], v[196:199], v[92:95]
	v_mfma_f32_16x16x32_f16 v[96:99], v[180:183], v[200:203], v[96:99]
	s_add_u32 m0, s28, 0x1e000
	s_nop 0
	global_load_lds_dwordx4 v12, s[4:5]
	v_mfma_f32_16x16x32_f16 v[100:103], v[180:183], v[204:207], v[100:103]
	s_waitcnt lgkmcnt(8)
	v_mfma_f32_16x16x32_f16 v[104:107], v[184:187], v[192:195], v[104:107]
	v_mfma_f32_16x16x32_f16 v[108:111], v[184:187], v[196:199], v[108:111]
	v_mfma_f32_16x16x32_f16 v[112:115], v[184:187], v[200:203], v[112:115]
	v_mfma_f32_16x16x32_f16 v[116:119], v[184:187], v[204:207], v[116:119]
	s_waitcnt lgkmcnt(7)
	ds_read_b128 v[172:175], v16
	ds_read_b128 v[192:195], v18
	ds_read_b128 v[196:199], v18 offset:2048
	ds_read_b128 v[200:203], v18 offset:4096
	ds_read_b128 v[204:207], v18 offset:6144
	ds_read_b128 v[176:179], v16 offset:2048
	ds_read_b128 v[180:183], v16 offset:4096
	ds_read_b128 v[184:187], v16 offset:6144
	s_waitcnt lgkmcnt(14)
	v_mfma_f32_16x16x32_f16 v[56:59], v[136:139], v[156:159], v[56:59]
	s_add_u32 m0, s28, 0x20000
	s_nop 0
	global_load_lds_dwordx4 v13, s[4:5]
	s_add_u32 s4, s4, s20
	s_addc_u32 s5, s5, 0
	s_waitcnt lgkmcnt(13)
	v_mfma_f32_16x16x32_f16 v[60:63], v[136:139], v[160:163], v[60:63]
	s_waitcnt lgkmcnt(12)
	v_mfma_f32_16x16x32_f16 v[64:67], v[136:139], v[164:167], v[64:67]
	s_waitcnt lgkmcnt(11)
	v_mfma_f32_16x16x32_f16 v[68:71], v[136:139], v[168:171], v[68:71]
	s_waitcnt lgkmcnt(10)
	v_mfma_f32_16x16x32_f16 v[72:75], v[140:143], v[156:159], v[72:75]
	v_mfma_f32_16x16x32_f16 v[76:79], v[140:143], v[160:163], v[76:79]
	s_add_u32 m0, s28, 0x23000
	s_nop 0
	global_load_lds_dwordx4 v10, s[6:7]
	v_mfma_f32_16x16x32_f16 v[80:83], v[140:143], v[164:167], v[80:83]
	v_mfma_f32_16x16x32_f16 v[84:87], v[140:143], v[168:171], v[84:87]
	s_waitcnt lgkmcnt(9)
	v_mfma_f32_16x16x32_f16 v[88:91], v[144:147], v[156:159], v[88:91]
	v_mfma_f32_16x16x32_f16 v[92:95], v[144:147], v[160:163], v[92:95]
	v_mfma_f32_16x16x32_f16 v[96:99], v[144:147], v[164:167], v[96:99]
	s_add_u32 m0, s28, 0x25000
	s_nop 0
	global_load_lds_dwordx4 v11, s[6:7]
	s_add_u32 s6, s6, s20
	s_addc_u32 s7, s7, 0
	v_mfma_f32_16x16x32_f16 v[100:103], v[144:147], v[168:171], v[100:103]
	s_waitcnt lgkmcnt(8)
	v_mfma_f32_16x16x32_f16 v[104:107], v[148:151], v[156:159], v[104:107]
	v_mfma_f32_16x16x32_f16 v[108:111], v[148:151], v[160:163], v[108:111]
	v_mfma_f32_16x16x32_f16 v[112:115], v[148:151], v[164:167], v[112:115]
	v_mfma_f32_16x16x32_f16 v[116:119], v[148:151], v[168:171], v[116:119]
	s_waitcnt vmcnt(6) lgkmcnt(0)
	s_barrier
	s_waitcnt lgkmcnt(7)
	ds_read_b128 v[136:139], v15 offset:53248
	ds_read_b128 v[156:159], v17 offset:53248
	ds_read_b128 v[160:163], v17 offset:55296
	ds_read_b128 v[164:167], v17 offset:57344
	ds_read_b128 v[168:171], v17 offset:59392
	ds_read_b128 v[140:143], v15 offset:55296
	ds_read_b128 v[144:147], v15 offset:57344
	ds_read_b128 v[148:151], v15 offset:59392
	s_waitcnt lgkmcnt(14)
	v_mfma_f32_16x16x32_f16 v[56:59], v[172:175], v[192:195], v[56:59]
	s_add_u32 m0, s28, 0x0
	s_nop 0
	global_load_lds_dwordx4 v10, s[4:5]
	s_waitcnt lgkmcnt(13)
	v_mfma_f32_16x16x32_f16 v[60:63], v[172:175], v[196:199], v[60:63]
	s_waitcnt lgkmcnt(12)
	v_mfma_f32_16x16x32_f16 v[64:67], v[172:175], v[200:203], v[64:67]
	s_waitcnt lgkmcnt(11)
	v_mfma_f32_16x16x32_f16 v[68:71], v[172:175], v[204:207], v[68:71]
	s_waitcnt lgkmcnt(10)
	v_mfma_f32_16x16x32_f16 v[72:75], v[176:179], v[192:195], v[72:75]
	v_mfma_f32_16x16x32_f16 v[76:79], v[176:179], v[196:199], v[76:79]
	s_add_u32 m0, s28, 0x2000
	s_nop 0
	global_load_lds_dwordx4 v11, s[4:5]
	v_mfma_f32_16x16x32_f16 v[80:83], v[176:179], v[200:203], v[80:83]
	v_mfma_f32_16x16x32_f16 v[84:87], v[176:179], v[204:207], v[84:87]
	s_waitcnt lgkmcnt(9)
	v_mfma_f32_16x16x32_f16 v[88:91], v[180:183], v[192:195], v[88:91]
	v_mfma_f32_16x16x32_f16 v[92:95], v[180:183], v[196:199], v[92:95]
	v_mfma_f32_16x16x32_f16 v[96:99], v[180:183], v[200:203], v[96:99]
	s_add_u32 m0, s28, 0x4000
	s_nop 0
	global_load_lds_dwordx4 v12, s[4:5]
	v_mfma_f32_16x16x32_f16 v[100:103], v[180:183], v[204:207], v[100:103]
	s_waitcnt lgkmcnt(8)
	v_mfma_f32_16x16x32_f16 v[104:107], v[184:187], v[192:195], v[104:107]
	v_mfma_f32_16x16x32_f16 v[108:111], v[184:187], v[196:199], v[108:111]
	v_mfma_f32_16x16x32_f16 v[112:115], v[184:187], v[200:203], v[112:115]
	v_mfma_f32_16x16x32_f16 v[116:119], v[184:187], v[204:207], v[116:119]
	s_waitcnt lgkmcnt(7)
	ds_read_b128 v[172:175], v16 offset:53248
	ds_read_b128 v[192:195], v18 offset:53248
	ds_read_b128 v[196:199], v18 offset:55296
	ds_read_b128 v[200:203], v18 offset:57344
	ds_read_b128 v[204:207], v18 offset:59392
	ds_read_b128 v[176:179], v16 offset:55296
	ds_read_b128 v[180:183], v16 offset:57344
	ds_read_b128 v[184:187], v16 offset:59392
	s_waitcnt lgkmcnt(14)
	v_mfma_f32_16x16x32_f16 v[56:59], v[136:139], v[156:159], v[56:59]
	s_add_u32 m0, s28, 0x6000
	s_nop 0
	global_load_lds_dwordx4 v13, s[4:5]
	s_add_u32 s4, s4, s20
	s_addc_u32 s5, s5, 0
	s_waitcnt lgkmcnt(13)
	v_mfma_f32_16x16x32_f16 v[60:63], v[136:139], v[160:163], v[60:63]
	s_waitcnt lgkmcnt(12)
	v_mfma_f32_16x16x32_f16 v[64:67], v[136:139], v[164:167], v[64:67]
	s_waitcnt lgkmcnt(11)
	v_mfma_f32_16x16x32_f16 v[68:71], v[136:139], v[168:171], v[68:71]
	s_waitcnt lgkmcnt(10)
	v_mfma_f32_16x16x32_f16 v[72:75], v[140:143], v[156:159], v[72:75]
	v_mfma_f32_16x16x32_f16 v[76:79], v[140:143], v[160:163], v[76:79]
	s_add_u32 m0, s28, 0x9000
	s_nop 0
	global_load_lds_dwordx4 v10, s[6:7]
	v_mfma_f32_16x16x32_f16 v[80:83], v[140:143], v[164:167], v[80:83]
	v_mfma_f32_16x16x32_f16 v[84:87], v[140:143], v[168:171], v[84:87]
	s_waitcnt lgkmcnt(9)
	v_mfma_f32_16x16x32_f16 v[88:91], v[144:147], v[156:159], v[88:91]
	v_mfma_f32_16x16x32_f16 v[92:95], v[144:147], v[160:163], v[92:95]
	v_mfma_f32_16x16x32_f16 v[96:99], v[144:147], v[164:167], v[96:99]
	s_add_u32 m0, s28, 0xb000
	s_nop 0
	global_load_lds_dwordx4 v11, s[6:7]
	s_add_u32 s6, s6, s20
	s_addc_u32 s7, s7, 0
	v_mfma_f32_16x16x32_f16 v[100:103], v[144:147], v[168:171], v[100:103]
	s_waitcnt lgkmcnt(8)
	v_mfma_f32_16x16x32_f16 v[104:107], v[148:151], v[156:159], v[104:107]
	v_mfma_f32_16x16x32_f16 v[108:111], v[148:151], v[160:163], v[108:111]
	v_mfma_f32_16x16x32_f16 v[112:115], v[148:151], v[164:167], v[112:115]
	v_mfma_f32_16x16x32_f16 v[116:119], v[148:151], v[168:171], v[116:119]
	s_waitcnt vmcnt(6) lgkmcnt(0)
	s_barrier
	s_waitcnt lgkmcnt(7)
	ds_read_b128 v[136:139], v19
	ds_read_b128 v[156:159], v21
	ds_read_b128 v[160:163], v21 offset:2048
	ds_read_b128 v[164:167], v21 offset:4096
	ds_read_b128 v[168:171], v21 offset:6144
	ds_read_b128 v[140:143], v19 offset:2048
	ds_read_b128 v[144:147], v19 offset:4096
	ds_read_b128 v[148:151], v19 offset:6144
	s_waitcnt lgkmcnt(14)
	v_mfma_f32_16x16x32_f16 v[56:59], v[172:175], v[192:195], v[56:59]
	s_add_u32 m0, s28, 0xd000
	s_nop 0
	global_load_lds_dwordx4 v10, s[4:5]
	s_waitcnt lgkmcnt(13)
	v_mfma_f32_16x16x32_f16 v[60:63], v[172:175], v[196:199], v[60:63]
	s_waitcnt lgkmcnt(12)
	v_mfma_f32_16x16x32_f16 v[64:67], v[172:175], v[200:203], v[64:67]
	s_waitcnt lgkmcnt(11)
	v_mfma_f32_16x16x32_f16 v[68:71], v[172:175], v[204:207], v[68:71]
	s_waitcnt lgkmcnt(10)
	v_mfma_f32_16x16x32_f16 v[72:75], v[176:179], v[192:195], v[72:75]
	v_mfma_f32_16x16x32_f16 v[76:79], v[176:179], v[196:199], v[76:79]
	s_add_u32 m0, s28, 0xf000
	s_nop 0
	global_load_lds_dwordx4 v11, s[4:5]
	v_mfma_f32_16x16x32_f16 v[80:83], v[176:179], v[200:203], v[80:83]
	v_mfma_f32_16x16x32_f16 v[84:87], v[176:179], v[204:207], v[84:87]
	s_waitcnt lgkmcnt(9)
	v_mfma_f32_16x16x32_f16 v[88:91], v[180:183], v[192:195], v[88:91]
	v_mfma_f32_16x16x32_f16 v[92:95], v[180:183], v[196:199], v[92:95]
	v_mfma_f32_16x16x32_f16 v[96:99], v[180:183], v[200:203], v[96:99]
	s_add_u32 m0, s28, 0x11000
	s_nop 0
	global_load_lds_dwordx4 v12, s[4:5]
	v_mfma_f32_16x16x32_f16 v[100:103], v[180:183], v[204:207], v[100:103]
	s_waitcnt lgkmcnt(8)
	v_mfma_f32_16x16x32_f16 v[104:107], v[184:187], v[192:195], v[104:107]
	v_mfma_f32_16x16x32_f16 v[108:111], v[184:187], v[196:199], v[108:111]
	v_mfma_f32_16x16x32_f16 v[112:115], v[184:187], v[200:203], v[112:115]
	v_mfma_f32_16x16x32_f16 v[116:119], v[184:187], v[204:207], v[116:119]
	s_waitcnt lgkmcnt(7)
	ds_read_b128 v[172:175], v20
	ds_read_b128 v[192:195], v22
	ds_read_b128 v[196:199], v22 offset:2048
	ds_read_b128 v[200:203], v22 offset:4096
	ds_read_b128 v[204:207], v22 offset:6144
	ds_read_b128 v[176:179], v20 offset:2048
	ds_read_b128 v[180:183], v20 offset:4096
	ds_read_b128 v[184:187], v20 offset:6144
	s_waitcnt lgkmcnt(14)
	v_mfma_f32_16x16x32_f16 v[56:59], v[136:139], v[156:159], v[56:59]
	s_add_u32 m0, s28, 0x13000
	s_nop 0
	global_load_lds_dwordx4 v13, s[4:5]
	s_add_u32 s4, s4, s20
	s_addc_u32 s5, s5, 0
	s_waitcnt lgkmcnt(13)
	v_mfma_f32_16x16x32_f16 v[60:63], v[136:139], v[160:163], v[60:63]
	s_waitcnt lgkmcnt(12)
	v_mfma_f32_16x16x32_f16 v[64:67], v[136:139], v[164:167], v[64:67]
	s_waitcnt lgkmcnt(11)
	v_mfma_f32_16x16x32_f16 v[68:71], v[136:139], v[168:171], v[68:71]
	s_waitcnt lgkmcnt(10)
	v_mfma_f32_16x16x32_f16 v[72:75], v[140:143], v[156:159], v[72:75]
	v_mfma_f32_16x16x32_f16 v[76:79], v[140:143], v[160:163], v[76:79]
	s_add_u32 m0, s28, 0x16000
	s_nop 0
	global_load_lds_dwordx4 v10, s[6:7]
	v_mfma_f32_16x16x32_f16 v[80:83], v[140:143], v[164:167], v[80:83]
	v_mfma_f32_16x16x32_f16 v[84:87], v[140:143], v[168:171], v[84:87]
	s_waitcnt lgkmcnt(9)
	v_mfma_f32_16x16x32_f16 v[88:91], v[144:147], v[156:159], v[88:91]
	v_mfma_f32_16x16x32_f16 v[92:95], v[144:147], v[160:163], v[92:95]
	v_mfma_f32_16x16x32_f16 v[96:99], v[144:147], v[164:167], v[96:99]
	s_add_u32 m0, s28, 0x18000
	s_nop 0
	global_load_lds_dwordx4 v11, s[6:7]
	s_add_u32 s6, s6, s20
	s_addc_u32 s7, s7, 0
	v_mfma_f32_16x16x32_f16 v[100:103], v[144:147], v[168:171], v[100:103]
	s_waitcnt lgkmcnt(8)
	v_mfma_f32_16x16x32_f16 v[104:107], v[148:151], v[156:159], v[104:107]
	v_mfma_f32_16x16x32_f16 v[108:111], v[148:151], v[160:163], v[108:111]
	v_mfma_f32_16x16x32_f16 v[112:115], v[148:151], v[164:167], v[112:115]
	v_mfma_f32_16x16x32_f16 v[116:119], v[148:151], v[168:171], v[116:119]
	s_waitcnt vmcnt(6) lgkmcnt(0)
	s_barrier
	s_waitcnt lgkmcnt(7)
	ds_read_b128 v[136:139], v15
	ds_read_b128 v[156:159], v17
	ds_read_b128 v[160:163], v17 offset:2048
	ds_read_b128 v[164:167], v17 offset:4096
	ds_read_b128 v[168:171], v17 offset:6144
	ds_read_b128 v[140:143], v15 offset:2048
	ds_read_b128 v[144:147], v15 offset:4096
	ds_read_b128 v[148:151], v15 offset:6144
	s_waitcnt lgkmcnt(14)
	v_mfma_f32_16x16x32_f16 v[56:59], v[172:175], v[192:195], v[56:59]
	s_add_u32 m0, s28, 0x1a000
	s_nop 0
	global_load_lds_dwordx4 v10, s[4:5]
	s_waitcnt lgkmcnt(13)
	v_mfma_f32_16x16x32_f16 v[60:63], v[172:175], v[196:199], v[60:63]
	s_waitcnt lgkmcnt(12)
	v_mfma_f32_16x16x32_f16 v[64:67], v[172:175], v[200:203], v[64:67]
	s_waitcnt lgkmcnt(11)
	v_mfma_f32_16x16x32_f16 v[68:71], v[172:175], v[204:207], v[68:71]
	s_waitcnt lgkmcnt(10)
	v_mfma_f32_16x16x32_f16 v[72:75], v[176:179], v[192:195], v[72:75]
	v_mfma_f32_16x16x32_f16 v[76:79], v[176:179], v[196:199], v[76:79]
	s_add_u32 m0, s28, 0x1c000
	s_nop 0
	global_load_lds_dwordx4 v11, s[4:5]
	v_mfma_f32_16x16x32_f16 v[80:83], v[176:179], v[200:203], v[80:83]
	v_mfma_f32_16x16x32_f16 v[84:87], v[176:179], v[204:207], v[84:87]
	s_waitcnt lgkmcnt(9)
	v_mfma_f32_16x16x32_f16 v[88:91], v[180:183], v[192:195], v[88:91]
	v_mfma_f32_16x16x32_f16 v[92:95], v[180:183], v[196:199], v[92:95]
	v_mfma_f32_16x16x32_f16 v[96:99], v[180:183], v[200:203], v[96:99]
	s_add_u32 m0, s28, 0x1e000
	s_nop 0
	global_load_lds_dwordx4 v12, s[4:5]
	v_mfma_f32_16x16x32_f16 v[100:103], v[180:183], v[204:207], v[100:103]
	s_waitcnt lgkmcnt(8)
	v_mfma_f32_16x16x32_f16 v[104:107], v[184:187], v[192:195], v[104:107]
	v_mfma_f32_16x16x32_f16 v[108:111], v[184:187], v[196:199], v[108:111]
	v_mfma_f32_16x16x32_f16 v[112:115], v[184:187], v[200:203], v[112:115]
	v_mfma_f32_16x16x32_f16 v[116:119], v[184:187], v[204:207], v[116:119]
	s_waitcnt lgkmcnt(7)
	ds_read_b128 v[172:175], v16
	ds_read_b128 v[192:195], v18
	ds_read_b128 v[196:199], v18 offset:2048
	ds_read_b128 v[200:203], v18 offset:4096
	ds_read_b128 v[204:207], v18 offset:6144
	ds_read_b128 v[176:179], v16 offset:2048
	ds_read_b128 v[180:183], v16 offset:4096
	ds_read_b128 v[184:187], v16 offset:6144
	s_waitcnt lgkmcnt(14)
	v_mfma_f32_16x16x32_f16 v[56:59], v[136:139], v[156:159], v[56:59]
	s_add_u32 m0, s28, 0x20000
	s_nop 0
	global_load_lds_dwordx4 v13, s[4:5]
	s_add_u32 s4, s4, s20
	s_addc_u32 s5, s5, 0
	s_waitcnt lgkmcnt(13)
	v_mfma_f32_16x16x32_f16 v[60:63], v[136:139], v[160:163], v[60:63]
	s_waitcnt lgkmcnt(12)
	v_mfma_f32_16x16x32_f16 v[64:67], v[136:139], v[164:167], v[64:67]
	s_waitcnt lgkmcnt(11)
	v_mfma_f32_16x16x32_f16 v[68:71], v[136:139], v[168:171], v[68:71]
	s_waitcnt lgkmcnt(10)
	v_mfma_f32_16x16x32_f16 v[72:75], v[140:143], v[156:159], v[72:75]
	v_mfma_f32_16x16x32_f16 v[76:79], v[140:143], v[160:163], v[76:79]
	s_add_u32 m0, s28, 0x23000
	s_nop 0
	global_load_lds_dwordx4 v10, s[6:7]
	v_mfma_f32_16x16x32_f16 v[80:83], v[140:143], v[164:167], v[80:83]
	v_mfma_f32_16x16x32_f16 v[84:87], v[140:143], v[168:171], v[84:87]
	s_waitcnt lgkmcnt(9)
	v_mfma_f32_16x16x32_f16 v[88:91], v[144:147], v[156:159], v[88:91]
	v_mfma_f32_16x16x32_f16 v[92:95], v[144:147], v[160:163], v[92:95]
	v_mfma_f32_16x16x32_f16 v[96:99], v[144:147], v[164:167], v[96:99]
	s_add_u32 m0, s28, 0x25000
	s_nop 0
	global_load_lds_dwordx4 v11, s[6:7]
	s_add_u32 s6, s6, s20
	s_addc_u32 s7, s7, 0
	v_mfma_f32_16x16x32_f16 v[100:103], v[144:147], v[168:171], v[100:103]
	s_waitcnt lgkmcnt(8)
	v_mfma_f32_16x16x32_f16 v[104:107], v[148:151], v[156:159], v[104:107]
	v_mfma_f32_16x16x32_f16 v[108:111], v[148:151], v[160:163], v[108:111]
	v_mfma_f32_16x16x32_f16 v[112:115], v[148:151], v[164:167], v[112:115]
	v_mfma_f32_16x16x32_f16 v[116:119], v[148:151], v[168:171], v[116:119]
	s_waitcnt vmcnt(6) lgkmcnt(0)
	s_barrier
	s_waitcnt lgkmcnt(7)
	ds_read_b128 v[136:139], v15 offset:53248
	ds_read_b128 v[156:159], v17 offset:53248
	ds_read_b128 v[160:163], v17 offset:55296
	ds_read_b128 v[164:167], v17 offset:57344
	ds_read_b128 v[168:171], v17 offset:59392
	ds_read_b128 v[140:143], v15 offset:55296
	ds_read_b128 v[144:147], v15 offset:57344
	ds_read_b128 v[148:151], v15 offset:59392
	s_waitcnt lgkmcnt(14)
	v_mfma_f32_16x16x32_f16 v[56:59], v[172:175], v[192:195], v[56:59]
	s_add_u32 m0, s28, 0x0
	s_nop 0
	global_load_lds_dwordx4 v10, s[4:5]
	s_waitcnt lgkmcnt(13)
	v_mfma_f32_16x16x32_f16 v[60:63], v[172:175], v[196:199], v[60:63]
	s_waitcnt lgkmcnt(12)
	v_mfma_f32_16x16x32_f16 v[64:67], v[172:175], v[200:203], v[64:67]
	s_waitcnt lgkmcnt(11)
	v_mfma_f32_16x16x32_f16 v[68:71], v[172:175], v[204:207], v[68:71]
	s_waitcnt lgkmcnt(10)
	v_mfma_f32_16x16x32_f16 v[72:75], v[176:179], v[192:195], v[72:75]
	v_mfma_f32_16x16x32_f16 v[76:79], v[176:179], v[196:199], v[76:79]
	s_add_u32 m0, s28, 0x2000
	s_nop 0
	global_load_lds_dwordx4 v11, s[4:5]
	v_mfma_f32_16x16x32_f16 v[80:83], v[176:179], v[200:203], v[80:83]
	v_mfma_f32_16x16x32_f16 v[84:87], v[176:179], v[204:207], v[84:87]
	s_waitcnt lgkmcnt(9)
	v_mfma_f32_16x16x32_f16 v[88:91], v[180:183], v[192:195], v[88:91]
	v_mfma_f32_16x16x32_f16 v[92:95], v[180:183], v[196:199], v[92:95]
	v_mfma_f32_16x16x32_f16 v[96:99], v[180:183], v[200:203], v[96:99]
	s_add_u32 m0, s28, 0x4000
	s_nop 0
	global_load_lds_dwordx4 v12, s[4:5]
	v_mfma_f32_16x16x32_f16 v[100:103], v[180:183], v[204:207], v[100:103]
	s_waitcnt lgkmcnt(8)
	v_mfma_f32_16x16x32_f16 v[104:107], v[184:187], v[192:195], v[104:107]
	v_mfma_f32_16x16x32_f16 v[108:111], v[184:187], v[196:199], v[108:111]
	v_mfma_f32_16x16x32_f16 v[112:115], v[184:187], v[200:203], v[112:115]
	v_mfma_f32_16x16x32_f16 v[116:119], v[184:187], v[204:207], v[116:119]
	s_waitcnt lgkmcnt(7)
	ds_read_b128 v[172:175], v16 offset:53248
	ds_read_b128 v[192:195], v18 offset:53248
	ds_read_b128 v[196:199], v18 offset:55296
	ds_read_b128 v[200:203], v18 offset:57344
	ds_read_b128 v[204:207], v18 offset:59392
	ds_read_b128 v[176:179], v16 offset:55296
	ds_read_b128 v[180:183], v16 offset:57344
	ds_read_b128 v[184:187], v16 offset:59392
	s_waitcnt lgkmcnt(14)
	v_mfma_f32_16x16x32_f16 v[56:59], v[136:139], v[156:159], v[56:59]
	s_add_u32 m0, s28, 0x6000
	s_nop 0
	global_load_lds_dwordx4 v13, s[4:5]
	s_add_u32 s4, s4, s20
	s_addc_u32 s5, s5, 0
	s_waitcnt lgkmcnt(13)
	v_mfma_f32_16x16x32_f16 v[60:63], v[136:139], v[160:163], v[60:63]
	s_waitcnt lgkmcnt(12)
	v_mfma_f32_16x16x32_f16 v[64:67], v[136:139], v[164:167], v[64:67]
	s_waitcnt lgkmcnt(11)
	v_mfma_f32_16x16x32_f16 v[68:71], v[136:139], v[168:171], v[68:71]
	s_waitcnt lgkmcnt(10)
	v_mfma_f32_16x16x32_f16 v[72:75], v[140:143], v[156:159], v[72:75]
	v_mfma_f32_16x16x32_f16 v[76:79], v[140:143], v[160:163], v[76:79]
	s_add_u32 m0, s28, 0x9000
	s_nop 0
	global_load_lds_dwordx4 v10, s[6:7]
	v_mfma_f32_16x16x32_f16 v[80:83], v[140:143], v[164:167], v[80:83]
	v_mfma_f32_16x16x32_f16 v[84:87], v[140:143], v[168:171], v[84:87]
	s_waitcnt lgkmcnt(9)
	v_mfma_f32_16x16x32_f16 v[88:91], v[144:147], v[156:159], v[88:91]
	v_mfma_f32_16x16x32_f16 v[92:95], v[144:147], v[160:163], v[92:95]
	v_mfma_f32_16x16x32_f16 v[96:99], v[144:147], v[164:167], v[96:99]
	s_add_u32 m0, s28, 0xb000
	s_nop 0
	global_load_lds_dwordx4 v11, s[6:7]
	s_add_u32 s6, s6, s20
	s_addc_u32 s7, s7, 0
	v_mfma_f32_16x16x32_f16 v[100:103], v[144:147], v[168:171], v[100:103]
	s_waitcnt lgkmcnt(8)
	v_mfma_f32_16x16x32_f16 v[104:107], v[148:151], v[156:159], v[104:107]
	v_mfma_f32_16x16x32_f16 v[108:111], v[148:151], v[160:163], v[108:111]
	v_mfma_f32_16x16x32_f16 v[112:115], v[148:151], v[164:167], v[112:115]
	v_mfma_f32_16x16x32_f16 v[116:119], v[148:151], v[168:171], v[116:119]
	s_waitcnt vmcnt(6) lgkmcnt(0)
	s_barrier
	s_waitcnt lgkmcnt(7)
	ds_read_b128 v[136:139], v19
	ds_read_b128 v[156:159], v21
	ds_read_b128 v[160:163], v21 offset:2048
	ds_read_b128 v[164:167], v21 offset:4096
	ds_read_b128 v[168:171], v21 offset:6144
	ds_read_b128 v[140:143], v19 offset:2048
	ds_read_b128 v[144:147], v19 offset:4096
	ds_read_b128 v[148:151], v19 offset:6144
	s_waitcnt lgkmcnt(14)
	v_mfma_f32_16x16x32_f16 v[56:59], v[172:175], v[192:195], v[56:59]
	s_add_u32 m0, s28, 0xd000
	s_nop 0
	global_load_lds_dwordx4 v10, s[4:5]
	s_waitcnt lgkmcnt(13)
	v_mfma_f32_16x16x32_f16 v[60:63], v[172:175], v[196:199], v[60:63]
	s_waitcnt lgkmcnt(12)
	v_mfma_f32_16x16x32_f16 v[64:67], v[172:175], v[200:203], v[64:67]
	s_waitcnt lgkmcnt(11)
	v_mfma_f32_16x16x32_f16 v[68:71], v[172:175], v[204:207], v[68:71]
	s_waitcnt lgkmcnt(10)
	v_mfma_f32_16x16x32_f16 v[72:75], v[176:179], v[192:195], v[72:75]
	v_mfma_f32_16x16x32_f16 v[76:79], v[176:179], v[196:199], v[76:79]
	s_add_u32 m0, s28, 0xf000
	s_nop 0
	global_load_lds_dwordx4 v11, s[4:5]
	v_mfma_f32_16x16x32_f16 v[80:83], v[176:179], v[200:203], v[80:83]
	v_mfma_f32_16x16x32_f16 v[84:87], v[176:179], v[204:207], v[84:87]
	s_waitcnt lgkmcnt(9)
	v_mfma_f32_16x16x32_f16 v[88:91], v[180:183], v[192:195], v[88:91]
	v_mfma_f32_16x16x32_f16 v[92:95], v[180:183], v[196:199], v[92:95]
	v_mfma_f32_16x16x32_f16 v[96:99], v[180:183], v[200:203], v[96:99]
	s_add_u32 m0, s28, 0x11000
	s_nop 0
	global_load_lds_dwordx4 v12, s[4:5]
	v_mfma_f32_16x16x32_f16 v[100:103], v[180:183], v[204:207], v[100:103]
	s_waitcnt lgkmcnt(8)
	v_mfma_f32_16x16x32_f16 v[104:107], v[184:187], v[192:195], v[104:107]
	v_mfma_f32_16x16x32_f16 v[108:111], v[184:187], v[196:199], v[108:111]
	v_mfma_f32_16x16x32_f16 v[112:115], v[184:187], v[200:203], v[112:115]
	v_mfma_f32_16x16x32_f16 v[116:119], v[184:187], v[204:207], v[116:119]
	s_waitcnt lgkmcnt(7)
	ds_read_b128 v[172:175], v20
	ds_read_b128 v[192:195], v22
	ds_read_b128 v[196:199], v22 offset:2048
	ds_read_b128 v[200:203], v22 offset:4096
	ds_read_b128 v[204:207], v22 offset:6144
	ds_read_b128 v[176:179], v20 offset:2048
	ds_read_b128 v[180:183], v20 offset:4096
	ds_read_b128 v[184:187], v20 offset:6144
	s_waitcnt lgkmcnt(14)
	v_mfma_f32_16x16x32_f16 v[56:59], v[136:139], v[156:159], v[56:59]
	s_add_u32 m0, s28, 0x13000
	s_nop 0
	global_load_lds_dwordx4 v13, s[4:5]
	s_add_u32 s4, s4, s20
	s_addc_u32 s5, s5, 0
	s_waitcnt lgkmcnt(13)
	v_mfma_f32_16x16x32_f16 v[60:63], v[136:139], v[160:163], v[60:63]
	s_waitcnt lgkmcnt(12)
	v_mfma_f32_16x16x32_f16 v[64:67], v[136:139], v[164:167], v[64:67]
	s_waitcnt lgkmcnt(11)
	v_mfma_f32_16x16x32_f16 v[68:71], v[136:139], v[168:171], v[68:71]
	s_waitcnt lgkmcnt(10)
	v_mfma_f32_16x16x32_f16 v[72:75], v[140:143], v[156:159], v[72:75]
	v_mfma_f32_16x16x32_f16 v[76:79], v[140:143], v[160:163], v[76:79]
	s_add_u32 m0, s28, 0x16000
	s_nop 0
	global_load_lds_dwordx4 v10, s[6:7]
	v_mfma_f32_16x16x32_f16 v[80:83], v[140:143], v[164:167], v[80:83]
	v_mfma_f32_16x16x32_f16 v[84:87], v[140:143], v[168:171], v[84:87]
	s_waitcnt lgkmcnt(9)
	v_mfma_f32_16x16x32_f16 v[88:91], v[144:147], v[156:159], v[88:91]
	v_mfma_f32_16x16x32_f16 v[92:95], v[144:147], v[160:163], v[92:95]
	v_mfma_f32_16x16x32_f16 v[96:99], v[144:147], v[164:167], v[96:99]
	s_add_u32 m0, s28, 0x18000
	s_nop 0
	global_load_lds_dwordx4 v11, s[6:7]
	s_add_u32 s6, s6, s20
	s_addc_u32 s7, s7, 0
	v_mfma_f32_16x16x32_f16 v[100:103], v[144:147], v[168:171], v[100:103]
	s_waitcnt lgkmcnt(8)
	v_mfma_f32_16x16x32_f16 v[104:107], v[148:151], v[156:159], v[104:107]
	v_mfma_f32_16x16x32_f16 v[108:111], v[148:151], v[160:163], v[108:111]
	v_mfma_f32_16x16x32_f16 v[112:115], v[148:151], v[164:167], v[112:115]
	v_mfma_f32_16x16x32_f16 v[116:119], v[148:151], v[168:171], v[116:119]
	s_waitcnt vmcnt(6) lgkmcnt(0)
	s_barrier
	s_waitcnt lgkmcnt(7)
	ds_read_b128 v[136:139], v15
	ds_read_b128 v[156:159], v17
	ds_read_b128 v[160:163], v17 offset:2048
	ds_read_b128 v[164:167], v17 offset:4096
	ds_read_b128 v[168:171], v17 offset:6144
	ds_read_b128 v[140:143], v15 offset:2048
	ds_read_b128 v[144:147], v15 offset:4096
	ds_read_b128 v[148:151], v15 offset:6144
	s_waitcnt lgkmcnt(14)
	v_mfma_f32_16x16x32_f16 v[56:59], v[172:175], v[192:195], v[56:59]
	s_add_u32 m0, s28, 0x1a000
	s_nop 0
	global_load_lds_dwordx4 v10, s[4:5]
	s_waitcnt lgkmcnt(13)
	v_mfma_f32_16x16x32_f16 v[60:63], v[172:175], v[196:199], v[60:63]
	s_waitcnt lgkmcnt(12)
	v_mfma_f32_16x16x32_f16 v[64:67], v[172:175], v[200:203], v[64:67]
	s_waitcnt lgkmcnt(11)
	v_mfma_f32_16x16x32_f16 v[68:71], v[172:175], v[204:207], v[68:71]
	s_waitcnt lgkmcnt(10)
	v_mfma_f32_16x16x32_f16 v[72:75], v[176:179], v[192:195], v[72:75]
	v_mfma_f32_16x16x32_f16 v[76:79], v[176:179], v[196:199], v[76:79]
	s_add_u32 m0, s28, 0x1c000
	s_nop 0
	global_load_lds_dwordx4 v11, s[4:5]
	v_mfma_f32_16x16x32_f16 v[80:83], v[176:179], v[200:203], v[80:83]
	v_mfma_f32_16x16x32_f16 v[84:87], v[176:179], v[204:207], v[84:87]
	s_waitcnt lgkmcnt(9)
	v_mfma_f32_16x16x32_f16 v[88:91], v[180:183], v[192:195], v[88:91]
	v_mfma_f32_16x16x32_f16 v[92:95], v[180:183], v[196:199], v[92:95]
	v_mfma_f32_16x16x32_f16 v[96:99], v[180:183], v[200:203], v[96:99]
	s_add_u32 m0, s28, 0x1e000
	s_nop 0
	global_load_lds_dwordx4 v12, s[4:5]
	v_mfma_f32_16x16x32_f16 v[100:103], v[180:183], v[204:207], v[100:103]
	s_waitcnt lgkmcnt(8)
	v_mfma_f32_16x16x32_f16 v[104:107], v[184:187], v[192:195], v[104:107]
	v_mfma_f32_16x16x32_f16 v[108:111], v[184:187], v[196:199], v[108:111]
	v_mfma_f32_16x16x32_f16 v[112:115], v[184:187], v[200:203], v[112:115]
	v_mfma_f32_16x16x32_f16 v[116:119], v[184:187], v[204:207], v[116:119]
	s_waitcnt lgkmcnt(7)
	ds_read_b128 v[172:175], v16
	ds_read_b128 v[192:195], v18
	ds_read_b128 v[196:199], v18 offset:2048
	ds_read_b128 v[200:203], v18 offset:4096
	ds_read_b128 v[204:207], v18 offset:6144
	ds_read_b128 v[176:179], v16 offset:2048
	ds_read_b128 v[180:183], v16 offset:4096
	ds_read_b128 v[184:187], v16 offset:6144
	s_waitcnt lgkmcnt(14)
	v_mfma_f32_16x16x32_f16 v[56:59], v[136:139], v[156:159], v[56:59]
	s_add_u32 m0, s28, 0x20000
	s_nop 0
	global_load_lds_dwordx4 v13, s[4:5]
	s_add_u32 s4, s4, s20
	s_addc_u32 s5, s5, 0
	s_waitcnt lgkmcnt(13)
	v_mfma_f32_16x16x32_f16 v[60:63], v[136:139], v[160:163], v[60:63]
	s_waitcnt lgkmcnt(12)
	v_mfma_f32_16x16x32_f16 v[64:67], v[136:139], v[164:167], v[64:67]
	s_waitcnt lgkmcnt(11)
	v_mfma_f32_16x16x32_f16 v[68:71], v[136:139], v[168:171], v[68:71]
	s_waitcnt lgkmcnt(10)
	v_mfma_f32_16x16x32_f16 v[72:75], v[140:143], v[156:159], v[72:75]
	v_mfma_f32_16x16x32_f16 v[76:79], v[140:143], v[160:163], v[76:79]
	s_add_u32 m0, s28, 0x23000
	s_nop 0
	global_load_lds_dwordx4 v10, s[6:7]
	v_mfma_f32_16x16x32_f16 v[80:83], v[140:143], v[164:167], v[80:83]
	v_mfma_f32_16x16x32_f16 v[84:87], v[140:143], v[168:171], v[84:87]
	s_waitcnt lgkmcnt(9)
	v_mfma_f32_16x16x32_f16 v[88:91], v[144:147], v[156:159], v[88:91]
	v_mfma_f32_16x16x32_f16 v[92:95], v[144:147], v[160:163], v[92:95]
	v_mfma_f32_16x16x32_f16 v[96:99], v[144:147], v[164:167], v[96:99]
	s_add_u32 m0, s28, 0x25000
	s_nop 0
	global_load_lds_dwordx4 v11, s[6:7]
	s_add_u32 s6, s6, s20
	s_addc_u32 s7, s7, 0
	v_mfma_f32_16x16x32_f16 v[100:103], v[144:147], v[168:171], v[100:103]
	s_waitcnt lgkmcnt(8)
	v_mfma_f32_16x16x32_f16 v[104:107], v[148:151], v[156:159], v[104:107]
	v_mfma_f32_16x16x32_f16 v[108:111], v[148:151], v[160:163], v[108:111]
	v_mfma_f32_16x16x32_f16 v[112:115], v[148:151], v[164:167], v[112:115]
	v_mfma_f32_16x16x32_f16 v[116:119], v[148:151], v[168:171], v[116:119]
	s_waitcnt vmcnt(6) lgkmcnt(0)
	s_barrier
	s_waitcnt lgkmcnt(7)
	ds_read_b128 v[136:139], v15 offset:53248
	ds_read_b128 v[156:159], v17 offset:53248
	ds_read_b128 v[160:163], v17 offset:55296
	ds_read_b128 v[164:167], v17 offset:57344
	ds_read_b128 v[168:171], v17 offset:59392
	ds_read_b128 v[140:143], v15 offset:55296
	ds_read_b128 v[144:147], v15 offset:57344
	ds_read_b128 v[148:151], v15 offset:59392
	s_waitcnt lgkmcnt(14)
	v_mfma_f32_16x16x32_f16 v[56:59], v[172:175], v[192:195], v[56:59]
	s_add_u32 m0, s28, 0x0
	s_nop 0
	global_load_lds_dwordx4 v10, s[4:5]
	s_waitcnt lgkmcnt(13)
	v_mfma_f32_16x16x32_f16 v[60:63], v[172:175], v[196:199], v[60:63]
	s_waitcnt lgkmcnt(12)
	v_mfma_f32_16x16x32_f16 v[64:67], v[172:175], v[200:203], v[64:67]
	s_waitcnt lgkmcnt(11)
	v_mfma_f32_16x16x32_f16 v[68:71], v[172:175], v[204:207], v[68:71]
	s_waitcnt lgkmcnt(10)
	v_mfma_f32_16x16x32_f16 v[72:75], v[176:179], v[192:195], v[72:75]
	v_mfma_f32_16x16x32_f16 v[76:79], v[176:179], v[196:199], v[76:79]
	s_add_u32 m0, s28, 0x2000
	s_nop 0
	global_load_lds_dwordx4 v11, s[4:5]
	v_mfma_f32_16x16x32_f16 v[80:83], v[176:179], v[200:203], v[80:83]
	v_mfma_f32_16x16x32_f16 v[84:87], v[176:179], v[204:207], v[84:87]
	s_waitcnt lgkmcnt(9)
	v_mfma_f32_16x16x32_f16 v[88:91], v[180:183], v[192:195], v[88:91]
	v_mfma_f32_16x16x32_f16 v[92:95], v[180:183], v[196:199], v[92:95]
	v_mfma_f32_16x16x32_f16 v[96:99], v[180:183], v[200:203], v[96:99]
	s_add_u32 m0, s28, 0x4000
	s_nop 0
	global_load_lds_dwordx4 v12, s[4:5]
	v_mfma_f32_16x16x32_f16 v[100:103], v[180:183], v[204:207], v[100:103]
	s_waitcnt lgkmcnt(8)
	v_mfma_f32_16x16x32_f16 v[104:107], v[184:187], v[192:195], v[104:107]
	v_mfma_f32_16x16x32_f16 v[108:111], v[184:187], v[196:199], v[108:111]
	v_mfma_f32_16x16x32_f16 v[112:115], v[184:187], v[200:203], v[112:115]
	v_mfma_f32_16x16x32_f16 v[116:119], v[184:187], v[204:207], v[116:119]
	s_waitcnt lgkmcnt(7)
	ds_read_b128 v[172:175], v16 offset:53248
	ds_read_b128 v[192:195], v18 offset:53248
	ds_read_b128 v[196:199], v18 offset:55296
	ds_read_b128 v[200:203], v18 offset:57344
	ds_read_b128 v[204:207], v18 offset:59392
	ds_read_b128 v[176:179], v16 offset:55296
	ds_read_b128 v[180:183], v16 offset:57344
	ds_read_b128 v[184:187], v16 offset:59392
	s_waitcnt lgkmcnt(14)
	v_mfma_f32_16x16x32_f16 v[56:59], v[136:139], v[156:159], v[56:59]
	s_add_u32 m0, s28, 0x6000
	s_nop 0
	global_load_lds_dwordx4 v13, s[4:5]
	s_add_u32 s4, s4, s20
	s_addc_u32 s5, s5, 0
	s_waitcnt lgkmcnt(13)
	v_mfma_f32_16x16x32_f16 v[60:63], v[136:139], v[160:163], v[60:63]
	s_waitcnt lgkmcnt(12)
	v_mfma_f32_16x16x32_f16 v[64:67], v[136:139], v[164:167], v[64:67]
	s_waitcnt lgkmcnt(11)
	v_mfma_f32_16x16x32_f16 v[68:71], v[136:139], v[168:171], v[68:71]
	s_waitcnt lgkmcnt(10)
	v_mfma_f32_16x16x32_f16 v[72:75], v[140:143], v[156:159], v[72:75]
	v_mfma_f32_16x16x32_f16 v[76:79], v[140:143], v[160:163], v[76:79]
	s_add_u32 m0, s28, 0x9000
	s_nop 0
	global_load_lds_dwordx4 v10, s[6:7]
	v_mfma_f32_16x16x32_f16 v[80:83], v[140:143], v[164:167], v[80:83]
	v_mfma_f32_16x16x32_f16 v[84:87], v[140:143], v[168:171], v[84:87]
	s_waitcnt lgkmcnt(9)
	v_mfma_f32_16x16x32_f16 v[88:91], v[144:147], v[156:159], v[88:91]
	v_mfma_f32_16x16x32_f16 v[92:95], v[144:147], v[160:163], v[92:95]
	v_mfma_f32_16x16x32_f16 v[96:99], v[144:147], v[164:167], v[96:99]
	s_add_u32 m0, s28, 0xb000
	s_nop 0
	global_load_lds_dwordx4 v11, s[6:7]
	s_add_u32 s6, s6, s20
	s_addc_u32 s7, s7, 0
	v_mfma_f32_16x16x32_f16 v[100:103], v[144:147], v[168:171], v[100:103]
	s_waitcnt lgkmcnt(8)
	v_mfma_f32_16x16x32_f16 v[104:107], v[148:151], v[156:159], v[104:107]
	v_mfma_f32_16x16x32_f16 v[108:111], v[148:151], v[160:163], v[108:111]
	v_mfma_f32_16x16x32_f16 v[112:115], v[148:151], v[164:167], v[112:115]
	v_mfma_f32_16x16x32_f16 v[116:119], v[148:151], v[168:171], v[116:119]
	s_waitcnt vmcnt(6) lgkmcnt(0)
	s_barrier
	s_waitcnt lgkmcnt(7)
	ds_read_b128 v[136:139], v19
	ds_read_b128 v[156:159], v21
	ds_read_b128 v[160:163], v21 offset:2048
	ds_read_b128 v[164:167], v21 offset:4096
	ds_read_b128 v[168:171], v21 offset:6144
	ds_read_b128 v[140:143], v19 offset:2048
	ds_read_b128 v[144:147], v19 offset:4096
	ds_read_b128 v[148:151], v19 offset:6144
	s_waitcnt lgkmcnt(14)
	v_mfma_f32_16x16x32_f16 v[56:59], v[172:175], v[192:195], v[56:59]
	s_add_u32 m0, s28, 0xd000
	s_nop 0
	global_load_lds_dwordx4 v10, s[4:5]
	s_waitcnt lgkmcnt(13)
	v_mfma_f32_16x16x32_f16 v[60:63], v[172:175], v[196:199], v[60:63]
	s_waitcnt lgkmcnt(12)
	v_mfma_f32_16x16x32_f16 v[64:67], v[172:175], v[200:203], v[64:67]
	s_waitcnt lgkmcnt(11)
	v_mfma_f32_16x16x32_f16 v[68:71], v[172:175], v[204:207], v[68:71]
	s_waitcnt lgkmcnt(10)
	v_mfma_f32_16x16x32_f16 v[72:75], v[176:179], v[192:195], v[72:75]
	v_mfma_f32_16x16x32_f16 v[76:79], v[176:179], v[196:199], v[76:79]
	s_add_u32 m0, s28, 0xf000
	s_nop 0
	global_load_lds_dwordx4 v11, s[4:5]
	v_mfma_f32_16x16x32_f16 v[80:83], v[176:179], v[200:203], v[80:83]
	v_mfma_f32_16x16x32_f16 v[84:87], v[176:179], v[204:207], v[84:87]
	s_waitcnt lgkmcnt(9)
	v_mfma_f32_16x16x32_f16 v[88:91], v[180:183], v[192:195], v[88:91]
	v_mfma_f32_16x16x32_f16 v[92:95], v[180:183], v[196:199], v[92:95]
	v_mfma_f32_16x16x32_f16 v[96:99], v[180:183], v[200:203], v[96:99]
	s_add_u32 m0, s28, 0x11000
	s_nop 0
	global_load_lds_dwordx4 v12, s[4:5]
	v_mfma_f32_16x16x32_f16 v[100:103], v[180:183], v[204:207], v[100:103]
	s_waitcnt lgkmcnt(8)
	v_mfma_f32_16x16x32_f16 v[104:107], v[184:187], v[192:195], v[104:107]
	v_mfma_f32_16x16x32_f16 v[108:111], v[184:187], v[196:199], v[108:111]
	v_mfma_f32_16x16x32_f16 v[112:115], v[184:187], v[200:203], v[112:115]
	v_mfma_f32_16x16x32_f16 v[116:119], v[184:187], v[204:207], v[116:119]
	s_waitcnt lgkmcnt(7)
	ds_read_b128 v[172:175], v20
	ds_read_b128 v[192:195], v22
	ds_read_b128 v[196:199], v22 offset:2048
	ds_read_b128 v[200:203], v22 offset:4096
	ds_read_b128 v[204:207], v22 offset:6144
	ds_read_b128 v[176:179], v20 offset:2048
	ds_read_b128 v[180:183], v20 offset:4096
	ds_read_b128 v[184:187], v20 offset:6144
	s_waitcnt lgkmcnt(14)
	v_mfma_f32_16x16x32_f16 v[56:59], v[136:139], v[156:159], v[56:59]
	s_add_u32 m0, s28, 0x13000
	s_nop 0
	global_load_lds_dwordx4 v13, s[4:5]
	s_add_u32 s4, s4, s20
	s_addc_u32 s5, s5, 0
	s_waitcnt lgkmcnt(13)
	v_mfma_f32_16x16x32_f16 v[60:63], v[136:139], v[160:163], v[60:63]
	s_waitcnt lgkmcnt(12)
	v_mfma_f32_16x16x32_f16 v[64:67], v[136:139], v[164:167], v[64:67]
	s_waitcnt lgkmcnt(11)
	v_mfma_f32_16x16x32_f16 v[68:71], v[136:139], v[168:171], v[68:71]
	s_waitcnt lgkmcnt(10)
	v_mfma_f32_16x16x32_f16 v[72:75], v[140:143], v[156:159], v[72:75]
	v_mfma_f32_16x16x32_f16 v[76:79], v[140:143], v[160:163], v[76:79]
	s_add_u32 m0, s28, 0x16000
	s_nop 0
	global_load_lds_dwordx4 v10, s[6:7]
	v_mfma_f32_16x16x32_f16 v[80:83], v[140:143], v[164:167], v[80:83]
	v_mfma_f32_16x16x32_f16 v[84:87], v[140:143], v[168:171], v[84:87]
	s_waitcnt lgkmcnt(9)
	v_mfma_f32_16x16x32_f16 v[88:91], v[144:147], v[156:159], v[88:91]
	v_mfma_f32_16x16x32_f16 v[92:95], v[144:147], v[160:163], v[92:95]
	v_mfma_f32_16x16x32_f16 v[96:99], v[144:147], v[164:167], v[96:99]
	s_add_u32 m0, s28, 0x18000
	s_nop 0
	global_load_lds_dwordx4 v11, s[6:7]
	s_add_u32 s6, s6, s20
	s_addc_u32 s7, s7, 0
	v_mfma_f32_16x16x32_f16 v[100:103], v[144:147], v[168:171], v[100:103]
	s_waitcnt lgkmcnt(8)
	v_mfma_f32_16x16x32_f16 v[104:107], v[148:151], v[156:159], v[104:107]
	v_mfma_f32_16x16x32_f16 v[108:111], v[148:151], v[160:163], v[108:111]
	v_mfma_f32_16x16x32_f16 v[112:115], v[148:151], v[164:167], v[112:115]
	v_mfma_f32_16x16x32_f16 v[116:119], v[148:151], v[168:171], v[116:119]
	s_waitcnt vmcnt(6) lgkmcnt(0)
	s_barrier
	s_waitcnt lgkmcnt(7)
	ds_read_b128 v[136:139], v15
	ds_read_b128 v[156:159], v17
	ds_read_b128 v[160:163], v17 offset:2048
	ds_read_b128 v[164:167], v17 offset:4096
	ds_read_b128 v[168:171], v17 offset:6144
	ds_read_b128 v[140:143], v15 offset:2048
	ds_read_b128 v[144:147], v15 offset:4096
	ds_read_b128 v[148:151], v15 offset:6144
	s_waitcnt lgkmcnt(14)
	v_mfma_f32_16x16x32_f16 v[56:59], v[172:175], v[192:195], v[56:59]
	s_add_u32 m0, s28, 0x1a000
	s_nop 0
	global_load_lds_dwordx4 v10, s[4:5]
	s_waitcnt lgkmcnt(13)
	v_mfma_f32_16x16x32_f16 v[60:63], v[172:175], v[196:199], v[60:63]
	s_waitcnt lgkmcnt(12)
	v_mfma_f32_16x16x32_f16 v[64:67], v[172:175], v[200:203], v[64:67]
	s_waitcnt lgkmcnt(11)
	v_mfma_f32_16x16x32_f16 v[68:71], v[172:175], v[204:207], v[68:71]
	s_waitcnt lgkmcnt(10)
	v_mfma_f32_16x16x32_f16 v[72:75], v[176:179], v[192:195], v[72:75]
	v_mfma_f32_16x16x32_f16 v[76:79], v[176:179], v[196:199], v[76:79]
	s_add_u32 m0, s28, 0x1c000
	s_nop 0
	global_load_lds_dwordx4 v11, s[4:5]
	v_mfma_f32_16x16x32_f16 v[80:83], v[176:179], v[200:203], v[80:83]
	v_mfma_f32_16x16x32_f16 v[84:87], v[176:179], v[204:207], v[84:87]
	s_waitcnt lgkmcnt(9)
	v_mfma_f32_16x16x32_f16 v[88:91], v[180:183], v[192:195], v[88:91]
	v_mfma_f32_16x16x32_f16 v[92:95], v[180:183], v[196:199], v[92:95]
	v_mfma_f32_16x16x32_f16 v[96:99], v[180:183], v[200:203], v[96:99]
	s_add_u32 m0, s28, 0x1e000
	s_nop 0
	global_load_lds_dwordx4 v12, s[4:5]
	v_mfma_f32_16x16x32_f16 v[100:103], v[180:183], v[204:207], v[100:103]
	s_waitcnt lgkmcnt(8)
	v_mfma_f32_16x16x32_f16 v[104:107], v[184:187], v[192:195], v[104:107]
	v_mfma_f32_16x16x32_f16 v[108:111], v[184:187], v[196:199], v[108:111]
	v_mfma_f32_16x16x32_f16 v[112:115], v[184:187], v[200:203], v[112:115]
	v_mfma_f32_16x16x32_f16 v[116:119], v[184:187], v[204:207], v[116:119]
	s_waitcnt lgkmcnt(7)
	ds_read_b128 v[172:175], v16
	ds_read_b128 v[192:195], v18
	ds_read_b128 v[196:199], v18 offset:2048
	ds_read_b128 v[200:203], v18 offset:4096
	ds_read_b128 v[204:207], v18 offset:6144
	ds_read_b128 v[176:179], v16 offset:2048
	ds_read_b128 v[180:183], v16 offset:4096
	ds_read_b128 v[184:187], v16 offset:6144
	s_waitcnt lgkmcnt(14)
	v_mfma_f32_16x16x32_f16 v[56:59], v[136:139], v[156:159], v[56:59]
	s_add_u32 m0, s28, 0x20000
	s_nop 0
	global_load_lds_dwordx4 v13, s[4:5]
	s_add_u32 s4, s4, s20
	s_addc_u32 s5, s5, 0
	s_waitcnt lgkmcnt(13)
	v_mfma_f32_16x16x32_f16 v[60:63], v[136:139], v[160:163], v[60:63]
	s_waitcnt lgkmcnt(12)
	v_mfma_f32_16x16x32_f16 v[64:67], v[136:139], v[164:167], v[64:67]
	s_waitcnt lgkmcnt(11)
	v_mfma_f32_16x16x32_f16 v[68:71], v[136:139], v[168:171], v[68:71]
	s_waitcnt lgkmcnt(10)
	v_mfma_f32_16x16x32_f16 v[72:75], v[140:143], v[156:159], v[72:75]
	v_mfma_f32_16x16x32_f16 v[76:79], v[140:143], v[160:163], v[76:79]
	s_add_u32 m0, s28, 0x23000
	s_nop 0
	global_load_lds_dwordx4 v10, s[6:7]
	v_mfma_f32_16x16x32_f16 v[80:83], v[140:143], v[164:167], v[80:83]
	v_mfma_f32_16x16x32_f16 v[84:87], v[140:143], v[168:171], v[84:87]
	s_waitcnt lgkmcnt(9)
	v_mfma_f32_16x16x32_f16 v[88:91], v[144:147], v[156:159], v[88:91]
	v_mfma_f32_16x16x32_f16 v[92:95], v[144:147], v[160:163], v[92:95]
	v_mfma_f32_16x16x32_f16 v[96:99], v[144:147], v[164:167], v[96:99]
	s_add_u32 m0, s28, 0x25000
	s_nop 0
	global_load_lds_dwordx4 v11, s[6:7]
	s_add_u32 s6, s6, s20
	s_addc_u32 s7, s7, 0
	v_mfma_f32_16x16x32_f16 v[100:103], v[144:147], v[168:171], v[100:103]
	s_waitcnt lgkmcnt(8)
	v_mfma_f32_16x16x32_f16 v[104:107], v[148:151], v[156:159], v[104:107]
	v_mfma_f32_16x16x32_f16 v[108:111], v[148:151], v[160:163], v[108:111]
	v_mfma_f32_16x16x32_f16 v[112:115], v[148:151], v[164:167], v[112:115]
	v_mfma_f32_16x16x32_f16 v[116:119], v[148:151], v[168:171], v[116:119]
	s_waitcnt vmcnt(6) lgkmcnt(0)
	s_barrier
	s_waitcnt lgkmcnt(7)
	ds_read_b128 v[136:139], v15 offset:53248
	ds_read_b128 v[156:159], v17 offset:53248
	ds_read_b128 v[160:163], v17 offset:55296
	ds_read_b128 v[164:167], v17 offset:57344
	ds_read_b128 v[168:171], v17 offset:59392
	ds_read_b128 v[140:143], v15 offset:55296
	ds_read_b128 v[144:147], v15 offset:57344
	ds_read_b128 v[148:151], v15 offset:59392
	s_waitcnt lgkmcnt(14)
	v_mfma_f32_16x16x32_f16 v[56:59], v[172:175], v[192:195], v[56:59]
	s_add_u32 m0, s28, 0x0
	s_nop 0
	global_load_lds_dwordx4 v10, s[4:5]
	s_waitcnt lgkmcnt(13)
	v_mfma_f32_16x16x32_f16 v[60:63], v[172:175], v[196:199], v[60:63]
	s_waitcnt lgkmcnt(12)
	v_mfma_f32_16x16x32_f16 v[64:67], v[172:175], v[200:203], v[64:67]
	s_waitcnt lgkmcnt(11)
	v_mfma_f32_16x16x32_f16 v[68:71], v[172:175], v[204:207], v[68:71]
	s_waitcnt lgkmcnt(10)
	v_mfma_f32_16x16x32_f16 v[72:75], v[176:179], v[192:195], v[72:75]
	v_mfma_f32_16x16x32_f16 v[76:79], v[176:179], v[196:199], v[76:79]
	s_add_u32 m0, s28, 0x2000
	s_nop 0
	global_load_lds_dwordx4 v11, s[4:5]
	v_mfma_f32_16x16x32_f16 v[80:83], v[176:179], v[200:203], v[80:83]
	v_mfma_f32_16x16x32_f16 v[84:87], v[176:179], v[204:207], v[84:87]
	s_waitcnt lgkmcnt(9)
	v_mfma_f32_16x16x32_f16 v[88:91], v[180:183], v[192:195], v[88:91]
	v_mfma_f32_16x16x32_f16 v[92:95], v[180:183], v[196:199], v[92:95]
	v_mfma_f32_16x16x32_f16 v[96:99], v[180:183], v[200:203], v[96:99]
	s_add_u32 m0, s28, 0x4000
	s_nop 0
	global_load_lds_dwordx4 v12, s[4:5]
	v_mfma_f32_16x16x32_f16 v[100:103], v[180:183], v[204:207], v[100:103]
	s_waitcnt lgkmcnt(8)
	v_mfma_f32_16x16x32_f16 v[104:107], v[184:187], v[192:195], v[104:107]
	v_mfma_f32_16x16x32_f16 v[108:111], v[184:187], v[196:199], v[108:111]
	v_mfma_f32_16x16x32_f16 v[112:115], v[184:187], v[200:203], v[112:115]
	v_mfma_f32_16x16x32_f16 v[116:119], v[184:187], v[204:207], v[116:119]
	s_waitcnt lgkmcnt(7)
	ds_read_b128 v[172:175], v16 offset:53248
	ds_read_b128 v[192:195], v18 offset:53248
	ds_read_b128 v[196:199], v18 offset:55296
	ds_read_b128 v[200:203], v18 offset:57344
	ds_read_b128 v[204:207], v18 offset:59392
	ds_read_b128 v[176:179], v16 offset:55296
	ds_read_b128 v[180:183], v16 offset:57344
	ds_read_b128 v[184:187], v16 offset:59392
	s_waitcnt lgkmcnt(14)
	v_mfma_f32_16x16x32_f16 v[56:59], v[136:139], v[156:159], v[56:59]
	s_add_u32 m0, s28, 0x6000
	s_nop 0
	global_load_lds_dwordx4 v13, s[4:5]
	s_add_u32 s4, s4, s20
	s_addc_u32 s5, s5, 0
	s_waitcnt lgkmcnt(13)
	v_mfma_f32_16x16x32_f16 v[60:63], v[136:139], v[160:163], v[60:63]
	s_waitcnt lgkmcnt(12)
	v_mfma_f32_16x16x32_f16 v[64:67], v[136:139], v[164:167], v[64:67]
	s_waitcnt lgkmcnt(11)
	v_mfma_f32_16x16x32_f16 v[68:71], v[136:139], v[168:171], v[68:71]
	s_waitcnt lgkmcnt(10)
	v_mfma_f32_16x16x32_f16 v[72:75], v[140:143], v[156:159], v[72:75]
	v_mfma_f32_16x16x32_f16 v[76:79], v[140:143], v[160:163], v[76:79]
	s_add_u32 m0, s28, 0x9000
	s_nop 0
	global_load_lds_dwordx4 v10, s[6:7]
	v_mfma_f32_16x16x32_f16 v[80:83], v[140:143], v[164:167], v[80:83]
	v_mfma_f32_16x16x32_f16 v[84:87], v[140:143], v[168:171], v[84:87]
	s_waitcnt lgkmcnt(9)
	v_mfma_f32_16x16x32_f16 v[88:91], v[144:147], v[156:159], v[88:91]
	v_mfma_f32_16x16x32_f16 v[92:95], v[144:147], v[160:163], v[92:95]
	v_mfma_f32_16x16x32_f16 v[96:99], v[144:147], v[164:167], v[96:99]
	s_add_u32 m0, s28, 0xb000
	s_nop 0
	global_load_lds_dwordx4 v11, s[6:7]
	s_add_u32 s6, s6, s20
	s_addc_u32 s7, s7, 0
	v_mfma_f32_16x16x32_f16 v[100:103], v[144:147], v[168:171], v[100:103]
	s_waitcnt lgkmcnt(8)
	v_mfma_f32_16x16x32_f16 v[104:107], v[148:151], v[156:159], v[104:107]
	v_mfma_f32_16x16x32_f16 v[108:111], v[148:151], v[160:163], v[108:111]
	v_mfma_f32_16x16x32_f16 v[112:115], v[148:151], v[164:167], v[112:115]
	v_mfma_f32_16x16x32_f16 v[116:119], v[148:151], v[168:171], v[116:119]
	s_waitcnt vmcnt(6) lgkmcnt(0)
	s_barrier
	s_waitcnt lgkmcnt(7)
	ds_read_b128 v[136:139], v19
	ds_read_b128 v[156:159], v21
	ds_read_b128 v[160:163], v21 offset:2048
	ds_read_b128 v[164:167], v21 offset:4096
	ds_read_b128 v[168:171], v21 offset:6144
	ds_read_b128 v[140:143], v19 offset:2048
	ds_read_b128 v[144:147], v19 offset:4096
	ds_read_b128 v[148:151], v19 offset:6144
	s_waitcnt lgkmcnt(14)
	v_mfma_f32_16x16x32_f16 v[56:59], v[172:175], v[192:195], v[56:59]
	s_waitcnt lgkmcnt(13)
	v_mfma_f32_16x16x32_f16 v[60:63], v[172:175], v[196:199], v[60:63]
	s_waitcnt lgkmcnt(12)
	v_mfma_f32_16x16x32_f16 v[64:67], v[172:175], v[200:203], v[64:67]
	s_waitcnt lgkmcnt(11)
	v_mfma_f32_16x16x32_f16 v[68:71], v[172:175], v[204:207], v[68:71]
	s_waitcnt lgkmcnt(10)
	v_mfma_f32_16x16x32_f16 v[72:75], v[176:179], v[192:195], v[72:75]
	v_mfma_f32_16x16x32_f16 v[76:79], v[176:179], v[196:199], v[76:79]
	v_mfma_f32_16x16x32_f16 v[80:83], v[176:179], v[200:203], v[80:83]
	v_mfma_f32_16x16x32_f16 v[84:87], v[176:179], v[204:207], v[84:87]
	s_waitcnt lgkmcnt(9)
	v_mfma_f32_16x16x32_f16 v[88:91], v[180:183], v[192:195], v[88:91]
	v_mfma_f32_16x16x32_f16 v[92:95], v[180:183], v[196:199], v[92:95]
	v_mfma_f32_16x16x32_f16 v[96:99], v[180:183], v[200:203], v[96:99]
	v_mfma_f32_16x16x32_f16 v[100:103], v[180:183], v[204:207], v[100:103]
	s_waitcnt lgkmcnt(8)
	v_mfma_f32_16x16x32_f16 v[104:107], v[184:187], v[192:195], v[104:107]
	v_mfma_f32_16x16x32_f16 v[108:111], v[184:187], v[196:199], v[108:111]
	v_mfma_f32_16x16x32_f16 v[112:115], v[184:187], v[200:203], v[112:115]
	v_mfma_f32_16x16x32_f16 v[116:119], v[184:187], v[204:207], v[116:119]
	s_waitcnt lgkmcnt(7)
	ds_read_b128 v[172:175], v20
	ds_read_b128 v[192:195], v22
	ds_read_b128 v[196:199], v22 offset:2048
	ds_read_b128 v[200:203], v22 offset:4096
	ds_read_b128 v[204:207], v22 offset:6144
	ds_read_b128 v[176:179], v20 offset:2048
	ds_read_b128 v[180:183], v20 offset:4096
	ds_read_b128 v[184:187], v20 offset:6144
	s_waitcnt lgkmcnt(14)
	v_mfma_f32_16x16x32_f16 v[56:59], v[136:139], v[156:159], v[56:59]
	s_waitcnt lgkmcnt(13)
	v_mfma_f32_16x16x32_f16 v[60:63], v[136:139], v[160:163], v[60:63]
	s_waitcnt lgkmcnt(12)
	v_mfma_f32_16x16x32_f16 v[64:67], v[136:139], v[164:167], v[64:67]
	s_waitcnt lgkmcnt(11)
	v_mfma_f32_16x16x32_f16 v[68:71], v[136:139], v[168:171], v[68:71]
	s_waitcnt lgkmcnt(10)
	v_mfma_f32_16x16x32_f16 v[72:75], v[140:143], v[156:159], v[72:75]
	v_mfma_f32_16x16x32_f16 v[76:79], v[140:143], v[160:163], v[76:79]
	v_mfma_f32_16x16x32_f16 v[80:83], v[140:143], v[164:167], v[80:83]
	v_mfma_f32_16x16x32_f16 v[84:87], v[140:143], v[168:171], v[84:87]
	s_waitcnt lgkmcnt(9)
	v_mfma_f32_16x16x32_f16 v[88:91], v[144:147], v[156:159], v[88:91]
	v_mfma_f32_16x16x32_f16 v[92:95], v[144:147], v[160:163], v[92:95]
	v_mfma_f32_16x16x32_f16 v[96:99], v[144:147], v[164:167], v[96:99]
	v_mfma_f32_16x16x32_f16 v[100:103], v[144:147], v[168:171], v[100:103]
	s_waitcnt lgkmcnt(8)
	v_mfma_f32_16x16x32_f16 v[104:107], v[148:151], v[156:159], v[104:107]
	v_mfma_f32_16x16x32_f16 v[108:111], v[148:151], v[160:163], v[108:111]
	v_mfma_f32_16x16x32_f16 v[112:115], v[148:151], v[164:167], v[112:115]
	v_mfma_f32_16x16x32_f16 v[116:119], v[148:151], v[168:171], v[116:119]
	s_waitcnt vmcnt(0) lgkmcnt(0)
	s_barrier
	s_waitcnt lgkmcnt(7)
	ds_read_b128 v[136:139], v15
	ds_read_b128 v[156:159], v17
	ds_read_b128 v[160:163], v17 offset:2048
	ds_read_b128 v[164:167], v17 offset:4096
	ds_read_b128 v[168:171], v17 offset:6144
	ds_read_b128 v[140:143], v15 offset:2048
	ds_read_b128 v[144:147], v15 offset:4096
	ds_read_b128 v[148:151], v15 offset:6144
	s_waitcnt lgkmcnt(14)
	v_mfma_f32_16x16x32_f16 v[56:59], v[172:175], v[192:195], v[56:59]
	s_waitcnt lgkmcnt(13)
	v_mfma_f32_16x16x32_f16 v[60:63], v[172:175], v[196:199], v[60:63]
	s_waitcnt lgkmcnt(12)
	v_mfma_f32_16x16x32_f16 v[64:67], v[172:175], v[200:203], v[64:67]
	s_waitcnt lgkmcnt(11)
	v_mfma_f32_16x16x32_f16 v[68:71], v[172:175], v[204:207], v[68:71]
	s_waitcnt lgkmcnt(10)
	v_mfma_f32_16x16x32_f16 v[72:75], v[176:179], v[192:195], v[72:75]
	v_mfma_f32_16x16x32_f16 v[76:79], v[176:179], v[196:199], v[76:79]
	v_mfma_f32_16x16x32_f16 v[80:83], v[176:179], v[200:203], v[80:83]
	v_mfma_f32_16x16x32_f16 v[84:87], v[176:179], v[204:207], v[84:87]
	s_waitcnt lgkmcnt(9)
	v_mfma_f32_16x16x32_f16 v[88:91], v[180:183], v[192:195], v[88:91]
	v_mfma_f32_16x16x32_f16 v[92:95], v[180:183], v[196:199], v[92:95]
	v_mfma_f32_16x16x32_f16 v[96:99], v[180:183], v[200:203], v[96:99]
	v_mfma_f32_16x16x32_f16 v[100:103], v[180:183], v[204:207], v[100:103]
	s_waitcnt lgkmcnt(8)
	v_mfma_f32_16x16x32_f16 v[104:107], v[184:187], v[192:195], v[104:107]
	v_mfma_f32_16x16x32_f16 v[108:111], v[184:187], v[196:199], v[108:111]
	v_mfma_f32_16x16x32_f16 v[112:115], v[184:187], v[200:203], v[112:115]
	v_mfma_f32_16x16x32_f16 v[116:119], v[184:187], v[204:207], v[116:119]
	s_waitcnt lgkmcnt(7)
	ds_read_b128 v[172:175], v16
	ds_read_b128 v[192:195], v18
	ds_read_b128 v[196:199], v18 offset:2048
	ds_read_b128 v[200:203], v18 offset:4096
	ds_read_b128 v[204:207], v18 offset:6144
	ds_read_b128 v[176:179], v16 offset:2048
	ds_read_b128 v[180:183], v16 offset:4096
	ds_read_b128 v[184:187], v16 offset:6144
	s_waitcnt lgkmcnt(14)
	v_mfma_f32_16x16x32_f16 v[56:59], v[136:139], v[156:159], v[56:59]
	s_waitcnt lgkmcnt(13)
	v_mfma_f32_16x16x32_f16 v[60:63], v[136:139], v[160:163], v[60:63]
	s_waitcnt lgkmcnt(12)
	v_mfma_f32_16x16x32_f16 v[64:67], v[136:139], v[164:167], v[64:67]
	s_waitcnt lgkmcnt(11)
	v_mfma_f32_16x16x32_f16 v[68:71], v[136:139], v[168:171], v[68:71]
	s_waitcnt lgkmcnt(10)
	v_mfma_f32_16x16x32_f16 v[72:75], v[140:143], v[156:159], v[72:75]
	v_mfma_f32_16x16x32_f16 v[76:79], v[140:143], v[160:163], v[76:79]
	v_mfma_f32_16x16x32_f16 v[80:83], v[140:143], v[164:167], v[80:83]
	v_mfma_f32_16x16x32_f16 v[84:87], v[140:143], v[168:171], v[84:87]
	s_waitcnt lgkmcnt(9)
	v_mfma_f32_16x16x32_f16 v[88:91], v[144:147], v[156:159], v[88:91]
	v_mfma_f32_16x16x32_f16 v[92:95], v[144:147], v[160:163], v[92:95]
	v_mfma_f32_16x16x32_f16 v[96:99], v[144:147], v[164:167], v[96:99]
	v_mfma_f32_16x16x32_f16 v[100:103], v[144:147], v[168:171], v[100:103]
	s_waitcnt lgkmcnt(8)
	v_mfma_f32_16x16x32_f16 v[104:107], v[148:151], v[156:159], v[104:107]
	v_mfma_f32_16x16x32_f16 v[108:111], v[148:151], v[160:163], v[108:111]
	v_mfma_f32_16x16x32_f16 v[112:115], v[148:151], v[164:167], v[112:115]
	v_mfma_f32_16x16x32_f16 v[116:119], v[148:151], v[168:171], v[116:119]
	s_waitcnt lgkmcnt(6)
	v_mfma_f32_16x16x32_f16 v[56:59], v[172:175], v[192:195], v[56:59]
	s_waitcnt lgkmcnt(5)
	v_mfma_f32_16x16x32_f16 v[60:63], v[172:175], v[196:199], v[60:63]
	s_waitcnt lgkmcnt(4)
	v_mfma_f32_16x16x32_f16 v[64:67], v[172:175], v[200:203], v[64:67]
	s_waitcnt lgkmcnt(3)
	v_mfma_f32_16x16x32_f16 v[68:71], v[172:175], v[204:207], v[68:71]
	s_waitcnt lgkmcnt(2)
	v_mfma_f32_16x16x32_f16 v[72:75], v[176:179], v[192:195], v[72:75]
	v_mfma_f32_16x16x32_f16 v[76:79], v[176:179], v[196:199], v[76:79]
	v_mfma_f32_16x16x32_f16 v[80:83], v[176:179], v[200:203], v[80:83]
	v_mfma_f32_16x16x32_f16 v[84:87], v[176:179], v[204:207], v[84:87]
	s_waitcnt lgkmcnt(1)
	v_mfma_f32_16x16x32_f16 v[88:91], v[180:183], v[192:195], v[88:91]
	v_mfma_f32_16x16x32_f16 v[92:95], v[180:183], v[196:199], v[92:95]
	v_mfma_f32_16x16x32_f16 v[96:99], v[180:183], v[200:203], v[96:99]
	v_mfma_f32_16x16x32_f16 v[100:103], v[180:183], v[204:207], v[100:103]
	s_waitcnt lgkmcnt(0)
	v_mfma_f32_16x16x32_f16 v[104:107], v[184:187], v[192:195], v[104:107]
	v_mfma_f32_16x16x32_f16 v[108:111], v[184:187], v[196:199], v[108:111]
	v_mfma_f32_16x16x32_f16 v[112:115], v[184:187], v[200:203], v[112:115]
	v_mfma_f32_16x16x32_f16 v[116:119], v[184:187], v[204:207], v[116:119]
	s_nop 7
	s_nop 1
	s_add_u32 s24, s29, 0
	s_lshl_b32 s8, s24, 11
	v_add_u32_e32 v212, s8, v23
	v_pk_add_f32 v[56:57], v[56:57], v[24:25] op_sel_hi:[1,0]
	v_pk_add_f32 v[58:59], v[58:59], v[24:25] op_sel_hi:[1,0]
	v_cvt_pk_f16_f32 v56, v56, v57
	v_cvt_pk_f16_f32 v57, v58, v59
	global_store_dwordx2 v212, v[56:57], s[22:23] offset:0 sc0 sc1
	v_pk_add_f32 v[60:61], v[60:61], v[26:27] op_sel_hi:[1,0]
	v_pk_add_f32 v[62:63], v[62:63], v[26:27] op_sel_hi:[1,0]
	v_cvt_pk_f16_f32 v60, v60, v61
	v_cvt_pk_f16_f32 v61, v62, v63
	global_store_dwordx2 v212, v[60:61], s[22:23] offset:256 sc0 sc1
	v_pk_add_f32 v[64:65], v[64:65], v[28:29] op_sel_hi:[1,0]
	v_pk_add_f32 v[66:67], v[66:67], v[28:29] op_sel_hi:[1,0]
	v_cvt_pk_f16_f32 v64, v64, v65
	v_cvt_pk_f16_f32 v65, v66, v67
	global_store_dwordx2 v212, v[64:65], s[22:23] offset:1024 sc0 sc1
	v_pk_add_f32 v[68:69], v[68:69], v[30:31] op_sel_hi:[1,0]
	v_pk_add_f32 v[70:71], v[70:71], v[30:31] op_sel_hi:[1,0]
	v_cvt_pk_f16_f32 v68, v68, v69
	v_cvt_pk_f16_f32 v69, v70, v71
	global_store_dwordx2 v212, v[68:69], s[22:23] offset:1280 sc0 sc1
	s_add_u32 s24, s29, 1
	s_lshl_b32 s8, s24, 11
	v_add_u32_e32 v212, s8, v23
	v_pk_add_f32 v[72:73], v[72:73], v[24:25] op_sel_hi:[1,0]
	v_pk_add_f32 v[74:75], v[74:75], v[24:25] op_sel_hi:[1,0]
	v_cvt_pk_f16_f32 v72, v72, v73
	v_cvt_pk_f16_f32 v73, v74, v75
	global_store_dwordx2 v212, v[72:73], s[22:23] offset:0 sc0 sc1
	v_pk_add_f32 v[76:77], v[76:77], v[26:27] op_sel_hi:[1,0]
	v_pk_add_f32 v[78:79], v[78:79], v[26:27] op_sel_hi:[1,0]
	v_cvt_pk_f16_f32 v76, v76, v77
	v_cvt_pk_f16_f32 v77, v78, v79
	global_store_dwordx2 v212, v[76:77], s[22:23] offset:256 sc0 sc1
	v_pk_add_f32 v[80:81], v[80:81], v[28:29] op_sel_hi:[1,0]
	v_pk_add_f32 v[82:83], v[82:83], v[28:29] op_sel_hi:[1,0]
	v_cvt_pk_f16_f32 v80, v80, v81
	v_cvt_pk_f16_f32 v81, v82, v83
	global_store_dwordx2 v212, v[80:81], s[22:23] offset:1024 sc0 sc1
	v_pk_add_f32 v[84:85], v[84:85], v[30:31] op_sel_hi:[1,0]
	v_pk_add_f32 v[86:87], v[86:87], v[30:31] op_sel_hi:[1,0]
	v_cvt_pk_f16_f32 v84, v84, v85
	v_cvt_pk_f16_f32 v85, v86, v87
	global_store_dwordx2 v212, v[84:85], s[22:23] offset:1280 sc0 sc1
	s_add_u32 s24, s29, 2
	s_lshl_b32 s8, s24, 11
	v_add_u32_e32 v212, s8, v23
	v_pk_add_f32 v[88:89], v[88:89], v[24:25] op_sel_hi:[1,0]
	v_pk_add_f32 v[90:91], v[90:91], v[24:25] op_sel_hi:[1,0]
	v_cvt_pk_f16_f32 v88, v88, v89
	v_cvt_pk_f16_f32 v89, v90, v91
	global_store_dwordx2 v212, v[88:89], s[22:23] offset:0 sc0 sc1
	v_pk_add_f32 v[92:93], v[92:93], v[26:27] op_sel_hi:[1,0]
	v_pk_add_f32 v[94:95], v[94:95], v[26:27] op_sel_hi:[1,0]
	v_cvt_pk_f16_f32 v92, v92, v93
	v_cvt_pk_f16_f32 v93, v94, v95
	global_store_dwordx2 v212, v[92:93], s[22:23] offset:256 sc0 sc1
	v_pk_add_f32 v[96:97], v[96:97], v[28:29] op_sel_hi:[1,0]
	v_pk_add_f32 v[98:99], v[98:99], v[28:29] op_sel_hi:[1,0]
	v_cvt_pk_f16_f32 v96, v96, v97
	v_cvt_pk_f16_f32 v97, v98, v99
	global_store_dwordx2 v212, v[96:97], s[22:23] offset:1024 sc0 sc1
	v_pk_add_f32 v[100:101], v[100:101], v[30:31] op_sel_hi:[1,0]
	v_pk_add_f32 v[102:103], v[102:103], v[30:31] op_sel_hi:[1,0]
	v_cvt_pk_f16_f32 v100, v100, v101
	v_cvt_pk_f16_f32 v101, v102, v103
	global_store_dwordx2 v212, v[100:101], s[22:23] offset:1280 sc0 sc1
	s_add_u32 s24, s29, 3
	s_lshl_b32 s8, s24, 11
	v_add_u32_e32 v212, s8, v23
	v_pk_add_f32 v[104:105], v[104:105], v[24:25] op_sel_hi:[1,0]
	v_pk_add_f32 v[106:107], v[106:107], v[24:25] op_sel_hi:[1,0]
	v_cvt_pk_f16_f32 v104, v104, v105
	v_cvt_pk_f16_f32 v105, v106, v107
	global_store_dwordx2 v212, v[104:105], s[22:23] offset:0 sc0 sc1
	v_pk_add_f32 v[108:109], v[108:109], v[26:27] op_sel_hi:[1,0]
	v_pk_add_f32 v[110:111], v[110:111], v[26:27] op_sel_hi:[1,0]
	v_cvt_pk_f16_f32 v108, v108, v109
	v_cvt_pk_f16_f32 v109, v110, v111
	global_store_dwordx2 v212, v[108:109], s[22:23] offset:256 sc0 sc1
	v_pk_add_f32 v[112:113], v[112:113], v[28:29] op_sel_hi:[1,0]
	v_pk_add_f32 v[114:115], v[114:115], v[28:29] op_sel_hi:[1,0]
	v_cvt_pk_f16_f32 v112, v112, v113
	v_cvt_pk_f16_f32 v113, v114, v115
	global_store_dwordx2 v212, v[112:113], s[22:23] offset:1024 sc0 sc1
	v_pk_add_f32 v[116:117], v[116:117], v[30:31] op_sel_hi:[1,0]
	v_pk_add_f32 v[118:119], v[118:119], v[30:31] op_sel_hi:[1,0]
	v_cvt_pk_f16_f32 v116, v116, v117
	v_cvt_pk_f16_f32 v117, v118, v119
	global_store_dwordx2 v212, v[116:117], s[22:23] offset:1280 sc0 sc1
	s_branch .Lpf_done
